# PEER gather V pass unrolled with one wait per batch of four rows
# speedup vs baseline: 1.0066x; 1.0008x over previous
.LBB0_1138:
	v_and_b32_e32 v4, 15, v148
	v_cmp_eq_u32_e32 vcc, 0, v4
	v_lshlrev_b32_e32 v5, 5, v40
	v_add_u32_e32 v10, 0x80, v148
	v_cndmask_b32_e32 v10, v10, v5, vcc
	v_cmp_gt_u32_e64 s[6:7], 8, v4
	v_lshl_add_u32 v32, v10, 2, v111
	v_and_b32_e32 v36, 12, v148
	v_cndmask_b32_e64 v10, 0, v252, s[6:7]
	v_cmp_lt_u32_e64 s[6:7], 3, v4
	v_lshl_or_b32 v4, v41, 3, v5
	v_add_u32_e32 v34, 0x400, v4
	v_lshlrev_b32_e32 v4, 4, v41
	v_lshl_or_b32 v35, v40, 6, v4
	ds_bpermute_b32 v4, v36, v130
	v_cmp_eq_u32_e32 vcc, 3, v41
	v_cmp_eq_u32_e64 s[2:3], 2, v41
	v_cmp_eq_u32_e64 s[4:5], 1, v41
	v_lshlrev_b32_e32 v129, 4, v148
	s_waitcnt lgkmcnt(0)
	v_mul_lo_u32 v4, v4, s43
	v_add_u32_e32 v5, v4, v35
	v_add_u32_e32 v4, v4, v34
	buffer_load_dwordx4 v[38:41], v5, s[44:47], 0 offen
	buffer_load_dwordx2 v[42:43], v4, s[44:47], 0 offen
	buffer_load_dwordx4 v[44:47], v5, s[44:47], s21 offen
	buffer_load_dwordx2 v[48:49], v4, s[44:47], s33 offen
	buffer_load_dwordx4 v[50:53], v5, s[44:47], s20 offen
	buffer_load_dwordx2 v[54:55], v4, s[44:47], s21 offen
	buffer_load_dwordx4 v[56:59], v5, s[44:47], s23 offen
	buffer_load_dwordx2 v[60:61], v4, s[44:47], s94 offen
	s_mov_b32 s0, 0
	v_cndmask_b32_e64 v33, 1.0, v10, s[6:7]
	ds_bpermute_b32 v4, v36, v130 offset:16
	s_waitcnt lgkmcnt(0)
	v_mul_lo_u32 v4, v4, s43
	v_add_u32_e32 v5, v4, v35
	v_add_u32_e32 v4, v4, v34
	buffer_load_dwordx4 v[62:65], v5, s[44:47], 0 offen
	buffer_load_dwordx4 v[68:71], v5, s[44:47], s20 offen
	buffer_load_dwordx4 v[74:77], v5, s[44:47], s21 offen
	buffer_load_dwordx4 v[86:89], v5, s[44:47], s23 offen
	buffer_load_dwordx2 v[66:67], v4, s[44:47], 0 offen
	buffer_load_dwordx2 v[78:79], v4, s[44:47], s33 offen
	buffer_load_dwordx2 v[72:73], v4, s[44:47], s21 offen
	buffer_load_dwordx2 v[90:91], v4, s[44:47], s94 offen
	ds_bpermute_b32 v4, v36, v130 offset:32
	s_waitcnt lgkmcnt(0)
	v_mul_lo_u32 v4, v4, s43
	v_add_u32_e32 v5, v4, v35
	v_add_u32_e32 v4, v4, v34
	buffer_load_dwordx4 v[92:95], v5, s[44:47], 0 offen
	buffer_load_dwordx4 v[98:101], v5, s[44:47], s20 offen
	buffer_load_dwordx4 v[150:153], v5, s[44:47], s21 offen
	buffer_load_dwordx4 v[156:159], v5, s[44:47], s23 offen
	buffer_load_dwordx2 v[96:97], v4, s[44:47], 0 offen
	buffer_load_dwordx2 v[154:155], v4, s[44:47], s33 offen
	buffer_load_dwordx2 v[102:103], v4, s[44:47], s21 offen
	buffer_load_dwordx2 v[160:161], v4, s[44:47], s94 offen
	ds_bpermute_b32 v4, v36, v130 offset:48
	s_waitcnt lgkmcnt(0)
	v_mul_lo_u32 v4, v4, s43
	v_add_u32_e32 v5, v4, v35
	v_add_u32_e32 v4, v4, v34
	buffer_load_dwordx4 v[162:165], v5, s[44:47], 0 offen
	buffer_load_dwordx4 v[168:171], v5, s[44:47], s20 offen
	buffer_load_dwordx4 v[174:177], v5, s[44:47], s21 offen
	buffer_load_dwordx4 v[216:219], v5, s[44:47], s23 offen
	buffer_load_dwordx2 v[166:167], v4, s[44:47], 0 offen
	buffer_load_dwordx2 v[178:179], v4, s[44:47], s33 offen
	buffer_load_dwordx2 v[172:173], v4, s[44:47], s21 offen
	buffer_load_dwordx2 v[220:221], v4, s[44:47], s94 offen
	v_mov_b32_e32 v22, v28
	v_mov_b32_e32 v23, v29
	v_mov_b32_e32 v16, v30
	v_mov_b32_e32 v17, v31
	s_waitcnt vmcnt(30)
	v_mfma_f32_16x16x128_f8f6f4 v[38:41], v[38:43], v[18:23], 0 cbsz:2 blgp:2
	v_mov_b32_e32 v10, v24
	v_mov_b32_e32 v11, v25
	v_mov_b32_e32 v4, v26
	s_waitcnt vmcnt(28)
	v_mfma_f32_16x16x128_f8f6f4 v[28:31], v[44:49], v[12:17], v[38:41] cbsz:2 blgp:2
	v_mov_b32_e32 v5, v27
	s_waitcnt vmcnt(26)
	v_mfma_f32_16x16x128_f8f6f4 v[28:31], v[50:55], v[6:11], v[28:31] cbsz:2 blgp:2
	s_waitcnt vmcnt(24)
	v_mfma_f32_16x16x128_f8f6f4 v[24:27], v[56:61], v[0:5], v[28:31] cbsz:2 blgp:2
	s_nop 7
	v_cndmask_b32_e64 v24, v24, v25, s[4:5]
	v_cndmask_b32_e64 v24, v24, v26, s[2:3]
	v_cndmask_b32_e32 v24, v24, v27, vcc
	v_mul_f32_e32 v25, v33, v24
	s_nop 1
	v_mov_b32_dpp v25, v25 quad_perm:[1,0,3,2] row_mask:0xf bank_mask:0xf bound_ctrl:1
	v_fmac_f32_e32 v25, v33, v24
	s_nop 1
	v_add_f32_dpp v24, v25, v25 quad_perm:[2,3,0,1] row_mask:0xf bank_mask:0xf bound_ctrl:1
	s_nop 1
	v_add_f32_dpp v24, v24, v24 row_half_mirror row_mask:0xf bank_mask:0xf bound_ctrl:1
	ds_write_b32 v32, v24 offset:49152
	ds_bpermute_b32 v24, v36, v130 offset:64
	s_waitcnt lgkmcnt(0)
	v_mul_lo_u32 v24, v24, s43
	v_add_u32_e32 v28, v24, v35
	v_add_u32_e32 v30, v24, v34
	buffer_load_dwordx4 v[24:27], v28, s[44:47], 0 offen
	buffer_load_dwordx4 v[38:41], v28, s[44:47], s20 offen
	buffer_load_dwordx4 v[44:47], v28, s[44:47], s21 offen
	buffer_load_dwordx4 v[50:53], v28, s[44:47], s23 offen
	s_nop 0
	buffer_load_dwordx2 v[28:29], v30, s[44:47], 0 offen
	buffer_load_dwordx2 v[48:49], v30, s[44:47], s33 offen
	buffer_load_dwordx2 v[42:43], v30, s[44:47], s21 offen
	buffer_load_dwordx2 v[54:55], v30, s[44:47], s94 offen
	s_waitcnt vmcnt(27)
	v_mfma_f32_16x16x128_f8f6f4 v[56:59], v[62:67], v[18:23], 0 cbsz:2 blgp:2
	s_waitcnt vmcnt(26)
	v_mfma_f32_16x16x128_f8f6f4 v[56:59], v[74:79], v[12:17], v[56:59] cbsz:2 blgp:2
	s_waitcnt vmcnt(25)
	v_mfma_f32_16x16x128_f8f6f4 v[56:59], v[68:73], v[6:11], v[56:59] cbsz:2 blgp:2
	s_waitcnt vmcnt(24)
	v_mfma_f32_16x16x128_f8f6f4 v[56:59], v[86:91], v[0:5], v[56:59] cbsz:2 blgp:2
	s_nop 7
	v_cndmask_b32_e64 v30, v56, v57, s[4:5]
	v_cndmask_b32_e64 v30, v30, v58, s[2:3]
	v_cndmask_b32_e32 v30, v30, v59, vcc
	v_mul_f32_e32 v31, v33, v30
	s_nop 1
	v_mov_b32_dpp v31, v31 quad_perm:[1,0,3,2] row_mask:0xf bank_mask:0xf bound_ctrl:1
	v_fmac_f32_e32 v31, v33, v30
	s_nop 1
	v_add_f32_dpp v30, v31, v31 quad_perm:[2,3,0,1] row_mask:0xf bank_mask:0xf bound_ctrl:1
	s_nop 1
	v_add_f32_dpp v30, v30, v30 row_half_mirror row_mask:0xf bank_mask:0xf bound_ctrl:1
	ds_write_b32 v32, v30 offset:49156
	ds_bpermute_b32 v30, v36, v130 offset:80
	s_waitcnt lgkmcnt(0)
	v_mul_lo_u32 v30, v30, s43
	v_add_u32_e32 v31, v30, v35
	v_add_u32_e32 v30, v30, v34
	buffer_load_dwordx4 v[56:59], v31, s[44:47], 0 offen
	buffer_load_dwordx4 v[62:65], v31, s[44:47], s20 offen
	buffer_load_dwordx4 v[68:71], v31, s[44:47], s21 offen
	buffer_load_dwordx4 v[74:77], v31, s[44:47], s23 offen
	buffer_load_dwordx2 v[60:61], v30, s[44:47], 0 offen
	buffer_load_dwordx2 v[72:73], v30, s[44:47], s33 offen
	buffer_load_dwordx2 v[66:67], v30, s[44:47], s21 offen
	buffer_load_dwordx2 v[78:79], v30, s[44:47], s94 offen
	s_waitcnt vmcnt(27)
	v_mfma_f32_16x16x128_f8f6f4 v[86:89], v[92:97], v[18:23], 0 cbsz:2 blgp:2
	s_waitcnt vmcnt(26)
	v_mfma_f32_16x16x128_f8f6f4 v[86:89], v[150:155], v[12:17], v[86:89] cbsz:2 blgp:2
	s_waitcnt vmcnt(25)
	v_mfma_f32_16x16x128_f8f6f4 v[86:89], v[98:103], v[6:11], v[86:89] cbsz:2 blgp:2
	s_waitcnt vmcnt(24)
	v_mfma_f32_16x16x128_f8f6f4 v[86:89], v[156:161], v[0:5], v[86:89] cbsz:2 blgp:2
	s_nop 7
	v_cndmask_b32_e64 v30, v86, v87, s[4:5]
	v_cndmask_b32_e64 v30, v30, v88, s[2:3]
	v_cndmask_b32_e32 v30, v30, v89, vcc
	v_mul_f32_e32 v31, v33, v30
	s_nop 1
	v_mov_b32_dpp v31, v31 quad_perm:[1,0,3,2] row_mask:0xf bank_mask:0xf bound_ctrl:1
	v_fmac_f32_e32 v31, v33, v30
	s_nop 1
	v_add_f32_dpp v30, v31, v31 quad_perm:[2,3,0,1] row_mask:0xf bank_mask:0xf bound_ctrl:1
	s_nop 1
	v_add_f32_dpp v30, v30, v30 row_half_mirror row_mask:0xf bank_mask:0xf bound_ctrl:1
	ds_write_b32 v32, v30 offset:49160
	ds_bpermute_b32 v30, v36, v130 offset:96
	s_waitcnt lgkmcnt(0)
	v_mul_lo_u32 v30, v30, s43
	v_add_u32_e32 v31, v30, v35
	v_add_u32_e32 v30, v30, v34
	buffer_load_dwordx4 v[86:89], v31, s[44:47], 0 offen
	buffer_load_dwordx4 v[92:95], v31, s[44:47], s20 offen
	buffer_load_dwordx4 v[98:101], v31, s[44:47], s21 offen
	buffer_load_dwordx4 v[150:153], v31, s[44:47], s23 offen
	buffer_load_dwordx2 v[90:91], v30, s[44:47], 0 offen
	buffer_load_dwordx2 v[102:103], v30, s[44:47], s33 offen
	buffer_load_dwordx2 v[96:97], v30, s[44:47], s21 offen
	buffer_load_dwordx2 v[154:155], v30, s[44:47], s94 offen
	s_waitcnt vmcnt(27)
	v_mfma_f32_16x16x128_f8f6f4 v[156:159], v[162:167], v[18:23], 0 cbsz:2 blgp:2
	s_waitcnt vmcnt(26)
	v_mfma_f32_16x16x128_f8f6f4 v[156:159], v[174:179], v[12:17], v[156:159] cbsz:2 blgp:2
	s_waitcnt vmcnt(25)
	v_mfma_f32_16x16x128_f8f6f4 v[156:159], v[168:173], v[6:11], v[156:159] cbsz:2 blgp:2
	s_waitcnt vmcnt(24)
	v_mfma_f32_16x16x128_f8f6f4 v[156:159], v[216:221], v[0:5], v[156:159] cbsz:2 blgp:2
	s_nop 7
	v_cndmask_b32_e64 v30, v156, v157, s[4:5]
	v_cndmask_b32_e64 v30, v30, v158, s[2:3]
	v_cndmask_b32_e32 v30, v30, v159, vcc
	v_mul_f32_e32 v31, v33, v30
	s_nop 1
	v_mov_b32_dpp v31, v31 quad_perm:[1,0,3,2] row_mask:0xf bank_mask:0xf bound_ctrl:1
	v_fmac_f32_e32 v31, v33, v30
	s_nop 1
	v_add_f32_dpp v30, v31, v31 quad_perm:[2,3,0,1] row_mask:0xf bank_mask:0xf bound_ctrl:1
	s_nop 1
	v_add_f32_dpp v30, v30, v30 row_half_mirror row_mask:0xf bank_mask:0xf bound_ctrl:1
	ds_write_b32 v32, v30 offset:49164
	ds_bpermute_b32 v30, v36, v130 offset:112
	s_waitcnt lgkmcnt(0)
	v_mul_lo_u32 v30, v30, s43
	v_add_u32_e32 v31, v30, v35
	v_add_u32_e32 v30, v30, v34
	buffer_load_dwordx4 v[156:159], v31, s[44:47], 0 offen
	buffer_load_dwordx4 v[162:165], v31, s[44:47], s20 offen
	buffer_load_dwordx4 v[168:171], v31, s[44:47], s21 offen
	buffer_load_dwordx4 v[174:177], v31, s[44:47], s23 offen
	buffer_load_dwordx2 v[160:161], v30, s[44:47], 0 offen
	buffer_load_dwordx2 v[172:173], v30, s[44:47], s33 offen
	buffer_load_dwordx2 v[166:167], v30, s[44:47], s21 offen
	buffer_load_dwordx2 v[178:179], v30, s[44:47], s94 offen
	s_waitcnt vmcnt(27)
	v_mfma_f32_16x16x128_f8f6f4 v[24:27], v[24:29], v[18:23], 0 cbsz:2 blgp:2
	s_waitcnt vmcnt(26)
	v_mfma_f32_16x16x128_f8f6f4 v[24:27], v[44:49], v[12:17], v[24:27] cbsz:2 blgp:2
	s_waitcnt vmcnt(25)
	v_mfma_f32_16x16x128_f8f6f4 v[24:27], v[38:43], v[6:11], v[24:27] cbsz:2 blgp:2
	s_waitcnt vmcnt(24)
	v_mfma_f32_16x16x128_f8f6f4 v[24:27], v[50:55], v[0:5], v[24:27] cbsz:2 blgp:2
	s_nop 7
	v_cndmask_b32_e64 v24, v24, v25, s[4:5]
	v_cndmask_b32_e64 v24, v24, v26, s[2:3]
	v_cndmask_b32_e32 v24, v24, v27, vcc
	v_mul_f32_e32 v25, v33, v24
	s_nop 1
	v_mov_b32_dpp v25, v25 quad_perm:[1,0,3,2] row_mask:0xf bank_mask:0xf bound_ctrl:1
	v_fmac_f32_e32 v25, v33, v24
	s_nop 1
	v_add_f32_dpp v24, v25, v25 quad_perm:[2,3,0,1] row_mask:0xf bank_mask:0xf bound_ctrl:1
	s_nop 1
	v_add_f32_dpp v24, v24, v24 row_half_mirror row_mask:0xf bank_mask:0xf bound_ctrl:1
	ds_write_b32 v32, v24 offset:49168
	ds_bpermute_b32 v24, v36, v130 offset:128
	s_waitcnt lgkmcnt(0)
	v_mul_lo_u32 v24, v24, s43
	v_add_u32_e32 v28, v24, v35
	v_add_u32_e32 v30, v24, v34
	buffer_load_dwordx4 v[24:27], v28, s[44:47], 0 offen
	buffer_load_dwordx4 v[38:41], v28, s[44:47], s20 offen
	buffer_load_dwordx4 v[44:47], v28, s[44:47], s21 offen
	buffer_load_dwordx4 v[50:53], v28, s[44:47], s23 offen
	s_nop 0
	buffer_load_dwordx2 v[28:29], v30, s[44:47], 0 offen
	buffer_load_dwordx2 v[48:49], v30, s[44:47], s33 offen
	buffer_load_dwordx2 v[42:43], v30, s[44:47], s21 offen
	buffer_load_dwordx2 v[54:55], v30, s[44:47], s94 offen
	s_waitcnt vmcnt(27)
	v_mfma_f32_16x16x128_f8f6f4 v[56:59], v[56:61], v[18:23], 0 cbsz:2 blgp:2
	s_waitcnt vmcnt(26)
	v_mfma_f32_16x16x128_f8f6f4 v[56:59], v[68:73], v[12:17], v[56:59] cbsz:2 blgp:2
	s_waitcnt vmcnt(25)
	v_mfma_f32_16x16x128_f8f6f4 v[56:59], v[62:67], v[6:11], v[56:59] cbsz:2 blgp:2
	s_waitcnt vmcnt(24)
	v_mfma_f32_16x16x128_f8f6f4 v[56:59], v[74:79], v[0:5], v[56:59] cbsz:2 blgp:2
	s_nop 7
	v_cndmask_b32_e64 v30, v56, v57, s[4:5]
	v_cndmask_b32_e64 v30, v30, v58, s[2:3]
	v_cndmask_b32_e32 v30, v30, v59, vcc
	v_mul_f32_e32 v31, v33, v30
	s_nop 1
	v_mov_b32_dpp v31, v31 quad_perm:[1,0,3,2] row_mask:0xf bank_mask:0xf bound_ctrl:1
	v_fmac_f32_e32 v31, v33, v30
	s_nop 1
	v_add_f32_dpp v30, v31, v31 quad_perm:[2,3,0,1] row_mask:0xf bank_mask:0xf bound_ctrl:1
	s_nop 1
	v_add_f32_dpp v30, v30, v30 row_half_mirror row_mask:0xf bank_mask:0xf bound_ctrl:1
	ds_write_b32 v32, v30 offset:49172
	ds_bpermute_b32 v30, v36, v130 offset:144
	s_waitcnt lgkmcnt(0)
	v_mul_lo_u32 v30, v30, s43
	v_add_u32_e32 v31, v30, v35
	v_add_u32_e32 v30, v30, v34
	buffer_load_dwordx4 v[56:59], v31, s[44:47], 0 offen
	buffer_load_dwordx4 v[62:65], v31, s[44:47], s20 offen
	buffer_load_dwordx4 v[68:71], v31, s[44:47], s21 offen
	buffer_load_dwordx4 v[74:77], v31, s[44:47], s23 offen
	buffer_load_dwordx2 v[60:61], v30, s[44:47], 0 offen
	buffer_load_dwordx2 v[72:73], v30, s[44:47], s33 offen
	buffer_load_dwordx2 v[66:67], v30, s[44:47], s21 offen
	buffer_load_dwordx2 v[78:79], v30, s[44:47], s94 offen
	s_waitcnt vmcnt(27)
	v_mfma_f32_16x16x128_f8f6f4 v[86:89], v[86:91], v[18:23], 0 cbsz:2 blgp:2
	s_waitcnt vmcnt(26)
	v_mfma_f32_16x16x128_f8f6f4 v[86:89], v[98:103], v[12:17], v[86:89] cbsz:2 blgp:2
	s_waitcnt vmcnt(25)
	v_mfma_f32_16x16x128_f8f6f4 v[86:89], v[92:97], v[6:11], v[86:89] cbsz:2 blgp:2
	s_waitcnt vmcnt(24)
	v_mfma_f32_16x16x128_f8f6f4 v[86:89], v[150:155], v[0:5], v[86:89] cbsz:2 blgp:2
	s_nop 7
	v_cndmask_b32_e64 v30, v86, v87, s[4:5]
	v_cndmask_b32_e64 v30, v30, v88, s[2:3]
	v_cndmask_b32_e32 v30, v30, v89, vcc
	v_mul_f32_e32 v31, v33, v30
	s_nop 1
	v_mov_b32_dpp v31, v31 quad_perm:[1,0,3,2] row_mask:0xf bank_mask:0xf bound_ctrl:1
	v_fmac_f32_e32 v31, v33, v30
	s_nop 1
	v_add_f32_dpp v30, v31, v31 quad_perm:[2,3,0,1] row_mask:0xf bank_mask:0xf bound_ctrl:1
	s_nop 1
	v_add_f32_dpp v30, v30, v30 row_half_mirror row_mask:0xf bank_mask:0xf bound_ctrl:1
	ds_write_b32 v32, v30 offset:49176
	ds_bpermute_b32 v30, v36, v130 offset:160
	s_waitcnt lgkmcnt(0)
	v_mul_lo_u32 v30, v30, s43
	v_add_u32_e32 v31, v30, v35
	v_add_u32_e32 v30, v30, v34
	buffer_load_dwordx4 v[86:89], v31, s[44:47], 0 offen
	buffer_load_dwordx4 v[92:95], v31, s[44:47], s20 offen
	buffer_load_dwordx4 v[98:101], v31, s[44:47], s21 offen
	buffer_load_dwordx4 v[150:153], v31, s[44:47], s23 offen
	buffer_load_dwordx2 v[90:91], v30, s[44:47], 0 offen
	buffer_load_dwordx2 v[102:103], v30, s[44:47], s33 offen
	buffer_load_dwordx2 v[96:97], v30, s[44:47], s21 offen
	buffer_load_dwordx2 v[154:155], v30, s[44:47], s94 offen
	s_waitcnt vmcnt(27)
	v_mfma_f32_16x16x128_f8f6f4 v[156:159], v[156:161], v[18:23], 0 cbsz:2 blgp:2
	s_waitcnt vmcnt(26)
	v_mfma_f32_16x16x128_f8f6f4 v[156:159], v[168:173], v[12:17], v[156:159] cbsz:2 blgp:2
	s_waitcnt vmcnt(25)
	v_mfma_f32_16x16x128_f8f6f4 v[156:159], v[162:167], v[6:11], v[156:159] cbsz:2 blgp:2
	s_waitcnt vmcnt(24)
	v_mfma_f32_16x16x128_f8f6f4 v[156:159], v[174:179], v[0:5], v[156:159] cbsz:2 blgp:2
	s_nop 7
	v_cndmask_b32_e64 v30, v156, v157, s[4:5]
	v_cndmask_b32_e64 v30, v30, v158, s[2:3]
	v_cndmask_b32_e32 v30, v30, v159, vcc
	v_mul_f32_e32 v31, v33, v30
	s_nop 1
	v_mov_b32_dpp v31, v31 quad_perm:[1,0,3,2] row_mask:0xf bank_mask:0xf bound_ctrl:1
	v_fmac_f32_e32 v31, v33, v30
	s_nop 1
	v_add_f32_dpp v30, v31, v31 quad_perm:[2,3,0,1] row_mask:0xf bank_mask:0xf bound_ctrl:1
	s_nop 1
	v_add_f32_dpp v30, v30, v30 row_half_mirror row_mask:0xf bank_mask:0xf bound_ctrl:1
	ds_write_b32 v32, v30 offset:49180
	ds_bpermute_b32 v30, v36, v130 offset:176
	s_waitcnt lgkmcnt(0)
	v_mul_lo_u32 v30, v30, s43
	v_add_u32_e32 v31, v30, v35
	v_add_u32_e32 v30, v30, v34
	buffer_load_dwordx4 v[156:159], v31, s[44:47], 0 offen
	buffer_load_dwordx4 v[162:165], v31, s[44:47], s20 offen
	buffer_load_dwordx4 v[168:171], v31, s[44:47], s21 offen
	buffer_load_dwordx4 v[174:177], v31, s[44:47], s23 offen
	buffer_load_dwordx2 v[160:161], v30, s[44:47], 0 offen
	buffer_load_dwordx2 v[172:173], v30, s[44:47], s33 offen
	buffer_load_dwordx2 v[166:167], v30, s[44:47], s21 offen
	buffer_load_dwordx2 v[178:179], v30, s[44:47], s94 offen
	s_waitcnt vmcnt(27)
	v_mfma_f32_16x16x128_f8f6f4 v[24:27], v[24:29], v[18:23], 0 cbsz:2 blgp:2
	s_waitcnt vmcnt(26)
	v_mfma_f32_16x16x128_f8f6f4 v[24:27], v[44:49], v[12:17], v[24:27] cbsz:2 blgp:2
	s_waitcnt vmcnt(25)
	v_mfma_f32_16x16x128_f8f6f4 v[24:27], v[38:43], v[6:11], v[24:27] cbsz:2 blgp:2
	s_waitcnt vmcnt(24)
	v_mfma_f32_16x16x128_f8f6f4 v[24:27], v[50:55], v[0:5], v[24:27] cbsz:2 blgp:2
	s_nop 7
	v_cndmask_b32_e64 v24, v24, v25, s[4:5]
	v_cndmask_b32_e64 v24, v24, v26, s[2:3]
	v_cndmask_b32_e32 v24, v24, v27, vcc
	v_mul_f32_e32 v25, v33, v24
	s_nop 1
	v_mov_b32_dpp v25, v25 quad_perm:[1,0,3,2] row_mask:0xf bank_mask:0xf bound_ctrl:1
	v_fmac_f32_e32 v25, v33, v24
	s_nop 1
	v_add_f32_dpp v24, v25, v25 quad_perm:[2,3,0,1] row_mask:0xf bank_mask:0xf bound_ctrl:1
	s_nop 1
	v_add_f32_dpp v24, v24, v24 row_half_mirror row_mask:0xf bank_mask:0xf bound_ctrl:1
	ds_write_b32 v32, v24 offset:49184
	ds_bpermute_b32 v24, v36, v130 offset:192
	s_waitcnt lgkmcnt(0)
	v_mul_lo_u32 v24, v24, s43
	v_add_u32_e32 v28, v24, v35
	v_add_u32_e32 v30, v24, v34
	buffer_load_dwordx4 v[24:27], v28, s[44:47], 0 offen
	buffer_load_dwordx4 v[38:41], v28, s[44:47], s20 offen
	buffer_load_dwordx4 v[44:47], v28, s[44:47], s21 offen
	buffer_load_dwordx4 v[50:53], v28, s[44:47], s23 offen
	s_nop 0
	buffer_load_dwordx2 v[28:29], v30, s[44:47], 0 offen
	buffer_load_dwordx2 v[48:49], v30, s[44:47], s33 offen
	buffer_load_dwordx2 v[42:43], v30, s[44:47], s21 offen
	buffer_load_dwordx2 v[54:55], v30, s[44:47], s94 offen
	s_waitcnt vmcnt(27)
	v_mfma_f32_16x16x128_f8f6f4 v[56:59], v[56:61], v[18:23], 0 cbsz:2 blgp:2
	s_waitcnt vmcnt(26)
	v_mfma_f32_16x16x128_f8f6f4 v[56:59], v[68:73], v[12:17], v[56:59] cbsz:2 blgp:2
	s_waitcnt vmcnt(25)
	v_mfma_f32_16x16x128_f8f6f4 v[56:59], v[62:67], v[6:11], v[56:59] cbsz:2 blgp:2
	s_waitcnt vmcnt(24)
	v_mfma_f32_16x16x128_f8f6f4 v[56:59], v[74:79], v[0:5], v[56:59] cbsz:2 blgp:2
	s_nop 7
	v_cndmask_b32_e64 v30, v56, v57, s[4:5]
	v_cndmask_b32_e64 v30, v30, v58, s[2:3]
	v_cndmask_b32_e32 v30, v30, v59, vcc
	v_mul_f32_e32 v31, v33, v30
	s_nop 1
	v_mov_b32_dpp v31, v31 quad_perm:[1,0,3,2] row_mask:0xf bank_mask:0xf bound_ctrl:1
	v_fmac_f32_e32 v31, v33, v30
	s_nop 1
	v_add_f32_dpp v30, v31, v31 quad_perm:[2,3,0,1] row_mask:0xf bank_mask:0xf bound_ctrl:1
	s_nop 1
	v_add_f32_dpp v30, v30, v30 row_half_mirror row_mask:0xf bank_mask:0xf bound_ctrl:1
	ds_write_b32 v32, v30 offset:49188
	ds_bpermute_b32 v30, v36, v130 offset:208
	s_waitcnt lgkmcnt(0)
	v_mul_lo_u32 v30, v30, s43
	v_add_u32_e32 v31, v30, v35
	v_add_u32_e32 v30, v30, v34
	buffer_load_dwordx4 v[56:59], v31, s[44:47], 0 offen
	buffer_load_dwordx4 v[62:65], v31, s[44:47], s20 offen
	buffer_load_dwordx4 v[68:71], v31, s[44:47], s21 offen
	buffer_load_dwordx4 v[74:77], v31, s[44:47], s23 offen
	buffer_load_dwordx2 v[60:61], v30, s[44:47], 0 offen
	buffer_load_dwordx2 v[72:73], v30, s[44:47], s33 offen
	buffer_load_dwordx2 v[66:67], v30, s[44:47], s21 offen
	buffer_load_dwordx2 v[78:79], v30, s[44:47], s94 offen
	s_waitcnt vmcnt(27)
	v_mfma_f32_16x16x128_f8f6f4 v[86:89], v[86:91], v[18:23], 0 cbsz:2 blgp:2
	s_waitcnt vmcnt(26)
	v_mfma_f32_16x16x128_f8f6f4 v[86:89], v[98:103], v[12:17], v[86:89] cbsz:2 blgp:2
	s_waitcnt vmcnt(25)
	v_mfma_f32_16x16x128_f8f6f4 v[86:89], v[92:97], v[6:11], v[86:89] cbsz:2 blgp:2
	s_waitcnt vmcnt(24)
	v_mfma_f32_16x16x128_f8f6f4 v[86:89], v[150:155], v[0:5], v[86:89] cbsz:2 blgp:2
	s_nop 7
	v_cndmask_b32_e64 v30, v86, v87, s[4:5]
	v_cndmask_b32_e64 v30, v30, v88, s[2:3]
	v_cndmask_b32_e32 v30, v30, v89, vcc
	v_mul_f32_e32 v31, v33, v30
	s_nop 1
	v_mov_b32_dpp v31, v31 quad_perm:[1,0,3,2] row_mask:0xf bank_mask:0xf bound_ctrl:1
	v_fmac_f32_e32 v31, v33, v30
	s_nop 1
	v_add_f32_dpp v30, v31, v31 quad_perm:[2,3,0,1] row_mask:0xf bank_mask:0xf bound_ctrl:1
	s_nop 1
	v_add_f32_dpp v30, v30, v30 row_half_mirror row_mask:0xf bank_mask:0xf bound_ctrl:1
	ds_write_b32 v32, v30 offset:49192
	ds_bpermute_b32 v30, v36, v130 offset:224
	s_waitcnt lgkmcnt(0)
	v_mul_lo_u32 v30, v30, s43
	v_add_u32_e32 v31, v30, v35
	v_add_u32_e32 v30, v30, v34
	buffer_load_dwordx4 v[86:89], v31, s[44:47], 0 offen
	buffer_load_dwordx4 v[92:95], v31, s[44:47], s20 offen
	buffer_load_dwordx4 v[98:101], v31, s[44:47], s21 offen
	buffer_load_dwordx4 v[150:153], v31, s[44:47], s23 offen
	buffer_load_dwordx2 v[90:91], v30, s[44:47], 0 offen
	buffer_load_dwordx2 v[102:103], v30, s[44:47], s33 offen
	buffer_load_dwordx2 v[96:97], v30, s[44:47], s21 offen
	buffer_load_dwordx2 v[154:155], v30, s[44:47], s94 offen
	s_waitcnt vmcnt(27)
	v_mfma_f32_16x16x128_f8f6f4 v[156:159], v[156:161], v[18:23], 0 cbsz:2 blgp:2
	s_waitcnt vmcnt(26)
	v_mfma_f32_16x16x128_f8f6f4 v[156:159], v[168:173], v[12:17], v[156:159] cbsz:2 blgp:2
	s_waitcnt vmcnt(25)
	v_mfma_f32_16x16x128_f8f6f4 v[156:159], v[162:167], v[6:11], v[156:159] cbsz:2 blgp:2
	s_waitcnt vmcnt(24)
	v_mfma_f32_16x16x128_f8f6f4 v[156:159], v[174:179], v[0:5], v[156:159] cbsz:2 blgp:2
	s_nop 7
	v_cndmask_b32_e64 v30, v156, v157, s[4:5]
	v_cndmask_b32_e64 v30, v30, v158, s[2:3]
	v_cndmask_b32_e32 v30, v30, v159, vcc
	v_mul_f32_e32 v31, v33, v30
	s_nop 1
	v_mov_b32_dpp v31, v31 quad_perm:[1,0,3,2] row_mask:0xf bank_mask:0xf bound_ctrl:1
	v_fmac_f32_e32 v31, v33, v30
	s_nop 1
	v_add_f32_dpp v30, v31, v31 quad_perm:[2,3,0,1] row_mask:0xf bank_mask:0xf bound_ctrl:1
	s_nop 1
	v_add_f32_dpp v30, v30, v30 row_half_mirror row_mask:0xf bank_mask:0xf bound_ctrl:1
	ds_write_b32 v32, v30 offset:49196
	ds_bpermute_b32 v30, v36, v130 offset:240
	s_waitcnt lgkmcnt(0)
	v_mul_lo_u32 v30, v30, s43
	v_add_u32_e32 v31, v30, v35
	v_add_u32_e32 v30, v30, v34
	buffer_load_dwordx4 v[156:159], v31, s[44:47], 0 offen
	buffer_load_dwordx4 v[162:165], v31, s[44:47], s20 offen
	buffer_load_dwordx4 v[168:171], v31, s[44:47], s21 offen
	buffer_load_dwordx4 v[174:177], v31, s[44:47], s23 offen
	buffer_load_dwordx2 v[160:161], v30, s[44:47], 0 offen
	buffer_load_dwordx2 v[172:173], v30, s[44:47], s33 offen
	buffer_load_dwordx2 v[166:167], v30, s[44:47], s21 offen
	buffer_load_dwordx2 v[178:179], v30, s[44:47], s94 offen
	s_waitcnt vmcnt(27)
	v_mfma_f32_16x16x128_f8f6f4 v[24:27], v[24:29], v[18:23], 0 cbsz:2 blgp:2
	s_waitcnt vmcnt(26)
	v_mfma_f32_16x16x128_f8f6f4 v[24:27], v[44:49], v[12:17], v[24:27] cbsz:2 blgp:2
	s_waitcnt vmcnt(25)
	v_mfma_f32_16x16x128_f8f6f4 v[24:27], v[38:43], v[6:11], v[24:27] cbsz:2 blgp:2
	s_waitcnt vmcnt(24)
	v_mfma_f32_16x16x128_f8f6f4 v[24:27], v[50:55], v[0:5], v[24:27] cbsz:2 blgp:2
	s_nop 7
	v_cndmask_b32_e64 v24, v24, v25, s[4:5]
	v_cndmask_b32_e64 v24, v24, v26, s[2:3]
	v_cndmask_b32_e32 v24, v24, v27, vcc
	v_mul_f32_e32 v25, v33, v24
	s_nop 1
	v_mov_b32_dpp v25, v25 quad_perm:[1,0,3,2] row_mask:0xf bank_mask:0xf bound_ctrl:1
	v_fmac_f32_e32 v25, v33, v24
	s_nop 1
	v_add_f32_dpp v24, v25, v25 quad_perm:[2,3,0,1] row_mask:0xf bank_mask:0xf bound_ctrl:1
	s_nop 1
	v_add_f32_dpp v24, v24, v24 row_half_mirror row_mask:0xf bank_mask:0xf bound_ctrl:1
	ds_write_b32 v32, v24 offset:49200
	ds_bpermute_b32 v24, v36, v128
	s_waitcnt lgkmcnt(0)
	v_mul_lo_u32 v24, v24, s43
	v_add_u32_e32 v28, v24, v35
	v_add_u32_e32 v30, v24, v34
	buffer_load_dwordx4 v[24:27], v28, s[44:47], 0 offen
	buffer_load_dwordx4 v[38:41], v28, s[44:47], s20 offen
	buffer_load_dwordx4 v[44:47], v28, s[44:47], s21 offen
	buffer_load_dwordx4 v[50:53], v28, s[44:47], s23 offen
	s_nop 0
	buffer_load_dwordx2 v[28:29], v30, s[44:47], 0 offen
	buffer_load_dwordx2 v[48:49], v30, s[44:47], s33 offen
	buffer_load_dwordx2 v[42:43], v30, s[44:47], s21 offen
	buffer_load_dwordx2 v[54:55], v30, s[44:47], s94 offen
	s_waitcnt vmcnt(27)
	v_mfma_f32_16x16x128_f8f6f4 v[56:59], v[56:61], v[18:23], 0 cbsz:2 blgp:2
	s_waitcnt vmcnt(26)
	v_mfma_f32_16x16x128_f8f6f4 v[56:59], v[68:73], v[12:17], v[56:59] cbsz:2 blgp:2
	s_waitcnt vmcnt(25)
	v_mfma_f32_16x16x128_f8f6f4 v[56:59], v[62:67], v[6:11], v[56:59] cbsz:2 blgp:2
	s_waitcnt vmcnt(24)
	v_mfma_f32_16x16x128_f8f6f4 v[56:59], v[74:79], v[0:5], v[56:59] cbsz:2 blgp:2
	s_nop 7
	v_cndmask_b32_e64 v30, v56, v57, s[4:5]
	v_cndmask_b32_e64 v30, v30, v58, s[2:3]
	v_cndmask_b32_e32 v30, v30, v59, vcc
	v_mul_f32_e32 v31, v33, v30
	s_nop 1
	v_mov_b32_dpp v31, v31 quad_perm:[1,0,3,2] row_mask:0xf bank_mask:0xf bound_ctrl:1
	v_fmac_f32_e32 v31, v33, v30
	s_nop 1
	v_add_f32_dpp v30, v31, v31 quad_perm:[2,3,0,1] row_mask:0xf bank_mask:0xf bound_ctrl:1
	s_nop 1
	v_add_f32_dpp v30, v30, v30 row_half_mirror row_mask:0xf bank_mask:0xf bound_ctrl:1
	ds_write_b32 v32, v30 offset:49204
	ds_bpermute_b32 v30, v36, v128 offset:16
	s_waitcnt lgkmcnt(0)
	v_mul_lo_u32 v30, v30, s43
	v_add_u32_e32 v31, v30, v35
	v_add_u32_e32 v30, v30, v34
	buffer_load_dwordx4 v[56:59], v31, s[44:47], 0 offen
	buffer_load_dwordx4 v[62:65], v31, s[44:47], s20 offen
	buffer_load_dwordx4 v[68:71], v31, s[44:47], s21 offen
	buffer_load_dwordx4 v[74:77], v31, s[44:47], s23 offen
	buffer_load_dwordx2 v[60:61], v30, s[44:47], 0 offen
	buffer_load_dwordx2 v[72:73], v30, s[44:47], s33 offen
	buffer_load_dwordx2 v[66:67], v30, s[44:47], s21 offen
	buffer_load_dwordx2 v[78:79], v30, s[44:47], s94 offen
	s_waitcnt vmcnt(27)
	v_mfma_f32_16x16x128_f8f6f4 v[86:89], v[86:91], v[18:23], 0 cbsz:2 blgp:2
	s_waitcnt vmcnt(26)
	v_mfma_f32_16x16x128_f8f6f4 v[86:89], v[98:103], v[12:17], v[86:89] cbsz:2 blgp:2
	s_waitcnt vmcnt(25)
	v_mfma_f32_16x16x128_f8f6f4 v[86:89], v[92:97], v[6:11], v[86:89] cbsz:2 blgp:2
	s_waitcnt vmcnt(24)
	v_mfma_f32_16x16x128_f8f6f4 v[86:89], v[150:155], v[0:5], v[86:89] cbsz:2 blgp:2
	s_nop 7
	v_cndmask_b32_e64 v30, v86, v87, s[4:5]
	v_cndmask_b32_e64 v30, v30, v88, s[2:3]
	v_cndmask_b32_e32 v30, v30, v89, vcc
	v_mul_f32_e32 v31, v33, v30
	s_nop 1
	v_mov_b32_dpp v31, v31 quad_perm:[1,0,3,2] row_mask:0xf bank_mask:0xf bound_ctrl:1
	v_fmac_f32_e32 v31, v33, v30
	s_nop 1
	v_add_f32_dpp v30, v31, v31 quad_perm:[2,3,0,1] row_mask:0xf bank_mask:0xf bound_ctrl:1
	s_nop 1
	v_add_f32_dpp v30, v30, v30 row_half_mirror row_mask:0xf bank_mask:0xf bound_ctrl:1
	ds_write_b32 v32, v30 offset:49208
	ds_bpermute_b32 v30, v36, v128 offset:32
	s_waitcnt lgkmcnt(0)
	v_mul_lo_u32 v30, v30, s43
	v_add_u32_e32 v31, v30, v35
	v_add_u32_e32 v30, v30, v34
	buffer_load_dwordx4 v[86:89], v31, s[44:47], 0 offen
	buffer_load_dwordx4 v[92:95], v31, s[44:47], s20 offen
	buffer_load_dwordx4 v[98:101], v31, s[44:47], s21 offen
	buffer_load_dwordx4 v[150:153], v31, s[44:47], s23 offen
	buffer_load_dwordx2 v[90:91], v30, s[44:47], 0 offen
	buffer_load_dwordx2 v[102:103], v30, s[44:47], s33 offen
	buffer_load_dwordx2 v[96:97], v30, s[44:47], s21 offen
	buffer_load_dwordx2 v[154:155], v30, s[44:47], s94 offen
	s_waitcnt vmcnt(27)
	v_mfma_f32_16x16x128_f8f6f4 v[156:159], v[156:161], v[18:23], 0 cbsz:2 blgp:2
	s_waitcnt vmcnt(26)
	v_mfma_f32_16x16x128_f8f6f4 v[156:159], v[168:173], v[12:17], v[156:159] cbsz:2 blgp:2
	s_waitcnt vmcnt(25)
	v_mfma_f32_16x16x128_f8f6f4 v[156:159], v[162:167], v[6:11], v[156:159] cbsz:2 blgp:2
	s_waitcnt vmcnt(24)
	v_mfma_f32_16x16x128_f8f6f4 v[156:159], v[174:179], v[0:5], v[156:159] cbsz:2 blgp:2
	s_nop 7
	v_cndmask_b32_e64 v30, v156, v157, s[4:5]
	v_cndmask_b32_e64 v30, v30, v158, s[2:3]
	v_cndmask_b32_e32 v30, v30, v159, vcc
	v_mul_f32_e32 v31, v33, v30
	s_nop 1
	v_mov_b32_dpp v31, v31 quad_perm:[1,0,3,2] row_mask:0xf bank_mask:0xf bound_ctrl:1
	v_fmac_f32_e32 v31, v33, v30
	s_nop 1
	v_add_f32_dpp v30, v31, v31 quad_perm:[2,3,0,1] row_mask:0xf bank_mask:0xf bound_ctrl:1
	s_nop 1
	v_add_f32_dpp v30, v30, v30 row_half_mirror row_mask:0xf bank_mask:0xf bound_ctrl:1
	ds_write_b32 v32, v30 offset:49212
	ds_bpermute_b32 v30, v36, v128 offset:48
	s_waitcnt lgkmcnt(0)
	v_mul_lo_u32 v30, v30, s43
	v_add_u32_e32 v31, v30, v35
	v_add_u32_e32 v30, v30, v34
	buffer_load_dwordx4 v[156:159], v31, s[44:47], 0 offen
	buffer_load_dwordx4 v[162:165], v31, s[44:47], s20 offen
	buffer_load_dwordx4 v[168:171], v31, s[44:47], s21 offen
	buffer_load_dwordx4 v[174:177], v31, s[44:47], s23 offen
	buffer_load_dwordx2 v[160:161], v30, s[44:47], 0 offen
	buffer_load_dwordx2 v[172:173], v30, s[44:47], s33 offen
	buffer_load_dwordx2 v[166:167], v30, s[44:47], s21 offen
	buffer_load_dwordx2 v[178:179], v30, s[44:47], s94 offen
	s_waitcnt vmcnt(27)
	v_mfma_f32_16x16x128_f8f6f4 v[24:27], v[24:29], v[18:23], 0 cbsz:2 blgp:2
	s_waitcnt vmcnt(26)
	v_mfma_f32_16x16x128_f8f6f4 v[24:27], v[44:49], v[12:17], v[24:27] cbsz:2 blgp:2
	s_waitcnt vmcnt(25)
	v_mfma_f32_16x16x128_f8f6f4 v[24:27], v[38:43], v[6:11], v[24:27] cbsz:2 blgp:2
	s_waitcnt vmcnt(24)
	v_mfma_f32_16x16x128_f8f6f4 v[24:27], v[50:55], v[0:5], v[24:27] cbsz:2 blgp:2
	s_nop 7
	v_cndmask_b32_e64 v24, v24, v25, s[4:5]
	v_cndmask_b32_e64 v24, v24, v26, s[2:3]
	v_cndmask_b32_e32 v24, v24, v27, vcc
	v_mul_f32_e32 v25, v33, v24
	s_nop 1
	v_mov_b32_dpp v25, v25 quad_perm:[1,0,3,2] row_mask:0xf bank_mask:0xf bound_ctrl:1
	v_fmac_f32_e32 v25, v33, v24
	s_nop 1
	v_add_f32_dpp v24, v25, v25 quad_perm:[2,3,0,1] row_mask:0xf bank_mask:0xf bound_ctrl:1
	s_nop 1
	v_add_f32_dpp v24, v24, v24 row_half_mirror row_mask:0xf bank_mask:0xf bound_ctrl:1
	ds_write_b32 v32, v24 offset:49216
	ds_bpermute_b32 v24, v36, v128 offset:64
	s_waitcnt lgkmcnt(0)
	v_mul_lo_u32 v24, v24, s43
	v_add_u32_e32 v28, v24, v35
	v_add_u32_e32 v30, v24, v34
	buffer_load_dwordx4 v[24:27], v28, s[44:47], 0 offen
	buffer_load_dwordx4 v[38:41], v28, s[44:47], s20 offen
	buffer_load_dwordx4 v[44:47], v28, s[44:47], s21 offen
	buffer_load_dwordx4 v[50:53], v28, s[44:47], s23 offen
	s_nop 0
	buffer_load_dwordx2 v[28:29], v30, s[44:47], 0 offen
	buffer_load_dwordx2 v[48:49], v30, s[44:47], s33 offen
	buffer_load_dwordx2 v[42:43], v30, s[44:47], s21 offen
	buffer_load_dwordx2 v[54:55], v30, s[44:47], s94 offen
	s_waitcnt vmcnt(27)
	v_mfma_f32_16x16x128_f8f6f4 v[56:59], v[56:61], v[18:23], 0 cbsz:2 blgp:2
	s_waitcnt vmcnt(26)
	v_mfma_f32_16x16x128_f8f6f4 v[56:59], v[68:73], v[12:17], v[56:59] cbsz:2 blgp:2
	s_waitcnt vmcnt(25)
	v_mfma_f32_16x16x128_f8f6f4 v[56:59], v[62:67], v[6:11], v[56:59] cbsz:2 blgp:2
	s_waitcnt vmcnt(24)
	v_mfma_f32_16x16x128_f8f6f4 v[56:59], v[74:79], v[0:5], v[56:59] cbsz:2 blgp:2
	s_nop 7
	v_cndmask_b32_e64 v30, v56, v57, s[4:5]
	v_cndmask_b32_e64 v30, v30, v58, s[2:3]
	v_cndmask_b32_e32 v30, v30, v59, vcc
	v_mul_f32_e32 v31, v33, v30
	s_nop 1
	v_mov_b32_dpp v31, v31 quad_perm:[1,0,3,2] row_mask:0xf bank_mask:0xf bound_ctrl:1
	v_fmac_f32_e32 v31, v33, v30
	s_nop 1
	v_add_f32_dpp v30, v31, v31 quad_perm:[2,3,0,1] row_mask:0xf bank_mask:0xf bound_ctrl:1
	s_nop 1
	v_add_f32_dpp v30, v30, v30 row_half_mirror row_mask:0xf bank_mask:0xf bound_ctrl:1
	ds_write_b32 v32, v30 offset:49220
	ds_bpermute_b32 v30, v36, v128 offset:80
	s_waitcnt lgkmcnt(0)
	v_mul_lo_u32 v30, v30, s43
	v_add_u32_e32 v31, v30, v35
	v_add_u32_e32 v30, v30, v34
	buffer_load_dwordx4 v[56:59], v31, s[44:47], 0 offen
	buffer_load_dwordx4 v[62:65], v31, s[44:47], s20 offen
	buffer_load_dwordx4 v[68:71], v31, s[44:47], s21 offen
	buffer_load_dwordx4 v[74:77], v31, s[44:47], s23 offen
	buffer_load_dwordx2 v[60:61], v30, s[44:47], 0 offen
	buffer_load_dwordx2 v[72:73], v30, s[44:47], s33 offen
	buffer_load_dwordx2 v[66:67], v30, s[44:47], s21 offen
	buffer_load_dwordx2 v[78:79], v30, s[44:47], s94 offen
	s_waitcnt vmcnt(27)
	v_mfma_f32_16x16x128_f8f6f4 v[86:89], v[86:91], v[18:23], 0 cbsz:2 blgp:2
	s_waitcnt vmcnt(26)
	v_mfma_f32_16x16x128_f8f6f4 v[86:89], v[98:103], v[12:17], v[86:89] cbsz:2 blgp:2
	s_waitcnt vmcnt(25)
	v_mfma_f32_16x16x128_f8f6f4 v[86:89], v[92:97], v[6:11], v[86:89] cbsz:2 blgp:2
	s_waitcnt vmcnt(24)
	v_mfma_f32_16x16x128_f8f6f4 v[86:89], v[150:155], v[0:5], v[86:89] cbsz:2 blgp:2
	s_nop 7
	v_cndmask_b32_e64 v30, v86, v87, s[4:5]
	v_cndmask_b32_e64 v30, v30, v88, s[2:3]
	v_cndmask_b32_e32 v30, v30, v89, vcc
	v_mul_f32_e32 v31, v33, v30
	s_nop 1
	v_mov_b32_dpp v31, v31 quad_perm:[1,0,3,2] row_mask:0xf bank_mask:0xf bound_ctrl:1
	v_fmac_f32_e32 v31, v33, v30
	s_nop 1
	v_add_f32_dpp v30, v31, v31 quad_perm:[2,3,0,1] row_mask:0xf bank_mask:0xf bound_ctrl:1
	s_nop 1
	v_add_f32_dpp v30, v30, v30 row_half_mirror row_mask:0xf bank_mask:0xf bound_ctrl:1
	ds_write_b32 v32, v30 offset:49224
	ds_bpermute_b32 v30, v36, v128 offset:96
	s_waitcnt lgkmcnt(0)
	v_mul_lo_u32 v30, v30, s43
	v_add_u32_e32 v31, v30, v35
	v_add_u32_e32 v30, v30, v34
	buffer_load_dwordx4 v[86:89], v31, s[44:47], 0 offen
	buffer_load_dwordx4 v[92:95], v31, s[44:47], s20 offen
	buffer_load_dwordx4 v[98:101], v31, s[44:47], s21 offen
	buffer_load_dwordx4 v[150:153], v31, s[44:47], s23 offen
	buffer_load_dwordx2 v[90:91], v30, s[44:47], 0 offen
	buffer_load_dwordx2 v[102:103], v30, s[44:47], s33 offen
	buffer_load_dwordx2 v[96:97], v30, s[44:47], s21 offen
	buffer_load_dwordx2 v[154:155], v30, s[44:47], s94 offen
	s_waitcnt vmcnt(27)
	v_mfma_f32_16x16x128_f8f6f4 v[156:159], v[156:161], v[18:23], 0 cbsz:2 blgp:2
	s_waitcnt vmcnt(26)
	v_mfma_f32_16x16x128_f8f6f4 v[156:159], v[168:173], v[12:17], v[156:159] cbsz:2 blgp:2
	s_waitcnt vmcnt(25)
	v_mfma_f32_16x16x128_f8f6f4 v[156:159], v[162:167], v[6:11], v[156:159] cbsz:2 blgp:2
	s_waitcnt vmcnt(24)
	v_mfma_f32_16x16x128_f8f6f4 v[156:159], v[174:179], v[0:5], v[156:159] cbsz:2 blgp:2
	s_nop 7
	v_cndmask_b32_e64 v30, v156, v157, s[4:5]
	v_cndmask_b32_e64 v30, v30, v158, s[2:3]
	v_cndmask_b32_e32 v30, v30, v159, vcc
	v_mul_f32_e32 v31, v33, v30
	s_nop 1
	v_mov_b32_dpp v31, v31 quad_perm:[1,0,3,2] row_mask:0xf bank_mask:0xf bound_ctrl:1
	v_fmac_f32_e32 v31, v33, v30
	s_nop 1
	v_add_f32_dpp v30, v31, v31 quad_perm:[2,3,0,1] row_mask:0xf bank_mask:0xf bound_ctrl:1
	s_nop 1
	v_add_f32_dpp v30, v30, v30 row_half_mirror row_mask:0xf bank_mask:0xf bound_ctrl:1
	ds_write_b32 v32, v30 offset:49228
	ds_bpermute_b32 v30, v36, v128 offset:112
	s_waitcnt lgkmcnt(0)
	v_mul_lo_u32 v30, v30, s43
	v_add_u32_e32 v31, v30, v35
	v_add_u32_e32 v30, v30, v34
	buffer_load_dwordx4 v[156:159], v31, s[44:47], 0 offen
	buffer_load_dwordx4 v[162:165], v31, s[44:47], s20 offen
	buffer_load_dwordx4 v[168:171], v31, s[44:47], s21 offen
	buffer_load_dwordx4 v[174:177], v31, s[44:47], s23 offen
	buffer_load_dwordx2 v[160:161], v30, s[44:47], 0 offen
	buffer_load_dwordx2 v[172:173], v30, s[44:47], s33 offen
	buffer_load_dwordx2 v[166:167], v30, s[44:47], s21 offen
	buffer_load_dwordx2 v[178:179], v30, s[44:47], s94 offen
	s_waitcnt vmcnt(27)
	v_mfma_f32_16x16x128_f8f6f4 v[24:27], v[24:29], v[18:23], 0 cbsz:2 blgp:2
	s_waitcnt vmcnt(26)
	v_mfma_f32_16x16x128_f8f6f4 v[24:27], v[44:49], v[12:17], v[24:27] cbsz:2 blgp:2
	s_waitcnt vmcnt(25)
	v_mfma_f32_16x16x128_f8f6f4 v[24:27], v[38:43], v[6:11], v[24:27] cbsz:2 blgp:2
	s_waitcnt vmcnt(24)
	v_mfma_f32_16x16x128_f8f6f4 v[24:27], v[50:55], v[0:5], v[24:27] cbsz:2 blgp:2
	s_nop 7
	v_cndmask_b32_e64 v24, v24, v25, s[4:5]
	v_cndmask_b32_e64 v24, v24, v26, s[2:3]
	v_cndmask_b32_e32 v24, v24, v27, vcc
	v_mul_f32_e32 v25, v33, v24
	s_nop 1
	v_mov_b32_dpp v25, v25 quad_perm:[1,0,3,2] row_mask:0xf bank_mask:0xf bound_ctrl:1
	v_fmac_f32_e32 v25, v33, v24
	s_nop 1
	v_add_f32_dpp v24, v25, v25 quad_perm:[2,3,0,1] row_mask:0xf bank_mask:0xf bound_ctrl:1
	s_nop 1
	v_add_f32_dpp v24, v24, v24 row_half_mirror row_mask:0xf bank_mask:0xf bound_ctrl:1
	ds_write_b32 v32, v24 offset:49232
	ds_bpermute_b32 v24, v36, v128 offset:128
	s_waitcnt lgkmcnt(0)
	v_mul_lo_u32 v24, v24, s43
	v_add_u32_e32 v28, v24, v35
	v_add_u32_e32 v30, v24, v34
	buffer_load_dwordx4 v[24:27], v28, s[44:47], 0 offen
	buffer_load_dwordx4 v[38:41], v28, s[44:47], s20 offen
	buffer_load_dwordx4 v[44:47], v28, s[44:47], s21 offen
	buffer_load_dwordx4 v[50:53], v28, s[44:47], s23 offen
	s_nop 0
	buffer_load_dwordx2 v[28:29], v30, s[44:47], 0 offen
	buffer_load_dwordx2 v[48:49], v30, s[44:47], s33 offen
	buffer_load_dwordx2 v[42:43], v30, s[44:47], s21 offen
	buffer_load_dwordx2 v[54:55], v30, s[44:47], s94 offen
	s_waitcnt vmcnt(27)
	v_mfma_f32_16x16x128_f8f6f4 v[56:59], v[56:61], v[18:23], 0 cbsz:2 blgp:2
	s_waitcnt vmcnt(26)
	v_mfma_f32_16x16x128_f8f6f4 v[56:59], v[68:73], v[12:17], v[56:59] cbsz:2 blgp:2
	s_waitcnt vmcnt(25)
	v_mfma_f32_16x16x128_f8f6f4 v[56:59], v[62:67], v[6:11], v[56:59] cbsz:2 blgp:2
	s_waitcnt vmcnt(24)
	v_mfma_f32_16x16x128_f8f6f4 v[56:59], v[74:79], v[0:5], v[56:59] cbsz:2 blgp:2
	s_nop 7
	v_cndmask_b32_e64 v30, v56, v57, s[4:5]
	v_cndmask_b32_e64 v30, v30, v58, s[2:3]
	v_cndmask_b32_e32 v30, v30, v59, vcc
	v_mul_f32_e32 v31, v33, v30
	s_nop 1
	v_mov_b32_dpp v31, v31 quad_perm:[1,0,3,2] row_mask:0xf bank_mask:0xf bound_ctrl:1
	v_fmac_f32_e32 v31, v33, v30
	s_nop 1
	v_add_f32_dpp v30, v31, v31 quad_perm:[2,3,0,1] row_mask:0xf bank_mask:0xf bound_ctrl:1
	s_nop 1
	v_add_f32_dpp v30, v30, v30 row_half_mirror row_mask:0xf bank_mask:0xf bound_ctrl:1
	ds_write_b32 v32, v30 offset:49236
	ds_bpermute_b32 v30, v36, v128 offset:144
	s_waitcnt lgkmcnt(0)
	v_mul_lo_u32 v30, v30, s43
	v_add_u32_e32 v31, v30, v35
	v_add_u32_e32 v30, v30, v34
	buffer_load_dwordx4 v[56:59], v31, s[44:47], 0 offen
	buffer_load_dwordx4 v[62:65], v31, s[44:47], s20 offen
	buffer_load_dwordx4 v[68:71], v31, s[44:47], s21 offen
	buffer_load_dwordx4 v[74:77], v31, s[44:47], s23 offen
	buffer_load_dwordx2 v[60:61], v30, s[44:47], 0 offen
	buffer_load_dwordx2 v[72:73], v30, s[44:47], s33 offen
	buffer_load_dwordx2 v[66:67], v30, s[44:47], s21 offen
	buffer_load_dwordx2 v[78:79], v30, s[44:47], s94 offen
	s_waitcnt vmcnt(27)
	v_mfma_f32_16x16x128_f8f6f4 v[86:89], v[86:91], v[18:23], 0 cbsz:2 blgp:2
	s_waitcnt vmcnt(26)
	v_mfma_f32_16x16x128_f8f6f4 v[86:89], v[98:103], v[12:17], v[86:89] cbsz:2 blgp:2
	s_waitcnt vmcnt(25)
	v_mfma_f32_16x16x128_f8f6f4 v[86:89], v[92:97], v[6:11], v[86:89] cbsz:2 blgp:2
	s_waitcnt vmcnt(24)
	v_mfma_f32_16x16x128_f8f6f4 v[86:89], v[150:155], v[0:5], v[86:89] cbsz:2 blgp:2
	s_nop 7
	v_cndmask_b32_e64 v30, v86, v87, s[4:5]
	v_cndmask_b32_e64 v30, v30, v88, s[2:3]
	v_cndmask_b32_e32 v30, v30, v89, vcc
	v_mul_f32_e32 v31, v33, v30
	s_nop 1
	v_mov_b32_dpp v31, v31 quad_perm:[1,0,3,2] row_mask:0xf bank_mask:0xf bound_ctrl:1
	v_fmac_f32_e32 v31, v33, v30
	s_nop 1
	v_add_f32_dpp v30, v31, v31 quad_perm:[2,3,0,1] row_mask:0xf bank_mask:0xf bound_ctrl:1
	s_nop 1
	v_add_f32_dpp v30, v30, v30 row_half_mirror row_mask:0xf bank_mask:0xf bound_ctrl:1
	ds_write_b32 v32, v30 offset:49240
	ds_bpermute_b32 v30, v36, v128 offset:160
	s_waitcnt lgkmcnt(0)
	v_mul_lo_u32 v30, v30, s43
	v_add_u32_e32 v31, v30, v35
	v_add_u32_e32 v30, v30, v34
	buffer_load_dwordx4 v[86:89], v31, s[44:47], 0 offen
	buffer_load_dwordx4 v[92:95], v31, s[44:47], s20 offen
	buffer_load_dwordx4 v[98:101], v31, s[44:47], s21 offen
	buffer_load_dwordx4 v[150:153], v31, s[44:47], s23 offen
	buffer_load_dwordx2 v[90:91], v30, s[44:47], 0 offen
	buffer_load_dwordx2 v[102:103], v30, s[44:47], s33 offen
	buffer_load_dwordx2 v[96:97], v30, s[44:47], s21 offen
	buffer_load_dwordx2 v[154:155], v30, s[44:47], s94 offen
	s_waitcnt vmcnt(27)
	v_mfma_f32_16x16x128_f8f6f4 v[156:159], v[156:161], v[18:23], 0 cbsz:2 blgp:2
	s_waitcnt vmcnt(26)
	v_mfma_f32_16x16x128_f8f6f4 v[156:159], v[168:173], v[12:17], v[156:159] cbsz:2 blgp:2
	s_waitcnt vmcnt(25)
	v_mfma_f32_16x16x128_f8f6f4 v[156:159], v[162:167], v[6:11], v[156:159] cbsz:2 blgp:2
	s_waitcnt vmcnt(24)
	v_mfma_f32_16x16x128_f8f6f4 v[156:159], v[174:179], v[0:5], v[156:159] cbsz:2 blgp:2
	s_nop 7
	v_cndmask_b32_e64 v30, v156, v157, s[4:5]
	v_cndmask_b32_e64 v30, v30, v158, s[2:3]
	v_cndmask_b32_e32 v30, v30, v159, vcc
	v_mul_f32_e32 v31, v33, v30
	s_nop 1
	v_mov_b32_dpp v31, v31 quad_perm:[1,0,3,2] row_mask:0xf bank_mask:0xf bound_ctrl:1
	v_fmac_f32_e32 v31, v33, v30
	s_nop 1
	v_add_f32_dpp v30, v31, v31 quad_perm:[2,3,0,1] row_mask:0xf bank_mask:0xf bound_ctrl:1
	s_nop 1
	v_add_f32_dpp v30, v30, v30 row_half_mirror row_mask:0xf bank_mask:0xf bound_ctrl:1
	ds_write_b32 v32, v30 offset:49244
	ds_bpermute_b32 v30, v36, v128 offset:176
	s_waitcnt lgkmcnt(0)
	v_mul_lo_u32 v30, v30, s43
	v_add_u32_e32 v31, v30, v35
	v_add_u32_e32 v30, v30, v34
	buffer_load_dwordx4 v[156:159], v31, s[44:47], 0 offen
	buffer_load_dwordx4 v[162:165], v31, s[44:47], s20 offen
	buffer_load_dwordx4 v[168:171], v31, s[44:47], s21 offen
	buffer_load_dwordx4 v[174:177], v31, s[44:47], s23 offen
	buffer_load_dwordx2 v[160:161], v30, s[44:47], 0 offen
	buffer_load_dwordx2 v[172:173], v30, s[44:47], s33 offen
	buffer_load_dwordx2 v[166:167], v30, s[44:47], s21 offen
	buffer_load_dwordx2 v[178:179], v30, s[44:47], s94 offen
	s_waitcnt vmcnt(27)
	v_mfma_f32_16x16x128_f8f6f4 v[24:27], v[24:29], v[18:23], 0 cbsz:2 blgp:2
	s_waitcnt vmcnt(26)
	v_mfma_f32_16x16x128_f8f6f4 v[24:27], v[44:49], v[12:17], v[24:27] cbsz:2 blgp:2
	s_waitcnt vmcnt(25)
	v_mfma_f32_16x16x128_f8f6f4 v[24:27], v[38:43], v[6:11], v[24:27] cbsz:2 blgp:2
	s_waitcnt vmcnt(24)
	v_mfma_f32_16x16x128_f8f6f4 v[24:27], v[50:55], v[0:5], v[24:27] cbsz:2 blgp:2
	s_nop 7
	v_cndmask_b32_e64 v24, v24, v25, s[4:5]
	v_cndmask_b32_e64 v24, v24, v26, s[2:3]
	v_cndmask_b32_e32 v24, v24, v27, vcc
	v_mul_f32_e32 v25, v33, v24
	s_nop 1
	v_mov_b32_dpp v25, v25 quad_perm:[1,0,3,2] row_mask:0xf bank_mask:0xf bound_ctrl:1
	v_fmac_f32_e32 v25, v33, v24
	s_nop 1
	v_add_f32_dpp v24, v25, v25 quad_perm:[2,3,0,1] row_mask:0xf bank_mask:0xf bound_ctrl:1
	s_nop 1
	v_add_f32_dpp v24, v24, v24 row_half_mirror row_mask:0xf bank_mask:0xf bound_ctrl:1
	ds_write_b32 v32, v24 offset:49248
	ds_bpermute_b32 v24, v36, v128 offset:192
	s_waitcnt lgkmcnt(0)
	v_mul_lo_u32 v24, v24, s43
	v_add_u32_e32 v28, v24, v35
	v_add_u32_e32 v30, v24, v34
	buffer_load_dwordx4 v[24:27], v28, s[44:47], 0 offen
	buffer_load_dwordx4 v[38:41], v28, s[44:47], s20 offen
	buffer_load_dwordx4 v[44:47], v28, s[44:47], s21 offen
	buffer_load_dwordx4 v[50:53], v28, s[44:47], s23 offen
	s_nop 0
	buffer_load_dwordx2 v[28:29], v30, s[44:47], 0 offen
	buffer_load_dwordx2 v[48:49], v30, s[44:47], s33 offen
	buffer_load_dwordx2 v[42:43], v30, s[44:47], s21 offen
	buffer_load_dwordx2 v[54:55], v30, s[44:47], s94 offen
	s_waitcnt vmcnt(27)
	v_mfma_f32_16x16x128_f8f6f4 v[56:59], v[56:61], v[18:23], 0 cbsz:2 blgp:2
	s_waitcnt vmcnt(26)
	v_mfma_f32_16x16x128_f8f6f4 v[56:59], v[68:73], v[12:17], v[56:59] cbsz:2 blgp:2
	s_waitcnt vmcnt(25)
	v_mfma_f32_16x16x128_f8f6f4 v[56:59], v[62:67], v[6:11], v[56:59] cbsz:2 blgp:2
	s_waitcnt vmcnt(24)
	v_mfma_f32_16x16x128_f8f6f4 v[56:59], v[74:79], v[0:5], v[56:59] cbsz:2 blgp:2
	s_nop 7
	v_cndmask_b32_e64 v30, v56, v57, s[4:5]
	v_cndmask_b32_e64 v30, v30, v58, s[2:3]
	v_cndmask_b32_e32 v30, v30, v59, vcc
	v_mul_f32_e32 v31, v33, v30
	s_nop 1
	v_mov_b32_dpp v31, v31 quad_perm:[1,0,3,2] row_mask:0xf bank_mask:0xf bound_ctrl:1
	v_fmac_f32_e32 v31, v33, v30
	s_nop 1
	v_add_f32_dpp v30, v31, v31 quad_perm:[2,3,0,1] row_mask:0xf bank_mask:0xf bound_ctrl:1
	s_nop 1
	v_add_f32_dpp v30, v30, v30 row_half_mirror row_mask:0xf bank_mask:0xf bound_ctrl:1
	ds_write_b32 v32, v30 offset:49252
	ds_bpermute_b32 v30, v36, v128 offset:208
	s_waitcnt lgkmcnt(0)
	v_mul_lo_u32 v30, v30, s43
	v_add_u32_e32 v31, v30, v35
	v_add_u32_e32 v30, v30, v34
	buffer_load_dwordx4 v[56:59], v31, s[44:47], 0 offen
	buffer_load_dwordx4 v[62:65], v31, s[44:47], s20 offen
	buffer_load_dwordx4 v[68:71], v31, s[44:47], s21 offen
	buffer_load_dwordx4 v[74:77], v31, s[44:47], s23 offen
	buffer_load_dwordx2 v[60:61], v30, s[44:47], 0 offen
	buffer_load_dwordx2 v[72:73], v30, s[44:47], s33 offen
	buffer_load_dwordx2 v[66:67], v30, s[44:47], s21 offen
	buffer_load_dwordx2 v[78:79], v30, s[44:47], s94 offen
	s_waitcnt vmcnt(27)
	v_mfma_f32_16x16x128_f8f6f4 v[86:89], v[86:91], v[18:23], 0 cbsz:2 blgp:2
	s_waitcnt vmcnt(26)
	v_mfma_f32_16x16x128_f8f6f4 v[86:89], v[98:103], v[12:17], v[86:89] cbsz:2 blgp:2
	s_waitcnt vmcnt(25)
	v_mfma_f32_16x16x128_f8f6f4 v[86:89], v[92:97], v[6:11], v[86:89] cbsz:2 blgp:2
	s_waitcnt vmcnt(24)
	v_mfma_f32_16x16x128_f8f6f4 v[86:89], v[150:155], v[0:5], v[86:89] cbsz:2 blgp:2
	s_nop 7
	v_cndmask_b32_e64 v30, v86, v87, s[4:5]
	v_cndmask_b32_e64 v30, v30, v88, s[2:3]
	v_cndmask_b32_e32 v30, v30, v89, vcc
	v_mul_f32_e32 v31, v33, v30
	s_nop 1
	v_mov_b32_dpp v31, v31 quad_perm:[1,0,3,2] row_mask:0xf bank_mask:0xf bound_ctrl:1
	v_fmac_f32_e32 v31, v33, v30
	s_nop 1
	v_add_f32_dpp v30, v31, v31 quad_perm:[2,3,0,1] row_mask:0xf bank_mask:0xf bound_ctrl:1
	s_nop 1
	v_add_f32_dpp v30, v30, v30 row_half_mirror row_mask:0xf bank_mask:0xf bound_ctrl:1
	ds_write_b32 v32, v30 offset:49256
	ds_bpermute_b32 v30, v36, v128 offset:224
	s_waitcnt lgkmcnt(0)
	v_mul_lo_u32 v30, v30, s43
	v_add_u32_e32 v31, v30, v35
	v_add_u32_e32 v30, v30, v34
	buffer_load_dwordx4 v[86:89], v31, s[44:47], 0 offen
	buffer_load_dwordx4 v[92:95], v31, s[44:47], s20 offen
	buffer_load_dwordx4 v[98:101], v31, s[44:47], s21 offen
	buffer_load_dwordx4 v[150:153], v31, s[44:47], s23 offen
	buffer_load_dwordx2 v[90:91], v30, s[44:47], 0 offen
	buffer_load_dwordx2 v[102:103], v30, s[44:47], s33 offen
	buffer_load_dwordx2 v[96:97], v30, s[44:47], s21 offen
	buffer_load_dwordx2 v[154:155], v30, s[44:47], s94 offen
	s_waitcnt vmcnt(27)
	v_mfma_f32_16x16x128_f8f6f4 v[156:159], v[156:161], v[18:23], 0 cbsz:2 blgp:2
	s_waitcnt vmcnt(26)
	v_mfma_f32_16x16x128_f8f6f4 v[156:159], v[168:173], v[12:17], v[156:159] cbsz:2 blgp:2
	s_waitcnt vmcnt(25)
	v_mfma_f32_16x16x128_f8f6f4 v[156:159], v[162:167], v[6:11], v[156:159] cbsz:2 blgp:2
	s_waitcnt vmcnt(24)
	v_mfma_f32_16x16x128_f8f6f4 v[156:159], v[174:179], v[0:5], v[156:159] cbsz:2 blgp:2
	s_nop 7
	v_cndmask_b32_e64 v30, v156, v157, s[4:5]
	v_cndmask_b32_e64 v30, v30, v158, s[2:3]
	v_cndmask_b32_e32 v30, v30, v159, vcc
	v_mul_f32_e32 v31, v33, v30
	s_nop 1
	v_mov_b32_dpp v31, v31 quad_perm:[1,0,3,2] row_mask:0xf bank_mask:0xf bound_ctrl:1
	v_fmac_f32_e32 v31, v33, v30
	s_nop 1
	v_add_f32_dpp v30, v31, v31 quad_perm:[2,3,0,1] row_mask:0xf bank_mask:0xf bound_ctrl:1
	s_nop 1
	v_add_f32_dpp v30, v30, v30 row_half_mirror row_mask:0xf bank_mask:0xf bound_ctrl:1
	ds_write_b32 v32, v30 offset:49260
	ds_bpermute_b32 v30, v36, v128 offset:240
	s_waitcnt lgkmcnt(0)
	v_mul_lo_u32 v30, v30, s43
	v_add_u32_e32 v31, v30, v35
	v_add_u32_e32 v30, v30, v34
	buffer_load_dwordx4 v[156:159], v31, s[44:47], 0 offen
	buffer_load_dwordx4 v[162:165], v31, s[44:47], s20 offen
	buffer_load_dwordx4 v[168:171], v31, s[44:47], s21 offen
	buffer_load_dwordx4 v[174:177], v31, s[44:47], s23 offen
	buffer_load_dwordx2 v[160:161], v30, s[44:47], 0 offen
	buffer_load_dwordx2 v[172:173], v30, s[44:47], s33 offen
	buffer_load_dwordx2 v[166:167], v30, s[44:47], s21 offen
	buffer_load_dwordx2 v[178:179], v30, s[44:47], s94 offen
	s_waitcnt vmcnt(27)
	v_mfma_f32_16x16x128_f8f6f4 v[24:27], v[24:29], v[18:23], 0 cbsz:2 blgp:2
	s_waitcnt vmcnt(26)
	v_mfma_f32_16x16x128_f8f6f4 v[24:27], v[44:49], v[12:17], v[24:27] cbsz:2 blgp:2
	s_waitcnt vmcnt(25)
	v_mfma_f32_16x16x128_f8f6f4 v[24:27], v[38:43], v[6:11], v[24:27] cbsz:2 blgp:2
	s_waitcnt vmcnt(24)
	v_mfma_f32_16x16x128_f8f6f4 v[24:27], v[50:55], v[0:5], v[24:27] cbsz:2 blgp:2
	s_nop 7
	v_cndmask_b32_e64 v24, v24, v25, s[4:5]
	v_cndmask_b32_e64 v24, v24, v26, s[2:3]
	v_cndmask_b32_e32 v24, v24, v27, vcc
	v_mul_f32_e32 v25, v33, v24
	s_nop 1
	v_mov_b32_dpp v25, v25 quad_perm:[1,0,3,2] row_mask:0xf bank_mask:0xf bound_ctrl:1
	v_fmac_f32_e32 v25, v33, v24
	s_nop 1
	v_add_f32_dpp v24, v25, v25 quad_perm:[2,3,0,1] row_mask:0xf bank_mask:0xf bound_ctrl:1
	s_nop 1
	v_add_f32_dpp v24, v24, v24 row_half_mirror row_mask:0xf bank_mask:0xf bound_ctrl:1
	ds_write_b32 v32, v24 offset:49264
	s_waitcnt vmcnt(19)
	v_mfma_f32_16x16x128_f8f6f4 v[24:27], v[56:61], v[18:23], 0 cbsz:2 blgp:2
	s_waitcnt vmcnt(18)
	v_mfma_f32_16x16x128_f8f6f4 v[24:27], v[68:73], v[12:17], v[24:27] cbsz:2 blgp:2
	s_waitcnt vmcnt(17)
	v_mfma_f32_16x16x128_f8f6f4 v[24:27], v[62:67], v[6:11], v[24:27] cbsz:2 blgp:2
	s_waitcnt vmcnt(16)
	v_mfma_f32_16x16x128_f8f6f4 v[24:27], v[74:79], v[0:5], v[24:27] cbsz:2 blgp:2
	s_nop 7
	v_cndmask_b32_e64 v24, v24, v25, s[4:5]
	v_cndmask_b32_e64 v24, v24, v26, s[2:3]
	v_cndmask_b32_e32 v24, v24, v27, vcc
	v_mul_f32_e32 v25, v33, v24
	s_nop 1
	v_mov_b32_dpp v25, v25 quad_perm:[1,0,3,2] row_mask:0xf bank_mask:0xf bound_ctrl:1
	v_fmac_f32_e32 v25, v33, v24
	s_nop 1
	v_add_f32_dpp v24, v25, v25 quad_perm:[2,3,0,1] row_mask:0xf bank_mask:0xf bound_ctrl:1
	s_nop 1
	v_add_f32_dpp v24, v24, v24 row_half_mirror row_mask:0xf bank_mask:0xf bound_ctrl:1
	ds_write_b32 v32, v24 offset:49268
	s_waitcnt vmcnt(11)
	v_mfma_f32_16x16x128_f8f6f4 v[24:27], v[86:91], v[18:23], 0 cbsz:2 blgp:2
	s_waitcnt vmcnt(10)
	v_mfma_f32_16x16x128_f8f6f4 v[24:27], v[98:103], v[12:17], v[24:27] cbsz:2 blgp:2
	s_waitcnt vmcnt(9)
	v_mfma_f32_16x16x128_f8f6f4 v[24:27], v[92:97], v[6:11], v[24:27] cbsz:2 blgp:2
	s_waitcnt vmcnt(8)
	v_mfma_f32_16x16x128_f8f6f4 v[24:27], v[150:155], v[0:5], v[24:27] cbsz:2 blgp:2
	s_nop 7
	v_cndmask_b32_e64 v24, v24, v25, s[4:5]
	v_cndmask_b32_e64 v24, v24, v26, s[2:3]
	v_cndmask_b32_e32 v24, v24, v27, vcc
	v_mul_f32_e32 v25, v33, v24
	s_nop 1
	v_mov_b32_dpp v25, v25 quad_perm:[1,0,3,2] row_mask:0xf bank_mask:0xf bound_ctrl:1
	v_fmac_f32_e32 v25, v33, v24
	s_nop 1
	v_add_f32_dpp v24, v25, v25 quad_perm:[2,3,0,1] row_mask:0xf bank_mask:0xf bound_ctrl:1
	s_nop 1
	v_add_f32_dpp v24, v24, v24 row_half_mirror row_mask:0xf bank_mask:0xf bound_ctrl:1
	ds_write_b32 v32, v24 offset:49272
	s_waitcnt vmcnt(3)
	v_mfma_f32_16x16x128_f8f6f4 v[18:21], v[156:161], v[18:23], 0 cbsz:2 blgp:2
	s_waitcnt vmcnt(2)
	v_mfma_f32_16x16x128_f8f6f4 v[12:15], v[168:173], v[12:17], v[18:21] cbsz:2 blgp:2
	s_waitcnt vmcnt(1)
	v_mfma_f32_16x16x128_f8f6f4 v[6:9], v[162:167], v[6:11], v[12:15] cbsz:2 blgp:2
	s_waitcnt vmcnt(0)
	v_mfma_f32_16x16x128_f8f6f4 v[0:3], v[174:179], v[0:5], v[6:9] cbsz:2 blgp:2
	s_nop 7
	v_cndmask_b32_e64 v0, v0, v1, s[4:5]
	v_cndmask_b32_e64 v0, v0, v2, s[2:3]
	v_cndmask_b32_e32 v0, v0, v3, vcc
	v_mul_f32_e32 v1, v33, v0
	s_nop 1
	v_mov_b32_dpp v1, v1 quad_perm:[1,0,3,2] row_mask:0xf bank_mask:0xf bound_ctrl:1
	v_fmac_f32_e32 v1, v33, v0
	s_nop 1
	v_add_f32_dpp v0, v1, v1 quad_perm:[2,3,0,1] row_mask:0xf bank_mask:0xf bound_ctrl:1
	s_nop 1
	v_add_f32_dpp v0, v0, v0 row_half_mirror row_mask:0xf bank_mask:0xf bound_ctrl:1
	ds_write_b32 v32, v0 offset:49276
	v_mul_u32_u24_e32 v240, 0x600, v130
	v_mul_u32_u24_e32 v241, 0x600, v128
	v_add_u32_e32 v240, 0x8000000, v240
	v_add_u32_e32 v241, 0x8000000, v241
	v_lshrrev_b32_e32 v0, 1, v129
	v_readlane_b32 s100, v240, 0
	v_readlane_b32 s101, v240, 1
	v_readlane_b32 s2, v240, 2
	v_readlane_b32 s3, v240, 3
	s_nop 1
	buffer_load_dwordx4 v[74:77], v129, s[44:47], s100 offen
	buffer_load_dwordx2 v[78:79], v0, s[44:47], s100 offen offset:1024
	buffer_load_dwordx4 v[68:71], v129, s[44:47], s101 offen
	buffer_load_dwordx2 v[72:73], v0, s[44:47], s101 offen offset:1024
	buffer_load_dwordx4 v[56:59], v129, s[44:47], s2 offen
	buffer_load_dwordx2 v[60:61], v0, s[44:47], s2 offen offset:1024
	buffer_load_dwordx4 v[44:47], v129, s[44:47], s3 offen
	buffer_load_dwordx2 v[48:49], v0, s[44:47], s3 offen offset:1024
	v_add_u32_e32 v210, 0x400, v0
	v_readlane_b32 s100, v240, 4
	v_readlane_b32 s101, v240, 5
	v_readlane_b32 s2, v240, 6
	v_readlane_b32 s3, v240, 7
	s_nop 1
	buffer_load_dwordx4 v[62:65], v129, s[44:47], s100 offen
	buffer_load_dwordx2 v[66:67], v0, s[44:47], s100 offen offset:1024
	buffer_load_dwordx4 v[50:53], v129, s[44:47], s101 offen
	buffer_load_dwordx2 v[54:55], v0, s[44:47], s101 offen offset:1024
	buffer_load_dwordx4 v[38:41], v129, s[44:47], s2 offen
	buffer_load_dwordx2 v[42:43], v0, s[44:47], s2 offen offset:1024
	buffer_load_dwordx4 v[32:35], v129, s[44:47], s3 offen
	buffer_load_dwordx2 v[36:37], v0, s[44:47], s3 offen offset:1024
	v_div_scale_f32 v2, s[2:3], v80, v80, 1.0
	v_rcp_f32_e32 v3, v2
	v_div_scale_f32 v4, vcc, 1.0, v80, 1.0
	v_and_b32_e32 v1, -4, v148
	v_fma_f32 v0, -v2, v3, 1.0
	v_fmac_f32_e32 v3, v0, v3
	v_mul_f32_e32 v5, v4, v3
	v_fma_f32 v0, -v2, v5, v4
	v_fmac_f32_e32 v5, v0, v3
	v_lshlrev_b32_e32 v0, 7, v148
	v_and_b32_e32 v0, 0x180, v0
	v_add3_u32 v0, v111, v0, v1
	v_add_u32_e32 v0, 0xc000, v0
	ds_read2_b32 v[0:1], v0 offset1:16
	v_fma_f32 v2, -v2, v5, v4
	v_div_fmas_f32 v2, v2, v3, v5
	v_div_fixup_f32 v2, v2, v80, 1.0
	s_mov_b32 s1, 0x3e6d3388
	s_waitcnt lgkmcnt(0)
	v_mul_f32_e32 v0, v2, v0
	v_mul_f32_e32 v0, v83, v0
	v_fma_f32 v3, |v0|, s1, 1.0
	v_rcp_f32_e32 v3, v3
	v_mul_f32_e32 v5, v0, v0
	v_mul_f32_e32 v5, 0xbf38aa3b, v5
	v_exp_f32_e32 v5, v5
	v_fmamk_f32 v4, v3, 0x3f07dc22, v184
	v_fmaak_f32 v4, v3, v4, 0x3f35f0e3
	v_fmaak_f32 v4, v3, v4, 0xbe11a98e
	v_mul_f32_e32 v1, v2, v1
	v_fmaak_f32 v4, v3, v4, 0x3e027906
	v_mul_f32_e32 v3, v3, v4
	v_mul_f32_e32 v1, v82, v1
	v_mul_f32_e32 v3, v5, v3
	v_fma_f32 v5, |v1|, s1, 1.0
	v_rcp_f32_e32 v5, v5
	v_mul_f32_e32 v4, v0, v3
	v_fma_f32 v3, -v0, v3, v0
	v_cmp_gt_f32_e32 vcc, 0, v0
	v_mul_f32_e32 v2, v206, v84
	v_mov_b32_e32 v180, 0
	v_cndmask_b32_e32 v0, v3, v4, vcc
	v_mul_f32_e32 v211, v2, v0
	v_mul_f32_e32 v2, v1, v1
	v_fmamk_f32 v0, v5, 0x3f07dc22, v184
	v_mul_f32_e32 v2, 0xbf38aa3b, v2
	v_fmaak_f32 v0, v5, v0, 0x3f35f0e3
	v_exp_f32_e32 v2, v2
	v_fmaak_f32 v0, v5, v0, 0xbe11a98e
	v_fmaak_f32 v0, v5, v0, 0x3e027906
	v_mul_f32_e32 v0, v5, v0
	v_mul_f32_e32 v0, v2, v0
	v_mul_f32_e32 v2, v1, v0
	v_fma_f32 v0, -v1, v0, v1
	v_cmp_gt_f32_e32 vcc, 0, v1
	v_mul_f32_e32 v1, v205, v81
	v_mov_b32_e32 v181, v180
	v_cndmask_b32_e32 v0, v0, v2, vcc
	v_mul_f32_e32 v131, v1, v0
	v_mov_b32_e32 v178, v180
	v_mov_b32_e32 v179, v180
	v_mov_b32_e32 v176, v180
	v_mov_b32_e32 v177, v180
	v_mov_b32_e32 v174, v180
	v_mov_b32_e32 v175, v180
	v_mov_b32_e32 v172, v180
	v_mov_b32_e32 v173, v180
	v_mov_b32_e32 v170, v180
	v_mov_b32_e32 v171, v180
	v_mov_b32_e32 v168, v180
	v_mov_b32_e32 v169, v180
	v_mov_b32_e32 v166, v180
	v_mov_b32_e32 v167, v180
	v_mov_b32_e32 v164, v180
	v_mov_b32_e32 v165, v180
	v_mov_b32_e32 v162, v180
	v_mov_b32_e32 v163, v180
	v_mov_b32_e32 v160, v180
	v_mov_b32_e32 v161, v180
	v_mov_b32_e32 v158, v180
	v_mov_b32_e32 v159, v180
	v_mov_b32_e32 v156, v180
	v_mov_b32_e32 v157, v180
	v_mov_b32_e32 v154, v180
	v_mov_b32_e32 v155, v180
	v_mov_b32_e32 v152, v180
	v_mov_b32_e32 v153, v180
	v_mov_b32_e32 v150, v180
	v_mov_b32_e32 v151, v180
	v_readlane_b32 s2, v240, 8
	v_readlane_b32 s3, v240, 9
	v_readlane_b32 s100, v240, 10
	v_readlane_b32 s101, v240, 11
	s_nop 1
	buffer_load_dwordx4 v[98:101], v129, s[44:47], s2 offen
	buffer_load_dwordx2 v[102:103], v210, s[44:47], s2 offen
	buffer_load_dwordx4 v[92:95], v129, s[44:47], s3 offen
	buffer_load_dwordx2 v[96:97], v210, s[44:47], s3 offen
	buffer_load_dwordx4 v[86:89], v129, s[44:47], s100 offen
	buffer_load_dwordx2 v[90:91], v210, s[44:47], s100 offen
	buffer_load_dwordx4 v[80:83], v129, s[44:47], s101 offen
	buffer_load_dwordx2 v[84:85], v210, s[44:47], s101 offen
	s_waitcnt vmcnt(16)
	v_readlane_b32 s2, v211, 0
	s_nop 0
	v_cvt_scalef32_pk32_f32_fp6 v[0:31], v[74:79], 1.0
	v_pk_fma_f32 v[74:75], v[0:1], s[2:3], v[180:181] op_sel_hi:[1,0,1]
	v_pk_fma_f32 v[76:77], v[2:3], s[2:3], v[178:179] op_sel_hi:[1,0,1]
	v_pk_fma_f32 v[78:79], v[4:5], s[2:3], v[176:177] op_sel_hi:[1,0,1]
	v_pk_fma_f32 v[174:175], v[6:7], s[2:3], v[174:175] op_sel_hi:[1,0,1]
	v_pk_fma_f32 v[172:173], v[8:9], s[2:3], v[172:173] op_sel_hi:[1,0,1]
	v_pk_fma_f32 v[170:171], v[10:11], s[2:3], v[170:171] op_sel_hi:[1,0,1]
	v_pk_fma_f32 v[168:169], v[12:13], s[2:3], v[168:169] op_sel_hi:[1,0,1]
	v_pk_fma_f32 v[166:167], v[14:15], s[2:3], v[166:167] op_sel_hi:[1,0,1]
	v_pk_fma_f32 v[164:165], v[16:17], s[2:3], v[164:165] op_sel_hi:[1,0,1]
	v_pk_fma_f32 v[162:163], v[18:19], s[2:3], v[162:163] op_sel_hi:[1,0,1]
	v_pk_fma_f32 v[160:161], v[20:21], s[2:3], v[160:161] op_sel_hi:[1,0,1]
	v_pk_fma_f32 v[158:159], v[22:23], s[2:3], v[158:159] op_sel_hi:[1,0,1]
	v_pk_fma_f32 v[156:157], v[24:25], s[2:3], v[156:157] op_sel_hi:[1,0,1]
	v_pk_fma_f32 v[154:155], v[26:27], s[2:3], v[154:155] op_sel_hi:[1,0,1]
	v_pk_fma_f32 v[152:153], v[28:29], s[2:3], v[152:153] op_sel_hi:[1,0,1]
	v_pk_fma_f32 v[150:151], v[30:31], s[2:3], v[150:151] op_sel_hi:[1,0,1]
	v_readlane_b32 s2, v211, 1
	v_cvt_scalef32_pk32_f32_fp6 v[0:31], v[68:73], 1.0
	v_pk_fma_f32 v[68:69], v[0:1], s[2:3], v[74:75] op_sel_hi:[1,0,1]
	v_pk_fma_f32 v[70:71], v[2:3], s[2:3], v[76:77] op_sel_hi:[1,0,1]
	v_pk_fma_f32 v[72:73], v[4:5], s[2:3], v[78:79] op_sel_hi:[1,0,1]
	v_pk_fma_f32 v[74:75], v[6:7], s[2:3], v[174:175] op_sel_hi:[1,0,1]
	v_pk_fma_f32 v[76:77], v[8:9], s[2:3], v[172:173] op_sel_hi:[1,0,1]
	v_pk_fma_f32 v[78:79], v[10:11], s[2:3], v[170:171] op_sel_hi:[1,0,1]
	v_pk_fma_f32 v[168:169], v[12:13], s[2:3], v[168:169] op_sel_hi:[1,0,1]
	v_pk_fma_f32 v[166:167], v[14:15], s[2:3], v[166:167] op_sel_hi:[1,0,1]
	v_pk_fma_f32 v[164:165], v[16:17], s[2:3], v[164:165] op_sel_hi:[1,0,1]
	v_pk_fma_f32 v[162:163], v[18:19], s[2:3], v[162:163] op_sel_hi:[1,0,1]
	v_pk_fma_f32 v[160:161], v[20:21], s[2:3], v[160:161] op_sel_hi:[1,0,1]
	v_pk_fma_f32 v[158:159], v[22:23], s[2:3], v[158:159] op_sel_hi:[1,0,1]
	v_pk_fma_f32 v[156:157], v[24:25], s[2:3], v[156:157] op_sel_hi:[1,0,1]
	v_pk_fma_f32 v[154:155], v[26:27], s[2:3], v[154:155] op_sel_hi:[1,0,1]
	v_pk_fma_f32 v[152:153], v[28:29], s[2:3], v[152:153] op_sel_hi:[1,0,1]
	v_pk_fma_f32 v[150:151], v[30:31], s[2:3], v[150:151] op_sel_hi:[1,0,1]
	v_readlane_b32 s2, v211, 2
	v_cvt_scalef32_pk32_f32_fp6 v[0:31], v[56:61], 1.0
	v_pk_fma_f32 v[56:57], v[0:1], s[2:3], v[68:69] op_sel_hi:[1,0,1]
	v_pk_fma_f32 v[58:59], v[2:3], s[2:3], v[70:71] op_sel_hi:[1,0,1]
	v_pk_fma_f32 v[60:61], v[4:5], s[2:3], v[72:73] op_sel_hi:[1,0,1]
	v_pk_fma_f32 v[68:69], v[6:7], s[2:3], v[74:75] op_sel_hi:[1,0,1]
	v_pk_fma_f32 v[70:71], v[8:9], s[2:3], v[76:77] op_sel_hi:[1,0,1]
	v_pk_fma_f32 v[72:73], v[10:11], s[2:3], v[78:79] op_sel_hi:[1,0,1]
	v_pk_fma_f32 v[74:75], v[12:13], s[2:3], v[168:169] op_sel_hi:[1,0,1]
	v_pk_fma_f32 v[76:77], v[14:15], s[2:3], v[166:167] op_sel_hi:[1,0,1]
	v_pk_fma_f32 v[78:79], v[16:17], s[2:3], v[164:165] op_sel_hi:[1,0,1]
	v_pk_fma_f32 v[162:163], v[18:19], s[2:3], v[162:163] op_sel_hi:[1,0,1]
	v_pk_fma_f32 v[160:161], v[20:21], s[2:3], v[160:161] op_sel_hi:[1,0,1]
	v_pk_fma_f32 v[158:159], v[22:23], s[2:3], v[158:159] op_sel_hi:[1,0,1]
	v_pk_fma_f32 v[156:157], v[24:25], s[2:3], v[156:157] op_sel_hi:[1,0,1]
	v_pk_fma_f32 v[154:155], v[26:27], s[2:3], v[154:155] op_sel_hi:[1,0,1]
	v_pk_fma_f32 v[152:153], v[28:29], s[2:3], v[152:153] op_sel_hi:[1,0,1]
	v_pk_fma_f32 v[150:151], v[30:31], s[2:3], v[150:151] op_sel_hi:[1,0,1]
	v_readlane_b32 s2, v211, 3
	v_cvt_scalef32_pk32_f32_fp6 v[0:31], v[44:49], 1.0
	v_pk_fma_f32 v[164:165], v[0:1], s[2:3], v[56:57] op_sel_hi:[1,0,1]
	v_pk_fma_f32 v[166:167], v[2:3], s[2:3], v[58:59] op_sel_hi:[1,0,1]
	v_pk_fma_f32 v[168:169], v[4:5], s[2:3], v[60:61] op_sel_hi:[1,0,1]
	v_pk_fma_f32 v[170:171], v[6:7], s[2:3], v[68:69] op_sel_hi:[1,0,1]
	v_pk_fma_f32 v[172:173], v[8:9], s[2:3], v[70:71] op_sel_hi:[1,0,1]
	v_pk_fma_f32 v[174:175], v[10:11], s[2:3], v[72:73] op_sel_hi:[1,0,1]
	v_pk_fma_f32 v[176:177], v[12:13], s[2:3], v[74:75] op_sel_hi:[1,0,1]
	v_pk_fma_f32 v[178:179], v[14:15], s[2:3], v[76:77] op_sel_hi:[1,0,1]
	v_pk_fma_f32 v[180:181], v[16:17], s[2:3], v[78:79] op_sel_hi:[1,0,1]
	v_pk_fma_f32 v[162:163], v[18:19], s[2:3], v[162:163] op_sel_hi:[1,0,1]
	v_pk_fma_f32 v[160:161], v[20:21], s[2:3], v[160:161] op_sel_hi:[1,0,1]
	v_pk_fma_f32 v[158:159], v[22:23], s[2:3], v[158:159] op_sel_hi:[1,0,1]
	v_pk_fma_f32 v[156:157], v[24:25], s[2:3], v[156:157] op_sel_hi:[1,0,1]
	v_pk_fma_f32 v[154:155], v[26:27], s[2:3], v[154:155] op_sel_hi:[1,0,1]
	v_pk_fma_f32 v[152:153], v[28:29], s[2:3], v[152:153] op_sel_hi:[1,0,1]
	v_pk_fma_f32 v[150:151], v[30:31], s[2:3], v[150:151] op_sel_hi:[1,0,1]
	v_readlane_b32 s2, v240, 12
	v_readlane_b32 s3, v240, 13
	v_readlane_b32 s100, v240, 14
	v_readlane_b32 s101, v240, 15
	s_nop 1
	buffer_load_dwordx4 v[74:77], v129, s[44:47], s2 offen
	buffer_load_dwordx2 v[78:79], v210, s[44:47], s2 offen
	buffer_load_dwordx4 v[68:71], v129, s[44:47], s3 offen
	buffer_load_dwordx2 v[72:73], v210, s[44:47], s3 offen
	buffer_load_dwordx4 v[56:59], v129, s[44:47], s100 offen
	buffer_load_dwordx2 v[60:61], v210, s[44:47], s100 offen
	buffer_load_dwordx4 v[44:47], v129, s[44:47], s101 offen
	buffer_load_dwordx2 v[48:49], v210, s[44:47], s101 offen
	s_waitcnt vmcnt(16)
	v_readlane_b32 s2, v211, 4
	s_nop 0
	v_cvt_scalef32_pk32_f32_fp6 v[0:31], v[62:67], 1.0
	v_pk_fma_f32 v[62:63], v[0:1], s[2:3], v[164:165] op_sel_hi:[1,0,1]
	v_pk_fma_f32 v[64:65], v[2:3], s[2:3], v[166:167] op_sel_hi:[1,0,1]
	v_pk_fma_f32 v[66:67], v[4:5], s[2:3], v[168:169] op_sel_hi:[1,0,1]
	v_pk_fma_f32 v[164:165], v[6:7], s[2:3], v[170:171] op_sel_hi:[1,0,1]
	v_pk_fma_f32 v[166:167], v[8:9], s[2:3], v[172:173] op_sel_hi:[1,0,1]
	v_pk_fma_f32 v[168:169], v[10:11], s[2:3], v[174:175] op_sel_hi:[1,0,1]
	v_pk_fma_f32 v[170:171], v[12:13], s[2:3], v[176:177] op_sel_hi:[1,0,1]
	v_pk_fma_f32 v[172:173], v[14:15], s[2:3], v[178:179] op_sel_hi:[1,0,1]
	v_pk_fma_f32 v[174:175], v[16:17], s[2:3], v[180:181] op_sel_hi:[1,0,1]
	v_pk_fma_f32 v[162:163], v[18:19], s[2:3], v[162:163] op_sel_hi:[1,0,1]
	v_pk_fma_f32 v[160:161], v[20:21], s[2:3], v[160:161] op_sel_hi:[1,0,1]
	v_pk_fma_f32 v[158:159], v[22:23], s[2:3], v[158:159] op_sel_hi:[1,0,1]
	v_pk_fma_f32 v[156:157], v[24:25], s[2:3], v[156:157] op_sel_hi:[1,0,1]
	v_pk_fma_f32 v[154:155], v[26:27], s[2:3], v[154:155] op_sel_hi:[1,0,1]
	v_pk_fma_f32 v[152:153], v[28:29], s[2:3], v[152:153] op_sel_hi:[1,0,1]
	v_pk_fma_f32 v[150:151], v[30:31], s[2:3], v[150:151] op_sel_hi:[1,0,1]
	v_readlane_b32 s2, v211, 5
	v_cvt_scalef32_pk32_f32_fp6 v[0:31], v[50:55], 1.0
	v_pk_fma_f32 v[50:51], v[0:1], s[2:3], v[62:63] op_sel_hi:[1,0,1]
	v_pk_fma_f32 v[52:53], v[2:3], s[2:3], v[64:65] op_sel_hi:[1,0,1]
	v_pk_fma_f32 v[54:55], v[4:5], s[2:3], v[66:67] op_sel_hi:[1,0,1]
	v_pk_fma_f32 v[62:63], v[6:7], s[2:3], v[164:165] op_sel_hi:[1,0,1]
	v_pk_fma_f32 v[64:65], v[8:9], s[2:3], v[166:167] op_sel_hi:[1,0,1]
	v_pk_fma_f32 v[66:67], v[10:11], s[2:3], v[168:169] op_sel_hi:[1,0,1]
	v_pk_fma_f32 v[164:165], v[12:13], s[2:3], v[170:171] op_sel_hi:[1,0,1]
	v_pk_fma_f32 v[166:167], v[14:15], s[2:3], v[172:173] op_sel_hi:[1,0,1]
	v_pk_fma_f32 v[168:169], v[16:17], s[2:3], v[174:175] op_sel_hi:[1,0,1]
	v_pk_fma_f32 v[162:163], v[18:19], s[2:3], v[162:163] op_sel_hi:[1,0,1]
	v_pk_fma_f32 v[160:161], v[20:21], s[2:3], v[160:161] op_sel_hi:[1,0,1]
	v_pk_fma_f32 v[158:159], v[22:23], s[2:3], v[158:159] op_sel_hi:[1,0,1]
	v_pk_fma_f32 v[156:157], v[24:25], s[2:3], v[156:157] op_sel_hi:[1,0,1]
	v_pk_fma_f32 v[154:155], v[26:27], s[2:3], v[154:155] op_sel_hi:[1,0,1]
	v_pk_fma_f32 v[152:153], v[28:29], s[2:3], v[152:153] op_sel_hi:[1,0,1]
	v_pk_fma_f32 v[150:151], v[30:31], s[2:3], v[150:151] op_sel_hi:[1,0,1]
	v_readlane_b32 s2, v211, 6
	v_cvt_scalef32_pk32_f32_fp6 v[0:31], v[38:43], 1.0
	v_pk_fma_f32 v[38:39], v[0:1], s[2:3], v[50:51] op_sel_hi:[1,0,1]
	v_pk_fma_f32 v[40:41], v[2:3], s[2:3], v[52:53] op_sel_hi:[1,0,1]
	v_pk_fma_f32 v[42:43], v[4:5], s[2:3], v[54:55] op_sel_hi:[1,0,1]
	v_pk_fma_f32 v[50:51], v[6:7], s[2:3], v[62:63] op_sel_hi:[1,0,1]
	v_pk_fma_f32 v[52:53], v[8:9], s[2:3], v[64:65] op_sel_hi:[1,0,1]
	v_pk_fma_f32 v[54:55], v[10:11], s[2:3], v[66:67] op_sel_hi:[1,0,1]
	v_pk_fma_f32 v[62:63], v[12:13], s[2:3], v[164:165] op_sel_hi:[1,0,1]
	v_pk_fma_f32 v[64:65], v[14:15], s[2:3], v[166:167] op_sel_hi:[1,0,1]
	v_pk_fma_f32 v[66:67], v[16:17], s[2:3], v[168:169] op_sel_hi:[1,0,1]
	v_pk_fma_f32 v[162:163], v[18:19], s[2:3], v[162:163] op_sel_hi:[1,0,1]
	v_pk_fma_f32 v[160:161], v[20:21], s[2:3], v[160:161] op_sel_hi:[1,0,1]
	v_pk_fma_f32 v[158:159], v[22:23], s[2:3], v[158:159] op_sel_hi:[1,0,1]
	v_pk_fma_f32 v[156:157], v[24:25], s[2:3], v[156:157] op_sel_hi:[1,0,1]
	v_pk_fma_f32 v[154:155], v[26:27], s[2:3], v[154:155] op_sel_hi:[1,0,1]
	v_pk_fma_f32 v[152:153], v[28:29], s[2:3], v[152:153] op_sel_hi:[1,0,1]
	v_pk_fma_f32 v[150:151], v[30:31], s[2:3], v[150:151] op_sel_hi:[1,0,1]
	v_readlane_b32 s2, v211, 7
	v_cvt_scalef32_pk32_f32_fp6 v[0:31], v[32:37], 1.0
	v_pk_fma_f32 v[164:165], v[0:1], s[2:3], v[38:39] op_sel_hi:[1,0,1]
	v_pk_fma_f32 v[166:167], v[2:3], s[2:3], v[40:41] op_sel_hi:[1,0,1]
	v_pk_fma_f32 v[168:169], v[4:5], s[2:3], v[42:43] op_sel_hi:[1,0,1]
	v_pk_fma_f32 v[170:171], v[6:7], s[2:3], v[50:51] op_sel_hi:[1,0,1]
	v_pk_fma_f32 v[172:173], v[8:9], s[2:3], v[52:53] op_sel_hi:[1,0,1]
	v_pk_fma_f32 v[174:175], v[10:11], s[2:3], v[54:55] op_sel_hi:[1,0,1]
	v_pk_fma_f32 v[176:177], v[12:13], s[2:3], v[62:63] op_sel_hi:[1,0,1]
	v_pk_fma_f32 v[178:179], v[14:15], s[2:3], v[64:65] op_sel_hi:[1,0,1]
	v_pk_fma_f32 v[180:181], v[16:17], s[2:3], v[66:67] op_sel_hi:[1,0,1]
	v_pk_fma_f32 v[162:163], v[18:19], s[2:3], v[162:163] op_sel_hi:[1,0,1]
	v_pk_fma_f32 v[160:161], v[20:21], s[2:3], v[160:161] op_sel_hi:[1,0,1]
	v_pk_fma_f32 v[158:159], v[22:23], s[2:3], v[158:159] op_sel_hi:[1,0,1]
	v_pk_fma_f32 v[156:157], v[24:25], s[2:3], v[156:157] op_sel_hi:[1,0,1]
	v_pk_fma_f32 v[154:155], v[26:27], s[2:3], v[154:155] op_sel_hi:[1,0,1]
	v_pk_fma_f32 v[152:153], v[28:29], s[2:3], v[152:153] op_sel_hi:[1,0,1]
	v_pk_fma_f32 v[150:151], v[30:31], s[2:3], v[150:151] op_sel_hi:[1,0,1]
	v_readlane_b32 s2, v240, 16
	v_readlane_b32 s3, v240, 17
	v_readlane_b32 s100, v240, 18
	v_readlane_b32 s101, v240, 19
	s_nop 1
	buffer_load_dwordx4 v[62:65], v129, s[44:47], s2 offen
	buffer_load_dwordx2 v[66:67], v210, s[44:47], s2 offen
	buffer_load_dwordx4 v[50:53], v129, s[44:47], s3 offen
	buffer_load_dwordx2 v[54:55], v210, s[44:47], s3 offen
	buffer_load_dwordx4 v[38:41], v129, s[44:47], s100 offen
	buffer_load_dwordx2 v[42:43], v210, s[44:47], s100 offen
	buffer_load_dwordx4 v[32:35], v129, s[44:47], s101 offen
	buffer_load_dwordx2 v[36:37], v210, s[44:47], s101 offen
	s_waitcnt vmcnt(16)
	v_readlane_b32 s2, v211, 8
	s_nop 0
	v_cvt_scalef32_pk32_f32_fp6 v[0:31], v[98:103], 1.0
	v_pk_fma_f32 v[98:99], v[0:1], s[2:3], v[164:165] op_sel_hi:[1,0,1]
	v_pk_fma_f32 v[100:101], v[2:3], s[2:3], v[166:167] op_sel_hi:[1,0,1]
	v_pk_fma_f32 v[102:103], v[4:5], s[2:3], v[168:169] op_sel_hi:[1,0,1]
	v_pk_fma_f32 v[164:165], v[6:7], s[2:3], v[170:171] op_sel_hi:[1,0,1]
	v_pk_fma_f32 v[166:167], v[8:9], s[2:3], v[172:173] op_sel_hi:[1,0,1]
	v_pk_fma_f32 v[168:169], v[10:11], s[2:3], v[174:175] op_sel_hi:[1,0,1]
	v_pk_fma_f32 v[170:171], v[12:13], s[2:3], v[176:177] op_sel_hi:[1,0,1]
	v_pk_fma_f32 v[172:173], v[14:15], s[2:3], v[178:179] op_sel_hi:[1,0,1]
	v_pk_fma_f32 v[174:175], v[16:17], s[2:3], v[180:181] op_sel_hi:[1,0,1]
	v_pk_fma_f32 v[162:163], v[18:19], s[2:3], v[162:163] op_sel_hi:[1,0,1]
	v_pk_fma_f32 v[160:161], v[20:21], s[2:3], v[160:161] op_sel_hi:[1,0,1]
	v_pk_fma_f32 v[158:159], v[22:23], s[2:3], v[158:159] op_sel_hi:[1,0,1]
	v_pk_fma_f32 v[156:157], v[24:25], s[2:3], v[156:157] op_sel_hi:[1,0,1]
	v_pk_fma_f32 v[154:155], v[26:27], s[2:3], v[154:155] op_sel_hi:[1,0,1]
	v_pk_fma_f32 v[152:153], v[28:29], s[2:3], v[152:153] op_sel_hi:[1,0,1]
	v_pk_fma_f32 v[150:151], v[30:31], s[2:3], v[150:151] op_sel_hi:[1,0,1]
	v_readlane_b32 s2, v211, 9
	v_cvt_scalef32_pk32_f32_fp6 v[0:31], v[92:97], 1.0
	v_pk_fma_f32 v[92:93], v[0:1], s[2:3], v[98:99] op_sel_hi:[1,0,1]
	v_pk_fma_f32 v[94:95], v[2:3], s[2:3], v[100:101] op_sel_hi:[1,0,1]
	v_pk_fma_f32 v[96:97], v[4:5], s[2:3], v[102:103] op_sel_hi:[1,0,1]
	v_pk_fma_f32 v[98:99], v[6:7], s[2:3], v[164:165] op_sel_hi:[1,0,1]
	v_pk_fma_f32 v[100:101], v[8:9], s[2:3], v[166:167] op_sel_hi:[1,0,1]
	v_pk_fma_f32 v[102:103], v[10:11], s[2:3], v[168:169] op_sel_hi:[1,0,1]
	v_pk_fma_f32 v[164:165], v[12:13], s[2:3], v[170:171] op_sel_hi:[1,0,1]
	v_pk_fma_f32 v[166:167], v[14:15], s[2:3], v[172:173] op_sel_hi:[1,0,1]
	v_pk_fma_f32 v[168:169], v[16:17], s[2:3], v[174:175] op_sel_hi:[1,0,1]
	v_pk_fma_f32 v[162:163], v[18:19], s[2:3], v[162:163] op_sel_hi:[1,0,1]
	v_pk_fma_f32 v[160:161], v[20:21], s[2:3], v[160:161] op_sel_hi:[1,0,1]
	v_pk_fma_f32 v[158:159], v[22:23], s[2:3], v[158:159] op_sel_hi:[1,0,1]
	v_pk_fma_f32 v[156:157], v[24:25], s[2:3], v[156:157] op_sel_hi:[1,0,1]
	v_pk_fma_f32 v[154:155], v[26:27], s[2:3], v[154:155] op_sel_hi:[1,0,1]
	v_pk_fma_f32 v[152:153], v[28:29], s[2:3], v[152:153] op_sel_hi:[1,0,1]
	v_pk_fma_f32 v[150:151], v[30:31], s[2:3], v[150:151] op_sel_hi:[1,0,1]
	v_readlane_b32 s2, v211, 10
	v_cvt_scalef32_pk32_f32_fp6 v[0:31], v[86:91], 1.0
	v_pk_fma_f32 v[86:87], v[0:1], s[2:3], v[92:93] op_sel_hi:[1,0,1]
	v_pk_fma_f32 v[88:89], v[2:3], s[2:3], v[94:95] op_sel_hi:[1,0,1]
	v_pk_fma_f32 v[90:91], v[4:5], s[2:3], v[96:97] op_sel_hi:[1,0,1]
	v_pk_fma_f32 v[92:93], v[6:7], s[2:3], v[98:99] op_sel_hi:[1,0,1]
	v_pk_fma_f32 v[94:95], v[8:9], s[2:3], v[100:101] op_sel_hi:[1,0,1]
	v_pk_fma_f32 v[96:97], v[10:11], s[2:3], v[102:103] op_sel_hi:[1,0,1]
	v_pk_fma_f32 v[98:99], v[12:13], s[2:3], v[164:165] op_sel_hi:[1,0,1]
	v_pk_fma_f32 v[100:101], v[14:15], s[2:3], v[166:167] op_sel_hi:[1,0,1]
	v_pk_fma_f32 v[102:103], v[16:17], s[2:3], v[168:169] op_sel_hi:[1,0,1]
	v_pk_fma_f32 v[162:163], v[18:19], s[2:3], v[162:163] op_sel_hi:[1,0,1]
	v_pk_fma_f32 v[160:161], v[20:21], s[2:3], v[160:161] op_sel_hi:[1,0,1]
	v_pk_fma_f32 v[158:159], v[22:23], s[2:3], v[158:159] op_sel_hi:[1,0,1]
	v_pk_fma_f32 v[156:157], v[24:25], s[2:3], v[156:157] op_sel_hi:[1,0,1]
	v_pk_fma_f32 v[154:155], v[26:27], s[2:3], v[154:155] op_sel_hi:[1,0,1]
	v_pk_fma_f32 v[152:153], v[28:29], s[2:3], v[152:153] op_sel_hi:[1,0,1]
	v_pk_fma_f32 v[150:151], v[30:31], s[2:3], v[150:151] op_sel_hi:[1,0,1]
	v_readlane_b32 s2, v211, 11
	v_cvt_scalef32_pk32_f32_fp6 v[0:31], v[80:85], 1.0
	v_pk_fma_f32 v[180:181], v[0:1], s[2:3], v[86:87] op_sel_hi:[1,0,1]
	v_pk_fma_f32 v[178:179], v[2:3], s[2:3], v[88:89] op_sel_hi:[1,0,1]
	v_pk_fma_f32 v[176:177], v[4:5], s[2:3], v[90:91] op_sel_hi:[1,0,1]
	v_pk_fma_f32 v[174:175], v[6:7], s[2:3], v[92:93] op_sel_hi:[1,0,1]
	v_pk_fma_f32 v[172:173], v[8:9], s[2:3], v[94:95] op_sel_hi:[1,0,1]
	v_pk_fma_f32 v[170:171], v[10:11], s[2:3], v[96:97] op_sel_hi:[1,0,1]
	v_pk_fma_f32 v[168:169], v[12:13], s[2:3], v[98:99] op_sel_hi:[1,0,1]
	v_pk_fma_f32 v[166:167], v[14:15], s[2:3], v[100:101] op_sel_hi:[1,0,1]
	v_pk_fma_f32 v[164:165], v[16:17], s[2:3], v[102:103] op_sel_hi:[1,0,1]
	v_pk_fma_f32 v[162:163], v[18:19], s[2:3], v[162:163] op_sel_hi:[1,0,1]
	v_pk_fma_f32 v[160:161], v[20:21], s[2:3], v[160:161] op_sel_hi:[1,0,1]
	v_pk_fma_f32 v[158:159], v[22:23], s[2:3], v[158:159] op_sel_hi:[1,0,1]
	v_pk_fma_f32 v[156:157], v[24:25], s[2:3], v[156:157] op_sel_hi:[1,0,1]
	v_pk_fma_f32 v[154:155], v[26:27], s[2:3], v[154:155] op_sel_hi:[1,0,1]
	v_pk_fma_f32 v[152:153], v[28:29], s[2:3], v[152:153] op_sel_hi:[1,0,1]
	v_pk_fma_f32 v[150:151], v[30:31], s[2:3], v[150:151] op_sel_hi:[1,0,1]
	v_readlane_b32 s2, v240, 20
	v_readlane_b32 s3, v240, 21
	v_readlane_b32 s100, v240, 22
	v_readlane_b32 s101, v240, 23
	s_nop 1
	buffer_load_dwordx4 v[98:101], v129, s[44:47], s2 offen
	buffer_load_dwordx2 v[102:103], v210, s[44:47], s2 offen
	buffer_load_dwordx4 v[92:95], v129, s[44:47], s3 offen
	buffer_load_dwordx2 v[96:97], v210, s[44:47], s3 offen
	buffer_load_dwordx4 v[86:89], v129, s[44:47], s100 offen
	buffer_load_dwordx2 v[90:91], v210, s[44:47], s100 offen
	buffer_load_dwordx4 v[80:83], v129, s[44:47], s101 offen
	buffer_load_dwordx2 v[84:85], v210, s[44:47], s101 offen
	s_waitcnt vmcnt(16)
	v_readlane_b32 s2, v211, 12
	s_nop 0
	v_cvt_scalef32_pk32_f32_fp6 v[0:31], v[74:79], 1.0
	v_pk_fma_f32 v[74:75], v[0:1], s[2:3], v[180:181] op_sel_hi:[1,0,1]
	v_pk_fma_f32 v[76:77], v[2:3], s[2:3], v[178:179] op_sel_hi:[1,0,1]
	v_pk_fma_f32 v[78:79], v[4:5], s[2:3], v[176:177] op_sel_hi:[1,0,1]
	v_pk_fma_f32 v[174:175], v[6:7], s[2:3], v[174:175] op_sel_hi:[1,0,1]
	v_pk_fma_f32 v[172:173], v[8:9], s[2:3], v[172:173] op_sel_hi:[1,0,1]
	v_pk_fma_f32 v[170:171], v[10:11], s[2:3], v[170:171] op_sel_hi:[1,0,1]
	v_pk_fma_f32 v[168:169], v[12:13], s[2:3], v[168:169] op_sel_hi:[1,0,1]
	v_pk_fma_f32 v[166:167], v[14:15], s[2:3], v[166:167] op_sel_hi:[1,0,1]
	v_pk_fma_f32 v[164:165], v[16:17], s[2:3], v[164:165] op_sel_hi:[1,0,1]
	v_pk_fma_f32 v[162:163], v[18:19], s[2:3], v[162:163] op_sel_hi:[1,0,1]
	v_pk_fma_f32 v[160:161], v[20:21], s[2:3], v[160:161] op_sel_hi:[1,0,1]
	v_pk_fma_f32 v[158:159], v[22:23], s[2:3], v[158:159] op_sel_hi:[1,0,1]
	v_pk_fma_f32 v[156:157], v[24:25], s[2:3], v[156:157] op_sel_hi:[1,0,1]
	v_pk_fma_f32 v[154:155], v[26:27], s[2:3], v[154:155] op_sel_hi:[1,0,1]
	v_pk_fma_f32 v[152:153], v[28:29], s[2:3], v[152:153] op_sel_hi:[1,0,1]
	v_pk_fma_f32 v[150:151], v[30:31], s[2:3], v[150:151] op_sel_hi:[1,0,1]
	v_readlane_b32 s2, v211, 13
	v_cvt_scalef32_pk32_f32_fp6 v[0:31], v[68:73], 1.0
	v_pk_fma_f32 v[68:69], v[0:1], s[2:3], v[74:75] op_sel_hi:[1,0,1]
	v_pk_fma_f32 v[70:71], v[2:3], s[2:3], v[76:77] op_sel_hi:[1,0,1]
	v_pk_fma_f32 v[72:73], v[4:5], s[2:3], v[78:79] op_sel_hi:[1,0,1]
	v_pk_fma_f32 v[74:75], v[6:7], s[2:3], v[174:175] op_sel_hi:[1,0,1]
	v_pk_fma_f32 v[76:77], v[8:9], s[2:3], v[172:173] op_sel_hi:[1,0,1]
	v_pk_fma_f32 v[78:79], v[10:11], s[2:3], v[170:171] op_sel_hi:[1,0,1]
	v_pk_fma_f32 v[168:169], v[12:13], s[2:3], v[168:169] op_sel_hi:[1,0,1]
	v_pk_fma_f32 v[166:167], v[14:15], s[2:3], v[166:167] op_sel_hi:[1,0,1]
	v_pk_fma_f32 v[164:165], v[16:17], s[2:3], v[164:165] op_sel_hi:[1,0,1]
	v_pk_fma_f32 v[162:163], v[18:19], s[2:3], v[162:163] op_sel_hi:[1,0,1]
	v_pk_fma_f32 v[160:161], v[20:21], s[2:3], v[160:161] op_sel_hi:[1,0,1]
	v_pk_fma_f32 v[158:159], v[22:23], s[2:3], v[158:159] op_sel_hi:[1,0,1]
	v_pk_fma_f32 v[156:157], v[24:25], s[2:3], v[156:157] op_sel_hi:[1,0,1]
	v_pk_fma_f32 v[154:155], v[26:27], s[2:3], v[154:155] op_sel_hi:[1,0,1]
	v_pk_fma_f32 v[152:153], v[28:29], s[2:3], v[152:153] op_sel_hi:[1,0,1]
	v_pk_fma_f32 v[150:151], v[30:31], s[2:3], v[150:151] op_sel_hi:[1,0,1]
	v_readlane_b32 s2, v211, 14
	v_cvt_scalef32_pk32_f32_fp6 v[0:31], v[56:61], 1.0
	v_pk_fma_f32 v[56:57], v[0:1], s[2:3], v[68:69] op_sel_hi:[1,0,1]
	v_pk_fma_f32 v[58:59], v[2:3], s[2:3], v[70:71] op_sel_hi:[1,0,1]
	v_pk_fma_f32 v[60:61], v[4:5], s[2:3], v[72:73] op_sel_hi:[1,0,1]
	v_pk_fma_f32 v[68:69], v[6:7], s[2:3], v[74:75] op_sel_hi:[1,0,1]
	v_pk_fma_f32 v[70:71], v[8:9], s[2:3], v[76:77] op_sel_hi:[1,0,1]
	v_pk_fma_f32 v[72:73], v[10:11], s[2:3], v[78:79] op_sel_hi:[1,0,1]
	v_pk_fma_f32 v[74:75], v[12:13], s[2:3], v[168:169] op_sel_hi:[1,0,1]
	v_pk_fma_f32 v[76:77], v[14:15], s[2:3], v[166:167] op_sel_hi:[1,0,1]
	v_pk_fma_f32 v[78:79], v[16:17], s[2:3], v[164:165] op_sel_hi:[1,0,1]
	v_pk_fma_f32 v[162:163], v[18:19], s[2:3], v[162:163] op_sel_hi:[1,0,1]
	v_pk_fma_f32 v[160:161], v[20:21], s[2:3], v[160:161] op_sel_hi:[1,0,1]
	v_pk_fma_f32 v[158:159], v[22:23], s[2:3], v[158:159] op_sel_hi:[1,0,1]
	v_pk_fma_f32 v[156:157], v[24:25], s[2:3], v[156:157] op_sel_hi:[1,0,1]
	v_pk_fma_f32 v[154:155], v[26:27], s[2:3], v[154:155] op_sel_hi:[1,0,1]
	v_pk_fma_f32 v[152:153], v[28:29], s[2:3], v[152:153] op_sel_hi:[1,0,1]
	v_pk_fma_f32 v[150:151], v[30:31], s[2:3], v[150:151] op_sel_hi:[1,0,1]
	v_readlane_b32 s2, v211, 15
	v_cvt_scalef32_pk32_f32_fp6 v[0:31], v[44:49], 1.0
	v_pk_fma_f32 v[164:165], v[0:1], s[2:3], v[56:57] op_sel_hi:[1,0,1]
	v_pk_fma_f32 v[166:167], v[2:3], s[2:3], v[58:59] op_sel_hi:[1,0,1]
	v_pk_fma_f32 v[168:169], v[4:5], s[2:3], v[60:61] op_sel_hi:[1,0,1]
	v_pk_fma_f32 v[170:171], v[6:7], s[2:3], v[68:69] op_sel_hi:[1,0,1]
	v_pk_fma_f32 v[172:173], v[8:9], s[2:3], v[70:71] op_sel_hi:[1,0,1]
	v_pk_fma_f32 v[174:175], v[10:11], s[2:3], v[72:73] op_sel_hi:[1,0,1]
	v_pk_fma_f32 v[176:177], v[12:13], s[2:3], v[74:75] op_sel_hi:[1,0,1]
	v_pk_fma_f32 v[178:179], v[14:15], s[2:3], v[76:77] op_sel_hi:[1,0,1]
	v_pk_fma_f32 v[180:181], v[16:17], s[2:3], v[78:79] op_sel_hi:[1,0,1]
	v_pk_fma_f32 v[162:163], v[18:19], s[2:3], v[162:163] op_sel_hi:[1,0,1]
	v_pk_fma_f32 v[160:161], v[20:21], s[2:3], v[160:161] op_sel_hi:[1,0,1]
	v_pk_fma_f32 v[158:159], v[22:23], s[2:3], v[158:159] op_sel_hi:[1,0,1]
	v_pk_fma_f32 v[156:157], v[24:25], s[2:3], v[156:157] op_sel_hi:[1,0,1]
	v_pk_fma_f32 v[154:155], v[26:27], s[2:3], v[154:155] op_sel_hi:[1,0,1]
	v_pk_fma_f32 v[152:153], v[28:29], s[2:3], v[152:153] op_sel_hi:[1,0,1]
	v_pk_fma_f32 v[150:151], v[30:31], s[2:3], v[150:151] op_sel_hi:[1,0,1]
	v_readlane_b32 s2, v240, 24
	v_readlane_b32 s3, v240, 25
	v_readlane_b32 s100, v240, 26
	v_readlane_b32 s101, v240, 27
	s_nop 1
	buffer_load_dwordx4 v[74:77], v129, s[44:47], s2 offen
	buffer_load_dwordx2 v[78:79], v210, s[44:47], s2 offen
	buffer_load_dwordx4 v[68:71], v129, s[44:47], s3 offen
	buffer_load_dwordx2 v[72:73], v210, s[44:47], s3 offen
	buffer_load_dwordx4 v[56:59], v129, s[44:47], s100 offen
	buffer_load_dwordx2 v[60:61], v210, s[44:47], s100 offen
	buffer_load_dwordx4 v[44:47], v129, s[44:47], s101 offen
	buffer_load_dwordx2 v[48:49], v210, s[44:47], s101 offen
	s_waitcnt vmcnt(16)
	v_readlane_b32 s2, v211, 16
	s_nop 0
	v_cvt_scalef32_pk32_f32_fp6 v[0:31], v[62:67], 1.0
	v_pk_fma_f32 v[62:63], v[0:1], s[2:3], v[164:165] op_sel_hi:[1,0,1]
	v_pk_fma_f32 v[64:65], v[2:3], s[2:3], v[166:167] op_sel_hi:[1,0,1]
	v_pk_fma_f32 v[66:67], v[4:5], s[2:3], v[168:169] op_sel_hi:[1,0,1]
	v_pk_fma_f32 v[164:165], v[6:7], s[2:3], v[170:171] op_sel_hi:[1,0,1]
	v_pk_fma_f32 v[166:167], v[8:9], s[2:3], v[172:173] op_sel_hi:[1,0,1]
	v_pk_fma_f32 v[168:169], v[10:11], s[2:3], v[174:175] op_sel_hi:[1,0,1]
	v_pk_fma_f32 v[170:171], v[12:13], s[2:3], v[176:177] op_sel_hi:[1,0,1]
	v_pk_fma_f32 v[172:173], v[14:15], s[2:3], v[178:179] op_sel_hi:[1,0,1]
	v_pk_fma_f32 v[174:175], v[16:17], s[2:3], v[180:181] op_sel_hi:[1,0,1]
	v_pk_fma_f32 v[162:163], v[18:19], s[2:3], v[162:163] op_sel_hi:[1,0,1]
	v_pk_fma_f32 v[160:161], v[20:21], s[2:3], v[160:161] op_sel_hi:[1,0,1]
	v_pk_fma_f32 v[158:159], v[22:23], s[2:3], v[158:159] op_sel_hi:[1,0,1]
	v_pk_fma_f32 v[156:157], v[24:25], s[2:3], v[156:157] op_sel_hi:[1,0,1]
	v_pk_fma_f32 v[154:155], v[26:27], s[2:3], v[154:155] op_sel_hi:[1,0,1]
	v_pk_fma_f32 v[152:153], v[28:29], s[2:3], v[152:153] op_sel_hi:[1,0,1]
	v_pk_fma_f32 v[150:151], v[30:31], s[2:3], v[150:151] op_sel_hi:[1,0,1]
	v_readlane_b32 s2, v211, 17
	v_cvt_scalef32_pk32_f32_fp6 v[0:31], v[50:55], 1.0
	v_pk_fma_f32 v[50:51], v[0:1], s[2:3], v[62:63] op_sel_hi:[1,0,1]
	v_pk_fma_f32 v[52:53], v[2:3], s[2:3], v[64:65] op_sel_hi:[1,0,1]
	v_pk_fma_f32 v[54:55], v[4:5], s[2:3], v[66:67] op_sel_hi:[1,0,1]
	v_pk_fma_f32 v[62:63], v[6:7], s[2:3], v[164:165] op_sel_hi:[1,0,1]
	v_pk_fma_f32 v[64:65], v[8:9], s[2:3], v[166:167] op_sel_hi:[1,0,1]
	v_pk_fma_f32 v[66:67], v[10:11], s[2:3], v[168:169] op_sel_hi:[1,0,1]
	v_pk_fma_f32 v[164:165], v[12:13], s[2:3], v[170:171] op_sel_hi:[1,0,1]
	v_pk_fma_f32 v[166:167], v[14:15], s[2:3], v[172:173] op_sel_hi:[1,0,1]
	v_pk_fma_f32 v[168:169], v[16:17], s[2:3], v[174:175] op_sel_hi:[1,0,1]
	v_pk_fma_f32 v[162:163], v[18:19], s[2:3], v[162:163] op_sel_hi:[1,0,1]
	v_pk_fma_f32 v[160:161], v[20:21], s[2:3], v[160:161] op_sel_hi:[1,0,1]
	v_pk_fma_f32 v[158:159], v[22:23], s[2:3], v[158:159] op_sel_hi:[1,0,1]
	v_pk_fma_f32 v[156:157], v[24:25], s[2:3], v[156:157] op_sel_hi:[1,0,1]
	v_pk_fma_f32 v[154:155], v[26:27], s[2:3], v[154:155] op_sel_hi:[1,0,1]
	v_pk_fma_f32 v[152:153], v[28:29], s[2:3], v[152:153] op_sel_hi:[1,0,1]
	v_pk_fma_f32 v[150:151], v[30:31], s[2:3], v[150:151] op_sel_hi:[1,0,1]
	v_readlane_b32 s2, v211, 18
	v_cvt_scalef32_pk32_f32_fp6 v[0:31], v[38:43], 1.0
	v_pk_fma_f32 v[38:39], v[0:1], s[2:3], v[50:51] op_sel_hi:[1,0,1]
	v_pk_fma_f32 v[40:41], v[2:3], s[2:3], v[52:53] op_sel_hi:[1,0,1]
	v_pk_fma_f32 v[42:43], v[4:5], s[2:3], v[54:55] op_sel_hi:[1,0,1]
	v_pk_fma_f32 v[50:51], v[6:7], s[2:3], v[62:63] op_sel_hi:[1,0,1]
	v_pk_fma_f32 v[52:53], v[8:9], s[2:3], v[64:65] op_sel_hi:[1,0,1]
	v_pk_fma_f32 v[54:55], v[10:11], s[2:3], v[66:67] op_sel_hi:[1,0,1]
	v_pk_fma_f32 v[62:63], v[12:13], s[2:3], v[164:165] op_sel_hi:[1,0,1]
	v_pk_fma_f32 v[64:65], v[14:15], s[2:3], v[166:167] op_sel_hi:[1,0,1]
	v_pk_fma_f32 v[66:67], v[16:17], s[2:3], v[168:169] op_sel_hi:[1,0,1]
	v_pk_fma_f32 v[162:163], v[18:19], s[2:3], v[162:163] op_sel_hi:[1,0,1]
	v_pk_fma_f32 v[160:161], v[20:21], s[2:3], v[160:161] op_sel_hi:[1,0,1]
	v_pk_fma_f32 v[158:159], v[22:23], s[2:3], v[158:159] op_sel_hi:[1,0,1]
	v_pk_fma_f32 v[156:157], v[24:25], s[2:3], v[156:157] op_sel_hi:[1,0,1]
	v_pk_fma_f32 v[154:155], v[26:27], s[2:3], v[154:155] op_sel_hi:[1,0,1]
	v_pk_fma_f32 v[152:153], v[28:29], s[2:3], v[152:153] op_sel_hi:[1,0,1]
	v_pk_fma_f32 v[150:151], v[30:31], s[2:3], v[150:151] op_sel_hi:[1,0,1]
	v_readlane_b32 s2, v211, 19
	v_cvt_scalef32_pk32_f32_fp6 v[0:31], v[32:37], 1.0
	v_pk_fma_f32 v[164:165], v[0:1], s[2:3], v[38:39] op_sel_hi:[1,0,1]
	v_pk_fma_f32 v[166:167], v[2:3], s[2:3], v[40:41] op_sel_hi:[1,0,1]
	v_pk_fma_f32 v[168:169], v[4:5], s[2:3], v[42:43] op_sel_hi:[1,0,1]
	v_pk_fma_f32 v[170:171], v[6:7], s[2:3], v[50:51] op_sel_hi:[1,0,1]
	v_pk_fma_f32 v[172:173], v[8:9], s[2:3], v[52:53] op_sel_hi:[1,0,1]
	v_pk_fma_f32 v[174:175], v[10:11], s[2:3], v[54:55] op_sel_hi:[1,0,1]
	v_pk_fma_f32 v[176:177], v[12:13], s[2:3], v[62:63] op_sel_hi:[1,0,1]
	v_pk_fma_f32 v[178:179], v[14:15], s[2:3], v[64:65] op_sel_hi:[1,0,1]
	v_pk_fma_f32 v[180:181], v[16:17], s[2:3], v[66:67] op_sel_hi:[1,0,1]
	v_pk_fma_f32 v[162:163], v[18:19], s[2:3], v[162:163] op_sel_hi:[1,0,1]
	v_pk_fma_f32 v[160:161], v[20:21], s[2:3], v[160:161] op_sel_hi:[1,0,1]
	v_pk_fma_f32 v[158:159], v[22:23], s[2:3], v[158:159] op_sel_hi:[1,0,1]
	v_pk_fma_f32 v[156:157], v[24:25], s[2:3], v[156:157] op_sel_hi:[1,0,1]
	v_pk_fma_f32 v[154:155], v[26:27], s[2:3], v[154:155] op_sel_hi:[1,0,1]
	v_pk_fma_f32 v[152:153], v[28:29], s[2:3], v[152:153] op_sel_hi:[1,0,1]
	v_pk_fma_f32 v[150:151], v[30:31], s[2:3], v[150:151] op_sel_hi:[1,0,1]
	v_readlane_b32 s2, v240, 28
	v_readlane_b32 s3, v240, 29
	v_readlane_b32 s100, v240, 30
	v_readlane_b32 s101, v240, 31
	s_nop 1
	buffer_load_dwordx4 v[62:65], v129, s[44:47], s2 offen
	buffer_load_dwordx2 v[66:67], v210, s[44:47], s2 offen
	buffer_load_dwordx4 v[50:53], v129, s[44:47], s3 offen
	buffer_load_dwordx2 v[54:55], v210, s[44:47], s3 offen
	buffer_load_dwordx4 v[38:41], v129, s[44:47], s100 offen
	buffer_load_dwordx2 v[42:43], v210, s[44:47], s100 offen
	buffer_load_dwordx4 v[32:35], v129, s[44:47], s101 offen
	buffer_load_dwordx2 v[36:37], v210, s[44:47], s101 offen
	s_waitcnt vmcnt(16)
	v_readlane_b32 s2, v211, 20
	s_nop 0
	v_cvt_scalef32_pk32_f32_fp6 v[0:31], v[98:103], 1.0
	v_pk_fma_f32 v[98:99], v[0:1], s[2:3], v[164:165] op_sel_hi:[1,0,1]
	v_pk_fma_f32 v[100:101], v[2:3], s[2:3], v[166:167] op_sel_hi:[1,0,1]
	v_pk_fma_f32 v[102:103], v[4:5], s[2:3], v[168:169] op_sel_hi:[1,0,1]
	v_pk_fma_f32 v[164:165], v[6:7], s[2:3], v[170:171] op_sel_hi:[1,0,1]
	v_pk_fma_f32 v[166:167], v[8:9], s[2:3], v[172:173] op_sel_hi:[1,0,1]
	v_pk_fma_f32 v[168:169], v[10:11], s[2:3], v[174:175] op_sel_hi:[1,0,1]
	v_pk_fma_f32 v[170:171], v[12:13], s[2:3], v[176:177] op_sel_hi:[1,0,1]
	v_pk_fma_f32 v[172:173], v[14:15], s[2:3], v[178:179] op_sel_hi:[1,0,1]
	v_pk_fma_f32 v[174:175], v[16:17], s[2:3], v[180:181] op_sel_hi:[1,0,1]
	v_pk_fma_f32 v[162:163], v[18:19], s[2:3], v[162:163] op_sel_hi:[1,0,1]
	v_pk_fma_f32 v[160:161], v[20:21], s[2:3], v[160:161] op_sel_hi:[1,0,1]
	v_pk_fma_f32 v[158:159], v[22:23], s[2:3], v[158:159] op_sel_hi:[1,0,1]
	v_pk_fma_f32 v[156:157], v[24:25], s[2:3], v[156:157] op_sel_hi:[1,0,1]
	v_pk_fma_f32 v[154:155], v[26:27], s[2:3], v[154:155] op_sel_hi:[1,0,1]
	v_pk_fma_f32 v[152:153], v[28:29], s[2:3], v[152:153] op_sel_hi:[1,0,1]
	v_pk_fma_f32 v[150:151], v[30:31], s[2:3], v[150:151] op_sel_hi:[1,0,1]
	v_readlane_b32 s2, v211, 21
	v_cvt_scalef32_pk32_f32_fp6 v[0:31], v[92:97], 1.0
	v_pk_fma_f32 v[92:93], v[0:1], s[2:3], v[98:99] op_sel_hi:[1,0,1]
	v_pk_fma_f32 v[94:95], v[2:3], s[2:3], v[100:101] op_sel_hi:[1,0,1]
	v_pk_fma_f32 v[96:97], v[4:5], s[2:3], v[102:103] op_sel_hi:[1,0,1]
	v_pk_fma_f32 v[98:99], v[6:7], s[2:3], v[164:165] op_sel_hi:[1,0,1]
	v_pk_fma_f32 v[100:101], v[8:9], s[2:3], v[166:167] op_sel_hi:[1,0,1]
	v_pk_fma_f32 v[102:103], v[10:11], s[2:3], v[168:169] op_sel_hi:[1,0,1]
	v_pk_fma_f32 v[164:165], v[12:13], s[2:3], v[170:171] op_sel_hi:[1,0,1]
	v_pk_fma_f32 v[166:167], v[14:15], s[2:3], v[172:173] op_sel_hi:[1,0,1]
	v_pk_fma_f32 v[168:169], v[16:17], s[2:3], v[174:175] op_sel_hi:[1,0,1]
	v_pk_fma_f32 v[162:163], v[18:19], s[2:3], v[162:163] op_sel_hi:[1,0,1]
	v_pk_fma_f32 v[160:161], v[20:21], s[2:3], v[160:161] op_sel_hi:[1,0,1]
	v_pk_fma_f32 v[158:159], v[22:23], s[2:3], v[158:159] op_sel_hi:[1,0,1]
	v_pk_fma_f32 v[156:157], v[24:25], s[2:3], v[156:157] op_sel_hi:[1,0,1]
	v_pk_fma_f32 v[154:155], v[26:27], s[2:3], v[154:155] op_sel_hi:[1,0,1]
	v_pk_fma_f32 v[152:153], v[28:29], s[2:3], v[152:153] op_sel_hi:[1,0,1]
	v_pk_fma_f32 v[150:151], v[30:31], s[2:3], v[150:151] op_sel_hi:[1,0,1]
	v_readlane_b32 s2, v211, 22
	v_cvt_scalef32_pk32_f32_fp6 v[0:31], v[86:91], 1.0
	v_pk_fma_f32 v[86:87], v[0:1], s[2:3], v[92:93] op_sel_hi:[1,0,1]
	v_pk_fma_f32 v[88:89], v[2:3], s[2:3], v[94:95] op_sel_hi:[1,0,1]
	v_pk_fma_f32 v[90:91], v[4:5], s[2:3], v[96:97] op_sel_hi:[1,0,1]
	v_pk_fma_f32 v[92:93], v[6:7], s[2:3], v[98:99] op_sel_hi:[1,0,1]
	v_pk_fma_f32 v[94:95], v[8:9], s[2:3], v[100:101] op_sel_hi:[1,0,1]
	v_pk_fma_f32 v[96:97], v[10:11], s[2:3], v[102:103] op_sel_hi:[1,0,1]
	v_pk_fma_f32 v[98:99], v[12:13], s[2:3], v[164:165] op_sel_hi:[1,0,1]
	v_pk_fma_f32 v[100:101], v[14:15], s[2:3], v[166:167] op_sel_hi:[1,0,1]
	v_pk_fma_f32 v[102:103], v[16:17], s[2:3], v[168:169] op_sel_hi:[1,0,1]
	v_pk_fma_f32 v[162:163], v[18:19], s[2:3], v[162:163] op_sel_hi:[1,0,1]
	v_pk_fma_f32 v[160:161], v[20:21], s[2:3], v[160:161] op_sel_hi:[1,0,1]
	v_pk_fma_f32 v[158:159], v[22:23], s[2:3], v[158:159] op_sel_hi:[1,0,1]
	v_pk_fma_f32 v[156:157], v[24:25], s[2:3], v[156:157] op_sel_hi:[1,0,1]
	v_pk_fma_f32 v[154:155], v[26:27], s[2:3], v[154:155] op_sel_hi:[1,0,1]
	v_pk_fma_f32 v[152:153], v[28:29], s[2:3], v[152:153] op_sel_hi:[1,0,1]
	v_pk_fma_f32 v[150:151], v[30:31], s[2:3], v[150:151] op_sel_hi:[1,0,1]
	v_readlane_b32 s2, v211, 23
	v_cvt_scalef32_pk32_f32_fp6 v[0:31], v[80:85], 1.0
	v_pk_fma_f32 v[180:181], v[0:1], s[2:3], v[86:87] op_sel_hi:[1,0,1]
	v_pk_fma_f32 v[178:179], v[2:3], s[2:3], v[88:89] op_sel_hi:[1,0,1]
	v_pk_fma_f32 v[176:177], v[4:5], s[2:3], v[90:91] op_sel_hi:[1,0,1]
	v_pk_fma_f32 v[174:175], v[6:7], s[2:3], v[92:93] op_sel_hi:[1,0,1]
	v_pk_fma_f32 v[172:173], v[8:9], s[2:3], v[94:95] op_sel_hi:[1,0,1]
	v_pk_fma_f32 v[170:171], v[10:11], s[2:3], v[96:97] op_sel_hi:[1,0,1]
	v_pk_fma_f32 v[168:169], v[12:13], s[2:3], v[98:99] op_sel_hi:[1,0,1]
	v_pk_fma_f32 v[166:167], v[14:15], s[2:3], v[100:101] op_sel_hi:[1,0,1]
	v_pk_fma_f32 v[164:165], v[16:17], s[2:3], v[102:103] op_sel_hi:[1,0,1]
	v_pk_fma_f32 v[162:163], v[18:19], s[2:3], v[162:163] op_sel_hi:[1,0,1]
	v_pk_fma_f32 v[160:161], v[20:21], s[2:3], v[160:161] op_sel_hi:[1,0,1]
	v_pk_fma_f32 v[158:159], v[22:23], s[2:3], v[158:159] op_sel_hi:[1,0,1]
	v_pk_fma_f32 v[156:157], v[24:25], s[2:3], v[156:157] op_sel_hi:[1,0,1]
	v_pk_fma_f32 v[154:155], v[26:27], s[2:3], v[154:155] op_sel_hi:[1,0,1]
	v_pk_fma_f32 v[152:153], v[28:29], s[2:3], v[152:153] op_sel_hi:[1,0,1]
	v_pk_fma_f32 v[150:151], v[30:31], s[2:3], v[150:151] op_sel_hi:[1,0,1]
	v_readlane_b32 s2, v240, 32
	v_readlane_b32 s3, v240, 33
	v_readlane_b32 s100, v240, 34
	v_readlane_b32 s101, v240, 35
	s_nop 1
	buffer_load_dwordx4 v[98:101], v129, s[44:47], s2 offen
	buffer_load_dwordx2 v[102:103], v210, s[44:47], s2 offen
	buffer_load_dwordx4 v[92:95], v129, s[44:47], s3 offen
	buffer_load_dwordx2 v[96:97], v210, s[44:47], s3 offen
	buffer_load_dwordx4 v[86:89], v129, s[44:47], s100 offen
	buffer_load_dwordx2 v[90:91], v210, s[44:47], s100 offen
	buffer_load_dwordx4 v[80:83], v129, s[44:47], s101 offen
	buffer_load_dwordx2 v[84:85], v210, s[44:47], s101 offen
	s_waitcnt vmcnt(16)
	v_readlane_b32 s2, v211, 24
	s_nop 0
	v_cvt_scalef32_pk32_f32_fp6 v[0:31], v[74:79], 1.0
	v_pk_fma_f32 v[74:75], v[0:1], s[2:3], v[180:181] op_sel_hi:[1,0,1]
	v_pk_fma_f32 v[76:77], v[2:3], s[2:3], v[178:179] op_sel_hi:[1,0,1]
	v_pk_fma_f32 v[78:79], v[4:5], s[2:3], v[176:177] op_sel_hi:[1,0,1]
	v_pk_fma_f32 v[174:175], v[6:7], s[2:3], v[174:175] op_sel_hi:[1,0,1]
	v_pk_fma_f32 v[172:173], v[8:9], s[2:3], v[172:173] op_sel_hi:[1,0,1]
	v_pk_fma_f32 v[170:171], v[10:11], s[2:3], v[170:171] op_sel_hi:[1,0,1]
	v_pk_fma_f32 v[168:169], v[12:13], s[2:3], v[168:169] op_sel_hi:[1,0,1]
	v_pk_fma_f32 v[166:167], v[14:15], s[2:3], v[166:167] op_sel_hi:[1,0,1]
	v_pk_fma_f32 v[164:165], v[16:17], s[2:3], v[164:165] op_sel_hi:[1,0,1]
	v_pk_fma_f32 v[162:163], v[18:19], s[2:3], v[162:163] op_sel_hi:[1,0,1]
	v_pk_fma_f32 v[160:161], v[20:21], s[2:3], v[160:161] op_sel_hi:[1,0,1]
	v_pk_fma_f32 v[158:159], v[22:23], s[2:3], v[158:159] op_sel_hi:[1,0,1]
	v_pk_fma_f32 v[156:157], v[24:25], s[2:3], v[156:157] op_sel_hi:[1,0,1]
	v_pk_fma_f32 v[154:155], v[26:27], s[2:3], v[154:155] op_sel_hi:[1,0,1]
	v_pk_fma_f32 v[152:153], v[28:29], s[2:3], v[152:153] op_sel_hi:[1,0,1]
	v_pk_fma_f32 v[150:151], v[30:31], s[2:3], v[150:151] op_sel_hi:[1,0,1]
	v_readlane_b32 s2, v211, 25
	v_cvt_scalef32_pk32_f32_fp6 v[0:31], v[68:73], 1.0
	v_pk_fma_f32 v[68:69], v[0:1], s[2:3], v[74:75] op_sel_hi:[1,0,1]
	v_pk_fma_f32 v[70:71], v[2:3], s[2:3], v[76:77] op_sel_hi:[1,0,1]
	v_pk_fma_f32 v[72:73], v[4:5], s[2:3], v[78:79] op_sel_hi:[1,0,1]
	v_pk_fma_f32 v[74:75], v[6:7], s[2:3], v[174:175] op_sel_hi:[1,0,1]
	v_pk_fma_f32 v[76:77], v[8:9], s[2:3], v[172:173] op_sel_hi:[1,0,1]
	v_pk_fma_f32 v[78:79], v[10:11], s[2:3], v[170:171] op_sel_hi:[1,0,1]
	v_pk_fma_f32 v[168:169], v[12:13], s[2:3], v[168:169] op_sel_hi:[1,0,1]
	v_pk_fma_f32 v[166:167], v[14:15], s[2:3], v[166:167] op_sel_hi:[1,0,1]
	v_pk_fma_f32 v[164:165], v[16:17], s[2:3], v[164:165] op_sel_hi:[1,0,1]
	v_pk_fma_f32 v[162:163], v[18:19], s[2:3], v[162:163] op_sel_hi:[1,0,1]
	v_pk_fma_f32 v[160:161], v[20:21], s[2:3], v[160:161] op_sel_hi:[1,0,1]
	v_pk_fma_f32 v[158:159], v[22:23], s[2:3], v[158:159] op_sel_hi:[1,0,1]
	v_pk_fma_f32 v[156:157], v[24:25], s[2:3], v[156:157] op_sel_hi:[1,0,1]
	v_pk_fma_f32 v[154:155], v[26:27], s[2:3], v[154:155] op_sel_hi:[1,0,1]
	v_pk_fma_f32 v[152:153], v[28:29], s[2:3], v[152:153] op_sel_hi:[1,0,1]
	v_pk_fma_f32 v[150:151], v[30:31], s[2:3], v[150:151] op_sel_hi:[1,0,1]
	v_readlane_b32 s2, v211, 26
	v_cvt_scalef32_pk32_f32_fp6 v[0:31], v[56:61], 1.0
	v_pk_fma_f32 v[56:57], v[0:1], s[2:3], v[68:69] op_sel_hi:[1,0,1]
	v_pk_fma_f32 v[58:59], v[2:3], s[2:3], v[70:71] op_sel_hi:[1,0,1]
	v_pk_fma_f32 v[60:61], v[4:5], s[2:3], v[72:73] op_sel_hi:[1,0,1]
	v_pk_fma_f32 v[68:69], v[6:7], s[2:3], v[74:75] op_sel_hi:[1,0,1]
	v_pk_fma_f32 v[70:71], v[8:9], s[2:3], v[76:77] op_sel_hi:[1,0,1]
	v_pk_fma_f32 v[72:73], v[10:11], s[2:3], v[78:79] op_sel_hi:[1,0,1]
	v_pk_fma_f32 v[74:75], v[12:13], s[2:3], v[168:169] op_sel_hi:[1,0,1]
	v_pk_fma_f32 v[76:77], v[14:15], s[2:3], v[166:167] op_sel_hi:[1,0,1]
	v_pk_fma_f32 v[78:79], v[16:17], s[2:3], v[164:165] op_sel_hi:[1,0,1]
	v_pk_fma_f32 v[162:163], v[18:19], s[2:3], v[162:163] op_sel_hi:[1,0,1]
	v_pk_fma_f32 v[160:161], v[20:21], s[2:3], v[160:161] op_sel_hi:[1,0,1]
	v_pk_fma_f32 v[158:159], v[22:23], s[2:3], v[158:159] op_sel_hi:[1,0,1]
	v_pk_fma_f32 v[156:157], v[24:25], s[2:3], v[156:157] op_sel_hi:[1,0,1]
	v_pk_fma_f32 v[154:155], v[26:27], s[2:3], v[154:155] op_sel_hi:[1,0,1]
	v_pk_fma_f32 v[152:153], v[28:29], s[2:3], v[152:153] op_sel_hi:[1,0,1]
	v_pk_fma_f32 v[150:151], v[30:31], s[2:3], v[150:151] op_sel_hi:[1,0,1]
	v_readlane_b32 s2, v211, 27
	v_cvt_scalef32_pk32_f32_fp6 v[0:31], v[44:49], 1.0
	v_pk_fma_f32 v[164:165], v[0:1], s[2:3], v[56:57] op_sel_hi:[1,0,1]
	v_pk_fma_f32 v[166:167], v[2:3], s[2:3], v[58:59] op_sel_hi:[1,0,1]
	v_pk_fma_f32 v[168:169], v[4:5], s[2:3], v[60:61] op_sel_hi:[1,0,1]
	v_pk_fma_f32 v[170:171], v[6:7], s[2:3], v[68:69] op_sel_hi:[1,0,1]
	v_pk_fma_f32 v[172:173], v[8:9], s[2:3], v[70:71] op_sel_hi:[1,0,1]
	v_pk_fma_f32 v[174:175], v[10:11], s[2:3], v[72:73] op_sel_hi:[1,0,1]
	v_pk_fma_f32 v[176:177], v[12:13], s[2:3], v[74:75] op_sel_hi:[1,0,1]
	v_pk_fma_f32 v[178:179], v[14:15], s[2:3], v[76:77] op_sel_hi:[1,0,1]
	v_pk_fma_f32 v[180:181], v[16:17], s[2:3], v[78:79] op_sel_hi:[1,0,1]
	v_pk_fma_f32 v[162:163], v[18:19], s[2:3], v[162:163] op_sel_hi:[1,0,1]
	v_pk_fma_f32 v[160:161], v[20:21], s[2:3], v[160:161] op_sel_hi:[1,0,1]
	v_pk_fma_f32 v[158:159], v[22:23], s[2:3], v[158:159] op_sel_hi:[1,0,1]
	v_pk_fma_f32 v[156:157], v[24:25], s[2:3], v[156:157] op_sel_hi:[1,0,1]
	v_pk_fma_f32 v[154:155], v[26:27], s[2:3], v[154:155] op_sel_hi:[1,0,1]
	v_pk_fma_f32 v[152:153], v[28:29], s[2:3], v[152:153] op_sel_hi:[1,0,1]
	v_pk_fma_f32 v[150:151], v[30:31], s[2:3], v[150:151] op_sel_hi:[1,0,1]
	v_readlane_b32 s2, v240, 36
	v_readlane_b32 s3, v240, 37
	v_readlane_b32 s100, v240, 38
	v_readlane_b32 s101, v240, 39
	s_nop 1
	buffer_load_dwordx4 v[74:77], v129, s[44:47], s2 offen
	buffer_load_dwordx2 v[78:79], v210, s[44:47], s2 offen
	buffer_load_dwordx4 v[68:71], v129, s[44:47], s3 offen
	buffer_load_dwordx2 v[72:73], v210, s[44:47], s3 offen
	buffer_load_dwordx4 v[56:59], v129, s[44:47], s100 offen
	buffer_load_dwordx2 v[60:61], v210, s[44:47], s100 offen
	buffer_load_dwordx4 v[44:47], v129, s[44:47], s101 offen
	buffer_load_dwordx2 v[48:49], v210, s[44:47], s101 offen
	s_waitcnt vmcnt(16)
	v_readlane_b32 s2, v211, 28
	s_nop 0
	v_cvt_scalef32_pk32_f32_fp6 v[0:31], v[62:67], 1.0
	v_pk_fma_f32 v[62:63], v[0:1], s[2:3], v[164:165] op_sel_hi:[1,0,1]
	v_pk_fma_f32 v[64:65], v[2:3], s[2:3], v[166:167] op_sel_hi:[1,0,1]
	v_pk_fma_f32 v[66:67], v[4:5], s[2:3], v[168:169] op_sel_hi:[1,0,1]
	v_pk_fma_f32 v[164:165], v[6:7], s[2:3], v[170:171] op_sel_hi:[1,0,1]
	v_pk_fma_f32 v[166:167], v[8:9], s[2:3], v[172:173] op_sel_hi:[1,0,1]
	v_pk_fma_f32 v[168:169], v[10:11], s[2:3], v[174:175] op_sel_hi:[1,0,1]
	v_pk_fma_f32 v[170:171], v[12:13], s[2:3], v[176:177] op_sel_hi:[1,0,1]
	v_pk_fma_f32 v[172:173], v[14:15], s[2:3], v[178:179] op_sel_hi:[1,0,1]
	v_pk_fma_f32 v[174:175], v[16:17], s[2:3], v[180:181] op_sel_hi:[1,0,1]
	v_pk_fma_f32 v[162:163], v[18:19], s[2:3], v[162:163] op_sel_hi:[1,0,1]
	v_pk_fma_f32 v[160:161], v[20:21], s[2:3], v[160:161] op_sel_hi:[1,0,1]
	v_pk_fma_f32 v[158:159], v[22:23], s[2:3], v[158:159] op_sel_hi:[1,0,1]
	v_pk_fma_f32 v[156:157], v[24:25], s[2:3], v[156:157] op_sel_hi:[1,0,1]
	v_pk_fma_f32 v[154:155], v[26:27], s[2:3], v[154:155] op_sel_hi:[1,0,1]
	v_pk_fma_f32 v[152:153], v[28:29], s[2:3], v[152:153] op_sel_hi:[1,0,1]
	v_pk_fma_f32 v[150:151], v[30:31], s[2:3], v[150:151] op_sel_hi:[1,0,1]
	v_readlane_b32 s2, v211, 29
	v_cvt_scalef32_pk32_f32_fp6 v[0:31], v[50:55], 1.0
	v_pk_fma_f32 v[50:51], v[0:1], s[2:3], v[62:63] op_sel_hi:[1,0,1]
	v_pk_fma_f32 v[52:53], v[2:3], s[2:3], v[64:65] op_sel_hi:[1,0,1]
	v_pk_fma_f32 v[54:55], v[4:5], s[2:3], v[66:67] op_sel_hi:[1,0,1]
	v_pk_fma_f32 v[62:63], v[6:7], s[2:3], v[164:165] op_sel_hi:[1,0,1]
	v_pk_fma_f32 v[64:65], v[8:9], s[2:3], v[166:167] op_sel_hi:[1,0,1]
	v_pk_fma_f32 v[66:67], v[10:11], s[2:3], v[168:169] op_sel_hi:[1,0,1]
	v_pk_fma_f32 v[164:165], v[12:13], s[2:3], v[170:171] op_sel_hi:[1,0,1]
	v_pk_fma_f32 v[166:167], v[14:15], s[2:3], v[172:173] op_sel_hi:[1,0,1]
	v_pk_fma_f32 v[168:169], v[16:17], s[2:3], v[174:175] op_sel_hi:[1,0,1]
	v_pk_fma_f32 v[162:163], v[18:19], s[2:3], v[162:163] op_sel_hi:[1,0,1]
	v_pk_fma_f32 v[160:161], v[20:21], s[2:3], v[160:161] op_sel_hi:[1,0,1]
	v_pk_fma_f32 v[158:159], v[22:23], s[2:3], v[158:159] op_sel_hi:[1,0,1]
	v_pk_fma_f32 v[156:157], v[24:25], s[2:3], v[156:157] op_sel_hi:[1,0,1]
	v_pk_fma_f32 v[154:155], v[26:27], s[2:3], v[154:155] op_sel_hi:[1,0,1]
	v_pk_fma_f32 v[152:153], v[28:29], s[2:3], v[152:153] op_sel_hi:[1,0,1]
	v_pk_fma_f32 v[150:151], v[30:31], s[2:3], v[150:151] op_sel_hi:[1,0,1]
	v_readlane_b32 s2, v211, 30
	v_cvt_scalef32_pk32_f32_fp6 v[0:31], v[38:43], 1.0
	v_pk_fma_f32 v[38:39], v[0:1], s[2:3], v[50:51] op_sel_hi:[1,0,1]
	v_pk_fma_f32 v[40:41], v[2:3], s[2:3], v[52:53] op_sel_hi:[1,0,1]
	v_pk_fma_f32 v[42:43], v[4:5], s[2:3], v[54:55] op_sel_hi:[1,0,1]
	v_pk_fma_f32 v[50:51], v[6:7], s[2:3], v[62:63] op_sel_hi:[1,0,1]
	v_pk_fma_f32 v[52:53], v[8:9], s[2:3], v[64:65] op_sel_hi:[1,0,1]
	v_pk_fma_f32 v[54:55], v[10:11], s[2:3], v[66:67] op_sel_hi:[1,0,1]
	v_pk_fma_f32 v[62:63], v[12:13], s[2:3], v[164:165] op_sel_hi:[1,0,1]
	v_pk_fma_f32 v[64:65], v[14:15], s[2:3], v[166:167] op_sel_hi:[1,0,1]
	v_pk_fma_f32 v[66:67], v[16:17], s[2:3], v[168:169] op_sel_hi:[1,0,1]
	v_pk_fma_f32 v[162:163], v[18:19], s[2:3], v[162:163] op_sel_hi:[1,0,1]
	v_pk_fma_f32 v[160:161], v[20:21], s[2:3], v[160:161] op_sel_hi:[1,0,1]
	v_pk_fma_f32 v[158:159], v[22:23], s[2:3], v[158:159] op_sel_hi:[1,0,1]
	v_pk_fma_f32 v[156:157], v[24:25], s[2:3], v[156:157] op_sel_hi:[1,0,1]
	v_pk_fma_f32 v[154:155], v[26:27], s[2:3], v[154:155] op_sel_hi:[1,0,1]
	v_pk_fma_f32 v[152:153], v[28:29], s[2:3], v[152:153] op_sel_hi:[1,0,1]
	v_pk_fma_f32 v[150:151], v[30:31], s[2:3], v[150:151] op_sel_hi:[1,0,1]
	v_readlane_b32 s2, v211, 31
	v_cvt_scalef32_pk32_f32_fp6 v[0:31], v[32:37], 1.0
	v_pk_fma_f32 v[164:165], v[0:1], s[2:3], v[38:39] op_sel_hi:[1,0,1]
	v_pk_fma_f32 v[166:167], v[2:3], s[2:3], v[40:41] op_sel_hi:[1,0,1]
	v_pk_fma_f32 v[168:169], v[4:5], s[2:3], v[42:43] op_sel_hi:[1,0,1]
	v_pk_fma_f32 v[170:171], v[6:7], s[2:3], v[50:51] op_sel_hi:[1,0,1]
	v_pk_fma_f32 v[172:173], v[8:9], s[2:3], v[52:53] op_sel_hi:[1,0,1]
	v_pk_fma_f32 v[174:175], v[10:11], s[2:3], v[54:55] op_sel_hi:[1,0,1]
	v_pk_fma_f32 v[176:177], v[12:13], s[2:3], v[62:63] op_sel_hi:[1,0,1]
	v_pk_fma_f32 v[178:179], v[14:15], s[2:3], v[64:65] op_sel_hi:[1,0,1]
	v_pk_fma_f32 v[180:181], v[16:17], s[2:3], v[66:67] op_sel_hi:[1,0,1]
	v_pk_fma_f32 v[162:163], v[18:19], s[2:3], v[162:163] op_sel_hi:[1,0,1]
	v_pk_fma_f32 v[160:161], v[20:21], s[2:3], v[160:161] op_sel_hi:[1,0,1]
	v_pk_fma_f32 v[158:159], v[22:23], s[2:3], v[158:159] op_sel_hi:[1,0,1]
	v_pk_fma_f32 v[156:157], v[24:25], s[2:3], v[156:157] op_sel_hi:[1,0,1]
	v_pk_fma_f32 v[154:155], v[26:27], s[2:3], v[154:155] op_sel_hi:[1,0,1]
	v_pk_fma_f32 v[152:153], v[28:29], s[2:3], v[152:153] op_sel_hi:[1,0,1]
	v_pk_fma_f32 v[150:151], v[30:31], s[2:3], v[150:151] op_sel_hi:[1,0,1]
	v_readlane_b32 s2, v240, 40
	v_readlane_b32 s3, v240, 41
	v_readlane_b32 s100, v240, 42
	v_readlane_b32 s101, v240, 43
	s_nop 1
	buffer_load_dwordx4 v[62:65], v129, s[44:47], s2 offen
	buffer_load_dwordx2 v[66:67], v210, s[44:47], s2 offen
	buffer_load_dwordx4 v[50:53], v129, s[44:47], s3 offen
	buffer_load_dwordx2 v[54:55], v210, s[44:47], s3 offen
	buffer_load_dwordx4 v[38:41], v129, s[44:47], s100 offen
	buffer_load_dwordx2 v[42:43], v210, s[44:47], s100 offen
	buffer_load_dwordx4 v[32:35], v129, s[44:47], s101 offen
	buffer_load_dwordx2 v[36:37], v210, s[44:47], s101 offen
	s_waitcnt vmcnt(16)
	v_readlane_b32 s2, v211, 32
	s_nop 0
	v_cvt_scalef32_pk32_f32_fp6 v[0:31], v[98:103], 1.0
	v_pk_fma_f32 v[98:99], v[0:1], s[2:3], v[164:165] op_sel_hi:[1,0,1]
	v_pk_fma_f32 v[100:101], v[2:3], s[2:3], v[166:167] op_sel_hi:[1,0,1]
	v_pk_fma_f32 v[102:103], v[4:5], s[2:3], v[168:169] op_sel_hi:[1,0,1]
	v_pk_fma_f32 v[164:165], v[6:7], s[2:3], v[170:171] op_sel_hi:[1,0,1]
	v_pk_fma_f32 v[166:167], v[8:9], s[2:3], v[172:173] op_sel_hi:[1,0,1]
	v_pk_fma_f32 v[168:169], v[10:11], s[2:3], v[174:175] op_sel_hi:[1,0,1]
	v_pk_fma_f32 v[170:171], v[12:13], s[2:3], v[176:177] op_sel_hi:[1,0,1]
	v_pk_fma_f32 v[172:173], v[14:15], s[2:3], v[178:179] op_sel_hi:[1,0,1]
	v_pk_fma_f32 v[174:175], v[16:17], s[2:3], v[180:181] op_sel_hi:[1,0,1]
	v_pk_fma_f32 v[162:163], v[18:19], s[2:3], v[162:163] op_sel_hi:[1,0,1]
	v_pk_fma_f32 v[160:161], v[20:21], s[2:3], v[160:161] op_sel_hi:[1,0,1]
	v_pk_fma_f32 v[158:159], v[22:23], s[2:3], v[158:159] op_sel_hi:[1,0,1]
	v_pk_fma_f32 v[156:157], v[24:25], s[2:3], v[156:157] op_sel_hi:[1,0,1]
	v_pk_fma_f32 v[154:155], v[26:27], s[2:3], v[154:155] op_sel_hi:[1,0,1]
	v_pk_fma_f32 v[152:153], v[28:29], s[2:3], v[152:153] op_sel_hi:[1,0,1]
	v_pk_fma_f32 v[150:151], v[30:31], s[2:3], v[150:151] op_sel_hi:[1,0,1]
	v_readlane_b32 s2, v211, 33
	v_cvt_scalef32_pk32_f32_fp6 v[0:31], v[92:97], 1.0
	v_pk_fma_f32 v[92:93], v[0:1], s[2:3], v[98:99] op_sel_hi:[1,0,1]
	v_pk_fma_f32 v[94:95], v[2:3], s[2:3], v[100:101] op_sel_hi:[1,0,1]
	v_pk_fma_f32 v[96:97], v[4:5], s[2:3], v[102:103] op_sel_hi:[1,0,1]
	v_pk_fma_f32 v[98:99], v[6:7], s[2:3], v[164:165] op_sel_hi:[1,0,1]
	v_pk_fma_f32 v[100:101], v[8:9], s[2:3], v[166:167] op_sel_hi:[1,0,1]
	v_pk_fma_f32 v[102:103], v[10:11], s[2:3], v[168:169] op_sel_hi:[1,0,1]
	v_pk_fma_f32 v[164:165], v[12:13], s[2:3], v[170:171] op_sel_hi:[1,0,1]
	v_pk_fma_f32 v[166:167], v[14:15], s[2:3], v[172:173] op_sel_hi:[1,0,1]
	v_pk_fma_f32 v[168:169], v[16:17], s[2:3], v[174:175] op_sel_hi:[1,0,1]
	v_pk_fma_f32 v[162:163], v[18:19], s[2:3], v[162:163] op_sel_hi:[1,0,1]
	v_pk_fma_f32 v[160:161], v[20:21], s[2:3], v[160:161] op_sel_hi:[1,0,1]
	v_pk_fma_f32 v[158:159], v[22:23], s[2:3], v[158:159] op_sel_hi:[1,0,1]
	v_pk_fma_f32 v[156:157], v[24:25], s[2:3], v[156:157] op_sel_hi:[1,0,1]
	v_pk_fma_f32 v[154:155], v[26:27], s[2:3], v[154:155] op_sel_hi:[1,0,1]
	v_pk_fma_f32 v[152:153], v[28:29], s[2:3], v[152:153] op_sel_hi:[1,0,1]
	v_pk_fma_f32 v[150:151], v[30:31], s[2:3], v[150:151] op_sel_hi:[1,0,1]
	v_readlane_b32 s2, v211, 34
	v_cvt_scalef32_pk32_f32_fp6 v[0:31], v[86:91], 1.0
	v_pk_fma_f32 v[86:87], v[0:1], s[2:3], v[92:93] op_sel_hi:[1,0,1]
	v_pk_fma_f32 v[88:89], v[2:3], s[2:3], v[94:95] op_sel_hi:[1,0,1]
	v_pk_fma_f32 v[90:91], v[4:5], s[2:3], v[96:97] op_sel_hi:[1,0,1]
	v_pk_fma_f32 v[92:93], v[6:7], s[2:3], v[98:99] op_sel_hi:[1,0,1]
	v_pk_fma_f32 v[94:95], v[8:9], s[2:3], v[100:101] op_sel_hi:[1,0,1]
	v_pk_fma_f32 v[96:97], v[10:11], s[2:3], v[102:103] op_sel_hi:[1,0,1]
	v_pk_fma_f32 v[98:99], v[12:13], s[2:3], v[164:165] op_sel_hi:[1,0,1]
	v_pk_fma_f32 v[100:101], v[14:15], s[2:3], v[166:167] op_sel_hi:[1,0,1]
	v_pk_fma_f32 v[102:103], v[16:17], s[2:3], v[168:169] op_sel_hi:[1,0,1]
	v_pk_fma_f32 v[162:163], v[18:19], s[2:3], v[162:163] op_sel_hi:[1,0,1]
	v_pk_fma_f32 v[160:161], v[20:21], s[2:3], v[160:161] op_sel_hi:[1,0,1]
	v_pk_fma_f32 v[158:159], v[22:23], s[2:3], v[158:159] op_sel_hi:[1,0,1]
	v_pk_fma_f32 v[156:157], v[24:25], s[2:3], v[156:157] op_sel_hi:[1,0,1]
	v_pk_fma_f32 v[154:155], v[26:27], s[2:3], v[154:155] op_sel_hi:[1,0,1]
	v_pk_fma_f32 v[152:153], v[28:29], s[2:3], v[152:153] op_sel_hi:[1,0,1]
	v_pk_fma_f32 v[150:151], v[30:31], s[2:3], v[150:151] op_sel_hi:[1,0,1]
	v_readlane_b32 s2, v211, 35
	v_cvt_scalef32_pk32_f32_fp6 v[0:31], v[80:85], 1.0
	v_pk_fma_f32 v[180:181], v[0:1], s[2:3], v[86:87] op_sel_hi:[1,0,1]
	v_pk_fma_f32 v[178:179], v[2:3], s[2:3], v[88:89] op_sel_hi:[1,0,1]
	v_pk_fma_f32 v[176:177], v[4:5], s[2:3], v[90:91] op_sel_hi:[1,0,1]
	v_pk_fma_f32 v[174:175], v[6:7], s[2:3], v[92:93] op_sel_hi:[1,0,1]
	v_pk_fma_f32 v[172:173], v[8:9], s[2:3], v[94:95] op_sel_hi:[1,0,1]
	v_pk_fma_f32 v[170:171], v[10:11], s[2:3], v[96:97] op_sel_hi:[1,0,1]
	v_pk_fma_f32 v[168:169], v[12:13], s[2:3], v[98:99] op_sel_hi:[1,0,1]
	v_pk_fma_f32 v[166:167], v[14:15], s[2:3], v[100:101] op_sel_hi:[1,0,1]
	v_pk_fma_f32 v[164:165], v[16:17], s[2:3], v[102:103] op_sel_hi:[1,0,1]
	v_pk_fma_f32 v[162:163], v[18:19], s[2:3], v[162:163] op_sel_hi:[1,0,1]
	v_pk_fma_f32 v[160:161], v[20:21], s[2:3], v[160:161] op_sel_hi:[1,0,1]
	v_pk_fma_f32 v[158:159], v[22:23], s[2:3], v[158:159] op_sel_hi:[1,0,1]
	v_pk_fma_f32 v[156:157], v[24:25], s[2:3], v[156:157] op_sel_hi:[1,0,1]
	v_pk_fma_f32 v[154:155], v[26:27], s[2:3], v[154:155] op_sel_hi:[1,0,1]
	v_pk_fma_f32 v[152:153], v[28:29], s[2:3], v[152:153] op_sel_hi:[1,0,1]
	v_pk_fma_f32 v[150:151], v[30:31], s[2:3], v[150:151] op_sel_hi:[1,0,1]
	v_readlane_b32 s2, v240, 44
	v_readlane_b32 s3, v240, 45
	v_readlane_b32 s100, v240, 46
	v_readlane_b32 s101, v240, 47
	s_nop 1
	buffer_load_dwordx4 v[98:101], v129, s[44:47], s2 offen
	buffer_load_dwordx2 v[102:103], v210, s[44:47], s2 offen
	buffer_load_dwordx4 v[92:95], v129, s[44:47], s3 offen
	buffer_load_dwordx2 v[96:97], v210, s[44:47], s3 offen
	buffer_load_dwordx4 v[86:89], v129, s[44:47], s100 offen
	buffer_load_dwordx2 v[90:91], v210, s[44:47], s100 offen
	buffer_load_dwordx4 v[80:83], v129, s[44:47], s101 offen
	buffer_load_dwordx2 v[84:85], v210, s[44:47], s101 offen
	s_waitcnt vmcnt(16)
	v_readlane_b32 s2, v211, 36
	s_nop 0
	v_cvt_scalef32_pk32_f32_fp6 v[0:31], v[74:79], 1.0
	v_pk_fma_f32 v[74:75], v[0:1], s[2:3], v[180:181] op_sel_hi:[1,0,1]
	v_pk_fma_f32 v[76:77], v[2:3], s[2:3], v[178:179] op_sel_hi:[1,0,1]
	v_pk_fma_f32 v[78:79], v[4:5], s[2:3], v[176:177] op_sel_hi:[1,0,1]
	v_pk_fma_f32 v[174:175], v[6:7], s[2:3], v[174:175] op_sel_hi:[1,0,1]
	v_pk_fma_f32 v[172:173], v[8:9], s[2:3], v[172:173] op_sel_hi:[1,0,1]
	v_pk_fma_f32 v[170:171], v[10:11], s[2:3], v[170:171] op_sel_hi:[1,0,1]
	v_pk_fma_f32 v[168:169], v[12:13], s[2:3], v[168:169] op_sel_hi:[1,0,1]
	v_pk_fma_f32 v[166:167], v[14:15], s[2:3], v[166:167] op_sel_hi:[1,0,1]
	v_pk_fma_f32 v[164:165], v[16:17], s[2:3], v[164:165] op_sel_hi:[1,0,1]
	v_pk_fma_f32 v[162:163], v[18:19], s[2:3], v[162:163] op_sel_hi:[1,0,1]
	v_pk_fma_f32 v[160:161], v[20:21], s[2:3], v[160:161] op_sel_hi:[1,0,1]
	v_pk_fma_f32 v[158:159], v[22:23], s[2:3], v[158:159] op_sel_hi:[1,0,1]
	v_pk_fma_f32 v[156:157], v[24:25], s[2:3], v[156:157] op_sel_hi:[1,0,1]
	v_pk_fma_f32 v[154:155], v[26:27], s[2:3], v[154:155] op_sel_hi:[1,0,1]
	v_pk_fma_f32 v[152:153], v[28:29], s[2:3], v[152:153] op_sel_hi:[1,0,1]
	v_pk_fma_f32 v[150:151], v[30:31], s[2:3], v[150:151] op_sel_hi:[1,0,1]
	v_readlane_b32 s2, v211, 37
	v_cvt_scalef32_pk32_f32_fp6 v[0:31], v[68:73], 1.0
	v_pk_fma_f32 v[68:69], v[0:1], s[2:3], v[74:75] op_sel_hi:[1,0,1]
	v_pk_fma_f32 v[70:71], v[2:3], s[2:3], v[76:77] op_sel_hi:[1,0,1]
	v_pk_fma_f32 v[72:73], v[4:5], s[2:3], v[78:79] op_sel_hi:[1,0,1]
	v_pk_fma_f32 v[74:75], v[6:7], s[2:3], v[174:175] op_sel_hi:[1,0,1]
	v_pk_fma_f32 v[76:77], v[8:9], s[2:3], v[172:173] op_sel_hi:[1,0,1]
	v_pk_fma_f32 v[78:79], v[10:11], s[2:3], v[170:171] op_sel_hi:[1,0,1]
	v_pk_fma_f32 v[168:169], v[12:13], s[2:3], v[168:169] op_sel_hi:[1,0,1]
	v_pk_fma_f32 v[166:167], v[14:15], s[2:3], v[166:167] op_sel_hi:[1,0,1]
	v_pk_fma_f32 v[164:165], v[16:17], s[2:3], v[164:165] op_sel_hi:[1,0,1]
	v_pk_fma_f32 v[162:163], v[18:19], s[2:3], v[162:163] op_sel_hi:[1,0,1]
	v_pk_fma_f32 v[160:161], v[20:21], s[2:3], v[160:161] op_sel_hi:[1,0,1]
	v_pk_fma_f32 v[158:159], v[22:23], s[2:3], v[158:159] op_sel_hi:[1,0,1]
	v_pk_fma_f32 v[156:157], v[24:25], s[2:3], v[156:157] op_sel_hi:[1,0,1]
	v_pk_fma_f32 v[154:155], v[26:27], s[2:3], v[154:155] op_sel_hi:[1,0,1]
	v_pk_fma_f32 v[152:153], v[28:29], s[2:3], v[152:153] op_sel_hi:[1,0,1]
	v_pk_fma_f32 v[150:151], v[30:31], s[2:3], v[150:151] op_sel_hi:[1,0,1]
	v_readlane_b32 s2, v211, 38
	v_cvt_scalef32_pk32_f32_fp6 v[0:31], v[56:61], 1.0
	v_pk_fma_f32 v[56:57], v[0:1], s[2:3], v[68:69] op_sel_hi:[1,0,1]
	v_pk_fma_f32 v[58:59], v[2:3], s[2:3], v[70:71] op_sel_hi:[1,0,1]
	v_pk_fma_f32 v[60:61], v[4:5], s[2:3], v[72:73] op_sel_hi:[1,0,1]
	v_pk_fma_f32 v[68:69], v[6:7], s[2:3], v[74:75] op_sel_hi:[1,0,1]
	v_pk_fma_f32 v[70:71], v[8:9], s[2:3], v[76:77] op_sel_hi:[1,0,1]
	v_pk_fma_f32 v[72:73], v[10:11], s[2:3], v[78:79] op_sel_hi:[1,0,1]
	v_pk_fma_f32 v[74:75], v[12:13], s[2:3], v[168:169] op_sel_hi:[1,0,1]
	v_pk_fma_f32 v[76:77], v[14:15], s[2:3], v[166:167] op_sel_hi:[1,0,1]
	v_pk_fma_f32 v[78:79], v[16:17], s[2:3], v[164:165] op_sel_hi:[1,0,1]
	v_pk_fma_f32 v[162:163], v[18:19], s[2:3], v[162:163] op_sel_hi:[1,0,1]
	v_pk_fma_f32 v[160:161], v[20:21], s[2:3], v[160:161] op_sel_hi:[1,0,1]
	v_pk_fma_f32 v[158:159], v[22:23], s[2:3], v[158:159] op_sel_hi:[1,0,1]
	v_pk_fma_f32 v[156:157], v[24:25], s[2:3], v[156:157] op_sel_hi:[1,0,1]
	v_pk_fma_f32 v[154:155], v[26:27], s[2:3], v[154:155] op_sel_hi:[1,0,1]
	v_pk_fma_f32 v[152:153], v[28:29], s[2:3], v[152:153] op_sel_hi:[1,0,1]
	v_pk_fma_f32 v[150:151], v[30:31], s[2:3], v[150:151] op_sel_hi:[1,0,1]
	v_readlane_b32 s2, v211, 39
	v_cvt_scalef32_pk32_f32_fp6 v[0:31], v[44:49], 1.0
	v_pk_fma_f32 v[164:165], v[0:1], s[2:3], v[56:57] op_sel_hi:[1,0,1]
	v_pk_fma_f32 v[166:167], v[2:3], s[2:3], v[58:59] op_sel_hi:[1,0,1]
	v_pk_fma_f32 v[168:169], v[4:5], s[2:3], v[60:61] op_sel_hi:[1,0,1]
	v_pk_fma_f32 v[170:171], v[6:7], s[2:3], v[68:69] op_sel_hi:[1,0,1]
	v_pk_fma_f32 v[172:173], v[8:9], s[2:3], v[70:71] op_sel_hi:[1,0,1]
	v_pk_fma_f32 v[174:175], v[10:11], s[2:3], v[72:73] op_sel_hi:[1,0,1]
	v_pk_fma_f32 v[176:177], v[12:13], s[2:3], v[74:75] op_sel_hi:[1,0,1]
	v_pk_fma_f32 v[178:179], v[14:15], s[2:3], v[76:77] op_sel_hi:[1,0,1]
	v_pk_fma_f32 v[180:181], v[16:17], s[2:3], v[78:79] op_sel_hi:[1,0,1]
	v_pk_fma_f32 v[162:163], v[18:19], s[2:3], v[162:163] op_sel_hi:[1,0,1]
	v_pk_fma_f32 v[160:161], v[20:21], s[2:3], v[160:161] op_sel_hi:[1,0,1]
	v_pk_fma_f32 v[158:159], v[22:23], s[2:3], v[158:159] op_sel_hi:[1,0,1]
	v_pk_fma_f32 v[156:157], v[24:25], s[2:3], v[156:157] op_sel_hi:[1,0,1]
	v_pk_fma_f32 v[154:155], v[26:27], s[2:3], v[154:155] op_sel_hi:[1,0,1]
	v_pk_fma_f32 v[152:153], v[28:29], s[2:3], v[152:153] op_sel_hi:[1,0,1]
	v_pk_fma_f32 v[150:151], v[30:31], s[2:3], v[150:151] op_sel_hi:[1,0,1]
	v_readlane_b32 s2, v240, 48
	v_readlane_b32 s3, v240, 49
	v_readlane_b32 s100, v240, 50
	v_readlane_b32 s101, v240, 51
	s_nop 1
	buffer_load_dwordx4 v[74:77], v129, s[44:47], s2 offen
	buffer_load_dwordx2 v[78:79], v210, s[44:47], s2 offen
	buffer_load_dwordx4 v[68:71], v129, s[44:47], s3 offen
	buffer_load_dwordx2 v[72:73], v210, s[44:47], s3 offen
	buffer_load_dwordx4 v[56:59], v129, s[44:47], s100 offen
	buffer_load_dwordx2 v[60:61], v210, s[44:47], s100 offen
	buffer_load_dwordx4 v[44:47], v129, s[44:47], s101 offen
	buffer_load_dwordx2 v[48:49], v210, s[44:47], s101 offen
	s_waitcnt vmcnt(16)
	v_readlane_b32 s2, v211, 40
	s_nop 0
	v_cvt_scalef32_pk32_f32_fp6 v[0:31], v[62:67], 1.0
	v_pk_fma_f32 v[62:63], v[0:1], s[2:3], v[164:165] op_sel_hi:[1,0,1]
	v_pk_fma_f32 v[64:65], v[2:3], s[2:3], v[166:167] op_sel_hi:[1,0,1]
	v_pk_fma_f32 v[66:67], v[4:5], s[2:3], v[168:169] op_sel_hi:[1,0,1]
	v_pk_fma_f32 v[164:165], v[6:7], s[2:3], v[170:171] op_sel_hi:[1,0,1]
	v_pk_fma_f32 v[166:167], v[8:9], s[2:3], v[172:173] op_sel_hi:[1,0,1]
	v_pk_fma_f32 v[168:169], v[10:11], s[2:3], v[174:175] op_sel_hi:[1,0,1]
	v_pk_fma_f32 v[170:171], v[12:13], s[2:3], v[176:177] op_sel_hi:[1,0,1]
	v_pk_fma_f32 v[172:173], v[14:15], s[2:3], v[178:179] op_sel_hi:[1,0,1]
	v_pk_fma_f32 v[174:175], v[16:17], s[2:3], v[180:181] op_sel_hi:[1,0,1]
	v_pk_fma_f32 v[162:163], v[18:19], s[2:3], v[162:163] op_sel_hi:[1,0,1]
	v_pk_fma_f32 v[160:161], v[20:21], s[2:3], v[160:161] op_sel_hi:[1,0,1]
	v_pk_fma_f32 v[158:159], v[22:23], s[2:3], v[158:159] op_sel_hi:[1,0,1]
	v_pk_fma_f32 v[156:157], v[24:25], s[2:3], v[156:157] op_sel_hi:[1,0,1]
	v_pk_fma_f32 v[154:155], v[26:27], s[2:3], v[154:155] op_sel_hi:[1,0,1]
	v_pk_fma_f32 v[152:153], v[28:29], s[2:3], v[152:153] op_sel_hi:[1,0,1]
	v_pk_fma_f32 v[150:151], v[30:31], s[2:3], v[150:151] op_sel_hi:[1,0,1]
	v_readlane_b32 s2, v211, 41
	v_cvt_scalef32_pk32_f32_fp6 v[0:31], v[50:55], 1.0
	v_pk_fma_f32 v[50:51], v[0:1], s[2:3], v[62:63] op_sel_hi:[1,0,1]
	v_pk_fma_f32 v[52:53], v[2:3], s[2:3], v[64:65] op_sel_hi:[1,0,1]
	v_pk_fma_f32 v[54:55], v[4:5], s[2:3], v[66:67] op_sel_hi:[1,0,1]
	v_pk_fma_f32 v[62:63], v[6:7], s[2:3], v[164:165] op_sel_hi:[1,0,1]
	v_pk_fma_f32 v[64:65], v[8:9], s[2:3], v[166:167] op_sel_hi:[1,0,1]
	v_pk_fma_f32 v[66:67], v[10:11], s[2:3], v[168:169] op_sel_hi:[1,0,1]
	v_pk_fma_f32 v[164:165], v[12:13], s[2:3], v[170:171] op_sel_hi:[1,0,1]
	v_pk_fma_f32 v[166:167], v[14:15], s[2:3], v[172:173] op_sel_hi:[1,0,1]
	v_pk_fma_f32 v[168:169], v[16:17], s[2:3], v[174:175] op_sel_hi:[1,0,1]
	v_pk_fma_f32 v[162:163], v[18:19], s[2:3], v[162:163] op_sel_hi:[1,0,1]
	v_pk_fma_f32 v[160:161], v[20:21], s[2:3], v[160:161] op_sel_hi:[1,0,1]
	v_pk_fma_f32 v[158:159], v[22:23], s[2:3], v[158:159] op_sel_hi:[1,0,1]
	v_pk_fma_f32 v[156:157], v[24:25], s[2:3], v[156:157] op_sel_hi:[1,0,1]
	v_pk_fma_f32 v[154:155], v[26:27], s[2:3], v[154:155] op_sel_hi:[1,0,1]
	v_pk_fma_f32 v[152:153], v[28:29], s[2:3], v[152:153] op_sel_hi:[1,0,1]
	v_pk_fma_f32 v[150:151], v[30:31], s[2:3], v[150:151] op_sel_hi:[1,0,1]
	v_readlane_b32 s2, v211, 42
	v_cvt_scalef32_pk32_f32_fp6 v[0:31], v[38:43], 1.0
	v_pk_fma_f32 v[38:39], v[0:1], s[2:3], v[50:51] op_sel_hi:[1,0,1]
	v_pk_fma_f32 v[40:41], v[2:3], s[2:3], v[52:53] op_sel_hi:[1,0,1]
	v_pk_fma_f32 v[42:43], v[4:5], s[2:3], v[54:55] op_sel_hi:[1,0,1]
	v_pk_fma_f32 v[50:51], v[6:7], s[2:3], v[62:63] op_sel_hi:[1,0,1]
	v_pk_fma_f32 v[52:53], v[8:9], s[2:3], v[64:65] op_sel_hi:[1,0,1]
	v_pk_fma_f32 v[54:55], v[10:11], s[2:3], v[66:67] op_sel_hi:[1,0,1]
	v_pk_fma_f32 v[62:63], v[12:13], s[2:3], v[164:165] op_sel_hi:[1,0,1]
	v_pk_fma_f32 v[64:65], v[14:15], s[2:3], v[166:167] op_sel_hi:[1,0,1]
	v_pk_fma_f32 v[66:67], v[16:17], s[2:3], v[168:169] op_sel_hi:[1,0,1]
	v_pk_fma_f32 v[162:163], v[18:19], s[2:3], v[162:163] op_sel_hi:[1,0,1]
	v_pk_fma_f32 v[160:161], v[20:21], s[2:3], v[160:161] op_sel_hi:[1,0,1]
	v_pk_fma_f32 v[158:159], v[22:23], s[2:3], v[158:159] op_sel_hi:[1,0,1]
	v_pk_fma_f32 v[156:157], v[24:25], s[2:3], v[156:157] op_sel_hi:[1,0,1]
	v_pk_fma_f32 v[154:155], v[26:27], s[2:3], v[154:155] op_sel_hi:[1,0,1]
	v_pk_fma_f32 v[152:153], v[28:29], s[2:3], v[152:153] op_sel_hi:[1,0,1]
	v_pk_fma_f32 v[150:151], v[30:31], s[2:3], v[150:151] op_sel_hi:[1,0,1]
	v_readlane_b32 s2, v211, 43
	v_cvt_scalef32_pk32_f32_fp6 v[0:31], v[32:37], 1.0
	v_pk_fma_f32 v[164:165], v[0:1], s[2:3], v[38:39] op_sel_hi:[1,0,1]
	v_pk_fma_f32 v[166:167], v[2:3], s[2:3], v[40:41] op_sel_hi:[1,0,1]
	v_pk_fma_f32 v[168:169], v[4:5], s[2:3], v[42:43] op_sel_hi:[1,0,1]
	v_pk_fma_f32 v[170:171], v[6:7], s[2:3], v[50:51] op_sel_hi:[1,0,1]
	v_pk_fma_f32 v[172:173], v[8:9], s[2:3], v[52:53] op_sel_hi:[1,0,1]
	v_pk_fma_f32 v[174:175], v[10:11], s[2:3], v[54:55] op_sel_hi:[1,0,1]
	v_pk_fma_f32 v[176:177], v[12:13], s[2:3], v[62:63] op_sel_hi:[1,0,1]
	v_pk_fma_f32 v[178:179], v[14:15], s[2:3], v[64:65] op_sel_hi:[1,0,1]
	v_pk_fma_f32 v[180:181], v[16:17], s[2:3], v[66:67] op_sel_hi:[1,0,1]
	v_pk_fma_f32 v[162:163], v[18:19], s[2:3], v[162:163] op_sel_hi:[1,0,1]
	v_pk_fma_f32 v[160:161], v[20:21], s[2:3], v[160:161] op_sel_hi:[1,0,1]
	v_pk_fma_f32 v[158:159], v[22:23], s[2:3], v[158:159] op_sel_hi:[1,0,1]
	v_pk_fma_f32 v[156:157], v[24:25], s[2:3], v[156:157] op_sel_hi:[1,0,1]
	v_pk_fma_f32 v[154:155], v[26:27], s[2:3], v[154:155] op_sel_hi:[1,0,1]
	v_pk_fma_f32 v[152:153], v[28:29], s[2:3], v[152:153] op_sel_hi:[1,0,1]
	v_pk_fma_f32 v[150:151], v[30:31], s[2:3], v[150:151] op_sel_hi:[1,0,1]
	v_readlane_b32 s2, v240, 52
	v_readlane_b32 s3, v240, 53
	v_readlane_b32 s100, v240, 54
	v_readlane_b32 s101, v240, 55
	s_nop 1
	buffer_load_dwordx4 v[62:65], v129, s[44:47], s2 offen
	buffer_load_dwordx2 v[66:67], v210, s[44:47], s2 offen
	buffer_load_dwordx4 v[50:53], v129, s[44:47], s3 offen
	buffer_load_dwordx2 v[54:55], v210, s[44:47], s3 offen
	buffer_load_dwordx4 v[38:41], v129, s[44:47], s100 offen
	buffer_load_dwordx2 v[42:43], v210, s[44:47], s100 offen
	buffer_load_dwordx4 v[32:35], v129, s[44:47], s101 offen
	buffer_load_dwordx2 v[36:37], v210, s[44:47], s101 offen
	s_waitcnt vmcnt(16)
	v_readlane_b32 s2, v211, 44
	s_nop 0
	v_cvt_scalef32_pk32_f32_fp6 v[0:31], v[98:103], 1.0
	v_pk_fma_f32 v[98:99], v[0:1], s[2:3], v[164:165] op_sel_hi:[1,0,1]
	v_pk_fma_f32 v[100:101], v[2:3], s[2:3], v[166:167] op_sel_hi:[1,0,1]
	v_pk_fma_f32 v[102:103], v[4:5], s[2:3], v[168:169] op_sel_hi:[1,0,1]
	v_pk_fma_f32 v[164:165], v[6:7], s[2:3], v[170:171] op_sel_hi:[1,0,1]
	v_pk_fma_f32 v[166:167], v[8:9], s[2:3], v[172:173] op_sel_hi:[1,0,1]
	v_pk_fma_f32 v[168:169], v[10:11], s[2:3], v[174:175] op_sel_hi:[1,0,1]
	v_pk_fma_f32 v[170:171], v[12:13], s[2:3], v[176:177] op_sel_hi:[1,0,1]
	v_pk_fma_f32 v[172:173], v[14:15], s[2:3], v[178:179] op_sel_hi:[1,0,1]
	v_pk_fma_f32 v[174:175], v[16:17], s[2:3], v[180:181] op_sel_hi:[1,0,1]
	v_pk_fma_f32 v[162:163], v[18:19], s[2:3], v[162:163] op_sel_hi:[1,0,1]
	v_pk_fma_f32 v[160:161], v[20:21], s[2:3], v[160:161] op_sel_hi:[1,0,1]
	v_pk_fma_f32 v[158:159], v[22:23], s[2:3], v[158:159] op_sel_hi:[1,0,1]
	v_pk_fma_f32 v[156:157], v[24:25], s[2:3], v[156:157] op_sel_hi:[1,0,1]
	v_pk_fma_f32 v[154:155], v[26:27], s[2:3], v[154:155] op_sel_hi:[1,0,1]
	v_pk_fma_f32 v[152:153], v[28:29], s[2:3], v[152:153] op_sel_hi:[1,0,1]
	v_pk_fma_f32 v[150:151], v[30:31], s[2:3], v[150:151] op_sel_hi:[1,0,1]
	v_readlane_b32 s2, v211, 45
	v_cvt_scalef32_pk32_f32_fp6 v[0:31], v[92:97], 1.0
	v_pk_fma_f32 v[92:93], v[0:1], s[2:3], v[98:99] op_sel_hi:[1,0,1]
	v_pk_fma_f32 v[94:95], v[2:3], s[2:3], v[100:101] op_sel_hi:[1,0,1]
	v_pk_fma_f32 v[96:97], v[4:5], s[2:3], v[102:103] op_sel_hi:[1,0,1]
	v_pk_fma_f32 v[98:99], v[6:7], s[2:3], v[164:165] op_sel_hi:[1,0,1]
	v_pk_fma_f32 v[100:101], v[8:9], s[2:3], v[166:167] op_sel_hi:[1,0,1]
	v_pk_fma_f32 v[102:103], v[10:11], s[2:3], v[168:169] op_sel_hi:[1,0,1]
	v_pk_fma_f32 v[164:165], v[12:13], s[2:3], v[170:171] op_sel_hi:[1,0,1]
	v_pk_fma_f32 v[166:167], v[14:15], s[2:3], v[172:173] op_sel_hi:[1,0,1]
	v_pk_fma_f32 v[168:169], v[16:17], s[2:3], v[174:175] op_sel_hi:[1,0,1]
	v_pk_fma_f32 v[162:163], v[18:19], s[2:3], v[162:163] op_sel_hi:[1,0,1]
	v_pk_fma_f32 v[160:161], v[20:21], s[2:3], v[160:161] op_sel_hi:[1,0,1]
	v_pk_fma_f32 v[158:159], v[22:23], s[2:3], v[158:159] op_sel_hi:[1,0,1]
	v_pk_fma_f32 v[156:157], v[24:25], s[2:3], v[156:157] op_sel_hi:[1,0,1]
	v_pk_fma_f32 v[154:155], v[26:27], s[2:3], v[154:155] op_sel_hi:[1,0,1]
	v_pk_fma_f32 v[152:153], v[28:29], s[2:3], v[152:153] op_sel_hi:[1,0,1]
	v_pk_fma_f32 v[150:151], v[30:31], s[2:3], v[150:151] op_sel_hi:[1,0,1]
	v_readlane_b32 s2, v211, 46
	v_cvt_scalef32_pk32_f32_fp6 v[0:31], v[86:91], 1.0
	v_pk_fma_f32 v[86:87], v[0:1], s[2:3], v[92:93] op_sel_hi:[1,0,1]
	v_pk_fma_f32 v[88:89], v[2:3], s[2:3], v[94:95] op_sel_hi:[1,0,1]
	v_pk_fma_f32 v[90:91], v[4:5], s[2:3], v[96:97] op_sel_hi:[1,0,1]
	v_pk_fma_f32 v[92:93], v[6:7], s[2:3], v[98:99] op_sel_hi:[1,0,1]
	v_pk_fma_f32 v[94:95], v[8:9], s[2:3], v[100:101] op_sel_hi:[1,0,1]
	v_pk_fma_f32 v[96:97], v[10:11], s[2:3], v[102:103] op_sel_hi:[1,0,1]
	v_pk_fma_f32 v[98:99], v[12:13], s[2:3], v[164:165] op_sel_hi:[1,0,1]
	v_pk_fma_f32 v[100:101], v[14:15], s[2:3], v[166:167] op_sel_hi:[1,0,1]
	v_pk_fma_f32 v[102:103], v[16:17], s[2:3], v[168:169] op_sel_hi:[1,0,1]
	v_pk_fma_f32 v[162:163], v[18:19], s[2:3], v[162:163] op_sel_hi:[1,0,1]
	v_pk_fma_f32 v[160:161], v[20:21], s[2:3], v[160:161] op_sel_hi:[1,0,1]
	v_pk_fma_f32 v[158:159], v[22:23], s[2:3], v[158:159] op_sel_hi:[1,0,1]
	v_pk_fma_f32 v[156:157], v[24:25], s[2:3], v[156:157] op_sel_hi:[1,0,1]
	v_pk_fma_f32 v[154:155], v[26:27], s[2:3], v[154:155] op_sel_hi:[1,0,1]
	v_pk_fma_f32 v[152:153], v[28:29], s[2:3], v[152:153] op_sel_hi:[1,0,1]
	v_pk_fma_f32 v[150:151], v[30:31], s[2:3], v[150:151] op_sel_hi:[1,0,1]
	v_readlane_b32 s2, v211, 47
	v_cvt_scalef32_pk32_f32_fp6 v[0:31], v[80:85], 1.0
	v_pk_fma_f32 v[180:181], v[0:1], s[2:3], v[86:87] op_sel_hi:[1,0,1]
	v_pk_fma_f32 v[178:179], v[2:3], s[2:3], v[88:89] op_sel_hi:[1,0,1]
	v_pk_fma_f32 v[176:177], v[4:5], s[2:3], v[90:91] op_sel_hi:[1,0,1]
	v_pk_fma_f32 v[174:175], v[6:7], s[2:3], v[92:93] op_sel_hi:[1,0,1]
	v_pk_fma_f32 v[172:173], v[8:9], s[2:3], v[94:95] op_sel_hi:[1,0,1]
	v_pk_fma_f32 v[170:171], v[10:11], s[2:3], v[96:97] op_sel_hi:[1,0,1]
	v_pk_fma_f32 v[168:169], v[12:13], s[2:3], v[98:99] op_sel_hi:[1,0,1]
	v_pk_fma_f32 v[166:167], v[14:15], s[2:3], v[100:101] op_sel_hi:[1,0,1]
	v_pk_fma_f32 v[164:165], v[16:17], s[2:3], v[102:103] op_sel_hi:[1,0,1]
	v_pk_fma_f32 v[162:163], v[18:19], s[2:3], v[162:163] op_sel_hi:[1,0,1]
	v_pk_fma_f32 v[160:161], v[20:21], s[2:3], v[160:161] op_sel_hi:[1,0,1]
	v_pk_fma_f32 v[158:159], v[22:23], s[2:3], v[158:159] op_sel_hi:[1,0,1]
	v_pk_fma_f32 v[156:157], v[24:25], s[2:3], v[156:157] op_sel_hi:[1,0,1]
	v_pk_fma_f32 v[154:155], v[26:27], s[2:3], v[154:155] op_sel_hi:[1,0,1]
	v_pk_fma_f32 v[152:153], v[28:29], s[2:3], v[152:153] op_sel_hi:[1,0,1]
	v_pk_fma_f32 v[150:151], v[30:31], s[2:3], v[150:151] op_sel_hi:[1,0,1]
	v_readlane_b32 s2, v240, 56
	v_readlane_b32 s3, v240, 57
	v_readlane_b32 s100, v240, 58
	v_readlane_b32 s101, v240, 59
	s_nop 1
	buffer_load_dwordx4 v[98:101], v129, s[44:47], s2 offen
	buffer_load_dwordx2 v[102:103], v210, s[44:47], s2 offen
	buffer_load_dwordx4 v[92:95], v129, s[44:47], s3 offen
	buffer_load_dwordx2 v[96:97], v210, s[44:47], s3 offen
	buffer_load_dwordx4 v[86:89], v129, s[44:47], s100 offen
	buffer_load_dwordx2 v[90:91], v210, s[44:47], s100 offen
	buffer_load_dwordx4 v[80:83], v129, s[44:47], s101 offen
	buffer_load_dwordx2 v[84:85], v210, s[44:47], s101 offen
	s_waitcnt vmcnt(16)
	v_readlane_b32 s2, v211, 48
	s_nop 0
	v_cvt_scalef32_pk32_f32_fp6 v[0:31], v[74:79], 1.0
	v_pk_fma_f32 v[74:75], v[0:1], s[2:3], v[180:181] op_sel_hi:[1,0,1]
	v_pk_fma_f32 v[76:77], v[2:3], s[2:3], v[178:179] op_sel_hi:[1,0,1]
	v_pk_fma_f32 v[78:79], v[4:5], s[2:3], v[176:177] op_sel_hi:[1,0,1]
	v_pk_fma_f32 v[174:175], v[6:7], s[2:3], v[174:175] op_sel_hi:[1,0,1]
	v_pk_fma_f32 v[172:173], v[8:9], s[2:3], v[172:173] op_sel_hi:[1,0,1]
	v_pk_fma_f32 v[170:171], v[10:11], s[2:3], v[170:171] op_sel_hi:[1,0,1]
	v_pk_fma_f32 v[168:169], v[12:13], s[2:3], v[168:169] op_sel_hi:[1,0,1]
	v_pk_fma_f32 v[166:167], v[14:15], s[2:3], v[166:167] op_sel_hi:[1,0,1]
	v_pk_fma_f32 v[164:165], v[16:17], s[2:3], v[164:165] op_sel_hi:[1,0,1]
	v_pk_fma_f32 v[162:163], v[18:19], s[2:3], v[162:163] op_sel_hi:[1,0,1]
	v_pk_fma_f32 v[160:161], v[20:21], s[2:3], v[160:161] op_sel_hi:[1,0,1]
	v_pk_fma_f32 v[158:159], v[22:23], s[2:3], v[158:159] op_sel_hi:[1,0,1]
	v_pk_fma_f32 v[156:157], v[24:25], s[2:3], v[156:157] op_sel_hi:[1,0,1]
	v_pk_fma_f32 v[154:155], v[26:27], s[2:3], v[154:155] op_sel_hi:[1,0,1]
	v_pk_fma_f32 v[152:153], v[28:29], s[2:3], v[152:153] op_sel_hi:[1,0,1]
	v_pk_fma_f32 v[150:151], v[30:31], s[2:3], v[150:151] op_sel_hi:[1,0,1]
	v_readlane_b32 s2, v211, 49
	v_cvt_scalef32_pk32_f32_fp6 v[0:31], v[68:73], 1.0
	v_pk_fma_f32 v[68:69], v[0:1], s[2:3], v[74:75] op_sel_hi:[1,0,1]
	v_pk_fma_f32 v[70:71], v[2:3], s[2:3], v[76:77] op_sel_hi:[1,0,1]
	v_pk_fma_f32 v[72:73], v[4:5], s[2:3], v[78:79] op_sel_hi:[1,0,1]
	v_pk_fma_f32 v[74:75], v[6:7], s[2:3], v[174:175] op_sel_hi:[1,0,1]
	v_pk_fma_f32 v[76:77], v[8:9], s[2:3], v[172:173] op_sel_hi:[1,0,1]
	v_pk_fma_f32 v[78:79], v[10:11], s[2:3], v[170:171] op_sel_hi:[1,0,1]
	v_pk_fma_f32 v[168:169], v[12:13], s[2:3], v[168:169] op_sel_hi:[1,0,1]
	v_pk_fma_f32 v[166:167], v[14:15], s[2:3], v[166:167] op_sel_hi:[1,0,1]
	v_pk_fma_f32 v[164:165], v[16:17], s[2:3], v[164:165] op_sel_hi:[1,0,1]
	v_pk_fma_f32 v[162:163], v[18:19], s[2:3], v[162:163] op_sel_hi:[1,0,1]
	v_pk_fma_f32 v[160:161], v[20:21], s[2:3], v[160:161] op_sel_hi:[1,0,1]
	v_pk_fma_f32 v[158:159], v[22:23], s[2:3], v[158:159] op_sel_hi:[1,0,1]
	v_pk_fma_f32 v[156:157], v[24:25], s[2:3], v[156:157] op_sel_hi:[1,0,1]
	v_pk_fma_f32 v[154:155], v[26:27], s[2:3], v[154:155] op_sel_hi:[1,0,1]
	v_pk_fma_f32 v[152:153], v[28:29], s[2:3], v[152:153] op_sel_hi:[1,0,1]
	v_pk_fma_f32 v[150:151], v[30:31], s[2:3], v[150:151] op_sel_hi:[1,0,1]
	v_readlane_b32 s2, v211, 50
	v_cvt_scalef32_pk32_f32_fp6 v[0:31], v[56:61], 1.0
	v_pk_fma_f32 v[56:57], v[0:1], s[2:3], v[68:69] op_sel_hi:[1,0,1]
	v_pk_fma_f32 v[58:59], v[2:3], s[2:3], v[70:71] op_sel_hi:[1,0,1]
	v_pk_fma_f32 v[60:61], v[4:5], s[2:3], v[72:73] op_sel_hi:[1,0,1]
	v_pk_fma_f32 v[68:69], v[6:7], s[2:3], v[74:75] op_sel_hi:[1,0,1]
	v_pk_fma_f32 v[70:71], v[8:9], s[2:3], v[76:77] op_sel_hi:[1,0,1]
	v_pk_fma_f32 v[72:73], v[10:11], s[2:3], v[78:79] op_sel_hi:[1,0,1]
	v_pk_fma_f32 v[74:75], v[12:13], s[2:3], v[168:169] op_sel_hi:[1,0,1]
	v_pk_fma_f32 v[76:77], v[14:15], s[2:3], v[166:167] op_sel_hi:[1,0,1]
	v_pk_fma_f32 v[78:79], v[16:17], s[2:3], v[164:165] op_sel_hi:[1,0,1]
	v_pk_fma_f32 v[162:163], v[18:19], s[2:3], v[162:163] op_sel_hi:[1,0,1]
	v_pk_fma_f32 v[160:161], v[20:21], s[2:3], v[160:161] op_sel_hi:[1,0,1]
	v_pk_fma_f32 v[158:159], v[22:23], s[2:3], v[158:159] op_sel_hi:[1,0,1]
	v_pk_fma_f32 v[156:157], v[24:25], s[2:3], v[156:157] op_sel_hi:[1,0,1]
	v_pk_fma_f32 v[154:155], v[26:27], s[2:3], v[154:155] op_sel_hi:[1,0,1]
	v_pk_fma_f32 v[152:153], v[28:29], s[2:3], v[152:153] op_sel_hi:[1,0,1]
	v_pk_fma_f32 v[150:151], v[30:31], s[2:3], v[150:151] op_sel_hi:[1,0,1]
	v_readlane_b32 s2, v211, 51
	v_cvt_scalef32_pk32_f32_fp6 v[0:31], v[44:49], 1.0
	v_pk_fma_f32 v[164:165], v[0:1], s[2:3], v[56:57] op_sel_hi:[1,0,1]
	v_pk_fma_f32 v[166:167], v[2:3], s[2:3], v[58:59] op_sel_hi:[1,0,1]
	v_pk_fma_f32 v[168:169], v[4:5], s[2:3], v[60:61] op_sel_hi:[1,0,1]
	v_pk_fma_f32 v[170:171], v[6:7], s[2:3], v[68:69] op_sel_hi:[1,0,1]
	v_pk_fma_f32 v[172:173], v[8:9], s[2:3], v[70:71] op_sel_hi:[1,0,1]
	v_pk_fma_f32 v[174:175], v[10:11], s[2:3], v[72:73] op_sel_hi:[1,0,1]
	v_pk_fma_f32 v[176:177], v[12:13], s[2:3], v[74:75] op_sel_hi:[1,0,1]
	v_pk_fma_f32 v[178:179], v[14:15], s[2:3], v[76:77] op_sel_hi:[1,0,1]
	v_pk_fma_f32 v[180:181], v[16:17], s[2:3], v[78:79] op_sel_hi:[1,0,1]
	v_pk_fma_f32 v[162:163], v[18:19], s[2:3], v[162:163] op_sel_hi:[1,0,1]
	v_pk_fma_f32 v[160:161], v[20:21], s[2:3], v[160:161] op_sel_hi:[1,0,1]
	v_pk_fma_f32 v[158:159], v[22:23], s[2:3], v[158:159] op_sel_hi:[1,0,1]
	v_pk_fma_f32 v[156:157], v[24:25], s[2:3], v[156:157] op_sel_hi:[1,0,1]
	v_pk_fma_f32 v[154:155], v[26:27], s[2:3], v[154:155] op_sel_hi:[1,0,1]
	v_pk_fma_f32 v[152:153], v[28:29], s[2:3], v[152:153] op_sel_hi:[1,0,1]
	v_pk_fma_f32 v[150:151], v[30:31], s[2:3], v[150:151] op_sel_hi:[1,0,1]
	v_readlane_b32 s2, v240, 60
	v_readlane_b32 s3, v240, 61
	v_readlane_b32 s100, v240, 62
	v_readlane_b32 s101, v240, 63
	s_nop 1
	buffer_load_dwordx4 v[74:77], v129, s[44:47], s2 offen
	buffer_load_dwordx2 v[78:79], v210, s[44:47], s2 offen
	buffer_load_dwordx4 v[68:71], v129, s[44:47], s3 offen
	buffer_load_dwordx2 v[72:73], v210, s[44:47], s3 offen
	buffer_load_dwordx4 v[56:59], v129, s[44:47], s100 offen
	buffer_load_dwordx2 v[60:61], v210, s[44:47], s100 offen
	buffer_load_dwordx4 v[44:47], v129, s[44:47], s101 offen
	buffer_load_dwordx2 v[48:49], v210, s[44:47], s101 offen
	s_waitcnt vmcnt(16)
	v_readlane_b32 s2, v211, 52
	s_nop 0
	v_cvt_scalef32_pk32_f32_fp6 v[0:31], v[62:67], 1.0
	v_pk_fma_f32 v[62:63], v[0:1], s[2:3], v[164:165] op_sel_hi:[1,0,1]
	v_pk_fma_f32 v[64:65], v[2:3], s[2:3], v[166:167] op_sel_hi:[1,0,1]
	v_pk_fma_f32 v[66:67], v[4:5], s[2:3], v[168:169] op_sel_hi:[1,0,1]
	v_pk_fma_f32 v[164:165], v[6:7], s[2:3], v[170:171] op_sel_hi:[1,0,1]
	v_pk_fma_f32 v[166:167], v[8:9], s[2:3], v[172:173] op_sel_hi:[1,0,1]
	v_pk_fma_f32 v[168:169], v[10:11], s[2:3], v[174:175] op_sel_hi:[1,0,1]
	v_pk_fma_f32 v[170:171], v[12:13], s[2:3], v[176:177] op_sel_hi:[1,0,1]
	v_pk_fma_f32 v[172:173], v[14:15], s[2:3], v[178:179] op_sel_hi:[1,0,1]
	v_pk_fma_f32 v[174:175], v[16:17], s[2:3], v[180:181] op_sel_hi:[1,0,1]
	v_pk_fma_f32 v[162:163], v[18:19], s[2:3], v[162:163] op_sel_hi:[1,0,1]
	v_pk_fma_f32 v[160:161], v[20:21], s[2:3], v[160:161] op_sel_hi:[1,0,1]
	v_pk_fma_f32 v[158:159], v[22:23], s[2:3], v[158:159] op_sel_hi:[1,0,1]
	v_pk_fma_f32 v[156:157], v[24:25], s[2:3], v[156:157] op_sel_hi:[1,0,1]
	v_pk_fma_f32 v[154:155], v[26:27], s[2:3], v[154:155] op_sel_hi:[1,0,1]
	v_pk_fma_f32 v[152:153], v[28:29], s[2:3], v[152:153] op_sel_hi:[1,0,1]
	v_pk_fma_f32 v[150:151], v[30:31], s[2:3], v[150:151] op_sel_hi:[1,0,1]
	v_readlane_b32 s2, v211, 53
	v_cvt_scalef32_pk32_f32_fp6 v[0:31], v[50:55], 1.0
	v_pk_fma_f32 v[50:51], v[0:1], s[2:3], v[62:63] op_sel_hi:[1,0,1]
	v_pk_fma_f32 v[52:53], v[2:3], s[2:3], v[64:65] op_sel_hi:[1,0,1]
	v_pk_fma_f32 v[54:55], v[4:5], s[2:3], v[66:67] op_sel_hi:[1,0,1]
	v_pk_fma_f32 v[62:63], v[6:7], s[2:3], v[164:165] op_sel_hi:[1,0,1]
	v_pk_fma_f32 v[64:65], v[8:9], s[2:3], v[166:167] op_sel_hi:[1,0,1]
	v_pk_fma_f32 v[66:67], v[10:11], s[2:3], v[168:169] op_sel_hi:[1,0,1]
	v_pk_fma_f32 v[164:165], v[12:13], s[2:3], v[170:171] op_sel_hi:[1,0,1]
	v_pk_fma_f32 v[166:167], v[14:15], s[2:3], v[172:173] op_sel_hi:[1,0,1]
	v_pk_fma_f32 v[168:169], v[16:17], s[2:3], v[174:175] op_sel_hi:[1,0,1]
	v_pk_fma_f32 v[162:163], v[18:19], s[2:3], v[162:163] op_sel_hi:[1,0,1]
	v_pk_fma_f32 v[160:161], v[20:21], s[2:3], v[160:161] op_sel_hi:[1,0,1]
	v_pk_fma_f32 v[158:159], v[22:23], s[2:3], v[158:159] op_sel_hi:[1,0,1]
	v_pk_fma_f32 v[156:157], v[24:25], s[2:3], v[156:157] op_sel_hi:[1,0,1]
	v_pk_fma_f32 v[154:155], v[26:27], s[2:3], v[154:155] op_sel_hi:[1,0,1]
	v_pk_fma_f32 v[152:153], v[28:29], s[2:3], v[152:153] op_sel_hi:[1,0,1]
	v_pk_fma_f32 v[150:151], v[30:31], s[2:3], v[150:151] op_sel_hi:[1,0,1]
	v_readlane_b32 s2, v211, 54
	v_cvt_scalef32_pk32_f32_fp6 v[0:31], v[38:43], 1.0
	v_pk_fma_f32 v[38:39], v[0:1], s[2:3], v[50:51] op_sel_hi:[1,0,1]
	v_pk_fma_f32 v[40:41], v[2:3], s[2:3], v[52:53] op_sel_hi:[1,0,1]
	v_pk_fma_f32 v[42:43], v[4:5], s[2:3], v[54:55] op_sel_hi:[1,0,1]
	v_pk_fma_f32 v[50:51], v[6:7], s[2:3], v[62:63] op_sel_hi:[1,0,1]
	v_pk_fma_f32 v[52:53], v[8:9], s[2:3], v[64:65] op_sel_hi:[1,0,1]
	v_pk_fma_f32 v[54:55], v[10:11], s[2:3], v[66:67] op_sel_hi:[1,0,1]
	v_pk_fma_f32 v[62:63], v[12:13], s[2:3], v[164:165] op_sel_hi:[1,0,1]
	v_pk_fma_f32 v[64:65], v[14:15], s[2:3], v[166:167] op_sel_hi:[1,0,1]
	v_pk_fma_f32 v[66:67], v[16:17], s[2:3], v[168:169] op_sel_hi:[1,0,1]
	v_pk_fma_f32 v[162:163], v[18:19], s[2:3], v[162:163] op_sel_hi:[1,0,1]
	v_pk_fma_f32 v[160:161], v[20:21], s[2:3], v[160:161] op_sel_hi:[1,0,1]
	v_pk_fma_f32 v[158:159], v[22:23], s[2:3], v[158:159] op_sel_hi:[1,0,1]
	v_pk_fma_f32 v[156:157], v[24:25], s[2:3], v[156:157] op_sel_hi:[1,0,1]
	v_pk_fma_f32 v[154:155], v[26:27], s[2:3], v[154:155] op_sel_hi:[1,0,1]
	v_pk_fma_f32 v[152:153], v[28:29], s[2:3], v[152:153] op_sel_hi:[1,0,1]
	v_pk_fma_f32 v[150:151], v[30:31], s[2:3], v[150:151] op_sel_hi:[1,0,1]
	v_readlane_b32 s2, v211, 55
	v_cvt_scalef32_pk32_f32_fp6 v[0:31], v[32:37], 1.0
	v_pk_fma_f32 v[164:165], v[0:1], s[2:3], v[38:39] op_sel_hi:[1,0,1]
	v_pk_fma_f32 v[166:167], v[2:3], s[2:3], v[40:41] op_sel_hi:[1,0,1]
	v_pk_fma_f32 v[168:169], v[4:5], s[2:3], v[42:43] op_sel_hi:[1,0,1]
	v_pk_fma_f32 v[170:171], v[6:7], s[2:3], v[50:51] op_sel_hi:[1,0,1]
	v_pk_fma_f32 v[172:173], v[8:9], s[2:3], v[52:53] op_sel_hi:[1,0,1]
	v_pk_fma_f32 v[174:175], v[10:11], s[2:3], v[54:55] op_sel_hi:[1,0,1]
	v_pk_fma_f32 v[176:177], v[12:13], s[2:3], v[62:63] op_sel_hi:[1,0,1]
	v_pk_fma_f32 v[178:179], v[14:15], s[2:3], v[64:65] op_sel_hi:[1,0,1]
	v_pk_fma_f32 v[180:181], v[16:17], s[2:3], v[66:67] op_sel_hi:[1,0,1]
	v_pk_fma_f32 v[162:163], v[18:19], s[2:3], v[162:163] op_sel_hi:[1,0,1]
	v_pk_fma_f32 v[160:161], v[20:21], s[2:3], v[160:161] op_sel_hi:[1,0,1]
	v_pk_fma_f32 v[158:159], v[22:23], s[2:3], v[158:159] op_sel_hi:[1,0,1]
	v_pk_fma_f32 v[156:157], v[24:25], s[2:3], v[156:157] op_sel_hi:[1,0,1]
	v_pk_fma_f32 v[154:155], v[26:27], s[2:3], v[154:155] op_sel_hi:[1,0,1]
	v_pk_fma_f32 v[152:153], v[28:29], s[2:3], v[152:153] op_sel_hi:[1,0,1]
	v_pk_fma_f32 v[150:151], v[30:31], s[2:3], v[150:151] op_sel_hi:[1,0,1]
	v_readlane_b32 s2, v241, 0
	v_readlane_b32 s3, v241, 1
	v_readlane_b32 s100, v241, 2
	v_readlane_b32 s101, v241, 3
	s_nop 1
	buffer_load_dwordx4 v[62:65], v129, s[44:47], s2 offen
	buffer_load_dwordx2 v[66:67], v210, s[44:47], s2 offen
	buffer_load_dwordx4 v[50:53], v129, s[44:47], s3 offen
	buffer_load_dwordx2 v[54:55], v210, s[44:47], s3 offen
	buffer_load_dwordx4 v[38:41], v129, s[44:47], s100 offen
	buffer_load_dwordx2 v[42:43], v210, s[44:47], s100 offen
	buffer_load_dwordx4 v[32:35], v129, s[44:47], s101 offen
	buffer_load_dwordx2 v[36:37], v210, s[44:47], s101 offen
	s_waitcnt vmcnt(16)
	v_readlane_b32 s2, v211, 56
	s_nop 0
	v_cvt_scalef32_pk32_f32_fp6 v[0:31], v[98:103], 1.0
	v_pk_fma_f32 v[98:99], v[0:1], s[2:3], v[164:165] op_sel_hi:[1,0,1]
	v_pk_fma_f32 v[100:101], v[2:3], s[2:3], v[166:167] op_sel_hi:[1,0,1]
	v_pk_fma_f32 v[102:103], v[4:5], s[2:3], v[168:169] op_sel_hi:[1,0,1]
	v_pk_fma_f32 v[164:165], v[6:7], s[2:3], v[170:171] op_sel_hi:[1,0,1]
	v_pk_fma_f32 v[166:167], v[8:9], s[2:3], v[172:173] op_sel_hi:[1,0,1]
	v_pk_fma_f32 v[168:169], v[10:11], s[2:3], v[174:175] op_sel_hi:[1,0,1]
	v_pk_fma_f32 v[170:171], v[12:13], s[2:3], v[176:177] op_sel_hi:[1,0,1]
	v_pk_fma_f32 v[172:173], v[14:15], s[2:3], v[178:179] op_sel_hi:[1,0,1]
	v_pk_fma_f32 v[174:175], v[16:17], s[2:3], v[180:181] op_sel_hi:[1,0,1]
	v_pk_fma_f32 v[162:163], v[18:19], s[2:3], v[162:163] op_sel_hi:[1,0,1]
	v_pk_fma_f32 v[160:161], v[20:21], s[2:3], v[160:161] op_sel_hi:[1,0,1]
	v_pk_fma_f32 v[158:159], v[22:23], s[2:3], v[158:159] op_sel_hi:[1,0,1]
	v_pk_fma_f32 v[156:157], v[24:25], s[2:3], v[156:157] op_sel_hi:[1,0,1]
	v_pk_fma_f32 v[154:155], v[26:27], s[2:3], v[154:155] op_sel_hi:[1,0,1]
	v_pk_fma_f32 v[152:153], v[28:29], s[2:3], v[152:153] op_sel_hi:[1,0,1]
	v_pk_fma_f32 v[150:151], v[30:31], s[2:3], v[150:151] op_sel_hi:[1,0,1]
	v_readlane_b32 s2, v211, 57
	v_cvt_scalef32_pk32_f32_fp6 v[0:31], v[92:97], 1.0
	v_pk_fma_f32 v[92:93], v[0:1], s[2:3], v[98:99] op_sel_hi:[1,0,1]
	v_pk_fma_f32 v[94:95], v[2:3], s[2:3], v[100:101] op_sel_hi:[1,0,1]
	v_pk_fma_f32 v[96:97], v[4:5], s[2:3], v[102:103] op_sel_hi:[1,0,1]
	v_pk_fma_f32 v[98:99], v[6:7], s[2:3], v[164:165] op_sel_hi:[1,0,1]
	v_pk_fma_f32 v[100:101], v[8:9], s[2:3], v[166:167] op_sel_hi:[1,0,1]
	v_pk_fma_f32 v[102:103], v[10:11], s[2:3], v[168:169] op_sel_hi:[1,0,1]
	v_pk_fma_f32 v[164:165], v[12:13], s[2:3], v[170:171] op_sel_hi:[1,0,1]
	v_pk_fma_f32 v[166:167], v[14:15], s[2:3], v[172:173] op_sel_hi:[1,0,1]
	v_pk_fma_f32 v[168:169], v[16:17], s[2:3], v[174:175] op_sel_hi:[1,0,1]
	v_pk_fma_f32 v[162:163], v[18:19], s[2:3], v[162:163] op_sel_hi:[1,0,1]
	v_pk_fma_f32 v[160:161], v[20:21], s[2:3], v[160:161] op_sel_hi:[1,0,1]
	v_pk_fma_f32 v[158:159], v[22:23], s[2:3], v[158:159] op_sel_hi:[1,0,1]
	v_pk_fma_f32 v[156:157], v[24:25], s[2:3], v[156:157] op_sel_hi:[1,0,1]
	v_pk_fma_f32 v[154:155], v[26:27], s[2:3], v[154:155] op_sel_hi:[1,0,1]
	v_pk_fma_f32 v[152:153], v[28:29], s[2:3], v[152:153] op_sel_hi:[1,0,1]
	v_pk_fma_f32 v[150:151], v[30:31], s[2:3], v[150:151] op_sel_hi:[1,0,1]
	v_readlane_b32 s2, v211, 58
	v_cvt_scalef32_pk32_f32_fp6 v[0:31], v[86:91], 1.0
	v_pk_fma_f32 v[86:87], v[0:1], s[2:3], v[92:93] op_sel_hi:[1,0,1]
	v_pk_fma_f32 v[88:89], v[2:3], s[2:3], v[94:95] op_sel_hi:[1,0,1]
	v_pk_fma_f32 v[90:91], v[4:5], s[2:3], v[96:97] op_sel_hi:[1,0,1]
	v_pk_fma_f32 v[92:93], v[6:7], s[2:3], v[98:99] op_sel_hi:[1,0,1]
	v_pk_fma_f32 v[94:95], v[8:9], s[2:3], v[100:101] op_sel_hi:[1,0,1]
	v_pk_fma_f32 v[96:97], v[10:11], s[2:3], v[102:103] op_sel_hi:[1,0,1]
	v_pk_fma_f32 v[98:99], v[12:13], s[2:3], v[164:165] op_sel_hi:[1,0,1]
	v_pk_fma_f32 v[100:101], v[14:15], s[2:3], v[166:167] op_sel_hi:[1,0,1]
	v_pk_fma_f32 v[102:103], v[16:17], s[2:3], v[168:169] op_sel_hi:[1,0,1]
	v_pk_fma_f32 v[162:163], v[18:19], s[2:3], v[162:163] op_sel_hi:[1,0,1]
	v_pk_fma_f32 v[160:161], v[20:21], s[2:3], v[160:161] op_sel_hi:[1,0,1]
	v_pk_fma_f32 v[158:159], v[22:23], s[2:3], v[158:159] op_sel_hi:[1,0,1]
	v_pk_fma_f32 v[156:157], v[24:25], s[2:3], v[156:157] op_sel_hi:[1,0,1]
	v_pk_fma_f32 v[154:155], v[26:27], s[2:3], v[154:155] op_sel_hi:[1,0,1]
	v_pk_fma_f32 v[152:153], v[28:29], s[2:3], v[152:153] op_sel_hi:[1,0,1]
	v_pk_fma_f32 v[150:151], v[30:31], s[2:3], v[150:151] op_sel_hi:[1,0,1]
	v_readlane_b32 s2, v211, 59
	v_cvt_scalef32_pk32_f32_fp6 v[0:31], v[80:85], 1.0
	v_pk_fma_f32 v[180:181], v[0:1], s[2:3], v[86:87] op_sel_hi:[1,0,1]
	v_pk_fma_f32 v[178:179], v[2:3], s[2:3], v[88:89] op_sel_hi:[1,0,1]
	v_pk_fma_f32 v[176:177], v[4:5], s[2:3], v[90:91] op_sel_hi:[1,0,1]
	v_pk_fma_f32 v[174:175], v[6:7], s[2:3], v[92:93] op_sel_hi:[1,0,1]
	v_pk_fma_f32 v[172:173], v[8:9], s[2:3], v[94:95] op_sel_hi:[1,0,1]
	v_pk_fma_f32 v[170:171], v[10:11], s[2:3], v[96:97] op_sel_hi:[1,0,1]
	v_pk_fma_f32 v[168:169], v[12:13], s[2:3], v[98:99] op_sel_hi:[1,0,1]
	v_pk_fma_f32 v[166:167], v[14:15], s[2:3], v[100:101] op_sel_hi:[1,0,1]
	v_pk_fma_f32 v[164:165], v[16:17], s[2:3], v[102:103] op_sel_hi:[1,0,1]
	v_pk_fma_f32 v[162:163], v[18:19], s[2:3], v[162:163] op_sel_hi:[1,0,1]
	v_pk_fma_f32 v[160:161], v[20:21], s[2:3], v[160:161] op_sel_hi:[1,0,1]
	v_pk_fma_f32 v[158:159], v[22:23], s[2:3], v[158:159] op_sel_hi:[1,0,1]
	v_pk_fma_f32 v[156:157], v[24:25], s[2:3], v[156:157] op_sel_hi:[1,0,1]
	v_pk_fma_f32 v[154:155], v[26:27], s[2:3], v[154:155] op_sel_hi:[1,0,1]
	v_pk_fma_f32 v[152:153], v[28:29], s[2:3], v[152:153] op_sel_hi:[1,0,1]
	v_pk_fma_f32 v[150:151], v[30:31], s[2:3], v[150:151] op_sel_hi:[1,0,1]
	v_readlane_b32 s2, v241, 4
	v_readlane_b32 s3, v241, 5
	v_readlane_b32 s100, v241, 6
	v_readlane_b32 s101, v241, 7
	s_nop 1
	buffer_load_dwordx4 v[98:101], v129, s[44:47], s2 offen
	buffer_load_dwordx2 v[102:103], v210, s[44:47], s2 offen
	buffer_load_dwordx4 v[92:95], v129, s[44:47], s3 offen
	buffer_load_dwordx2 v[96:97], v210, s[44:47], s3 offen
	buffer_load_dwordx4 v[86:89], v129, s[44:47], s100 offen
	buffer_load_dwordx2 v[90:91], v210, s[44:47], s100 offen
	buffer_load_dwordx4 v[80:83], v129, s[44:47], s101 offen
	buffer_load_dwordx2 v[84:85], v210, s[44:47], s101 offen
	s_waitcnt vmcnt(16)
	v_readlane_b32 s2, v211, 60
	s_nop 0
	v_cvt_scalef32_pk32_f32_fp6 v[0:31], v[74:79], 1.0
	v_pk_fma_f32 v[74:75], v[0:1], s[2:3], v[180:181] op_sel_hi:[1,0,1]
	v_pk_fma_f32 v[76:77], v[2:3], s[2:3], v[178:179] op_sel_hi:[1,0,1]
	v_pk_fma_f32 v[78:79], v[4:5], s[2:3], v[176:177] op_sel_hi:[1,0,1]
	v_pk_fma_f32 v[174:175], v[6:7], s[2:3], v[174:175] op_sel_hi:[1,0,1]
	v_pk_fma_f32 v[172:173], v[8:9], s[2:3], v[172:173] op_sel_hi:[1,0,1]
	v_pk_fma_f32 v[170:171], v[10:11], s[2:3], v[170:171] op_sel_hi:[1,0,1]
	v_pk_fma_f32 v[168:169], v[12:13], s[2:3], v[168:169] op_sel_hi:[1,0,1]
	v_pk_fma_f32 v[166:167], v[14:15], s[2:3], v[166:167] op_sel_hi:[1,0,1]
	v_pk_fma_f32 v[164:165], v[16:17], s[2:3], v[164:165] op_sel_hi:[1,0,1]
	v_pk_fma_f32 v[162:163], v[18:19], s[2:3], v[162:163] op_sel_hi:[1,0,1]
	v_pk_fma_f32 v[160:161], v[20:21], s[2:3], v[160:161] op_sel_hi:[1,0,1]
	v_pk_fma_f32 v[158:159], v[22:23], s[2:3], v[158:159] op_sel_hi:[1,0,1]
	v_pk_fma_f32 v[156:157], v[24:25], s[2:3], v[156:157] op_sel_hi:[1,0,1]
	v_pk_fma_f32 v[154:155], v[26:27], s[2:3], v[154:155] op_sel_hi:[1,0,1]
	v_pk_fma_f32 v[152:153], v[28:29], s[2:3], v[152:153] op_sel_hi:[1,0,1]
	v_pk_fma_f32 v[150:151], v[30:31], s[2:3], v[150:151] op_sel_hi:[1,0,1]
	v_readlane_b32 s2, v211, 61
	v_cvt_scalef32_pk32_f32_fp6 v[0:31], v[68:73], 1.0
	v_pk_fma_f32 v[68:69], v[0:1], s[2:3], v[74:75] op_sel_hi:[1,0,1]
	v_pk_fma_f32 v[70:71], v[2:3], s[2:3], v[76:77] op_sel_hi:[1,0,1]
	v_pk_fma_f32 v[72:73], v[4:5], s[2:3], v[78:79] op_sel_hi:[1,0,1]
	v_pk_fma_f32 v[74:75], v[6:7], s[2:3], v[174:175] op_sel_hi:[1,0,1]
	v_pk_fma_f32 v[76:77], v[8:9], s[2:3], v[172:173] op_sel_hi:[1,0,1]
	v_pk_fma_f32 v[78:79], v[10:11], s[2:3], v[170:171] op_sel_hi:[1,0,1]
	v_pk_fma_f32 v[168:169], v[12:13], s[2:3], v[168:169] op_sel_hi:[1,0,1]
	v_pk_fma_f32 v[166:167], v[14:15], s[2:3], v[166:167] op_sel_hi:[1,0,1]
	v_pk_fma_f32 v[164:165], v[16:17], s[2:3], v[164:165] op_sel_hi:[1,0,1]
	v_pk_fma_f32 v[162:163], v[18:19], s[2:3], v[162:163] op_sel_hi:[1,0,1]
	v_pk_fma_f32 v[160:161], v[20:21], s[2:3], v[160:161] op_sel_hi:[1,0,1]
	v_pk_fma_f32 v[158:159], v[22:23], s[2:3], v[158:159] op_sel_hi:[1,0,1]
	v_pk_fma_f32 v[156:157], v[24:25], s[2:3], v[156:157] op_sel_hi:[1,0,1]
	v_pk_fma_f32 v[154:155], v[26:27], s[2:3], v[154:155] op_sel_hi:[1,0,1]
	v_pk_fma_f32 v[152:153], v[28:29], s[2:3], v[152:153] op_sel_hi:[1,0,1]
	v_pk_fma_f32 v[150:151], v[30:31], s[2:3], v[150:151] op_sel_hi:[1,0,1]
	v_readlane_b32 s2, v211, 62
	v_cvt_scalef32_pk32_f32_fp6 v[0:31], v[56:61], 1.0
	v_pk_fma_f32 v[56:57], v[0:1], s[2:3], v[68:69] op_sel_hi:[1,0,1]
	v_pk_fma_f32 v[58:59], v[2:3], s[2:3], v[70:71] op_sel_hi:[1,0,1]
	v_pk_fma_f32 v[60:61], v[4:5], s[2:3], v[72:73] op_sel_hi:[1,0,1]
	v_pk_fma_f32 v[68:69], v[6:7], s[2:3], v[74:75] op_sel_hi:[1,0,1]
	v_pk_fma_f32 v[70:71], v[8:9], s[2:3], v[76:77] op_sel_hi:[1,0,1]
	v_pk_fma_f32 v[72:73], v[10:11], s[2:3], v[78:79] op_sel_hi:[1,0,1]
	v_pk_fma_f32 v[74:75], v[12:13], s[2:3], v[168:169] op_sel_hi:[1,0,1]
	v_pk_fma_f32 v[76:77], v[14:15], s[2:3], v[166:167] op_sel_hi:[1,0,1]
	v_pk_fma_f32 v[78:79], v[16:17], s[2:3], v[164:165] op_sel_hi:[1,0,1]
	v_pk_fma_f32 v[162:163], v[18:19], s[2:3], v[162:163] op_sel_hi:[1,0,1]
	v_pk_fma_f32 v[160:161], v[20:21], s[2:3], v[160:161] op_sel_hi:[1,0,1]
	v_pk_fma_f32 v[158:159], v[22:23], s[2:3], v[158:159] op_sel_hi:[1,0,1]
	v_pk_fma_f32 v[156:157], v[24:25], s[2:3], v[156:157] op_sel_hi:[1,0,1]
	v_pk_fma_f32 v[154:155], v[26:27], s[2:3], v[154:155] op_sel_hi:[1,0,1]
	v_pk_fma_f32 v[152:153], v[28:29], s[2:3], v[152:153] op_sel_hi:[1,0,1]
	v_pk_fma_f32 v[150:151], v[30:31], s[2:3], v[150:151] op_sel_hi:[1,0,1]
	v_readlane_b32 s2, v211, 63
	v_cvt_scalef32_pk32_f32_fp6 v[0:31], v[44:49], 1.0
	v_pk_fma_f32 v[164:165], v[0:1], s[2:3], v[56:57] op_sel_hi:[1,0,1]
	v_pk_fma_f32 v[166:167], v[2:3], s[2:3], v[58:59] op_sel_hi:[1,0,1]
	v_pk_fma_f32 v[168:169], v[4:5], s[2:3], v[60:61] op_sel_hi:[1,0,1]
	v_pk_fma_f32 v[170:171], v[6:7], s[2:3], v[68:69] op_sel_hi:[1,0,1]
	v_pk_fma_f32 v[172:173], v[8:9], s[2:3], v[70:71] op_sel_hi:[1,0,1]
	v_pk_fma_f32 v[174:175], v[10:11], s[2:3], v[72:73] op_sel_hi:[1,0,1]
	v_pk_fma_f32 v[176:177], v[12:13], s[2:3], v[74:75] op_sel_hi:[1,0,1]
	v_pk_fma_f32 v[178:179], v[14:15], s[2:3], v[76:77] op_sel_hi:[1,0,1]
	v_pk_fma_f32 v[180:181], v[16:17], s[2:3], v[78:79] op_sel_hi:[1,0,1]
	v_pk_fma_f32 v[162:163], v[18:19], s[2:3], v[162:163] op_sel_hi:[1,0,1]
	v_pk_fma_f32 v[160:161], v[20:21], s[2:3], v[160:161] op_sel_hi:[1,0,1]
	v_pk_fma_f32 v[158:159], v[22:23], s[2:3], v[158:159] op_sel_hi:[1,0,1]
	v_pk_fma_f32 v[156:157], v[24:25], s[2:3], v[156:157] op_sel_hi:[1,0,1]
	v_pk_fma_f32 v[154:155], v[26:27], s[2:3], v[154:155] op_sel_hi:[1,0,1]
	v_pk_fma_f32 v[152:153], v[28:29], s[2:3], v[152:153] op_sel_hi:[1,0,1]
	v_pk_fma_f32 v[150:151], v[30:31], s[2:3], v[150:151] op_sel_hi:[1,0,1]
	v_readlane_b32 s2, v241, 8
	v_readlane_b32 s3, v241, 9
	v_readlane_b32 s100, v241, 10
	v_readlane_b32 s101, v241, 11
	s_nop 1
	buffer_load_dwordx4 v[74:77], v129, s[44:47], s2 offen
	buffer_load_dwordx2 v[78:79], v210, s[44:47], s2 offen
	buffer_load_dwordx4 v[68:71], v129, s[44:47], s3 offen
	buffer_load_dwordx2 v[72:73], v210, s[44:47], s3 offen
	buffer_load_dwordx4 v[56:59], v129, s[44:47], s100 offen
	buffer_load_dwordx2 v[60:61], v210, s[44:47], s100 offen
	buffer_load_dwordx4 v[44:47], v129, s[44:47], s101 offen
	buffer_load_dwordx2 v[48:49], v210, s[44:47], s101 offen
	s_waitcnt vmcnt(16)
	v_readlane_b32 s2, v131, 0
	s_nop 0
	v_cvt_scalef32_pk32_f32_fp6 v[0:31], v[62:67], 1.0
	v_pk_fma_f32 v[62:63], v[0:1], s[2:3], v[164:165] op_sel_hi:[1,0,1]
	v_pk_fma_f32 v[64:65], v[2:3], s[2:3], v[166:167] op_sel_hi:[1,0,1]
	v_pk_fma_f32 v[66:67], v[4:5], s[2:3], v[168:169] op_sel_hi:[1,0,1]
	v_pk_fma_f32 v[164:165], v[6:7], s[2:3], v[170:171] op_sel_hi:[1,0,1]
	v_pk_fma_f32 v[166:167], v[8:9], s[2:3], v[172:173] op_sel_hi:[1,0,1]
	v_pk_fma_f32 v[168:169], v[10:11], s[2:3], v[174:175] op_sel_hi:[1,0,1]
	v_pk_fma_f32 v[170:171], v[12:13], s[2:3], v[176:177] op_sel_hi:[1,0,1]
	v_pk_fma_f32 v[172:173], v[14:15], s[2:3], v[178:179] op_sel_hi:[1,0,1]
	v_pk_fma_f32 v[174:175], v[16:17], s[2:3], v[180:181] op_sel_hi:[1,0,1]
	v_pk_fma_f32 v[162:163], v[18:19], s[2:3], v[162:163] op_sel_hi:[1,0,1]
	v_pk_fma_f32 v[160:161], v[20:21], s[2:3], v[160:161] op_sel_hi:[1,0,1]
	v_pk_fma_f32 v[158:159], v[22:23], s[2:3], v[158:159] op_sel_hi:[1,0,1]
	v_pk_fma_f32 v[156:157], v[24:25], s[2:3], v[156:157] op_sel_hi:[1,0,1]
	v_pk_fma_f32 v[154:155], v[26:27], s[2:3], v[154:155] op_sel_hi:[1,0,1]
	v_pk_fma_f32 v[152:153], v[28:29], s[2:3], v[152:153] op_sel_hi:[1,0,1]
	v_pk_fma_f32 v[150:151], v[30:31], s[2:3], v[150:151] op_sel_hi:[1,0,1]
	v_readlane_b32 s2, v131, 1
	v_cvt_scalef32_pk32_f32_fp6 v[0:31], v[50:55], 1.0
	v_pk_fma_f32 v[50:51], v[0:1], s[2:3], v[62:63] op_sel_hi:[1,0,1]
	v_pk_fma_f32 v[52:53], v[2:3], s[2:3], v[64:65] op_sel_hi:[1,0,1]
	v_pk_fma_f32 v[54:55], v[4:5], s[2:3], v[66:67] op_sel_hi:[1,0,1]
	v_pk_fma_f32 v[62:63], v[6:7], s[2:3], v[164:165] op_sel_hi:[1,0,1]
	v_pk_fma_f32 v[64:65], v[8:9], s[2:3], v[166:167] op_sel_hi:[1,0,1]
	v_pk_fma_f32 v[66:67], v[10:11], s[2:3], v[168:169] op_sel_hi:[1,0,1]
	v_pk_fma_f32 v[164:165], v[12:13], s[2:3], v[170:171] op_sel_hi:[1,0,1]
	v_pk_fma_f32 v[166:167], v[14:15], s[2:3], v[172:173] op_sel_hi:[1,0,1]
	v_pk_fma_f32 v[168:169], v[16:17], s[2:3], v[174:175] op_sel_hi:[1,0,1]
	v_pk_fma_f32 v[162:163], v[18:19], s[2:3], v[162:163] op_sel_hi:[1,0,1]
	v_pk_fma_f32 v[160:161], v[20:21], s[2:3], v[160:161] op_sel_hi:[1,0,1]
	v_pk_fma_f32 v[158:159], v[22:23], s[2:3], v[158:159] op_sel_hi:[1,0,1]
	v_pk_fma_f32 v[156:157], v[24:25], s[2:3], v[156:157] op_sel_hi:[1,0,1]
	v_pk_fma_f32 v[154:155], v[26:27], s[2:3], v[154:155] op_sel_hi:[1,0,1]
	v_pk_fma_f32 v[152:153], v[28:29], s[2:3], v[152:153] op_sel_hi:[1,0,1]
	v_pk_fma_f32 v[150:151], v[30:31], s[2:3], v[150:151] op_sel_hi:[1,0,1]
	v_readlane_b32 s2, v131, 2
	v_cvt_scalef32_pk32_f32_fp6 v[0:31], v[38:43], 1.0
	v_pk_fma_f32 v[38:39], v[0:1], s[2:3], v[50:51] op_sel_hi:[1,0,1]
	v_pk_fma_f32 v[40:41], v[2:3], s[2:3], v[52:53] op_sel_hi:[1,0,1]
	v_pk_fma_f32 v[42:43], v[4:5], s[2:3], v[54:55] op_sel_hi:[1,0,1]
	v_pk_fma_f32 v[50:51], v[6:7], s[2:3], v[62:63] op_sel_hi:[1,0,1]
	v_pk_fma_f32 v[52:53], v[8:9], s[2:3], v[64:65] op_sel_hi:[1,0,1]
	v_pk_fma_f32 v[54:55], v[10:11], s[2:3], v[66:67] op_sel_hi:[1,0,1]
	v_pk_fma_f32 v[62:63], v[12:13], s[2:3], v[164:165] op_sel_hi:[1,0,1]
	v_pk_fma_f32 v[64:65], v[14:15], s[2:3], v[166:167] op_sel_hi:[1,0,1]
	v_pk_fma_f32 v[66:67], v[16:17], s[2:3], v[168:169] op_sel_hi:[1,0,1]
	v_pk_fma_f32 v[162:163], v[18:19], s[2:3], v[162:163] op_sel_hi:[1,0,1]
	v_pk_fma_f32 v[160:161], v[20:21], s[2:3], v[160:161] op_sel_hi:[1,0,1]
	v_pk_fma_f32 v[158:159], v[22:23], s[2:3], v[158:159] op_sel_hi:[1,0,1]
	v_pk_fma_f32 v[156:157], v[24:25], s[2:3], v[156:157] op_sel_hi:[1,0,1]
	v_pk_fma_f32 v[154:155], v[26:27], s[2:3], v[154:155] op_sel_hi:[1,0,1]
	v_pk_fma_f32 v[152:153], v[28:29], s[2:3], v[152:153] op_sel_hi:[1,0,1]
	v_pk_fma_f32 v[150:151], v[30:31], s[2:3], v[150:151] op_sel_hi:[1,0,1]
	v_readlane_b32 s2, v131, 3
	v_cvt_scalef32_pk32_f32_fp6 v[0:31], v[32:37], 1.0
	v_pk_fma_f32 v[164:165], v[0:1], s[2:3], v[38:39] op_sel_hi:[1,0,1]
	v_pk_fma_f32 v[166:167], v[2:3], s[2:3], v[40:41] op_sel_hi:[1,0,1]
	v_pk_fma_f32 v[168:169], v[4:5], s[2:3], v[42:43] op_sel_hi:[1,0,1]
	v_pk_fma_f32 v[170:171], v[6:7], s[2:3], v[50:51] op_sel_hi:[1,0,1]
	v_pk_fma_f32 v[172:173], v[8:9], s[2:3], v[52:53] op_sel_hi:[1,0,1]
	v_pk_fma_f32 v[174:175], v[10:11], s[2:3], v[54:55] op_sel_hi:[1,0,1]
	v_pk_fma_f32 v[176:177], v[12:13], s[2:3], v[62:63] op_sel_hi:[1,0,1]
	v_pk_fma_f32 v[178:179], v[14:15], s[2:3], v[64:65] op_sel_hi:[1,0,1]
	v_pk_fma_f32 v[180:181], v[16:17], s[2:3], v[66:67] op_sel_hi:[1,0,1]
	v_pk_fma_f32 v[162:163], v[18:19], s[2:3], v[162:163] op_sel_hi:[1,0,1]
	v_pk_fma_f32 v[160:161], v[20:21], s[2:3], v[160:161] op_sel_hi:[1,0,1]
	v_pk_fma_f32 v[158:159], v[22:23], s[2:3], v[158:159] op_sel_hi:[1,0,1]
	v_pk_fma_f32 v[156:157], v[24:25], s[2:3], v[156:157] op_sel_hi:[1,0,1]
	v_pk_fma_f32 v[154:155], v[26:27], s[2:3], v[154:155] op_sel_hi:[1,0,1]
	v_pk_fma_f32 v[152:153], v[28:29], s[2:3], v[152:153] op_sel_hi:[1,0,1]
	v_pk_fma_f32 v[150:151], v[30:31], s[2:3], v[150:151] op_sel_hi:[1,0,1]
	v_readlane_b32 s2, v241, 12
	v_readlane_b32 s3, v241, 13
	v_readlane_b32 s100, v241, 14
	v_readlane_b32 s101, v241, 15
	s_nop 1
	buffer_load_dwordx4 v[62:65], v129, s[44:47], s2 offen
	buffer_load_dwordx2 v[66:67], v210, s[44:47], s2 offen
	buffer_load_dwordx4 v[50:53], v129, s[44:47], s3 offen
	buffer_load_dwordx2 v[54:55], v210, s[44:47], s3 offen
	buffer_load_dwordx4 v[38:41], v129, s[44:47], s100 offen
	buffer_load_dwordx2 v[42:43], v210, s[44:47], s100 offen
	buffer_load_dwordx4 v[32:35], v129, s[44:47], s101 offen
	buffer_load_dwordx2 v[36:37], v210, s[44:47], s101 offen
	s_waitcnt vmcnt(16)
	v_readlane_b32 s2, v131, 4
	s_nop 0
	v_cvt_scalef32_pk32_f32_fp6 v[0:31], v[98:103], 1.0
	v_pk_fma_f32 v[98:99], v[0:1], s[2:3], v[164:165] op_sel_hi:[1,0,1]
	v_pk_fma_f32 v[100:101], v[2:3], s[2:3], v[166:167] op_sel_hi:[1,0,1]
	v_pk_fma_f32 v[102:103], v[4:5], s[2:3], v[168:169] op_sel_hi:[1,0,1]
	v_pk_fma_f32 v[164:165], v[6:7], s[2:3], v[170:171] op_sel_hi:[1,0,1]
	v_pk_fma_f32 v[166:167], v[8:9], s[2:3], v[172:173] op_sel_hi:[1,0,1]
	v_pk_fma_f32 v[168:169], v[10:11], s[2:3], v[174:175] op_sel_hi:[1,0,1]
	v_pk_fma_f32 v[170:171], v[12:13], s[2:3], v[176:177] op_sel_hi:[1,0,1]
	v_pk_fma_f32 v[172:173], v[14:15], s[2:3], v[178:179] op_sel_hi:[1,0,1]
	v_pk_fma_f32 v[174:175], v[16:17], s[2:3], v[180:181] op_sel_hi:[1,0,1]
	v_pk_fma_f32 v[162:163], v[18:19], s[2:3], v[162:163] op_sel_hi:[1,0,1]
	v_pk_fma_f32 v[160:161], v[20:21], s[2:3], v[160:161] op_sel_hi:[1,0,1]
	v_pk_fma_f32 v[158:159], v[22:23], s[2:3], v[158:159] op_sel_hi:[1,0,1]
	v_pk_fma_f32 v[156:157], v[24:25], s[2:3], v[156:157] op_sel_hi:[1,0,1]
	v_pk_fma_f32 v[154:155], v[26:27], s[2:3], v[154:155] op_sel_hi:[1,0,1]
	v_pk_fma_f32 v[152:153], v[28:29], s[2:3], v[152:153] op_sel_hi:[1,0,1]
	v_pk_fma_f32 v[150:151], v[30:31], s[2:3], v[150:151] op_sel_hi:[1,0,1]
	v_readlane_b32 s2, v131, 5
	v_cvt_scalef32_pk32_f32_fp6 v[0:31], v[92:97], 1.0
	v_pk_fma_f32 v[92:93], v[0:1], s[2:3], v[98:99] op_sel_hi:[1,0,1]
	v_pk_fma_f32 v[94:95], v[2:3], s[2:3], v[100:101] op_sel_hi:[1,0,1]
	v_pk_fma_f32 v[96:97], v[4:5], s[2:3], v[102:103] op_sel_hi:[1,0,1]
	v_pk_fma_f32 v[98:99], v[6:7], s[2:3], v[164:165] op_sel_hi:[1,0,1]
	v_pk_fma_f32 v[100:101], v[8:9], s[2:3], v[166:167] op_sel_hi:[1,0,1]
	v_pk_fma_f32 v[102:103], v[10:11], s[2:3], v[168:169] op_sel_hi:[1,0,1]
	v_pk_fma_f32 v[164:165], v[12:13], s[2:3], v[170:171] op_sel_hi:[1,0,1]
	v_pk_fma_f32 v[166:167], v[14:15], s[2:3], v[172:173] op_sel_hi:[1,0,1]
	v_pk_fma_f32 v[168:169], v[16:17], s[2:3], v[174:175] op_sel_hi:[1,0,1]
	v_pk_fma_f32 v[162:163], v[18:19], s[2:3], v[162:163] op_sel_hi:[1,0,1]
	v_pk_fma_f32 v[160:161], v[20:21], s[2:3], v[160:161] op_sel_hi:[1,0,1]
	v_pk_fma_f32 v[158:159], v[22:23], s[2:3], v[158:159] op_sel_hi:[1,0,1]
	v_pk_fma_f32 v[156:157], v[24:25], s[2:3], v[156:157] op_sel_hi:[1,0,1]
	v_pk_fma_f32 v[154:155], v[26:27], s[2:3], v[154:155] op_sel_hi:[1,0,1]
	v_pk_fma_f32 v[152:153], v[28:29], s[2:3], v[152:153] op_sel_hi:[1,0,1]
	v_pk_fma_f32 v[150:151], v[30:31], s[2:3], v[150:151] op_sel_hi:[1,0,1]
	v_readlane_b32 s2, v131, 6
	v_cvt_scalef32_pk32_f32_fp6 v[0:31], v[86:91], 1.0
	v_pk_fma_f32 v[86:87], v[0:1], s[2:3], v[92:93] op_sel_hi:[1,0,1]
	v_pk_fma_f32 v[88:89], v[2:3], s[2:3], v[94:95] op_sel_hi:[1,0,1]
	v_pk_fma_f32 v[90:91], v[4:5], s[2:3], v[96:97] op_sel_hi:[1,0,1]
	v_pk_fma_f32 v[92:93], v[6:7], s[2:3], v[98:99] op_sel_hi:[1,0,1]
	v_pk_fma_f32 v[94:95], v[8:9], s[2:3], v[100:101] op_sel_hi:[1,0,1]
	v_pk_fma_f32 v[96:97], v[10:11], s[2:3], v[102:103] op_sel_hi:[1,0,1]
	v_pk_fma_f32 v[98:99], v[12:13], s[2:3], v[164:165] op_sel_hi:[1,0,1]
	v_pk_fma_f32 v[100:101], v[14:15], s[2:3], v[166:167] op_sel_hi:[1,0,1]
	v_pk_fma_f32 v[102:103], v[16:17], s[2:3], v[168:169] op_sel_hi:[1,0,1]
	v_pk_fma_f32 v[162:163], v[18:19], s[2:3], v[162:163] op_sel_hi:[1,0,1]
	v_pk_fma_f32 v[160:161], v[20:21], s[2:3], v[160:161] op_sel_hi:[1,0,1]
	v_pk_fma_f32 v[158:159], v[22:23], s[2:3], v[158:159] op_sel_hi:[1,0,1]
	v_pk_fma_f32 v[156:157], v[24:25], s[2:3], v[156:157] op_sel_hi:[1,0,1]
	v_pk_fma_f32 v[154:155], v[26:27], s[2:3], v[154:155] op_sel_hi:[1,0,1]
	v_pk_fma_f32 v[152:153], v[28:29], s[2:3], v[152:153] op_sel_hi:[1,0,1]
	v_pk_fma_f32 v[150:151], v[30:31], s[2:3], v[150:151] op_sel_hi:[1,0,1]
	v_readlane_b32 s2, v131, 7
	v_cvt_scalef32_pk32_f32_fp6 v[0:31], v[80:85], 1.0
	v_pk_fma_f32 v[180:181], v[0:1], s[2:3], v[86:87] op_sel_hi:[1,0,1]
	v_pk_fma_f32 v[178:179], v[2:3], s[2:3], v[88:89] op_sel_hi:[1,0,1]
	v_pk_fma_f32 v[176:177], v[4:5], s[2:3], v[90:91] op_sel_hi:[1,0,1]
	v_pk_fma_f32 v[174:175], v[6:7], s[2:3], v[92:93] op_sel_hi:[1,0,1]
	v_pk_fma_f32 v[172:173], v[8:9], s[2:3], v[94:95] op_sel_hi:[1,0,1]
	v_pk_fma_f32 v[170:171], v[10:11], s[2:3], v[96:97] op_sel_hi:[1,0,1]
	v_pk_fma_f32 v[168:169], v[12:13], s[2:3], v[98:99] op_sel_hi:[1,0,1]
	v_pk_fma_f32 v[166:167], v[14:15], s[2:3], v[100:101] op_sel_hi:[1,0,1]
	v_pk_fma_f32 v[164:165], v[16:17], s[2:3], v[102:103] op_sel_hi:[1,0,1]
	v_pk_fma_f32 v[162:163], v[18:19], s[2:3], v[162:163] op_sel_hi:[1,0,1]
	v_pk_fma_f32 v[160:161], v[20:21], s[2:3], v[160:161] op_sel_hi:[1,0,1]
	v_pk_fma_f32 v[158:159], v[22:23], s[2:3], v[158:159] op_sel_hi:[1,0,1]
	v_pk_fma_f32 v[156:157], v[24:25], s[2:3], v[156:157] op_sel_hi:[1,0,1]
	v_pk_fma_f32 v[154:155], v[26:27], s[2:3], v[154:155] op_sel_hi:[1,0,1]
	v_pk_fma_f32 v[152:153], v[28:29], s[2:3], v[152:153] op_sel_hi:[1,0,1]
	v_pk_fma_f32 v[150:151], v[30:31], s[2:3], v[150:151] op_sel_hi:[1,0,1]
	v_readlane_b32 s2, v241, 16
	v_readlane_b32 s3, v241, 17
	v_readlane_b32 s100, v241, 18
	v_readlane_b32 s101, v241, 19
	s_nop 1
	buffer_load_dwordx4 v[98:101], v129, s[44:47], s2 offen
	buffer_load_dwordx2 v[102:103], v210, s[44:47], s2 offen
	buffer_load_dwordx4 v[92:95], v129, s[44:47], s3 offen
	buffer_load_dwordx2 v[96:97], v210, s[44:47], s3 offen
	buffer_load_dwordx4 v[86:89], v129, s[44:47], s100 offen
	buffer_load_dwordx2 v[90:91], v210, s[44:47], s100 offen
	buffer_load_dwordx4 v[80:83], v129, s[44:47], s101 offen
	buffer_load_dwordx2 v[84:85], v210, s[44:47], s101 offen
	s_waitcnt vmcnt(16)
	v_readlane_b32 s2, v131, 8
	s_nop 0
	v_cvt_scalef32_pk32_f32_fp6 v[0:31], v[74:79], 1.0
	v_pk_fma_f32 v[74:75], v[0:1], s[2:3], v[180:181] op_sel_hi:[1,0,1]
	v_pk_fma_f32 v[76:77], v[2:3], s[2:3], v[178:179] op_sel_hi:[1,0,1]
	v_pk_fma_f32 v[78:79], v[4:5], s[2:3], v[176:177] op_sel_hi:[1,0,1]
	v_pk_fma_f32 v[174:175], v[6:7], s[2:3], v[174:175] op_sel_hi:[1,0,1]
	v_pk_fma_f32 v[172:173], v[8:9], s[2:3], v[172:173] op_sel_hi:[1,0,1]
	v_pk_fma_f32 v[170:171], v[10:11], s[2:3], v[170:171] op_sel_hi:[1,0,1]
	v_pk_fma_f32 v[168:169], v[12:13], s[2:3], v[168:169] op_sel_hi:[1,0,1]
	v_pk_fma_f32 v[166:167], v[14:15], s[2:3], v[166:167] op_sel_hi:[1,0,1]
	v_pk_fma_f32 v[164:165], v[16:17], s[2:3], v[164:165] op_sel_hi:[1,0,1]
	v_pk_fma_f32 v[162:163], v[18:19], s[2:3], v[162:163] op_sel_hi:[1,0,1]
	v_pk_fma_f32 v[160:161], v[20:21], s[2:3], v[160:161] op_sel_hi:[1,0,1]
	v_pk_fma_f32 v[158:159], v[22:23], s[2:3], v[158:159] op_sel_hi:[1,0,1]
	v_pk_fma_f32 v[156:157], v[24:25], s[2:3], v[156:157] op_sel_hi:[1,0,1]
	v_pk_fma_f32 v[154:155], v[26:27], s[2:3], v[154:155] op_sel_hi:[1,0,1]
	v_pk_fma_f32 v[152:153], v[28:29], s[2:3], v[152:153] op_sel_hi:[1,0,1]
	v_pk_fma_f32 v[150:151], v[30:31], s[2:3], v[150:151] op_sel_hi:[1,0,1]
	v_readlane_b32 s2, v131, 9
	v_cvt_scalef32_pk32_f32_fp6 v[0:31], v[68:73], 1.0
	v_pk_fma_f32 v[68:69], v[0:1], s[2:3], v[74:75] op_sel_hi:[1,0,1]
	v_pk_fma_f32 v[70:71], v[2:3], s[2:3], v[76:77] op_sel_hi:[1,0,1]
	v_pk_fma_f32 v[72:73], v[4:5], s[2:3], v[78:79] op_sel_hi:[1,0,1]
	v_pk_fma_f32 v[74:75], v[6:7], s[2:3], v[174:175] op_sel_hi:[1,0,1]
	v_pk_fma_f32 v[76:77], v[8:9], s[2:3], v[172:173] op_sel_hi:[1,0,1]
	v_pk_fma_f32 v[78:79], v[10:11], s[2:3], v[170:171] op_sel_hi:[1,0,1]
	v_pk_fma_f32 v[168:169], v[12:13], s[2:3], v[168:169] op_sel_hi:[1,0,1]
	v_pk_fma_f32 v[166:167], v[14:15], s[2:3], v[166:167] op_sel_hi:[1,0,1]
	v_pk_fma_f32 v[164:165], v[16:17], s[2:3], v[164:165] op_sel_hi:[1,0,1]
	v_pk_fma_f32 v[162:163], v[18:19], s[2:3], v[162:163] op_sel_hi:[1,0,1]
	v_pk_fma_f32 v[160:161], v[20:21], s[2:3], v[160:161] op_sel_hi:[1,0,1]
	v_pk_fma_f32 v[158:159], v[22:23], s[2:3], v[158:159] op_sel_hi:[1,0,1]
	v_pk_fma_f32 v[156:157], v[24:25], s[2:3], v[156:157] op_sel_hi:[1,0,1]
	v_pk_fma_f32 v[154:155], v[26:27], s[2:3], v[154:155] op_sel_hi:[1,0,1]
	v_pk_fma_f32 v[152:153], v[28:29], s[2:3], v[152:153] op_sel_hi:[1,0,1]
	v_pk_fma_f32 v[150:151], v[30:31], s[2:3], v[150:151] op_sel_hi:[1,0,1]
	v_readlane_b32 s2, v131, 10
	v_cvt_scalef32_pk32_f32_fp6 v[0:31], v[56:61], 1.0
	v_pk_fma_f32 v[56:57], v[0:1], s[2:3], v[68:69] op_sel_hi:[1,0,1]
	v_pk_fma_f32 v[58:59], v[2:3], s[2:3], v[70:71] op_sel_hi:[1,0,1]
	v_pk_fma_f32 v[60:61], v[4:5], s[2:3], v[72:73] op_sel_hi:[1,0,1]
	v_pk_fma_f32 v[68:69], v[6:7], s[2:3], v[74:75] op_sel_hi:[1,0,1]
	v_pk_fma_f32 v[70:71], v[8:9], s[2:3], v[76:77] op_sel_hi:[1,0,1]
	v_pk_fma_f32 v[72:73], v[10:11], s[2:3], v[78:79] op_sel_hi:[1,0,1]
	v_pk_fma_f32 v[74:75], v[12:13], s[2:3], v[168:169] op_sel_hi:[1,0,1]
	v_pk_fma_f32 v[76:77], v[14:15], s[2:3], v[166:167] op_sel_hi:[1,0,1]
	v_pk_fma_f32 v[78:79], v[16:17], s[2:3], v[164:165] op_sel_hi:[1,0,1]
	v_pk_fma_f32 v[162:163], v[18:19], s[2:3], v[162:163] op_sel_hi:[1,0,1]
	v_pk_fma_f32 v[160:161], v[20:21], s[2:3], v[160:161] op_sel_hi:[1,0,1]
	v_pk_fma_f32 v[158:159], v[22:23], s[2:3], v[158:159] op_sel_hi:[1,0,1]
	v_pk_fma_f32 v[156:157], v[24:25], s[2:3], v[156:157] op_sel_hi:[1,0,1]
	v_pk_fma_f32 v[154:155], v[26:27], s[2:3], v[154:155] op_sel_hi:[1,0,1]
	v_pk_fma_f32 v[152:153], v[28:29], s[2:3], v[152:153] op_sel_hi:[1,0,1]
	v_pk_fma_f32 v[150:151], v[30:31], s[2:3], v[150:151] op_sel_hi:[1,0,1]
	v_readlane_b32 s2, v131, 11
	v_cvt_scalef32_pk32_f32_fp6 v[0:31], v[44:49], 1.0
	v_pk_fma_f32 v[164:165], v[0:1], s[2:3], v[56:57] op_sel_hi:[1,0,1]
	v_pk_fma_f32 v[166:167], v[2:3], s[2:3], v[58:59] op_sel_hi:[1,0,1]
	v_pk_fma_f32 v[168:169], v[4:5], s[2:3], v[60:61] op_sel_hi:[1,0,1]
	v_pk_fma_f32 v[170:171], v[6:7], s[2:3], v[68:69] op_sel_hi:[1,0,1]
	v_pk_fma_f32 v[172:173], v[8:9], s[2:3], v[70:71] op_sel_hi:[1,0,1]
	v_pk_fma_f32 v[174:175], v[10:11], s[2:3], v[72:73] op_sel_hi:[1,0,1]
	v_pk_fma_f32 v[176:177], v[12:13], s[2:3], v[74:75] op_sel_hi:[1,0,1]
	v_pk_fma_f32 v[178:179], v[14:15], s[2:3], v[76:77] op_sel_hi:[1,0,1]
	v_pk_fma_f32 v[180:181], v[16:17], s[2:3], v[78:79] op_sel_hi:[1,0,1]
	v_pk_fma_f32 v[162:163], v[18:19], s[2:3], v[162:163] op_sel_hi:[1,0,1]
	v_pk_fma_f32 v[160:161], v[20:21], s[2:3], v[160:161] op_sel_hi:[1,0,1]
	v_pk_fma_f32 v[158:159], v[22:23], s[2:3], v[158:159] op_sel_hi:[1,0,1]
	v_pk_fma_f32 v[156:157], v[24:25], s[2:3], v[156:157] op_sel_hi:[1,0,1]
	v_pk_fma_f32 v[154:155], v[26:27], s[2:3], v[154:155] op_sel_hi:[1,0,1]
	v_pk_fma_f32 v[152:153], v[28:29], s[2:3], v[152:153] op_sel_hi:[1,0,1]
	v_pk_fma_f32 v[150:151], v[30:31], s[2:3], v[150:151] op_sel_hi:[1,0,1]
	v_readlane_b32 s2, v241, 20
	v_readlane_b32 s3, v241, 21
	v_readlane_b32 s100, v241, 22
	v_readlane_b32 s101, v241, 23
	s_nop 1
	buffer_load_dwordx4 v[74:77], v129, s[44:47], s2 offen
	buffer_load_dwordx2 v[78:79], v210, s[44:47], s2 offen
	buffer_load_dwordx4 v[68:71], v129, s[44:47], s3 offen
	buffer_load_dwordx2 v[72:73], v210, s[44:47], s3 offen
	buffer_load_dwordx4 v[56:59], v129, s[44:47], s100 offen
	buffer_load_dwordx2 v[60:61], v210, s[44:47], s100 offen
	buffer_load_dwordx4 v[44:47], v129, s[44:47], s101 offen
	buffer_load_dwordx2 v[48:49], v210, s[44:47], s101 offen
	s_waitcnt vmcnt(16)
	v_readlane_b32 s2, v131, 12
	s_nop 0
	v_cvt_scalef32_pk32_f32_fp6 v[0:31], v[62:67], 1.0
	v_pk_fma_f32 v[62:63], v[0:1], s[2:3], v[164:165] op_sel_hi:[1,0,1]
	v_pk_fma_f32 v[64:65], v[2:3], s[2:3], v[166:167] op_sel_hi:[1,0,1]
	v_pk_fma_f32 v[66:67], v[4:5], s[2:3], v[168:169] op_sel_hi:[1,0,1]
	v_pk_fma_f32 v[164:165], v[6:7], s[2:3], v[170:171] op_sel_hi:[1,0,1]
	v_pk_fma_f32 v[166:167], v[8:9], s[2:3], v[172:173] op_sel_hi:[1,0,1]
	v_pk_fma_f32 v[168:169], v[10:11], s[2:3], v[174:175] op_sel_hi:[1,0,1]
	v_pk_fma_f32 v[170:171], v[12:13], s[2:3], v[176:177] op_sel_hi:[1,0,1]
	v_pk_fma_f32 v[172:173], v[14:15], s[2:3], v[178:179] op_sel_hi:[1,0,1]
	v_pk_fma_f32 v[174:175], v[16:17], s[2:3], v[180:181] op_sel_hi:[1,0,1]
	v_pk_fma_f32 v[162:163], v[18:19], s[2:3], v[162:163] op_sel_hi:[1,0,1]
	v_pk_fma_f32 v[160:161], v[20:21], s[2:3], v[160:161] op_sel_hi:[1,0,1]
	v_pk_fma_f32 v[158:159], v[22:23], s[2:3], v[158:159] op_sel_hi:[1,0,1]
	v_pk_fma_f32 v[156:157], v[24:25], s[2:3], v[156:157] op_sel_hi:[1,0,1]
	v_pk_fma_f32 v[154:155], v[26:27], s[2:3], v[154:155] op_sel_hi:[1,0,1]
	v_pk_fma_f32 v[152:153], v[28:29], s[2:3], v[152:153] op_sel_hi:[1,0,1]
	v_pk_fma_f32 v[150:151], v[30:31], s[2:3], v[150:151] op_sel_hi:[1,0,1]
	v_readlane_b32 s2, v131, 13
	v_cvt_scalef32_pk32_f32_fp6 v[0:31], v[50:55], 1.0
	v_pk_fma_f32 v[50:51], v[0:1], s[2:3], v[62:63] op_sel_hi:[1,0,1]
	v_pk_fma_f32 v[52:53], v[2:3], s[2:3], v[64:65] op_sel_hi:[1,0,1]
	v_pk_fma_f32 v[54:55], v[4:5], s[2:3], v[66:67] op_sel_hi:[1,0,1]
	v_pk_fma_f32 v[62:63], v[6:7], s[2:3], v[164:165] op_sel_hi:[1,0,1]
	v_pk_fma_f32 v[64:65], v[8:9], s[2:3], v[166:167] op_sel_hi:[1,0,1]
	v_pk_fma_f32 v[66:67], v[10:11], s[2:3], v[168:169] op_sel_hi:[1,0,1]
	v_pk_fma_f32 v[164:165], v[12:13], s[2:3], v[170:171] op_sel_hi:[1,0,1]
	v_pk_fma_f32 v[166:167], v[14:15], s[2:3], v[172:173] op_sel_hi:[1,0,1]
	v_pk_fma_f32 v[168:169], v[16:17], s[2:3], v[174:175] op_sel_hi:[1,0,1]
	v_pk_fma_f32 v[162:163], v[18:19], s[2:3], v[162:163] op_sel_hi:[1,0,1]
	v_pk_fma_f32 v[160:161], v[20:21], s[2:3], v[160:161] op_sel_hi:[1,0,1]
	v_pk_fma_f32 v[158:159], v[22:23], s[2:3], v[158:159] op_sel_hi:[1,0,1]
	v_pk_fma_f32 v[156:157], v[24:25], s[2:3], v[156:157] op_sel_hi:[1,0,1]
	v_pk_fma_f32 v[154:155], v[26:27], s[2:3], v[154:155] op_sel_hi:[1,0,1]
	v_pk_fma_f32 v[152:153], v[28:29], s[2:3], v[152:153] op_sel_hi:[1,0,1]
	v_pk_fma_f32 v[150:151], v[30:31], s[2:3], v[150:151] op_sel_hi:[1,0,1]
	v_readlane_b32 s2, v131, 14
	v_cvt_scalef32_pk32_f32_fp6 v[0:31], v[38:43], 1.0
	v_pk_fma_f32 v[38:39], v[0:1], s[2:3], v[50:51] op_sel_hi:[1,0,1]
	v_pk_fma_f32 v[40:41], v[2:3], s[2:3], v[52:53] op_sel_hi:[1,0,1]
	v_pk_fma_f32 v[42:43], v[4:5], s[2:3], v[54:55] op_sel_hi:[1,0,1]
	v_pk_fma_f32 v[50:51], v[6:7], s[2:3], v[62:63] op_sel_hi:[1,0,1]
	v_pk_fma_f32 v[52:53], v[8:9], s[2:3], v[64:65] op_sel_hi:[1,0,1]
	v_pk_fma_f32 v[54:55], v[10:11], s[2:3], v[66:67] op_sel_hi:[1,0,1]
	v_pk_fma_f32 v[62:63], v[12:13], s[2:3], v[164:165] op_sel_hi:[1,0,1]
	v_pk_fma_f32 v[64:65], v[14:15], s[2:3], v[166:167] op_sel_hi:[1,0,1]
	v_pk_fma_f32 v[66:67], v[16:17], s[2:3], v[168:169] op_sel_hi:[1,0,1]
	v_pk_fma_f32 v[162:163], v[18:19], s[2:3], v[162:163] op_sel_hi:[1,0,1]
	v_pk_fma_f32 v[160:161], v[20:21], s[2:3], v[160:161] op_sel_hi:[1,0,1]
	v_pk_fma_f32 v[158:159], v[22:23], s[2:3], v[158:159] op_sel_hi:[1,0,1]
	v_pk_fma_f32 v[156:157], v[24:25], s[2:3], v[156:157] op_sel_hi:[1,0,1]
	v_pk_fma_f32 v[154:155], v[26:27], s[2:3], v[154:155] op_sel_hi:[1,0,1]
	v_pk_fma_f32 v[152:153], v[28:29], s[2:3], v[152:153] op_sel_hi:[1,0,1]
	v_pk_fma_f32 v[150:151], v[30:31], s[2:3], v[150:151] op_sel_hi:[1,0,1]
	v_readlane_b32 s2, v131, 15
	v_cvt_scalef32_pk32_f32_fp6 v[0:31], v[32:37], 1.0
	v_pk_fma_f32 v[164:165], v[0:1], s[2:3], v[38:39] op_sel_hi:[1,0,1]
	v_pk_fma_f32 v[166:167], v[2:3], s[2:3], v[40:41] op_sel_hi:[1,0,1]
	v_pk_fma_f32 v[168:169], v[4:5], s[2:3], v[42:43] op_sel_hi:[1,0,1]
	v_pk_fma_f32 v[170:171], v[6:7], s[2:3], v[50:51] op_sel_hi:[1,0,1]
	v_pk_fma_f32 v[172:173], v[8:9], s[2:3], v[52:53] op_sel_hi:[1,0,1]
	v_pk_fma_f32 v[174:175], v[10:11], s[2:3], v[54:55] op_sel_hi:[1,0,1]
	v_pk_fma_f32 v[176:177], v[12:13], s[2:3], v[62:63] op_sel_hi:[1,0,1]
	v_pk_fma_f32 v[178:179], v[14:15], s[2:3], v[64:65] op_sel_hi:[1,0,1]
	v_pk_fma_f32 v[180:181], v[16:17], s[2:3], v[66:67] op_sel_hi:[1,0,1]
	v_pk_fma_f32 v[162:163], v[18:19], s[2:3], v[162:163] op_sel_hi:[1,0,1]
	v_pk_fma_f32 v[160:161], v[20:21], s[2:3], v[160:161] op_sel_hi:[1,0,1]
	v_pk_fma_f32 v[158:159], v[22:23], s[2:3], v[158:159] op_sel_hi:[1,0,1]
	v_pk_fma_f32 v[156:157], v[24:25], s[2:3], v[156:157] op_sel_hi:[1,0,1]
	v_pk_fma_f32 v[154:155], v[26:27], s[2:3], v[154:155] op_sel_hi:[1,0,1]
	v_pk_fma_f32 v[152:153], v[28:29], s[2:3], v[152:153] op_sel_hi:[1,0,1]
	v_pk_fma_f32 v[150:151], v[30:31], s[2:3], v[150:151] op_sel_hi:[1,0,1]
	v_readlane_b32 s2, v241, 24
	v_readlane_b32 s3, v241, 25
	v_readlane_b32 s100, v241, 26
	v_readlane_b32 s101, v241, 27
	s_nop 1
	buffer_load_dwordx4 v[62:65], v129, s[44:47], s2 offen
	buffer_load_dwordx2 v[66:67], v210, s[44:47], s2 offen
	buffer_load_dwordx4 v[50:53], v129, s[44:47], s3 offen
	buffer_load_dwordx2 v[54:55], v210, s[44:47], s3 offen
	buffer_load_dwordx4 v[38:41], v129, s[44:47], s100 offen
	buffer_load_dwordx2 v[42:43], v210, s[44:47], s100 offen
	buffer_load_dwordx4 v[32:35], v129, s[44:47], s101 offen
	buffer_load_dwordx2 v[36:37], v210, s[44:47], s101 offen
	s_waitcnt vmcnt(16)
	v_readlane_b32 s2, v131, 16
	s_nop 0
	v_cvt_scalef32_pk32_f32_fp6 v[0:31], v[98:103], 1.0
	v_pk_fma_f32 v[98:99], v[0:1], s[2:3], v[164:165] op_sel_hi:[1,0,1]
	v_pk_fma_f32 v[100:101], v[2:3], s[2:3], v[166:167] op_sel_hi:[1,0,1]
	v_pk_fma_f32 v[102:103], v[4:5], s[2:3], v[168:169] op_sel_hi:[1,0,1]
	v_pk_fma_f32 v[164:165], v[6:7], s[2:3], v[170:171] op_sel_hi:[1,0,1]
	v_pk_fma_f32 v[166:167], v[8:9], s[2:3], v[172:173] op_sel_hi:[1,0,1]
	v_pk_fma_f32 v[168:169], v[10:11], s[2:3], v[174:175] op_sel_hi:[1,0,1]
	v_pk_fma_f32 v[170:171], v[12:13], s[2:3], v[176:177] op_sel_hi:[1,0,1]
	v_pk_fma_f32 v[172:173], v[14:15], s[2:3], v[178:179] op_sel_hi:[1,0,1]
	v_pk_fma_f32 v[174:175], v[16:17], s[2:3], v[180:181] op_sel_hi:[1,0,1]
	v_pk_fma_f32 v[162:163], v[18:19], s[2:3], v[162:163] op_sel_hi:[1,0,1]
	v_pk_fma_f32 v[160:161], v[20:21], s[2:3], v[160:161] op_sel_hi:[1,0,1]
	v_pk_fma_f32 v[158:159], v[22:23], s[2:3], v[158:159] op_sel_hi:[1,0,1]
	v_pk_fma_f32 v[156:157], v[24:25], s[2:3], v[156:157] op_sel_hi:[1,0,1]
	v_pk_fma_f32 v[154:155], v[26:27], s[2:3], v[154:155] op_sel_hi:[1,0,1]
	v_pk_fma_f32 v[152:153], v[28:29], s[2:3], v[152:153] op_sel_hi:[1,0,1]
	v_pk_fma_f32 v[150:151], v[30:31], s[2:3], v[150:151] op_sel_hi:[1,0,1]
	v_readlane_b32 s2, v131, 17
	v_cvt_scalef32_pk32_f32_fp6 v[0:31], v[92:97], 1.0
	v_pk_fma_f32 v[92:93], v[0:1], s[2:3], v[98:99] op_sel_hi:[1,0,1]
	v_pk_fma_f32 v[94:95], v[2:3], s[2:3], v[100:101] op_sel_hi:[1,0,1]
	v_pk_fma_f32 v[96:97], v[4:5], s[2:3], v[102:103] op_sel_hi:[1,0,1]
	v_pk_fma_f32 v[98:99], v[6:7], s[2:3], v[164:165] op_sel_hi:[1,0,1]
	v_pk_fma_f32 v[100:101], v[8:9], s[2:3], v[166:167] op_sel_hi:[1,0,1]
	v_pk_fma_f32 v[102:103], v[10:11], s[2:3], v[168:169] op_sel_hi:[1,0,1]
	v_pk_fma_f32 v[164:165], v[12:13], s[2:3], v[170:171] op_sel_hi:[1,0,1]
	v_pk_fma_f32 v[166:167], v[14:15], s[2:3], v[172:173] op_sel_hi:[1,0,1]
	v_pk_fma_f32 v[168:169], v[16:17], s[2:3], v[174:175] op_sel_hi:[1,0,1]
	v_pk_fma_f32 v[162:163], v[18:19], s[2:3], v[162:163] op_sel_hi:[1,0,1]
	v_pk_fma_f32 v[160:161], v[20:21], s[2:3], v[160:161] op_sel_hi:[1,0,1]
	v_pk_fma_f32 v[158:159], v[22:23], s[2:3], v[158:159] op_sel_hi:[1,0,1]
	v_pk_fma_f32 v[156:157], v[24:25], s[2:3], v[156:157] op_sel_hi:[1,0,1]
	v_pk_fma_f32 v[154:155], v[26:27], s[2:3], v[154:155] op_sel_hi:[1,0,1]
	v_pk_fma_f32 v[152:153], v[28:29], s[2:3], v[152:153] op_sel_hi:[1,0,1]
	v_pk_fma_f32 v[150:151], v[30:31], s[2:3], v[150:151] op_sel_hi:[1,0,1]
	v_readlane_b32 s2, v131, 18
	v_cvt_scalef32_pk32_f32_fp6 v[0:31], v[86:91], 1.0
	v_pk_fma_f32 v[86:87], v[0:1], s[2:3], v[92:93] op_sel_hi:[1,0,1]
	v_pk_fma_f32 v[88:89], v[2:3], s[2:3], v[94:95] op_sel_hi:[1,0,1]
	v_pk_fma_f32 v[90:91], v[4:5], s[2:3], v[96:97] op_sel_hi:[1,0,1]
	v_pk_fma_f32 v[92:93], v[6:7], s[2:3], v[98:99] op_sel_hi:[1,0,1]
	v_pk_fma_f32 v[94:95], v[8:9], s[2:3], v[100:101] op_sel_hi:[1,0,1]
	v_pk_fma_f32 v[96:97], v[10:11], s[2:3], v[102:103] op_sel_hi:[1,0,1]
	v_pk_fma_f32 v[98:99], v[12:13], s[2:3], v[164:165] op_sel_hi:[1,0,1]
	v_pk_fma_f32 v[100:101], v[14:15], s[2:3], v[166:167] op_sel_hi:[1,0,1]
	v_pk_fma_f32 v[102:103], v[16:17], s[2:3], v[168:169] op_sel_hi:[1,0,1]
	v_pk_fma_f32 v[162:163], v[18:19], s[2:3], v[162:163] op_sel_hi:[1,0,1]
	v_pk_fma_f32 v[160:161], v[20:21], s[2:3], v[160:161] op_sel_hi:[1,0,1]
	v_pk_fma_f32 v[158:159], v[22:23], s[2:3], v[158:159] op_sel_hi:[1,0,1]
	v_pk_fma_f32 v[156:157], v[24:25], s[2:3], v[156:157] op_sel_hi:[1,0,1]
	v_pk_fma_f32 v[154:155], v[26:27], s[2:3], v[154:155] op_sel_hi:[1,0,1]
	v_pk_fma_f32 v[152:153], v[28:29], s[2:3], v[152:153] op_sel_hi:[1,0,1]
	v_pk_fma_f32 v[150:151], v[30:31], s[2:3], v[150:151] op_sel_hi:[1,0,1]
	v_readlane_b32 s2, v131, 19
	v_cvt_scalef32_pk32_f32_fp6 v[0:31], v[80:85], 1.0
	v_pk_fma_f32 v[180:181], v[0:1], s[2:3], v[86:87] op_sel_hi:[1,0,1]
	v_pk_fma_f32 v[178:179], v[2:3], s[2:3], v[88:89] op_sel_hi:[1,0,1]
	v_pk_fma_f32 v[176:177], v[4:5], s[2:3], v[90:91] op_sel_hi:[1,0,1]
	v_pk_fma_f32 v[174:175], v[6:7], s[2:3], v[92:93] op_sel_hi:[1,0,1]
	v_pk_fma_f32 v[172:173], v[8:9], s[2:3], v[94:95] op_sel_hi:[1,0,1]
	v_pk_fma_f32 v[170:171], v[10:11], s[2:3], v[96:97] op_sel_hi:[1,0,1]
	v_pk_fma_f32 v[168:169], v[12:13], s[2:3], v[98:99] op_sel_hi:[1,0,1]
	v_pk_fma_f32 v[166:167], v[14:15], s[2:3], v[100:101] op_sel_hi:[1,0,1]
	v_pk_fma_f32 v[164:165], v[16:17], s[2:3], v[102:103] op_sel_hi:[1,0,1]
	v_pk_fma_f32 v[162:163], v[18:19], s[2:3], v[162:163] op_sel_hi:[1,0,1]
	v_pk_fma_f32 v[160:161], v[20:21], s[2:3], v[160:161] op_sel_hi:[1,0,1]
	v_pk_fma_f32 v[158:159], v[22:23], s[2:3], v[158:159] op_sel_hi:[1,0,1]
	v_pk_fma_f32 v[156:157], v[24:25], s[2:3], v[156:157] op_sel_hi:[1,0,1]
	v_pk_fma_f32 v[154:155], v[26:27], s[2:3], v[154:155] op_sel_hi:[1,0,1]
	v_pk_fma_f32 v[152:153], v[28:29], s[2:3], v[152:153] op_sel_hi:[1,0,1]
	v_pk_fma_f32 v[150:151], v[30:31], s[2:3], v[150:151] op_sel_hi:[1,0,1]
	v_readlane_b32 s2, v241, 28
	v_readlane_b32 s3, v241, 29
	v_readlane_b32 s100, v241, 30
	v_readlane_b32 s101, v241, 31
	s_nop 1
	buffer_load_dwordx4 v[98:101], v129, s[44:47], s2 offen
	buffer_load_dwordx2 v[102:103], v210, s[44:47], s2 offen
	buffer_load_dwordx4 v[92:95], v129, s[44:47], s3 offen
	buffer_load_dwordx2 v[96:97], v210, s[44:47], s3 offen
	buffer_load_dwordx4 v[86:89], v129, s[44:47], s100 offen
	buffer_load_dwordx2 v[90:91], v210, s[44:47], s100 offen
	buffer_load_dwordx4 v[80:83], v129, s[44:47], s101 offen
	buffer_load_dwordx2 v[84:85], v210, s[44:47], s101 offen
	s_waitcnt vmcnt(16)
	v_readlane_b32 s2, v131, 20
	s_nop 0
	v_cvt_scalef32_pk32_f32_fp6 v[0:31], v[74:79], 1.0
	v_pk_fma_f32 v[74:75], v[0:1], s[2:3], v[180:181] op_sel_hi:[1,0,1]
	v_pk_fma_f32 v[76:77], v[2:3], s[2:3], v[178:179] op_sel_hi:[1,0,1]
	v_pk_fma_f32 v[78:79], v[4:5], s[2:3], v[176:177] op_sel_hi:[1,0,1]
	v_pk_fma_f32 v[174:175], v[6:7], s[2:3], v[174:175] op_sel_hi:[1,0,1]
	v_pk_fma_f32 v[172:173], v[8:9], s[2:3], v[172:173] op_sel_hi:[1,0,1]
	v_pk_fma_f32 v[170:171], v[10:11], s[2:3], v[170:171] op_sel_hi:[1,0,1]
	v_pk_fma_f32 v[168:169], v[12:13], s[2:3], v[168:169] op_sel_hi:[1,0,1]
	v_pk_fma_f32 v[166:167], v[14:15], s[2:3], v[166:167] op_sel_hi:[1,0,1]
	v_pk_fma_f32 v[164:165], v[16:17], s[2:3], v[164:165] op_sel_hi:[1,0,1]
	v_pk_fma_f32 v[162:163], v[18:19], s[2:3], v[162:163] op_sel_hi:[1,0,1]
	v_pk_fma_f32 v[160:161], v[20:21], s[2:3], v[160:161] op_sel_hi:[1,0,1]
	v_pk_fma_f32 v[158:159], v[22:23], s[2:3], v[158:159] op_sel_hi:[1,0,1]
	v_pk_fma_f32 v[156:157], v[24:25], s[2:3], v[156:157] op_sel_hi:[1,0,1]
	v_pk_fma_f32 v[154:155], v[26:27], s[2:3], v[154:155] op_sel_hi:[1,0,1]
	v_pk_fma_f32 v[152:153], v[28:29], s[2:3], v[152:153] op_sel_hi:[1,0,1]
	v_pk_fma_f32 v[150:151], v[30:31], s[2:3], v[150:151] op_sel_hi:[1,0,1]
	v_readlane_b32 s2, v131, 21
	v_cvt_scalef32_pk32_f32_fp6 v[0:31], v[68:73], 1.0
	v_pk_fma_f32 v[68:69], v[0:1], s[2:3], v[74:75] op_sel_hi:[1,0,1]
	v_pk_fma_f32 v[70:71], v[2:3], s[2:3], v[76:77] op_sel_hi:[1,0,1]
	v_pk_fma_f32 v[72:73], v[4:5], s[2:3], v[78:79] op_sel_hi:[1,0,1]
	v_pk_fma_f32 v[74:75], v[6:7], s[2:3], v[174:175] op_sel_hi:[1,0,1]
	v_pk_fma_f32 v[76:77], v[8:9], s[2:3], v[172:173] op_sel_hi:[1,0,1]
	v_pk_fma_f32 v[78:79], v[10:11], s[2:3], v[170:171] op_sel_hi:[1,0,1]
	v_pk_fma_f32 v[168:169], v[12:13], s[2:3], v[168:169] op_sel_hi:[1,0,1]
	v_pk_fma_f32 v[166:167], v[14:15], s[2:3], v[166:167] op_sel_hi:[1,0,1]
	v_pk_fma_f32 v[164:165], v[16:17], s[2:3], v[164:165] op_sel_hi:[1,0,1]
	v_pk_fma_f32 v[162:163], v[18:19], s[2:3], v[162:163] op_sel_hi:[1,0,1]
	v_pk_fma_f32 v[160:161], v[20:21], s[2:3], v[160:161] op_sel_hi:[1,0,1]
	v_pk_fma_f32 v[158:159], v[22:23], s[2:3], v[158:159] op_sel_hi:[1,0,1]
	v_pk_fma_f32 v[156:157], v[24:25], s[2:3], v[156:157] op_sel_hi:[1,0,1]
	v_pk_fma_f32 v[154:155], v[26:27], s[2:3], v[154:155] op_sel_hi:[1,0,1]
	v_pk_fma_f32 v[152:153], v[28:29], s[2:3], v[152:153] op_sel_hi:[1,0,1]
	v_pk_fma_f32 v[150:151], v[30:31], s[2:3], v[150:151] op_sel_hi:[1,0,1]
	v_readlane_b32 s2, v131, 22
	v_cvt_scalef32_pk32_f32_fp6 v[0:31], v[56:61], 1.0
	v_pk_fma_f32 v[56:57], v[0:1], s[2:3], v[68:69] op_sel_hi:[1,0,1]
	v_pk_fma_f32 v[58:59], v[2:3], s[2:3], v[70:71] op_sel_hi:[1,0,1]
	v_pk_fma_f32 v[60:61], v[4:5], s[2:3], v[72:73] op_sel_hi:[1,0,1]
	v_pk_fma_f32 v[68:69], v[6:7], s[2:3], v[74:75] op_sel_hi:[1,0,1]
	v_pk_fma_f32 v[70:71], v[8:9], s[2:3], v[76:77] op_sel_hi:[1,0,1]
	v_pk_fma_f32 v[72:73], v[10:11], s[2:3], v[78:79] op_sel_hi:[1,0,1]
	v_pk_fma_f32 v[74:75], v[12:13], s[2:3], v[168:169] op_sel_hi:[1,0,1]
	v_pk_fma_f32 v[76:77], v[14:15], s[2:3], v[166:167] op_sel_hi:[1,0,1]
	v_pk_fma_f32 v[78:79], v[16:17], s[2:3], v[164:165] op_sel_hi:[1,0,1]
	v_pk_fma_f32 v[162:163], v[18:19], s[2:3], v[162:163] op_sel_hi:[1,0,1]
	v_pk_fma_f32 v[160:161], v[20:21], s[2:3], v[160:161] op_sel_hi:[1,0,1]
	v_pk_fma_f32 v[158:159], v[22:23], s[2:3], v[158:159] op_sel_hi:[1,0,1]
	v_pk_fma_f32 v[156:157], v[24:25], s[2:3], v[156:157] op_sel_hi:[1,0,1]
	v_pk_fma_f32 v[154:155], v[26:27], s[2:3], v[154:155] op_sel_hi:[1,0,1]
	v_pk_fma_f32 v[152:153], v[28:29], s[2:3], v[152:153] op_sel_hi:[1,0,1]
	v_pk_fma_f32 v[150:151], v[30:31], s[2:3], v[150:151] op_sel_hi:[1,0,1]
	v_readlane_b32 s2, v131, 23
	v_cvt_scalef32_pk32_f32_fp6 v[0:31], v[44:49], 1.0
	v_pk_fma_f32 v[164:165], v[0:1], s[2:3], v[56:57] op_sel_hi:[1,0,1]
	v_pk_fma_f32 v[166:167], v[2:3], s[2:3], v[58:59] op_sel_hi:[1,0,1]
	v_pk_fma_f32 v[168:169], v[4:5], s[2:3], v[60:61] op_sel_hi:[1,0,1]
	v_pk_fma_f32 v[170:171], v[6:7], s[2:3], v[68:69] op_sel_hi:[1,0,1]
	v_pk_fma_f32 v[172:173], v[8:9], s[2:3], v[70:71] op_sel_hi:[1,0,1]
	v_pk_fma_f32 v[174:175], v[10:11], s[2:3], v[72:73] op_sel_hi:[1,0,1]
	v_pk_fma_f32 v[176:177], v[12:13], s[2:3], v[74:75] op_sel_hi:[1,0,1]
	v_pk_fma_f32 v[178:179], v[14:15], s[2:3], v[76:77] op_sel_hi:[1,0,1]
	v_pk_fma_f32 v[180:181], v[16:17], s[2:3], v[78:79] op_sel_hi:[1,0,1]
	v_pk_fma_f32 v[162:163], v[18:19], s[2:3], v[162:163] op_sel_hi:[1,0,1]
	v_pk_fma_f32 v[160:161], v[20:21], s[2:3], v[160:161] op_sel_hi:[1,0,1]
	v_pk_fma_f32 v[158:159], v[22:23], s[2:3], v[158:159] op_sel_hi:[1,0,1]
	v_pk_fma_f32 v[156:157], v[24:25], s[2:3], v[156:157] op_sel_hi:[1,0,1]
	v_pk_fma_f32 v[154:155], v[26:27], s[2:3], v[154:155] op_sel_hi:[1,0,1]
	v_pk_fma_f32 v[152:153], v[28:29], s[2:3], v[152:153] op_sel_hi:[1,0,1]
	v_pk_fma_f32 v[150:151], v[30:31], s[2:3], v[150:151] op_sel_hi:[1,0,1]
	v_readlane_b32 s2, v241, 32
	v_readlane_b32 s3, v241, 33
	v_readlane_b32 s100, v241, 34
	v_readlane_b32 s101, v241, 35
	s_nop 1
	buffer_load_dwordx4 v[74:77], v129, s[44:47], s2 offen
	buffer_load_dwordx2 v[78:79], v210, s[44:47], s2 offen
	buffer_load_dwordx4 v[68:71], v129, s[44:47], s3 offen
	buffer_load_dwordx2 v[72:73], v210, s[44:47], s3 offen
	buffer_load_dwordx4 v[56:59], v129, s[44:47], s100 offen
	buffer_load_dwordx2 v[60:61], v210, s[44:47], s100 offen
	buffer_load_dwordx4 v[44:47], v129, s[44:47], s101 offen
	buffer_load_dwordx2 v[48:49], v210, s[44:47], s101 offen
	s_waitcnt vmcnt(16)
	v_readlane_b32 s2, v131, 24
	s_nop 0
	v_cvt_scalef32_pk32_f32_fp6 v[0:31], v[62:67], 1.0
	v_pk_fma_f32 v[62:63], v[0:1], s[2:3], v[164:165] op_sel_hi:[1,0,1]
	v_pk_fma_f32 v[64:65], v[2:3], s[2:3], v[166:167] op_sel_hi:[1,0,1]
	v_pk_fma_f32 v[66:67], v[4:5], s[2:3], v[168:169] op_sel_hi:[1,0,1]
	v_pk_fma_f32 v[164:165], v[6:7], s[2:3], v[170:171] op_sel_hi:[1,0,1]
	v_pk_fma_f32 v[166:167], v[8:9], s[2:3], v[172:173] op_sel_hi:[1,0,1]
	v_pk_fma_f32 v[168:169], v[10:11], s[2:3], v[174:175] op_sel_hi:[1,0,1]
	v_pk_fma_f32 v[170:171], v[12:13], s[2:3], v[176:177] op_sel_hi:[1,0,1]
	v_pk_fma_f32 v[172:173], v[14:15], s[2:3], v[178:179] op_sel_hi:[1,0,1]
	v_pk_fma_f32 v[174:175], v[16:17], s[2:3], v[180:181] op_sel_hi:[1,0,1]
	v_pk_fma_f32 v[162:163], v[18:19], s[2:3], v[162:163] op_sel_hi:[1,0,1]
	v_pk_fma_f32 v[160:161], v[20:21], s[2:3], v[160:161] op_sel_hi:[1,0,1]
	v_pk_fma_f32 v[158:159], v[22:23], s[2:3], v[158:159] op_sel_hi:[1,0,1]
	v_pk_fma_f32 v[156:157], v[24:25], s[2:3], v[156:157] op_sel_hi:[1,0,1]
	v_pk_fma_f32 v[154:155], v[26:27], s[2:3], v[154:155] op_sel_hi:[1,0,1]
	v_pk_fma_f32 v[152:153], v[28:29], s[2:3], v[152:153] op_sel_hi:[1,0,1]
	v_pk_fma_f32 v[150:151], v[30:31], s[2:3], v[150:151] op_sel_hi:[1,0,1]
	v_readlane_b32 s2, v131, 25
	v_cvt_scalef32_pk32_f32_fp6 v[0:31], v[50:55], 1.0
	v_pk_fma_f32 v[50:51], v[0:1], s[2:3], v[62:63] op_sel_hi:[1,0,1]
	v_pk_fma_f32 v[52:53], v[2:3], s[2:3], v[64:65] op_sel_hi:[1,0,1]
	v_pk_fma_f32 v[54:55], v[4:5], s[2:3], v[66:67] op_sel_hi:[1,0,1]
	v_pk_fma_f32 v[62:63], v[6:7], s[2:3], v[164:165] op_sel_hi:[1,0,1]
	v_pk_fma_f32 v[64:65], v[8:9], s[2:3], v[166:167] op_sel_hi:[1,0,1]
	v_pk_fma_f32 v[66:67], v[10:11], s[2:3], v[168:169] op_sel_hi:[1,0,1]
	v_pk_fma_f32 v[164:165], v[12:13], s[2:3], v[170:171] op_sel_hi:[1,0,1]
	v_pk_fma_f32 v[166:167], v[14:15], s[2:3], v[172:173] op_sel_hi:[1,0,1]
	v_pk_fma_f32 v[168:169], v[16:17], s[2:3], v[174:175] op_sel_hi:[1,0,1]
	v_pk_fma_f32 v[162:163], v[18:19], s[2:3], v[162:163] op_sel_hi:[1,0,1]
	v_pk_fma_f32 v[160:161], v[20:21], s[2:3], v[160:161] op_sel_hi:[1,0,1]
	v_pk_fma_f32 v[158:159], v[22:23], s[2:3], v[158:159] op_sel_hi:[1,0,1]
	v_pk_fma_f32 v[156:157], v[24:25], s[2:3], v[156:157] op_sel_hi:[1,0,1]
	v_pk_fma_f32 v[154:155], v[26:27], s[2:3], v[154:155] op_sel_hi:[1,0,1]
	v_pk_fma_f32 v[152:153], v[28:29], s[2:3], v[152:153] op_sel_hi:[1,0,1]
	v_pk_fma_f32 v[150:151], v[30:31], s[2:3], v[150:151] op_sel_hi:[1,0,1]
	v_readlane_b32 s2, v131, 26
	v_cvt_scalef32_pk32_f32_fp6 v[0:31], v[38:43], 1.0
	v_pk_fma_f32 v[38:39], v[0:1], s[2:3], v[50:51] op_sel_hi:[1,0,1]
	v_pk_fma_f32 v[40:41], v[2:3], s[2:3], v[52:53] op_sel_hi:[1,0,1]
	v_pk_fma_f32 v[42:43], v[4:5], s[2:3], v[54:55] op_sel_hi:[1,0,1]
	v_pk_fma_f32 v[50:51], v[6:7], s[2:3], v[62:63] op_sel_hi:[1,0,1]
	v_pk_fma_f32 v[52:53], v[8:9], s[2:3], v[64:65] op_sel_hi:[1,0,1]
	v_pk_fma_f32 v[54:55], v[10:11], s[2:3], v[66:67] op_sel_hi:[1,0,1]
	v_pk_fma_f32 v[62:63], v[12:13], s[2:3], v[164:165] op_sel_hi:[1,0,1]
	v_pk_fma_f32 v[64:65], v[14:15], s[2:3], v[166:167] op_sel_hi:[1,0,1]
	v_pk_fma_f32 v[66:67], v[16:17], s[2:3], v[168:169] op_sel_hi:[1,0,1]
	v_pk_fma_f32 v[162:163], v[18:19], s[2:3], v[162:163] op_sel_hi:[1,0,1]
	v_pk_fma_f32 v[160:161], v[20:21], s[2:3], v[160:161] op_sel_hi:[1,0,1]
	v_pk_fma_f32 v[158:159], v[22:23], s[2:3], v[158:159] op_sel_hi:[1,0,1]
	v_pk_fma_f32 v[156:157], v[24:25], s[2:3], v[156:157] op_sel_hi:[1,0,1]
	v_pk_fma_f32 v[154:155], v[26:27], s[2:3], v[154:155] op_sel_hi:[1,0,1]
	v_pk_fma_f32 v[152:153], v[28:29], s[2:3], v[152:153] op_sel_hi:[1,0,1]
	v_pk_fma_f32 v[150:151], v[30:31], s[2:3], v[150:151] op_sel_hi:[1,0,1]
	v_readlane_b32 s2, v131, 27
	v_cvt_scalef32_pk32_f32_fp6 v[0:31], v[32:37], 1.0
	v_pk_fma_f32 v[164:165], v[0:1], s[2:3], v[38:39] op_sel_hi:[1,0,1]
	v_pk_fma_f32 v[166:167], v[2:3], s[2:3], v[40:41] op_sel_hi:[1,0,1]
	v_pk_fma_f32 v[168:169], v[4:5], s[2:3], v[42:43] op_sel_hi:[1,0,1]
	v_pk_fma_f32 v[170:171], v[6:7], s[2:3], v[50:51] op_sel_hi:[1,0,1]
	v_pk_fma_f32 v[172:173], v[8:9], s[2:3], v[52:53] op_sel_hi:[1,0,1]
	v_pk_fma_f32 v[174:175], v[10:11], s[2:3], v[54:55] op_sel_hi:[1,0,1]
	v_pk_fma_f32 v[176:177], v[12:13], s[2:3], v[62:63] op_sel_hi:[1,0,1]
	v_pk_fma_f32 v[178:179], v[14:15], s[2:3], v[64:65] op_sel_hi:[1,0,1]
	v_pk_fma_f32 v[180:181], v[16:17], s[2:3], v[66:67] op_sel_hi:[1,0,1]
	v_pk_fma_f32 v[162:163], v[18:19], s[2:3], v[162:163] op_sel_hi:[1,0,1]
	v_pk_fma_f32 v[160:161], v[20:21], s[2:3], v[160:161] op_sel_hi:[1,0,1]
	v_pk_fma_f32 v[158:159], v[22:23], s[2:3], v[158:159] op_sel_hi:[1,0,1]
	v_pk_fma_f32 v[156:157], v[24:25], s[2:3], v[156:157] op_sel_hi:[1,0,1]
	v_pk_fma_f32 v[154:155], v[26:27], s[2:3], v[154:155] op_sel_hi:[1,0,1]
	v_pk_fma_f32 v[152:153], v[28:29], s[2:3], v[152:153] op_sel_hi:[1,0,1]
	v_pk_fma_f32 v[150:151], v[30:31], s[2:3], v[150:151] op_sel_hi:[1,0,1]
	v_readlane_b32 s2, v241, 36
	v_readlane_b32 s3, v241, 37
	v_readlane_b32 s100, v241, 38
	v_readlane_b32 s101, v241, 39
	s_nop 1
	buffer_load_dwordx4 v[62:65], v129, s[44:47], s2 offen
	buffer_load_dwordx2 v[66:67], v210, s[44:47], s2 offen
	buffer_load_dwordx4 v[50:53], v129, s[44:47], s3 offen
	buffer_load_dwordx2 v[54:55], v210, s[44:47], s3 offen
	buffer_load_dwordx4 v[38:41], v129, s[44:47], s100 offen
	buffer_load_dwordx2 v[42:43], v210, s[44:47], s100 offen
	buffer_load_dwordx4 v[32:35], v129, s[44:47], s101 offen
	buffer_load_dwordx2 v[36:37], v210, s[44:47], s101 offen
	s_waitcnt vmcnt(16)
	v_readlane_b32 s2, v131, 28
	s_nop 0
	v_cvt_scalef32_pk32_f32_fp6 v[0:31], v[98:103], 1.0
	v_pk_fma_f32 v[98:99], v[0:1], s[2:3], v[164:165] op_sel_hi:[1,0,1]
	v_pk_fma_f32 v[100:101], v[2:3], s[2:3], v[166:167] op_sel_hi:[1,0,1]
	v_pk_fma_f32 v[102:103], v[4:5], s[2:3], v[168:169] op_sel_hi:[1,0,1]
	v_pk_fma_f32 v[164:165], v[6:7], s[2:3], v[170:171] op_sel_hi:[1,0,1]
	v_pk_fma_f32 v[166:167], v[8:9], s[2:3], v[172:173] op_sel_hi:[1,0,1]
	v_pk_fma_f32 v[168:169], v[10:11], s[2:3], v[174:175] op_sel_hi:[1,0,1]
	v_pk_fma_f32 v[170:171], v[12:13], s[2:3], v[176:177] op_sel_hi:[1,0,1]
	v_pk_fma_f32 v[172:173], v[14:15], s[2:3], v[178:179] op_sel_hi:[1,0,1]
	v_pk_fma_f32 v[174:175], v[16:17], s[2:3], v[180:181] op_sel_hi:[1,0,1]
	v_pk_fma_f32 v[162:163], v[18:19], s[2:3], v[162:163] op_sel_hi:[1,0,1]
	v_pk_fma_f32 v[160:161], v[20:21], s[2:3], v[160:161] op_sel_hi:[1,0,1]
	v_pk_fma_f32 v[158:159], v[22:23], s[2:3], v[158:159] op_sel_hi:[1,0,1]
	v_pk_fma_f32 v[156:157], v[24:25], s[2:3], v[156:157] op_sel_hi:[1,0,1]
	v_pk_fma_f32 v[154:155], v[26:27], s[2:3], v[154:155] op_sel_hi:[1,0,1]
	v_pk_fma_f32 v[152:153], v[28:29], s[2:3], v[152:153] op_sel_hi:[1,0,1]
	v_pk_fma_f32 v[150:151], v[30:31], s[2:3], v[150:151] op_sel_hi:[1,0,1]
	v_readlane_b32 s2, v131, 29
	v_cvt_scalef32_pk32_f32_fp6 v[0:31], v[92:97], 1.0
	v_pk_fma_f32 v[92:93], v[0:1], s[2:3], v[98:99] op_sel_hi:[1,0,1]
	v_pk_fma_f32 v[94:95], v[2:3], s[2:3], v[100:101] op_sel_hi:[1,0,1]
	v_pk_fma_f32 v[96:97], v[4:5], s[2:3], v[102:103] op_sel_hi:[1,0,1]
	v_pk_fma_f32 v[98:99], v[6:7], s[2:3], v[164:165] op_sel_hi:[1,0,1]
	v_pk_fma_f32 v[100:101], v[8:9], s[2:3], v[166:167] op_sel_hi:[1,0,1]
	v_pk_fma_f32 v[102:103], v[10:11], s[2:3], v[168:169] op_sel_hi:[1,0,1]
	v_pk_fma_f32 v[164:165], v[12:13], s[2:3], v[170:171] op_sel_hi:[1,0,1]
	v_pk_fma_f32 v[166:167], v[14:15], s[2:3], v[172:173] op_sel_hi:[1,0,1]
	v_pk_fma_f32 v[168:169], v[16:17], s[2:3], v[174:175] op_sel_hi:[1,0,1]
	v_pk_fma_f32 v[162:163], v[18:19], s[2:3], v[162:163] op_sel_hi:[1,0,1]
	v_pk_fma_f32 v[160:161], v[20:21], s[2:3], v[160:161] op_sel_hi:[1,0,1]
	v_pk_fma_f32 v[158:159], v[22:23], s[2:3], v[158:159] op_sel_hi:[1,0,1]
	v_pk_fma_f32 v[156:157], v[24:25], s[2:3], v[156:157] op_sel_hi:[1,0,1]
	v_pk_fma_f32 v[154:155], v[26:27], s[2:3], v[154:155] op_sel_hi:[1,0,1]
	v_pk_fma_f32 v[152:153], v[28:29], s[2:3], v[152:153] op_sel_hi:[1,0,1]
	v_pk_fma_f32 v[150:151], v[30:31], s[2:3], v[150:151] op_sel_hi:[1,0,1]
	v_readlane_b32 s2, v131, 30
	v_cvt_scalef32_pk32_f32_fp6 v[0:31], v[86:91], 1.0
	v_pk_fma_f32 v[86:87], v[0:1], s[2:3], v[92:93] op_sel_hi:[1,0,1]
	v_pk_fma_f32 v[88:89], v[2:3], s[2:3], v[94:95] op_sel_hi:[1,0,1]
	v_pk_fma_f32 v[90:91], v[4:5], s[2:3], v[96:97] op_sel_hi:[1,0,1]
	v_pk_fma_f32 v[92:93], v[6:7], s[2:3], v[98:99] op_sel_hi:[1,0,1]
	v_pk_fma_f32 v[94:95], v[8:9], s[2:3], v[100:101] op_sel_hi:[1,0,1]
	v_pk_fma_f32 v[96:97], v[10:11], s[2:3], v[102:103] op_sel_hi:[1,0,1]
	v_pk_fma_f32 v[98:99], v[12:13], s[2:3], v[164:165] op_sel_hi:[1,0,1]
	v_pk_fma_f32 v[100:101], v[14:15], s[2:3], v[166:167] op_sel_hi:[1,0,1]
	v_pk_fma_f32 v[102:103], v[16:17], s[2:3], v[168:169] op_sel_hi:[1,0,1]
	v_pk_fma_f32 v[162:163], v[18:19], s[2:3], v[162:163] op_sel_hi:[1,0,1]
	v_pk_fma_f32 v[160:161], v[20:21], s[2:3], v[160:161] op_sel_hi:[1,0,1]
	v_pk_fma_f32 v[158:159], v[22:23], s[2:3], v[158:159] op_sel_hi:[1,0,1]
	v_pk_fma_f32 v[156:157], v[24:25], s[2:3], v[156:157] op_sel_hi:[1,0,1]
	v_pk_fma_f32 v[154:155], v[26:27], s[2:3], v[154:155] op_sel_hi:[1,0,1]
	v_pk_fma_f32 v[152:153], v[28:29], s[2:3], v[152:153] op_sel_hi:[1,0,1]
	v_pk_fma_f32 v[150:151], v[30:31], s[2:3], v[150:151] op_sel_hi:[1,0,1]
	v_readlane_b32 s2, v131, 31
	v_cvt_scalef32_pk32_f32_fp6 v[0:31], v[80:85], 1.0
	v_pk_fma_f32 v[180:181], v[0:1], s[2:3], v[86:87] op_sel_hi:[1,0,1]
	v_pk_fma_f32 v[178:179], v[2:3], s[2:3], v[88:89] op_sel_hi:[1,0,1]
	v_pk_fma_f32 v[176:177], v[4:5], s[2:3], v[90:91] op_sel_hi:[1,0,1]
	v_pk_fma_f32 v[174:175], v[6:7], s[2:3], v[92:93] op_sel_hi:[1,0,1]
	v_pk_fma_f32 v[172:173], v[8:9], s[2:3], v[94:95] op_sel_hi:[1,0,1]
	v_pk_fma_f32 v[170:171], v[10:11], s[2:3], v[96:97] op_sel_hi:[1,0,1]
	v_pk_fma_f32 v[168:169], v[12:13], s[2:3], v[98:99] op_sel_hi:[1,0,1]
	v_pk_fma_f32 v[166:167], v[14:15], s[2:3], v[100:101] op_sel_hi:[1,0,1]
	v_pk_fma_f32 v[164:165], v[16:17], s[2:3], v[102:103] op_sel_hi:[1,0,1]
	v_pk_fma_f32 v[162:163], v[18:19], s[2:3], v[162:163] op_sel_hi:[1,0,1]
	v_pk_fma_f32 v[160:161], v[20:21], s[2:3], v[160:161] op_sel_hi:[1,0,1]
	v_pk_fma_f32 v[158:159], v[22:23], s[2:3], v[158:159] op_sel_hi:[1,0,1]
	v_pk_fma_f32 v[156:157], v[24:25], s[2:3], v[156:157] op_sel_hi:[1,0,1]
	v_pk_fma_f32 v[154:155], v[26:27], s[2:3], v[154:155] op_sel_hi:[1,0,1]
	v_pk_fma_f32 v[152:153], v[28:29], s[2:3], v[152:153] op_sel_hi:[1,0,1]
	v_pk_fma_f32 v[150:151], v[30:31], s[2:3], v[150:151] op_sel_hi:[1,0,1]
	v_readlane_b32 s2, v241, 40
	v_readlane_b32 s3, v241, 41
	v_readlane_b32 s100, v241, 42
	v_readlane_b32 s101, v241, 43
	s_nop 1
	buffer_load_dwordx4 v[98:101], v129, s[44:47], s2 offen
	buffer_load_dwordx2 v[102:103], v210, s[44:47], s2 offen
	buffer_load_dwordx4 v[92:95], v129, s[44:47], s3 offen
	buffer_load_dwordx2 v[96:97], v210, s[44:47], s3 offen
	buffer_load_dwordx4 v[86:89], v129, s[44:47], s100 offen
	buffer_load_dwordx2 v[90:91], v210, s[44:47], s100 offen
	buffer_load_dwordx4 v[80:83], v129, s[44:47], s101 offen
	buffer_load_dwordx2 v[84:85], v210, s[44:47], s101 offen
	s_waitcnt vmcnt(16)
	v_readlane_b32 s2, v131, 32
	s_nop 0
	v_cvt_scalef32_pk32_f32_fp6 v[0:31], v[74:79], 1.0
	v_pk_fma_f32 v[74:75], v[0:1], s[2:3], v[180:181] op_sel_hi:[1,0,1]
	v_pk_fma_f32 v[76:77], v[2:3], s[2:3], v[178:179] op_sel_hi:[1,0,1]
	v_pk_fma_f32 v[78:79], v[4:5], s[2:3], v[176:177] op_sel_hi:[1,0,1]
	v_pk_fma_f32 v[174:175], v[6:7], s[2:3], v[174:175] op_sel_hi:[1,0,1]
	v_pk_fma_f32 v[172:173], v[8:9], s[2:3], v[172:173] op_sel_hi:[1,0,1]
	v_pk_fma_f32 v[170:171], v[10:11], s[2:3], v[170:171] op_sel_hi:[1,0,1]
	v_pk_fma_f32 v[168:169], v[12:13], s[2:3], v[168:169] op_sel_hi:[1,0,1]
	v_pk_fma_f32 v[166:167], v[14:15], s[2:3], v[166:167] op_sel_hi:[1,0,1]
	v_pk_fma_f32 v[164:165], v[16:17], s[2:3], v[164:165] op_sel_hi:[1,0,1]
	v_pk_fma_f32 v[162:163], v[18:19], s[2:3], v[162:163] op_sel_hi:[1,0,1]
	v_pk_fma_f32 v[160:161], v[20:21], s[2:3], v[160:161] op_sel_hi:[1,0,1]
	v_pk_fma_f32 v[158:159], v[22:23], s[2:3], v[158:159] op_sel_hi:[1,0,1]
	v_pk_fma_f32 v[156:157], v[24:25], s[2:3], v[156:157] op_sel_hi:[1,0,1]
	v_pk_fma_f32 v[154:155], v[26:27], s[2:3], v[154:155] op_sel_hi:[1,0,1]
	v_pk_fma_f32 v[152:153], v[28:29], s[2:3], v[152:153] op_sel_hi:[1,0,1]
	v_pk_fma_f32 v[150:151], v[30:31], s[2:3], v[150:151] op_sel_hi:[1,0,1]
	v_readlane_b32 s2, v131, 33
	v_cvt_scalef32_pk32_f32_fp6 v[0:31], v[68:73], 1.0
	v_pk_fma_f32 v[68:69], v[0:1], s[2:3], v[74:75] op_sel_hi:[1,0,1]
	v_pk_fma_f32 v[70:71], v[2:3], s[2:3], v[76:77] op_sel_hi:[1,0,1]
	v_pk_fma_f32 v[72:73], v[4:5], s[2:3], v[78:79] op_sel_hi:[1,0,1]
	v_pk_fma_f32 v[74:75], v[6:7], s[2:3], v[174:175] op_sel_hi:[1,0,1]
	v_pk_fma_f32 v[76:77], v[8:9], s[2:3], v[172:173] op_sel_hi:[1,0,1]
	v_pk_fma_f32 v[78:79], v[10:11], s[2:3], v[170:171] op_sel_hi:[1,0,1]
	v_pk_fma_f32 v[168:169], v[12:13], s[2:3], v[168:169] op_sel_hi:[1,0,1]
	v_pk_fma_f32 v[166:167], v[14:15], s[2:3], v[166:167] op_sel_hi:[1,0,1]
	v_pk_fma_f32 v[164:165], v[16:17], s[2:3], v[164:165] op_sel_hi:[1,0,1]
	v_pk_fma_f32 v[162:163], v[18:19], s[2:3], v[162:163] op_sel_hi:[1,0,1]
	v_pk_fma_f32 v[160:161], v[20:21], s[2:3], v[160:161] op_sel_hi:[1,0,1]
	v_pk_fma_f32 v[158:159], v[22:23], s[2:3], v[158:159] op_sel_hi:[1,0,1]
	v_pk_fma_f32 v[156:157], v[24:25], s[2:3], v[156:157] op_sel_hi:[1,0,1]
	v_pk_fma_f32 v[154:155], v[26:27], s[2:3], v[154:155] op_sel_hi:[1,0,1]
	v_pk_fma_f32 v[152:153], v[28:29], s[2:3], v[152:153] op_sel_hi:[1,0,1]
	v_pk_fma_f32 v[150:151], v[30:31], s[2:3], v[150:151] op_sel_hi:[1,0,1]
	v_readlane_b32 s2, v131, 34
	v_cvt_scalef32_pk32_f32_fp6 v[0:31], v[56:61], 1.0
	v_pk_fma_f32 v[56:57], v[0:1], s[2:3], v[68:69] op_sel_hi:[1,0,1]
	v_pk_fma_f32 v[58:59], v[2:3], s[2:3], v[70:71] op_sel_hi:[1,0,1]
	v_pk_fma_f32 v[60:61], v[4:5], s[2:3], v[72:73] op_sel_hi:[1,0,1]
	v_pk_fma_f32 v[68:69], v[6:7], s[2:3], v[74:75] op_sel_hi:[1,0,1]
	v_pk_fma_f32 v[70:71], v[8:9], s[2:3], v[76:77] op_sel_hi:[1,0,1]
	v_pk_fma_f32 v[72:73], v[10:11], s[2:3], v[78:79] op_sel_hi:[1,0,1]
	v_pk_fma_f32 v[74:75], v[12:13], s[2:3], v[168:169] op_sel_hi:[1,0,1]
	v_pk_fma_f32 v[76:77], v[14:15], s[2:3], v[166:167] op_sel_hi:[1,0,1]
	v_pk_fma_f32 v[78:79], v[16:17], s[2:3], v[164:165] op_sel_hi:[1,0,1]
	v_pk_fma_f32 v[162:163], v[18:19], s[2:3], v[162:163] op_sel_hi:[1,0,1]
	v_pk_fma_f32 v[160:161], v[20:21], s[2:3], v[160:161] op_sel_hi:[1,0,1]
	v_pk_fma_f32 v[158:159], v[22:23], s[2:3], v[158:159] op_sel_hi:[1,0,1]
	v_pk_fma_f32 v[156:157], v[24:25], s[2:3], v[156:157] op_sel_hi:[1,0,1]
	v_pk_fma_f32 v[154:155], v[26:27], s[2:3], v[154:155] op_sel_hi:[1,0,1]
	v_pk_fma_f32 v[152:153], v[28:29], s[2:3], v[152:153] op_sel_hi:[1,0,1]
	v_pk_fma_f32 v[150:151], v[30:31], s[2:3], v[150:151] op_sel_hi:[1,0,1]
	v_readlane_b32 s2, v131, 35
	v_cvt_scalef32_pk32_f32_fp6 v[0:31], v[44:49], 1.0
	v_pk_fma_f32 v[164:165], v[0:1], s[2:3], v[56:57] op_sel_hi:[1,0,1]
	v_pk_fma_f32 v[166:167], v[2:3], s[2:3], v[58:59] op_sel_hi:[1,0,1]
	v_pk_fma_f32 v[168:169], v[4:5], s[2:3], v[60:61] op_sel_hi:[1,0,1]
	v_pk_fma_f32 v[170:171], v[6:7], s[2:3], v[68:69] op_sel_hi:[1,0,1]
	v_pk_fma_f32 v[172:173], v[8:9], s[2:3], v[70:71] op_sel_hi:[1,0,1]
	v_pk_fma_f32 v[174:175], v[10:11], s[2:3], v[72:73] op_sel_hi:[1,0,1]
	v_pk_fma_f32 v[176:177], v[12:13], s[2:3], v[74:75] op_sel_hi:[1,0,1]
	v_pk_fma_f32 v[178:179], v[14:15], s[2:3], v[76:77] op_sel_hi:[1,0,1]
	v_pk_fma_f32 v[180:181], v[16:17], s[2:3], v[78:79] op_sel_hi:[1,0,1]
	v_pk_fma_f32 v[162:163], v[18:19], s[2:3], v[162:163] op_sel_hi:[1,0,1]
	v_pk_fma_f32 v[160:161], v[20:21], s[2:3], v[160:161] op_sel_hi:[1,0,1]
	v_pk_fma_f32 v[158:159], v[22:23], s[2:3], v[158:159] op_sel_hi:[1,0,1]
	v_pk_fma_f32 v[156:157], v[24:25], s[2:3], v[156:157] op_sel_hi:[1,0,1]
	v_pk_fma_f32 v[154:155], v[26:27], s[2:3], v[154:155] op_sel_hi:[1,0,1]
	v_pk_fma_f32 v[152:153], v[28:29], s[2:3], v[152:153] op_sel_hi:[1,0,1]
	v_pk_fma_f32 v[150:151], v[30:31], s[2:3], v[150:151] op_sel_hi:[1,0,1]
	v_readlane_b32 s2, v241, 44
	v_readlane_b32 s3, v241, 45
	v_readlane_b32 s100, v241, 46
	v_readlane_b32 s101, v241, 47
	s_nop 1
	buffer_load_dwordx4 v[74:77], v129, s[44:47], s2 offen
	buffer_load_dwordx2 v[78:79], v210, s[44:47], s2 offen
	buffer_load_dwordx4 v[68:71], v129, s[44:47], s3 offen
	buffer_load_dwordx2 v[72:73], v210, s[44:47], s3 offen
	buffer_load_dwordx4 v[56:59], v129, s[44:47], s100 offen
	buffer_load_dwordx2 v[60:61], v210, s[44:47], s100 offen
	buffer_load_dwordx4 v[44:47], v129, s[44:47], s101 offen
	buffer_load_dwordx2 v[48:49], v210, s[44:47], s101 offen
	s_waitcnt vmcnt(16)
	v_readlane_b32 s2, v131, 36
	s_nop 0
	v_cvt_scalef32_pk32_f32_fp6 v[0:31], v[62:67], 1.0
	v_pk_fma_f32 v[62:63], v[0:1], s[2:3], v[164:165] op_sel_hi:[1,0,1]
	v_pk_fma_f32 v[64:65], v[2:3], s[2:3], v[166:167] op_sel_hi:[1,0,1]
	v_pk_fma_f32 v[66:67], v[4:5], s[2:3], v[168:169] op_sel_hi:[1,0,1]
	v_pk_fma_f32 v[164:165], v[6:7], s[2:3], v[170:171] op_sel_hi:[1,0,1]
	v_pk_fma_f32 v[166:167], v[8:9], s[2:3], v[172:173] op_sel_hi:[1,0,1]
	v_pk_fma_f32 v[168:169], v[10:11], s[2:3], v[174:175] op_sel_hi:[1,0,1]
	v_pk_fma_f32 v[170:171], v[12:13], s[2:3], v[176:177] op_sel_hi:[1,0,1]
	v_pk_fma_f32 v[172:173], v[14:15], s[2:3], v[178:179] op_sel_hi:[1,0,1]
	v_pk_fma_f32 v[174:175], v[16:17], s[2:3], v[180:181] op_sel_hi:[1,0,1]
	v_pk_fma_f32 v[162:163], v[18:19], s[2:3], v[162:163] op_sel_hi:[1,0,1]
	v_pk_fma_f32 v[160:161], v[20:21], s[2:3], v[160:161] op_sel_hi:[1,0,1]
	v_pk_fma_f32 v[158:159], v[22:23], s[2:3], v[158:159] op_sel_hi:[1,0,1]
	v_pk_fma_f32 v[156:157], v[24:25], s[2:3], v[156:157] op_sel_hi:[1,0,1]
	v_pk_fma_f32 v[154:155], v[26:27], s[2:3], v[154:155] op_sel_hi:[1,0,1]
	v_pk_fma_f32 v[152:153], v[28:29], s[2:3], v[152:153] op_sel_hi:[1,0,1]
	v_pk_fma_f32 v[150:151], v[30:31], s[2:3], v[150:151] op_sel_hi:[1,0,1]
	v_readlane_b32 s2, v131, 37
	v_cvt_scalef32_pk32_f32_fp6 v[0:31], v[50:55], 1.0
	v_pk_fma_f32 v[50:51], v[0:1], s[2:3], v[62:63] op_sel_hi:[1,0,1]
	v_pk_fma_f32 v[52:53], v[2:3], s[2:3], v[64:65] op_sel_hi:[1,0,1]
	v_pk_fma_f32 v[54:55], v[4:5], s[2:3], v[66:67] op_sel_hi:[1,0,1]
	v_pk_fma_f32 v[62:63], v[6:7], s[2:3], v[164:165] op_sel_hi:[1,0,1]
	v_pk_fma_f32 v[64:65], v[8:9], s[2:3], v[166:167] op_sel_hi:[1,0,1]
	v_pk_fma_f32 v[66:67], v[10:11], s[2:3], v[168:169] op_sel_hi:[1,0,1]
	v_pk_fma_f32 v[164:165], v[12:13], s[2:3], v[170:171] op_sel_hi:[1,0,1]
	v_pk_fma_f32 v[166:167], v[14:15], s[2:3], v[172:173] op_sel_hi:[1,0,1]
	v_pk_fma_f32 v[168:169], v[16:17], s[2:3], v[174:175] op_sel_hi:[1,0,1]
	v_pk_fma_f32 v[162:163], v[18:19], s[2:3], v[162:163] op_sel_hi:[1,0,1]
	v_pk_fma_f32 v[160:161], v[20:21], s[2:3], v[160:161] op_sel_hi:[1,0,1]
	v_pk_fma_f32 v[158:159], v[22:23], s[2:3], v[158:159] op_sel_hi:[1,0,1]
	v_pk_fma_f32 v[156:157], v[24:25], s[2:3], v[156:157] op_sel_hi:[1,0,1]
	v_pk_fma_f32 v[154:155], v[26:27], s[2:3], v[154:155] op_sel_hi:[1,0,1]
	v_pk_fma_f32 v[152:153], v[28:29], s[2:3], v[152:153] op_sel_hi:[1,0,1]
	v_pk_fma_f32 v[150:151], v[30:31], s[2:3], v[150:151] op_sel_hi:[1,0,1]
	v_readlane_b32 s2, v131, 38
	v_cvt_scalef32_pk32_f32_fp6 v[0:31], v[38:43], 1.0
	v_pk_fma_f32 v[38:39], v[0:1], s[2:3], v[50:51] op_sel_hi:[1,0,1]
	v_pk_fma_f32 v[40:41], v[2:3], s[2:3], v[52:53] op_sel_hi:[1,0,1]
	v_pk_fma_f32 v[42:43], v[4:5], s[2:3], v[54:55] op_sel_hi:[1,0,1]
	v_pk_fma_f32 v[50:51], v[6:7], s[2:3], v[62:63] op_sel_hi:[1,0,1]
	v_pk_fma_f32 v[52:53], v[8:9], s[2:3], v[64:65] op_sel_hi:[1,0,1]
	v_pk_fma_f32 v[54:55], v[10:11], s[2:3], v[66:67] op_sel_hi:[1,0,1]
	v_pk_fma_f32 v[62:63], v[12:13], s[2:3], v[164:165] op_sel_hi:[1,0,1]
	v_pk_fma_f32 v[64:65], v[14:15], s[2:3], v[166:167] op_sel_hi:[1,0,1]
	v_pk_fma_f32 v[66:67], v[16:17], s[2:3], v[168:169] op_sel_hi:[1,0,1]
	v_pk_fma_f32 v[162:163], v[18:19], s[2:3], v[162:163] op_sel_hi:[1,0,1]
	v_pk_fma_f32 v[160:161], v[20:21], s[2:3], v[160:161] op_sel_hi:[1,0,1]
	v_pk_fma_f32 v[158:159], v[22:23], s[2:3], v[158:159] op_sel_hi:[1,0,1]
	v_pk_fma_f32 v[156:157], v[24:25], s[2:3], v[156:157] op_sel_hi:[1,0,1]
	v_pk_fma_f32 v[154:155], v[26:27], s[2:3], v[154:155] op_sel_hi:[1,0,1]
	v_pk_fma_f32 v[152:153], v[28:29], s[2:3], v[152:153] op_sel_hi:[1,0,1]
	v_pk_fma_f32 v[150:151], v[30:31], s[2:3], v[150:151] op_sel_hi:[1,0,1]
	v_readlane_b32 s2, v131, 39
	v_cvt_scalef32_pk32_f32_fp6 v[0:31], v[32:37], 1.0
	v_pk_fma_f32 v[164:165], v[0:1], s[2:3], v[38:39] op_sel_hi:[1,0,1]
	v_pk_fma_f32 v[166:167], v[2:3], s[2:3], v[40:41] op_sel_hi:[1,0,1]
	v_pk_fma_f32 v[168:169], v[4:5], s[2:3], v[42:43] op_sel_hi:[1,0,1]
	v_pk_fma_f32 v[170:171], v[6:7], s[2:3], v[50:51] op_sel_hi:[1,0,1]
	v_pk_fma_f32 v[172:173], v[8:9], s[2:3], v[52:53] op_sel_hi:[1,0,1]
	v_pk_fma_f32 v[174:175], v[10:11], s[2:3], v[54:55] op_sel_hi:[1,0,1]
	v_pk_fma_f32 v[176:177], v[12:13], s[2:3], v[62:63] op_sel_hi:[1,0,1]
	v_pk_fma_f32 v[178:179], v[14:15], s[2:3], v[64:65] op_sel_hi:[1,0,1]
	v_pk_fma_f32 v[180:181], v[16:17], s[2:3], v[66:67] op_sel_hi:[1,0,1]
	v_pk_fma_f32 v[162:163], v[18:19], s[2:3], v[162:163] op_sel_hi:[1,0,1]
	v_pk_fma_f32 v[160:161], v[20:21], s[2:3], v[160:161] op_sel_hi:[1,0,1]
	v_pk_fma_f32 v[158:159], v[22:23], s[2:3], v[158:159] op_sel_hi:[1,0,1]
	v_pk_fma_f32 v[156:157], v[24:25], s[2:3], v[156:157] op_sel_hi:[1,0,1]
	v_pk_fma_f32 v[154:155], v[26:27], s[2:3], v[154:155] op_sel_hi:[1,0,1]
	v_pk_fma_f32 v[152:153], v[28:29], s[2:3], v[152:153] op_sel_hi:[1,0,1]
	v_pk_fma_f32 v[150:151], v[30:31], s[2:3], v[150:151] op_sel_hi:[1,0,1]
	v_readlane_b32 s2, v241, 48
	v_readlane_b32 s3, v241, 49
	v_readlane_b32 s100, v241, 50
	v_readlane_b32 s101, v241, 51
	s_nop 1
	buffer_load_dwordx4 v[62:65], v129, s[44:47], s2 offen
	buffer_load_dwordx2 v[66:67], v210, s[44:47], s2 offen
	buffer_load_dwordx4 v[50:53], v129, s[44:47], s3 offen
	buffer_load_dwordx2 v[54:55], v210, s[44:47], s3 offen
	buffer_load_dwordx4 v[38:41], v129, s[44:47], s100 offen
	buffer_load_dwordx2 v[42:43], v210, s[44:47], s100 offen
	buffer_load_dwordx4 v[32:35], v129, s[44:47], s101 offen
	buffer_load_dwordx2 v[36:37], v210, s[44:47], s101 offen
	s_waitcnt vmcnt(16)
	v_readlane_b32 s2, v131, 40
	s_nop 0
	v_cvt_scalef32_pk32_f32_fp6 v[0:31], v[98:103], 1.0
	v_pk_fma_f32 v[98:99], v[0:1], s[2:3], v[164:165] op_sel_hi:[1,0,1]
	v_pk_fma_f32 v[100:101], v[2:3], s[2:3], v[166:167] op_sel_hi:[1,0,1]
	v_pk_fma_f32 v[102:103], v[4:5], s[2:3], v[168:169] op_sel_hi:[1,0,1]
	v_pk_fma_f32 v[164:165], v[6:7], s[2:3], v[170:171] op_sel_hi:[1,0,1]
	v_pk_fma_f32 v[166:167], v[8:9], s[2:3], v[172:173] op_sel_hi:[1,0,1]
	v_pk_fma_f32 v[168:169], v[10:11], s[2:3], v[174:175] op_sel_hi:[1,0,1]
	v_pk_fma_f32 v[170:171], v[12:13], s[2:3], v[176:177] op_sel_hi:[1,0,1]
	v_pk_fma_f32 v[172:173], v[14:15], s[2:3], v[178:179] op_sel_hi:[1,0,1]
	v_pk_fma_f32 v[174:175], v[16:17], s[2:3], v[180:181] op_sel_hi:[1,0,1]
	v_pk_fma_f32 v[162:163], v[18:19], s[2:3], v[162:163] op_sel_hi:[1,0,1]
	v_pk_fma_f32 v[160:161], v[20:21], s[2:3], v[160:161] op_sel_hi:[1,0,1]
	v_pk_fma_f32 v[158:159], v[22:23], s[2:3], v[158:159] op_sel_hi:[1,0,1]
	v_pk_fma_f32 v[156:157], v[24:25], s[2:3], v[156:157] op_sel_hi:[1,0,1]
	v_pk_fma_f32 v[154:155], v[26:27], s[2:3], v[154:155] op_sel_hi:[1,0,1]
	v_pk_fma_f32 v[152:153], v[28:29], s[2:3], v[152:153] op_sel_hi:[1,0,1]
	v_pk_fma_f32 v[150:151], v[30:31], s[2:3], v[150:151] op_sel_hi:[1,0,1]
	v_readlane_b32 s2, v131, 41
	v_cvt_scalef32_pk32_f32_fp6 v[0:31], v[92:97], 1.0
	v_pk_fma_f32 v[92:93], v[0:1], s[2:3], v[98:99] op_sel_hi:[1,0,1]
	v_pk_fma_f32 v[94:95], v[2:3], s[2:3], v[100:101] op_sel_hi:[1,0,1]
	v_pk_fma_f32 v[96:97], v[4:5], s[2:3], v[102:103] op_sel_hi:[1,0,1]
	v_pk_fma_f32 v[98:99], v[6:7], s[2:3], v[164:165] op_sel_hi:[1,0,1]
	v_pk_fma_f32 v[100:101], v[8:9], s[2:3], v[166:167] op_sel_hi:[1,0,1]
	v_pk_fma_f32 v[102:103], v[10:11], s[2:3], v[168:169] op_sel_hi:[1,0,1]
	v_pk_fma_f32 v[164:165], v[12:13], s[2:3], v[170:171] op_sel_hi:[1,0,1]
	v_pk_fma_f32 v[166:167], v[14:15], s[2:3], v[172:173] op_sel_hi:[1,0,1]
	v_pk_fma_f32 v[168:169], v[16:17], s[2:3], v[174:175] op_sel_hi:[1,0,1]
	v_pk_fma_f32 v[162:163], v[18:19], s[2:3], v[162:163] op_sel_hi:[1,0,1]
	v_pk_fma_f32 v[160:161], v[20:21], s[2:3], v[160:161] op_sel_hi:[1,0,1]
	v_pk_fma_f32 v[158:159], v[22:23], s[2:3], v[158:159] op_sel_hi:[1,0,1]
	v_pk_fma_f32 v[156:157], v[24:25], s[2:3], v[156:157] op_sel_hi:[1,0,1]
	v_pk_fma_f32 v[154:155], v[26:27], s[2:3], v[154:155] op_sel_hi:[1,0,1]
	v_pk_fma_f32 v[152:153], v[28:29], s[2:3], v[152:153] op_sel_hi:[1,0,1]
	v_pk_fma_f32 v[150:151], v[30:31], s[2:3], v[150:151] op_sel_hi:[1,0,1]
	v_readlane_b32 s2, v131, 42
	v_cvt_scalef32_pk32_f32_fp6 v[0:31], v[86:91], 1.0
	v_pk_fma_f32 v[86:87], v[0:1], s[2:3], v[92:93] op_sel_hi:[1,0,1]
	v_pk_fma_f32 v[88:89], v[2:3], s[2:3], v[94:95] op_sel_hi:[1,0,1]
	v_pk_fma_f32 v[90:91], v[4:5], s[2:3], v[96:97] op_sel_hi:[1,0,1]
	v_pk_fma_f32 v[92:93], v[6:7], s[2:3], v[98:99] op_sel_hi:[1,0,1]
	v_pk_fma_f32 v[94:95], v[8:9], s[2:3], v[100:101] op_sel_hi:[1,0,1]
	v_pk_fma_f32 v[96:97], v[10:11], s[2:3], v[102:103] op_sel_hi:[1,0,1]
	v_pk_fma_f32 v[98:99], v[12:13], s[2:3], v[164:165] op_sel_hi:[1,0,1]
	v_pk_fma_f32 v[100:101], v[14:15], s[2:3], v[166:167] op_sel_hi:[1,0,1]
	v_pk_fma_f32 v[102:103], v[16:17], s[2:3], v[168:169] op_sel_hi:[1,0,1]
	v_pk_fma_f32 v[162:163], v[18:19], s[2:3], v[162:163] op_sel_hi:[1,0,1]
	v_pk_fma_f32 v[160:161], v[20:21], s[2:3], v[160:161] op_sel_hi:[1,0,1]
	v_pk_fma_f32 v[158:159], v[22:23], s[2:3], v[158:159] op_sel_hi:[1,0,1]
	v_pk_fma_f32 v[156:157], v[24:25], s[2:3], v[156:157] op_sel_hi:[1,0,1]
	v_pk_fma_f32 v[154:155], v[26:27], s[2:3], v[154:155] op_sel_hi:[1,0,1]
	v_pk_fma_f32 v[152:153], v[28:29], s[2:3], v[152:153] op_sel_hi:[1,0,1]
	v_pk_fma_f32 v[150:151], v[30:31], s[2:3], v[150:151] op_sel_hi:[1,0,1]
	v_readlane_b32 s2, v131, 43
	v_cvt_scalef32_pk32_f32_fp6 v[0:31], v[80:85], 1.0
	v_pk_fma_f32 v[180:181], v[0:1], s[2:3], v[86:87] op_sel_hi:[1,0,1]
	v_pk_fma_f32 v[178:179], v[2:3], s[2:3], v[88:89] op_sel_hi:[1,0,1]
	v_pk_fma_f32 v[176:177], v[4:5], s[2:3], v[90:91] op_sel_hi:[1,0,1]
	v_pk_fma_f32 v[174:175], v[6:7], s[2:3], v[92:93] op_sel_hi:[1,0,1]
	v_pk_fma_f32 v[172:173], v[8:9], s[2:3], v[94:95] op_sel_hi:[1,0,1]
	v_pk_fma_f32 v[170:171], v[10:11], s[2:3], v[96:97] op_sel_hi:[1,0,1]
	v_pk_fma_f32 v[168:169], v[12:13], s[2:3], v[98:99] op_sel_hi:[1,0,1]
	v_pk_fma_f32 v[166:167], v[14:15], s[2:3], v[100:101] op_sel_hi:[1,0,1]
	v_pk_fma_f32 v[164:165], v[16:17], s[2:3], v[102:103] op_sel_hi:[1,0,1]
	v_pk_fma_f32 v[162:163], v[18:19], s[2:3], v[162:163] op_sel_hi:[1,0,1]
	v_pk_fma_f32 v[160:161], v[20:21], s[2:3], v[160:161] op_sel_hi:[1,0,1]
	v_pk_fma_f32 v[158:159], v[22:23], s[2:3], v[158:159] op_sel_hi:[1,0,1]
	v_pk_fma_f32 v[156:157], v[24:25], s[2:3], v[156:157] op_sel_hi:[1,0,1]
	v_pk_fma_f32 v[154:155], v[26:27], s[2:3], v[154:155] op_sel_hi:[1,0,1]
	v_pk_fma_f32 v[152:153], v[28:29], s[2:3], v[152:153] op_sel_hi:[1,0,1]
	v_pk_fma_f32 v[150:151], v[30:31], s[2:3], v[150:151] op_sel_hi:[1,0,1]
	v_readlane_b32 s2, v241, 52
	v_readlane_b32 s3, v241, 53
	v_readlane_b32 s100, v241, 54
	v_readlane_b32 s101, v241, 55
	s_nop 1
	buffer_load_dwordx4 v[98:101], v129, s[44:47], s2 offen
	buffer_load_dwordx2 v[102:103], v210, s[44:47], s2 offen
	buffer_load_dwordx4 v[92:95], v129, s[44:47], s3 offen
	buffer_load_dwordx2 v[96:97], v210, s[44:47], s3 offen
	buffer_load_dwordx4 v[86:89], v129, s[44:47], s100 offen
	buffer_load_dwordx2 v[90:91], v210, s[44:47], s100 offen
	buffer_load_dwordx4 v[80:83], v129, s[44:47], s101 offen
	buffer_load_dwordx2 v[84:85], v210, s[44:47], s101 offen
	s_waitcnt vmcnt(16)
	v_readlane_b32 s2, v131, 44
	s_nop 0
	v_cvt_scalef32_pk32_f32_fp6 v[0:31], v[74:79], 1.0
	v_pk_fma_f32 v[74:75], v[0:1], s[2:3], v[180:181] op_sel_hi:[1,0,1]
	v_pk_fma_f32 v[76:77], v[2:3], s[2:3], v[178:179] op_sel_hi:[1,0,1]
	v_pk_fma_f32 v[78:79], v[4:5], s[2:3], v[176:177] op_sel_hi:[1,0,1]
	v_pk_fma_f32 v[174:175], v[6:7], s[2:3], v[174:175] op_sel_hi:[1,0,1]
	v_pk_fma_f32 v[172:173], v[8:9], s[2:3], v[172:173] op_sel_hi:[1,0,1]
	v_pk_fma_f32 v[170:171], v[10:11], s[2:3], v[170:171] op_sel_hi:[1,0,1]
	v_pk_fma_f32 v[168:169], v[12:13], s[2:3], v[168:169] op_sel_hi:[1,0,1]
	v_pk_fma_f32 v[166:167], v[14:15], s[2:3], v[166:167] op_sel_hi:[1,0,1]
	v_pk_fma_f32 v[164:165], v[16:17], s[2:3], v[164:165] op_sel_hi:[1,0,1]
	v_pk_fma_f32 v[162:163], v[18:19], s[2:3], v[162:163] op_sel_hi:[1,0,1]
	v_pk_fma_f32 v[160:161], v[20:21], s[2:3], v[160:161] op_sel_hi:[1,0,1]
	v_pk_fma_f32 v[158:159], v[22:23], s[2:3], v[158:159] op_sel_hi:[1,0,1]
	v_pk_fma_f32 v[156:157], v[24:25], s[2:3], v[156:157] op_sel_hi:[1,0,1]
	v_pk_fma_f32 v[154:155], v[26:27], s[2:3], v[154:155] op_sel_hi:[1,0,1]
	v_pk_fma_f32 v[152:153], v[28:29], s[2:3], v[152:153] op_sel_hi:[1,0,1]
	v_pk_fma_f32 v[150:151], v[30:31], s[2:3], v[150:151] op_sel_hi:[1,0,1]
	v_readlane_b32 s2, v131, 45
	v_cvt_scalef32_pk32_f32_fp6 v[0:31], v[68:73], 1.0
	v_pk_fma_f32 v[68:69], v[0:1], s[2:3], v[74:75] op_sel_hi:[1,0,1]
	v_pk_fma_f32 v[70:71], v[2:3], s[2:3], v[76:77] op_sel_hi:[1,0,1]
	v_pk_fma_f32 v[72:73], v[4:5], s[2:3], v[78:79] op_sel_hi:[1,0,1]
	v_pk_fma_f32 v[74:75], v[6:7], s[2:3], v[174:175] op_sel_hi:[1,0,1]
	v_pk_fma_f32 v[76:77], v[8:9], s[2:3], v[172:173] op_sel_hi:[1,0,1]
	v_pk_fma_f32 v[78:79], v[10:11], s[2:3], v[170:171] op_sel_hi:[1,0,1]
	v_pk_fma_f32 v[168:169], v[12:13], s[2:3], v[168:169] op_sel_hi:[1,0,1]
	v_pk_fma_f32 v[166:167], v[14:15], s[2:3], v[166:167] op_sel_hi:[1,0,1]
	v_pk_fma_f32 v[164:165], v[16:17], s[2:3], v[164:165] op_sel_hi:[1,0,1]
	v_pk_fma_f32 v[162:163], v[18:19], s[2:3], v[162:163] op_sel_hi:[1,0,1]
	v_pk_fma_f32 v[160:161], v[20:21], s[2:3], v[160:161] op_sel_hi:[1,0,1]
	v_pk_fma_f32 v[158:159], v[22:23], s[2:3], v[158:159] op_sel_hi:[1,0,1]
	v_pk_fma_f32 v[156:157], v[24:25], s[2:3], v[156:157] op_sel_hi:[1,0,1]
	v_pk_fma_f32 v[154:155], v[26:27], s[2:3], v[154:155] op_sel_hi:[1,0,1]
	v_pk_fma_f32 v[152:153], v[28:29], s[2:3], v[152:153] op_sel_hi:[1,0,1]
	v_pk_fma_f32 v[150:151], v[30:31], s[2:3], v[150:151] op_sel_hi:[1,0,1]
	v_readlane_b32 s2, v131, 46
	v_cvt_scalef32_pk32_f32_fp6 v[0:31], v[56:61], 1.0
	v_pk_fma_f32 v[56:57], v[0:1], s[2:3], v[68:69] op_sel_hi:[1,0,1]
	v_pk_fma_f32 v[58:59], v[2:3], s[2:3], v[70:71] op_sel_hi:[1,0,1]
	v_pk_fma_f32 v[60:61], v[4:5], s[2:3], v[72:73] op_sel_hi:[1,0,1]
	v_pk_fma_f32 v[68:69], v[6:7], s[2:3], v[74:75] op_sel_hi:[1,0,1]
	v_pk_fma_f32 v[70:71], v[8:9], s[2:3], v[76:77] op_sel_hi:[1,0,1]
	v_pk_fma_f32 v[72:73], v[10:11], s[2:3], v[78:79] op_sel_hi:[1,0,1]
	v_pk_fma_f32 v[74:75], v[12:13], s[2:3], v[168:169] op_sel_hi:[1,0,1]
	v_pk_fma_f32 v[76:77], v[14:15], s[2:3], v[166:167] op_sel_hi:[1,0,1]
	v_pk_fma_f32 v[78:79], v[16:17], s[2:3], v[164:165] op_sel_hi:[1,0,1]
	v_pk_fma_f32 v[162:163], v[18:19], s[2:3], v[162:163] op_sel_hi:[1,0,1]
	v_pk_fma_f32 v[160:161], v[20:21], s[2:3], v[160:161] op_sel_hi:[1,0,1]
	v_pk_fma_f32 v[158:159], v[22:23], s[2:3], v[158:159] op_sel_hi:[1,0,1]
	v_pk_fma_f32 v[156:157], v[24:25], s[2:3], v[156:157] op_sel_hi:[1,0,1]
	v_pk_fma_f32 v[154:155], v[26:27], s[2:3], v[154:155] op_sel_hi:[1,0,1]
	v_pk_fma_f32 v[152:153], v[28:29], s[2:3], v[152:153] op_sel_hi:[1,0,1]
	v_pk_fma_f32 v[150:151], v[30:31], s[2:3], v[150:151] op_sel_hi:[1,0,1]
	v_readlane_b32 s2, v131, 47
	v_cvt_scalef32_pk32_f32_fp6 v[0:31], v[44:49], 1.0
	v_pk_fma_f32 v[164:165], v[0:1], s[2:3], v[56:57] op_sel_hi:[1,0,1]
	v_pk_fma_f32 v[166:167], v[2:3], s[2:3], v[58:59] op_sel_hi:[1,0,1]
	v_pk_fma_f32 v[168:169], v[4:5], s[2:3], v[60:61] op_sel_hi:[1,0,1]
	v_pk_fma_f32 v[170:171], v[6:7], s[2:3], v[68:69] op_sel_hi:[1,0,1]
	v_pk_fma_f32 v[172:173], v[8:9], s[2:3], v[70:71] op_sel_hi:[1,0,1]
	v_pk_fma_f32 v[174:175], v[10:11], s[2:3], v[72:73] op_sel_hi:[1,0,1]
	v_pk_fma_f32 v[176:177], v[12:13], s[2:3], v[74:75] op_sel_hi:[1,0,1]
	v_pk_fma_f32 v[178:179], v[14:15], s[2:3], v[76:77] op_sel_hi:[1,0,1]
	v_pk_fma_f32 v[180:181], v[16:17], s[2:3], v[78:79] op_sel_hi:[1,0,1]
	v_pk_fma_f32 v[162:163], v[18:19], s[2:3], v[162:163] op_sel_hi:[1,0,1]
	v_pk_fma_f32 v[160:161], v[20:21], s[2:3], v[160:161] op_sel_hi:[1,0,1]
	v_pk_fma_f32 v[158:159], v[22:23], s[2:3], v[158:159] op_sel_hi:[1,0,1]
	v_pk_fma_f32 v[156:157], v[24:25], s[2:3], v[156:157] op_sel_hi:[1,0,1]
	v_pk_fma_f32 v[154:155], v[26:27], s[2:3], v[154:155] op_sel_hi:[1,0,1]
	v_pk_fma_f32 v[152:153], v[28:29], s[2:3], v[152:153] op_sel_hi:[1,0,1]
	v_pk_fma_f32 v[150:151], v[30:31], s[2:3], v[150:151] op_sel_hi:[1,0,1]
	v_readlane_b32 s2, v241, 56
	v_readlane_b32 s3, v241, 57
	v_readlane_b32 s100, v241, 58
	v_readlane_b32 s101, v241, 59
	s_nop 1
	buffer_load_dwordx4 v[74:77], v129, s[44:47], s2 offen
	buffer_load_dwordx2 v[78:79], v210, s[44:47], s2 offen
	buffer_load_dwordx4 v[68:71], v129, s[44:47], s3 offen
	buffer_load_dwordx2 v[72:73], v210, s[44:47], s3 offen
	buffer_load_dwordx4 v[56:59], v129, s[44:47], s100 offen
	buffer_load_dwordx2 v[60:61], v210, s[44:47], s100 offen
	buffer_load_dwordx4 v[44:47], v129, s[44:47], s101 offen
	buffer_load_dwordx2 v[48:49], v210, s[44:47], s101 offen
	s_waitcnt vmcnt(16)
	v_readlane_b32 s2, v131, 48
	s_nop 0
	v_cvt_scalef32_pk32_f32_fp6 v[0:31], v[62:67], 1.0
	v_pk_fma_f32 v[62:63], v[0:1], s[2:3], v[164:165] op_sel_hi:[1,0,1]
	v_pk_fma_f32 v[64:65], v[2:3], s[2:3], v[166:167] op_sel_hi:[1,0,1]
	v_pk_fma_f32 v[66:67], v[4:5], s[2:3], v[168:169] op_sel_hi:[1,0,1]
	v_pk_fma_f32 v[164:165], v[6:7], s[2:3], v[170:171] op_sel_hi:[1,0,1]
	v_pk_fma_f32 v[166:167], v[8:9], s[2:3], v[172:173] op_sel_hi:[1,0,1]
	v_pk_fma_f32 v[168:169], v[10:11], s[2:3], v[174:175] op_sel_hi:[1,0,1]
	v_pk_fma_f32 v[170:171], v[12:13], s[2:3], v[176:177] op_sel_hi:[1,0,1]
	v_pk_fma_f32 v[172:173], v[14:15], s[2:3], v[178:179] op_sel_hi:[1,0,1]
	v_pk_fma_f32 v[174:175], v[16:17], s[2:3], v[180:181] op_sel_hi:[1,0,1]
	v_pk_fma_f32 v[162:163], v[18:19], s[2:3], v[162:163] op_sel_hi:[1,0,1]
	v_pk_fma_f32 v[160:161], v[20:21], s[2:3], v[160:161] op_sel_hi:[1,0,1]
	v_pk_fma_f32 v[158:159], v[22:23], s[2:3], v[158:159] op_sel_hi:[1,0,1]
	v_pk_fma_f32 v[156:157], v[24:25], s[2:3], v[156:157] op_sel_hi:[1,0,1]
	v_pk_fma_f32 v[154:155], v[26:27], s[2:3], v[154:155] op_sel_hi:[1,0,1]
	v_pk_fma_f32 v[152:153], v[28:29], s[2:3], v[152:153] op_sel_hi:[1,0,1]
	v_pk_fma_f32 v[150:151], v[30:31], s[2:3], v[150:151] op_sel_hi:[1,0,1]
	v_readlane_b32 s2, v131, 49
	v_cvt_scalef32_pk32_f32_fp6 v[0:31], v[50:55], 1.0
	v_pk_fma_f32 v[50:51], v[0:1], s[2:3], v[62:63] op_sel_hi:[1,0,1]
	v_pk_fma_f32 v[52:53], v[2:3], s[2:3], v[64:65] op_sel_hi:[1,0,1]
	v_pk_fma_f32 v[54:55], v[4:5], s[2:3], v[66:67] op_sel_hi:[1,0,1]
	v_pk_fma_f32 v[62:63], v[6:7], s[2:3], v[164:165] op_sel_hi:[1,0,1]
	v_pk_fma_f32 v[64:65], v[8:9], s[2:3], v[166:167] op_sel_hi:[1,0,1]
	v_pk_fma_f32 v[66:67], v[10:11], s[2:3], v[168:169] op_sel_hi:[1,0,1]
	v_pk_fma_f32 v[164:165], v[12:13], s[2:3], v[170:171] op_sel_hi:[1,0,1]
	v_pk_fma_f32 v[166:167], v[14:15], s[2:3], v[172:173] op_sel_hi:[1,0,1]
	v_pk_fma_f32 v[168:169], v[16:17], s[2:3], v[174:175] op_sel_hi:[1,0,1]
	v_pk_fma_f32 v[162:163], v[18:19], s[2:3], v[162:163] op_sel_hi:[1,0,1]
	v_pk_fma_f32 v[160:161], v[20:21], s[2:3], v[160:161] op_sel_hi:[1,0,1]
	v_pk_fma_f32 v[158:159], v[22:23], s[2:3], v[158:159] op_sel_hi:[1,0,1]
	v_pk_fma_f32 v[156:157], v[24:25], s[2:3], v[156:157] op_sel_hi:[1,0,1]
	v_pk_fma_f32 v[154:155], v[26:27], s[2:3], v[154:155] op_sel_hi:[1,0,1]
	v_pk_fma_f32 v[152:153], v[28:29], s[2:3], v[152:153] op_sel_hi:[1,0,1]
	v_pk_fma_f32 v[150:151], v[30:31], s[2:3], v[150:151] op_sel_hi:[1,0,1]
	v_readlane_b32 s2, v131, 50
	v_cvt_scalef32_pk32_f32_fp6 v[0:31], v[38:43], 1.0
	v_pk_fma_f32 v[38:39], v[0:1], s[2:3], v[50:51] op_sel_hi:[1,0,1]
	v_pk_fma_f32 v[40:41], v[2:3], s[2:3], v[52:53] op_sel_hi:[1,0,1]
	v_pk_fma_f32 v[42:43], v[4:5], s[2:3], v[54:55] op_sel_hi:[1,0,1]
	v_pk_fma_f32 v[50:51], v[6:7], s[2:3], v[62:63] op_sel_hi:[1,0,1]
	v_pk_fma_f32 v[52:53], v[8:9], s[2:3], v[64:65] op_sel_hi:[1,0,1]
	v_pk_fma_f32 v[54:55], v[10:11], s[2:3], v[66:67] op_sel_hi:[1,0,1]
	v_pk_fma_f32 v[62:63], v[12:13], s[2:3], v[164:165] op_sel_hi:[1,0,1]
	v_pk_fma_f32 v[64:65], v[14:15], s[2:3], v[166:167] op_sel_hi:[1,0,1]
	v_pk_fma_f32 v[66:67], v[16:17], s[2:3], v[168:169] op_sel_hi:[1,0,1]
	v_pk_fma_f32 v[162:163], v[18:19], s[2:3], v[162:163] op_sel_hi:[1,0,1]
	v_pk_fma_f32 v[160:161], v[20:21], s[2:3], v[160:161] op_sel_hi:[1,0,1]
	v_pk_fma_f32 v[158:159], v[22:23], s[2:3], v[158:159] op_sel_hi:[1,0,1]
	v_pk_fma_f32 v[156:157], v[24:25], s[2:3], v[156:157] op_sel_hi:[1,0,1]
	v_pk_fma_f32 v[154:155], v[26:27], s[2:3], v[154:155] op_sel_hi:[1,0,1]
	v_pk_fma_f32 v[152:153], v[28:29], s[2:3], v[152:153] op_sel_hi:[1,0,1]
	v_pk_fma_f32 v[150:151], v[30:31], s[2:3], v[150:151] op_sel_hi:[1,0,1]
	v_readlane_b32 s2, v131, 51
	v_cvt_scalef32_pk32_f32_fp6 v[0:31], v[32:37], 1.0
	v_pk_fma_f32 v[164:165], v[0:1], s[2:3], v[38:39] op_sel_hi:[1,0,1]
	v_pk_fma_f32 v[166:167], v[2:3], s[2:3], v[40:41] op_sel_hi:[1,0,1]
	v_pk_fma_f32 v[168:169], v[4:5], s[2:3], v[42:43] op_sel_hi:[1,0,1]
	v_pk_fma_f32 v[170:171], v[6:7], s[2:3], v[50:51] op_sel_hi:[1,0,1]
	v_pk_fma_f32 v[172:173], v[8:9], s[2:3], v[52:53] op_sel_hi:[1,0,1]
	v_pk_fma_f32 v[174:175], v[10:11], s[2:3], v[54:55] op_sel_hi:[1,0,1]
	v_pk_fma_f32 v[176:177], v[12:13], s[2:3], v[62:63] op_sel_hi:[1,0,1]
	v_pk_fma_f32 v[178:179], v[14:15], s[2:3], v[64:65] op_sel_hi:[1,0,1]
	v_pk_fma_f32 v[180:181], v[16:17], s[2:3], v[66:67] op_sel_hi:[1,0,1]
	v_pk_fma_f32 v[162:163], v[18:19], s[2:3], v[162:163] op_sel_hi:[1,0,1]
	v_pk_fma_f32 v[160:161], v[20:21], s[2:3], v[160:161] op_sel_hi:[1,0,1]
	v_pk_fma_f32 v[158:159], v[22:23], s[2:3], v[158:159] op_sel_hi:[1,0,1]
	v_pk_fma_f32 v[156:157], v[24:25], s[2:3], v[156:157] op_sel_hi:[1,0,1]
	v_pk_fma_f32 v[154:155], v[26:27], s[2:3], v[154:155] op_sel_hi:[1,0,1]
	v_pk_fma_f32 v[152:153], v[28:29], s[2:3], v[152:153] op_sel_hi:[1,0,1]
	v_pk_fma_f32 v[150:151], v[30:31], s[2:3], v[150:151] op_sel_hi:[1,0,1]
	v_readlane_b32 s2, v241, 60
	v_readlane_b32 s3, v241, 61
	v_readlane_b32 s100, v241, 62
	v_readlane_b32 s101, v241, 63
	s_nop 1
	buffer_load_dwordx4 v[62:65], v129, s[44:47], s2 offen
	buffer_load_dwordx2 v[66:67], v210, s[44:47], s2 offen
	buffer_load_dwordx4 v[50:53], v129, s[44:47], s3 offen
	buffer_load_dwordx2 v[54:55], v210, s[44:47], s3 offen
	buffer_load_dwordx4 v[38:41], v129, s[44:47], s100 offen
	buffer_load_dwordx2 v[42:43], v210, s[44:47], s100 offen
	buffer_load_dwordx4 v[32:35], v129, s[44:47], s101 offen
	buffer_load_dwordx2 v[36:37], v210, s[44:47], s101 offen
	s_waitcnt vmcnt(16)
	v_readlane_b32 s2, v131, 52
	s_nop 0
	v_cvt_scalef32_pk32_f32_fp6 v[0:31], v[98:103], 1.0
	v_pk_fma_f32 v[98:99], v[0:1], s[2:3], v[164:165] op_sel_hi:[1,0,1]
	v_pk_fma_f32 v[100:101], v[2:3], s[2:3], v[166:167] op_sel_hi:[1,0,1]
	v_pk_fma_f32 v[102:103], v[4:5], s[2:3], v[168:169] op_sel_hi:[1,0,1]
	v_pk_fma_f32 v[164:165], v[6:7], s[2:3], v[170:171] op_sel_hi:[1,0,1]
	v_pk_fma_f32 v[166:167], v[8:9], s[2:3], v[172:173] op_sel_hi:[1,0,1]
	v_pk_fma_f32 v[168:169], v[10:11], s[2:3], v[174:175] op_sel_hi:[1,0,1]
	v_pk_fma_f32 v[170:171], v[12:13], s[2:3], v[176:177] op_sel_hi:[1,0,1]
	v_pk_fma_f32 v[172:173], v[14:15], s[2:3], v[178:179] op_sel_hi:[1,0,1]
	v_pk_fma_f32 v[174:175], v[16:17], s[2:3], v[180:181] op_sel_hi:[1,0,1]
	v_pk_fma_f32 v[162:163], v[18:19], s[2:3], v[162:163] op_sel_hi:[1,0,1]
	v_pk_fma_f32 v[160:161], v[20:21], s[2:3], v[160:161] op_sel_hi:[1,0,1]
	v_pk_fma_f32 v[158:159], v[22:23], s[2:3], v[158:159] op_sel_hi:[1,0,1]
	v_pk_fma_f32 v[156:157], v[24:25], s[2:3], v[156:157] op_sel_hi:[1,0,1]
	v_pk_fma_f32 v[154:155], v[26:27], s[2:3], v[154:155] op_sel_hi:[1,0,1]
	v_pk_fma_f32 v[152:153], v[28:29], s[2:3], v[152:153] op_sel_hi:[1,0,1]
	v_pk_fma_f32 v[150:151], v[30:31], s[2:3], v[150:151] op_sel_hi:[1,0,1]
	v_readlane_b32 s2, v131, 53
	v_cvt_scalef32_pk32_f32_fp6 v[0:31], v[92:97], 1.0
	v_pk_fma_f32 v[92:93], v[0:1], s[2:3], v[98:99] op_sel_hi:[1,0,1]
	v_pk_fma_f32 v[94:95], v[2:3], s[2:3], v[100:101] op_sel_hi:[1,0,1]
	v_pk_fma_f32 v[96:97], v[4:5], s[2:3], v[102:103] op_sel_hi:[1,0,1]
	v_pk_fma_f32 v[98:99], v[6:7], s[2:3], v[164:165] op_sel_hi:[1,0,1]
	v_pk_fma_f32 v[100:101], v[8:9], s[2:3], v[166:167] op_sel_hi:[1,0,1]
	v_pk_fma_f32 v[102:103], v[10:11], s[2:3], v[168:169] op_sel_hi:[1,0,1]
	v_pk_fma_f32 v[164:165], v[12:13], s[2:3], v[170:171] op_sel_hi:[1,0,1]
	v_pk_fma_f32 v[166:167], v[14:15], s[2:3], v[172:173] op_sel_hi:[1,0,1]
	v_pk_fma_f32 v[168:169], v[16:17], s[2:3], v[174:175] op_sel_hi:[1,0,1]
	v_pk_fma_f32 v[162:163], v[18:19], s[2:3], v[162:163] op_sel_hi:[1,0,1]
	v_pk_fma_f32 v[160:161], v[20:21], s[2:3], v[160:161] op_sel_hi:[1,0,1]
	v_pk_fma_f32 v[158:159], v[22:23], s[2:3], v[158:159] op_sel_hi:[1,0,1]
	v_pk_fma_f32 v[156:157], v[24:25], s[2:3], v[156:157] op_sel_hi:[1,0,1]
	v_pk_fma_f32 v[154:155], v[26:27], s[2:3], v[154:155] op_sel_hi:[1,0,1]
	v_pk_fma_f32 v[152:153], v[28:29], s[2:3], v[152:153] op_sel_hi:[1,0,1]
	v_pk_fma_f32 v[150:151], v[30:31], s[2:3], v[150:151] op_sel_hi:[1,0,1]
	v_readlane_b32 s2, v131, 54
	v_cvt_scalef32_pk32_f32_fp6 v[0:31], v[86:91], 1.0
	v_pk_fma_f32 v[86:87], v[0:1], s[2:3], v[92:93] op_sel_hi:[1,0,1]
	v_pk_fma_f32 v[88:89], v[2:3], s[2:3], v[94:95] op_sel_hi:[1,0,1]
	v_pk_fma_f32 v[90:91], v[4:5], s[2:3], v[96:97] op_sel_hi:[1,0,1]
	v_pk_fma_f32 v[92:93], v[6:7], s[2:3], v[98:99] op_sel_hi:[1,0,1]
	v_pk_fma_f32 v[94:95], v[8:9], s[2:3], v[100:101] op_sel_hi:[1,0,1]
	v_pk_fma_f32 v[96:97], v[10:11], s[2:3], v[102:103] op_sel_hi:[1,0,1]
	v_pk_fma_f32 v[98:99], v[12:13], s[2:3], v[164:165] op_sel_hi:[1,0,1]
	v_pk_fma_f32 v[100:101], v[14:15], s[2:3], v[166:167] op_sel_hi:[1,0,1]
	v_pk_fma_f32 v[102:103], v[16:17], s[2:3], v[168:169] op_sel_hi:[1,0,1]
	v_pk_fma_f32 v[162:163], v[18:19], s[2:3], v[162:163] op_sel_hi:[1,0,1]
	v_pk_fma_f32 v[160:161], v[20:21], s[2:3], v[160:161] op_sel_hi:[1,0,1]
	v_pk_fma_f32 v[158:159], v[22:23], s[2:3], v[158:159] op_sel_hi:[1,0,1]
	v_pk_fma_f32 v[156:157], v[24:25], s[2:3], v[156:157] op_sel_hi:[1,0,1]
	v_pk_fma_f32 v[154:155], v[26:27], s[2:3], v[154:155] op_sel_hi:[1,0,1]
	v_pk_fma_f32 v[152:153], v[28:29], s[2:3], v[152:153] op_sel_hi:[1,0,1]
	v_pk_fma_f32 v[150:151], v[30:31], s[2:3], v[150:151] op_sel_hi:[1,0,1]
	v_readlane_b32 s2, v131, 55
	v_cvt_scalef32_pk32_f32_fp6 v[0:31], v[80:85], 1.0
	v_pk_fma_f32 v[180:181], v[0:1], s[2:3], v[86:87] op_sel_hi:[1,0,1]
	v_pk_fma_f32 v[178:179], v[2:3], s[2:3], v[88:89] op_sel_hi:[1,0,1]
	v_pk_fma_f32 v[176:177], v[4:5], s[2:3], v[90:91] op_sel_hi:[1,0,1]
	v_pk_fma_f32 v[174:175], v[6:7], s[2:3], v[92:93] op_sel_hi:[1,0,1]
	v_pk_fma_f32 v[172:173], v[8:9], s[2:3], v[94:95] op_sel_hi:[1,0,1]
	v_pk_fma_f32 v[170:171], v[10:11], s[2:3], v[96:97] op_sel_hi:[1,0,1]
	v_pk_fma_f32 v[168:169], v[12:13], s[2:3], v[98:99] op_sel_hi:[1,0,1]
	v_pk_fma_f32 v[166:167], v[14:15], s[2:3], v[100:101] op_sel_hi:[1,0,1]
	v_pk_fma_f32 v[164:165], v[16:17], s[2:3], v[102:103] op_sel_hi:[1,0,1]
	v_pk_fma_f32 v[162:163], v[18:19], s[2:3], v[162:163] op_sel_hi:[1,0,1]
	v_pk_fma_f32 v[160:161], v[20:21], s[2:3], v[160:161] op_sel_hi:[1,0,1]
	v_pk_fma_f32 v[158:159], v[22:23], s[2:3], v[158:159] op_sel_hi:[1,0,1]
	v_pk_fma_f32 v[156:157], v[24:25], s[2:3], v[156:157] op_sel_hi:[1,0,1]
	v_pk_fma_f32 v[154:155], v[26:27], s[2:3], v[154:155] op_sel_hi:[1,0,1]
	v_pk_fma_f32 v[152:153], v[28:29], s[2:3], v[152:153] op_sel_hi:[1,0,1]
	v_pk_fma_f32 v[150:151], v[30:31], s[2:3], v[150:151] op_sel_hi:[1,0,1]
	v_readlane_b32 s0, v131, 56
	s_waitcnt vmcnt(14)
	v_cvt_scalef32_pk32_f32_fp6 v[0:31], v[74:79], 1.0
	v_pk_fma_f32 v[74:75], v[0:1], s[0:1], v[180:181] op_sel_hi:[1,0,1]
	v_pk_fma_f32 v[76:77], v[2:3], s[0:1], v[178:179] op_sel_hi:[1,0,1]
	v_pk_fma_f32 v[78:79], v[4:5], s[0:1], v[176:177] op_sel_hi:[1,0,1]
	v_pk_fma_f32 v[80:81], v[6:7], s[0:1], v[174:175] op_sel_hi:[1,0,1]
	v_pk_fma_f32 v[82:83], v[8:9], s[0:1], v[172:173] op_sel_hi:[1,0,1]
	v_pk_fma_f32 v[84:85], v[10:11], s[0:1], v[170:171] op_sel_hi:[1,0,1]
	v_pk_fma_f32 v[86:87], v[12:13], s[0:1], v[168:169] op_sel_hi:[1,0,1]
	v_pk_fma_f32 v[88:89], v[14:15], s[0:1], v[166:167] op_sel_hi:[1,0,1]
	v_pk_fma_f32 v[90:91], v[16:17], s[0:1], v[164:165] op_sel_hi:[1,0,1]
	v_pk_fma_f32 v[92:93], v[18:19], s[0:1], v[162:163] op_sel_hi:[1,0,1]
	v_pk_fma_f32 v[94:95], v[20:21], s[0:1], v[160:161] op_sel_hi:[1,0,1]
	v_pk_fma_f32 v[96:97], v[22:23], s[0:1], v[158:159] op_sel_hi:[1,0,1]
	v_pk_fma_f32 v[98:99], v[24:25], s[0:1], v[156:157] op_sel_hi:[1,0,1]
	v_pk_fma_f32 v[100:101], v[26:27], s[0:1], v[154:155] op_sel_hi:[1,0,1]
	v_pk_fma_f32 v[102:103], v[28:29], s[0:1], v[152:153] op_sel_hi:[1,0,1]
	v_pk_fma_f32 v[150:151], v[30:31], s[0:1], v[150:151] op_sel_hi:[1,0,1]
	v_readlane_b32 s0, v131, 57
	s_waitcnt vmcnt(12)
	v_cvt_scalef32_pk32_f32_fp6 v[0:31], v[68:73], 1.0
	v_pk_fma_f32 v[68:69], v[0:1], s[0:1], v[74:75] op_sel_hi:[1,0,1]
	v_pk_fma_f32 v[70:71], v[2:3], s[0:1], v[76:77] op_sel_hi:[1,0,1]
	v_pk_fma_f32 v[72:73], v[4:5], s[0:1], v[78:79] op_sel_hi:[1,0,1]
	v_pk_fma_f32 v[74:75], v[6:7], s[0:1], v[80:81] op_sel_hi:[1,0,1]
	v_pk_fma_f32 v[76:77], v[8:9], s[0:1], v[82:83] op_sel_hi:[1,0,1]
	v_pk_fma_f32 v[78:79], v[10:11], s[0:1], v[84:85] op_sel_hi:[1,0,1]
	v_pk_fma_f32 v[80:81], v[12:13], s[0:1], v[86:87] op_sel_hi:[1,0,1]
	v_pk_fma_f32 v[82:83], v[14:15], s[0:1], v[88:89] op_sel_hi:[1,0,1]
	v_pk_fma_f32 v[84:85], v[16:17], s[0:1], v[90:91] op_sel_hi:[1,0,1]
	v_pk_fma_f32 v[86:87], v[18:19], s[0:1], v[92:93] op_sel_hi:[1,0,1]
	v_pk_fma_f32 v[88:89], v[20:21], s[0:1], v[94:95] op_sel_hi:[1,0,1]
	v_pk_fma_f32 v[90:91], v[22:23], s[0:1], v[96:97] op_sel_hi:[1,0,1]
	v_pk_fma_f32 v[92:93], v[24:25], s[0:1], v[98:99] op_sel_hi:[1,0,1]
	v_pk_fma_f32 v[94:95], v[26:27], s[0:1], v[100:101] op_sel_hi:[1,0,1]
	v_pk_fma_f32 v[96:97], v[28:29], s[0:1], v[102:103] op_sel_hi:[1,0,1]
	v_pk_fma_f32 v[98:99], v[30:31], s[0:1], v[150:151] op_sel_hi:[1,0,1]
	v_readlane_b32 s0, v131, 58
	s_waitcnt vmcnt(10)
	v_cvt_scalef32_pk32_f32_fp6 v[0:31], v[56:61], 1.0
	v_pk_fma_f32 v[56:57], v[0:1], s[0:1], v[68:69] op_sel_hi:[1,0,1]
	v_pk_fma_f32 v[58:59], v[2:3], s[0:1], v[70:71] op_sel_hi:[1,0,1]
	v_pk_fma_f32 v[60:61], v[4:5], s[0:1], v[72:73] op_sel_hi:[1,0,1]
	v_pk_fma_f32 v[68:69], v[6:7], s[0:1], v[74:75] op_sel_hi:[1,0,1]
	v_pk_fma_f32 v[70:71], v[8:9], s[0:1], v[76:77] op_sel_hi:[1,0,1]
	v_pk_fma_f32 v[72:73], v[10:11], s[0:1], v[78:79] op_sel_hi:[1,0,1]
	v_pk_fma_f32 v[74:75], v[12:13], s[0:1], v[80:81] op_sel_hi:[1,0,1]
	v_pk_fma_f32 v[76:77], v[14:15], s[0:1], v[82:83] op_sel_hi:[1,0,1]
	v_pk_fma_f32 v[78:79], v[16:17], s[0:1], v[84:85] op_sel_hi:[1,0,1]
	v_pk_fma_f32 v[80:81], v[18:19], s[0:1], v[86:87] op_sel_hi:[1,0,1]
	v_pk_fma_f32 v[82:83], v[20:21], s[0:1], v[88:89] op_sel_hi:[1,0,1]
	v_pk_fma_f32 v[84:85], v[22:23], s[0:1], v[90:91] op_sel_hi:[1,0,1]
	v_pk_fma_f32 v[86:87], v[24:25], s[0:1], v[92:93] op_sel_hi:[1,0,1]
	v_pk_fma_f32 v[88:89], v[26:27], s[0:1], v[94:95] op_sel_hi:[1,0,1]
	v_pk_fma_f32 v[90:91], v[28:29], s[0:1], v[96:97] op_sel_hi:[1,0,1]
	v_pk_fma_f32 v[92:93], v[30:31], s[0:1], v[98:99] op_sel_hi:[1,0,1]
	v_readlane_b32 s0, v131, 59
	s_waitcnt vmcnt(8)
	v_cvt_scalef32_pk32_f32_fp6 v[0:31], v[44:49], 1.0
	v_pk_fma_f32 v[46:47], v[2:3], s[0:1], v[58:59] op_sel_hi:[1,0,1]
	v_pk_fma_f32 v[44:45], v[0:1], s[0:1], v[56:57] op_sel_hi:[1,0,1]
	v_pk_fma_f32 v[48:49], v[4:5], s[0:1], v[60:61] op_sel_hi:[1,0,1]
	v_pk_fma_f32 v[56:57], v[6:7], s[0:1], v[68:69] op_sel_hi:[1,0,1]
	v_pk_fma_f32 v[58:59], v[8:9], s[0:1], v[70:71] op_sel_hi:[1,0,1]
	v_pk_fma_f32 v[60:61], v[10:11], s[0:1], v[72:73] op_sel_hi:[1,0,1]
	v_pk_fma_f32 v[68:69], v[12:13], s[0:1], v[74:75] op_sel_hi:[1,0,1]
	v_pk_fma_f32 v[70:71], v[14:15], s[0:1], v[76:77] op_sel_hi:[1,0,1]
	v_pk_fma_f32 v[72:73], v[16:17], s[0:1], v[78:79] op_sel_hi:[1,0,1]
	v_pk_fma_f32 v[74:75], v[18:19], s[0:1], v[80:81] op_sel_hi:[1,0,1]
	v_pk_fma_f32 v[76:77], v[20:21], s[0:1], v[82:83] op_sel_hi:[1,0,1]
	v_pk_fma_f32 v[78:79], v[22:23], s[0:1], v[84:85] op_sel_hi:[1,0,1]
	v_pk_fma_f32 v[80:81], v[24:25], s[0:1], v[86:87] op_sel_hi:[1,0,1]
	v_pk_fma_f32 v[82:83], v[26:27], s[0:1], v[88:89] op_sel_hi:[1,0,1]
	v_pk_fma_f32 v[84:85], v[28:29], s[0:1], v[90:91] op_sel_hi:[1,0,1]
	v_pk_fma_f32 v[86:87], v[30:31], s[0:1], v[92:93] op_sel_hi:[1,0,1]
	v_readlane_b32 s0, v131, 60
	s_waitcnt vmcnt(6)
	v_cvt_scalef32_pk32_f32_fp6 v[0:31], v[62:67], 1.0
	v_pk_fma_f32 v[44:45], v[0:1], s[0:1], v[44:45] op_sel_hi:[1,0,1]
	v_pk_fma_f32 v[46:47], v[2:3], s[0:1], v[46:47] op_sel_hi:[1,0,1]
	v_pk_fma_f32 v[48:49], v[4:5], s[0:1], v[48:49] op_sel_hi:[1,0,1]
	v_pk_fma_f32 v[56:57], v[6:7], s[0:1], v[56:57] op_sel_hi:[1,0,1]
	v_pk_fma_f32 v[58:59], v[8:9], s[0:1], v[58:59] op_sel_hi:[1,0,1]
	v_pk_fma_f32 v[60:61], v[10:11], s[0:1], v[60:61] op_sel_hi:[1,0,1]
	v_pk_fma_f32 v[62:63], v[12:13], s[0:1], v[68:69] op_sel_hi:[1,0,1]
	v_pk_fma_f32 v[64:65], v[14:15], s[0:1], v[70:71] op_sel_hi:[1,0,1]
	v_pk_fma_f32 v[66:67], v[16:17], s[0:1], v[72:73] op_sel_hi:[1,0,1]
	v_pk_fma_f32 v[68:69], v[18:19], s[0:1], v[74:75] op_sel_hi:[1,0,1]
	v_pk_fma_f32 v[70:71], v[20:21], s[0:1], v[76:77] op_sel_hi:[1,0,1]
	v_pk_fma_f32 v[72:73], v[22:23], s[0:1], v[78:79] op_sel_hi:[1,0,1]
	v_pk_fma_f32 v[74:75], v[24:25], s[0:1], v[80:81] op_sel_hi:[1,0,1]
	v_pk_fma_f32 v[76:77], v[26:27], s[0:1], v[82:83] op_sel_hi:[1,0,1]
	v_pk_fma_f32 v[78:79], v[28:29], s[0:1], v[84:85] op_sel_hi:[1,0,1]
	v_pk_fma_f32 v[80:81], v[30:31], s[0:1], v[86:87] op_sel_hi:[1,0,1]
	v_readlane_b32 s0, v131, 61
	s_waitcnt vmcnt(4)
	v_cvt_scalef32_pk32_f32_fp6 v[0:31], v[50:55], 1.0
	v_pk_fma_f32 v[44:45], v[0:1], s[0:1], v[44:45] op_sel_hi:[1,0,1]
	v_pk_fma_f32 v[46:47], v[2:3], s[0:1], v[46:47] op_sel_hi:[1,0,1]
	v_pk_fma_f32 v[48:49], v[4:5], s[0:1], v[48:49] op_sel_hi:[1,0,1]
	v_pk_fma_f32 v[50:51], v[6:7], s[0:1], v[56:57] op_sel_hi:[1,0,1]
	v_pk_fma_f32 v[52:53], v[8:9], s[0:1], v[58:59] op_sel_hi:[1,0,1]
	v_pk_fma_f32 v[54:55], v[10:11], s[0:1], v[60:61] op_sel_hi:[1,0,1]
	v_pk_fma_f32 v[56:57], v[12:13], s[0:1], v[62:63] op_sel_hi:[1,0,1]
	v_pk_fma_f32 v[58:59], v[14:15], s[0:1], v[64:65] op_sel_hi:[1,0,1]
	v_pk_fma_f32 v[60:61], v[16:17], s[0:1], v[66:67] op_sel_hi:[1,0,1]
	v_pk_fma_f32 v[62:63], v[18:19], s[0:1], v[68:69] op_sel_hi:[1,0,1]
	v_pk_fma_f32 v[64:65], v[20:21], s[0:1], v[70:71] op_sel_hi:[1,0,1]
	v_pk_fma_f32 v[66:67], v[22:23], s[0:1], v[72:73] op_sel_hi:[1,0,1]
	v_pk_fma_f32 v[68:69], v[24:25], s[0:1], v[74:75] op_sel_hi:[1,0,1]
	v_pk_fma_f32 v[70:71], v[26:27], s[0:1], v[76:77] op_sel_hi:[1,0,1]
	v_pk_fma_f32 v[72:73], v[28:29], s[0:1], v[78:79] op_sel_hi:[1,0,1]
	v_pk_fma_f32 v[74:75], v[30:31], s[0:1], v[80:81] op_sel_hi:[1,0,1]
	v_readlane_b32 s0, v131, 62
	s_waitcnt vmcnt(2)
	v_cvt_scalef32_pk32_f32_fp6 v[0:31], v[38:43], 1.0
	v_pk_fma_f32 v[38:39], v[0:1], s[0:1], v[44:45] op_sel_hi:[1,0,1]
	v_pk_fma_f32 v[40:41], v[2:3], s[0:1], v[46:47] op_sel_hi:[1,0,1]
	v_pk_fma_f32 v[42:43], v[4:5], s[0:1], v[48:49] op_sel_hi:[1,0,1]
	v_pk_fma_f32 v[44:45], v[6:7], s[0:1], v[50:51] op_sel_hi:[1,0,1]
	v_pk_fma_f32 v[46:47], v[8:9], s[0:1], v[52:53] op_sel_hi:[1,0,1]
	v_pk_fma_f32 v[48:49], v[10:11], s[0:1], v[54:55] op_sel_hi:[1,0,1]
	v_pk_fma_f32 v[50:51], v[12:13], s[0:1], v[56:57] op_sel_hi:[1,0,1]
	v_pk_fma_f32 v[52:53], v[14:15], s[0:1], v[58:59] op_sel_hi:[1,0,1]
	v_pk_fma_f32 v[54:55], v[16:17], s[0:1], v[60:61] op_sel_hi:[1,0,1]
	v_pk_fma_f32 v[56:57], v[18:19], s[0:1], v[62:63] op_sel_hi:[1,0,1]
	v_pk_fma_f32 v[58:59], v[20:21], s[0:1], v[64:65] op_sel_hi:[1,0,1]
	v_pk_fma_f32 v[62:63], v[22:23], s[0:1], v[66:67] op_sel_hi:[1,0,1]
	v_pk_fma_f32 v[64:65], v[24:25], s[0:1], v[68:69] op_sel_hi:[1,0,1]
	v_pk_fma_f32 v[66:67], v[26:27], s[0:1], v[70:71] op_sel_hi:[1,0,1]
	v_pk_fma_f32 v[68:69], v[28:29], s[0:1], v[72:73] op_sel_hi:[1,0,1]
	v_pk_fma_f32 v[70:71], v[30:31], s[0:1], v[74:75] op_sel_hi:[1,0,1]
	v_readlane_b32 s0, v131, 63
	s_waitcnt vmcnt(0)
	v_cvt_scalef32_pk32_f32_fp6 v[0:31], v[32:37], 1.0
	v_pk_fma_f32 v[34:35], v[0:1], s[0:1], v[38:39] op_sel_hi:[1,0,1]
	v_pk_fma_f32 v[32:33], v[2:3], s[0:1], v[40:41] op_sel_hi:[1,0,1]
	v_pk_fma_f32 v[38:39], v[4:5], s[0:1], v[42:43] op_sel_hi:[1,0,1]
	v_pk_fma_f32 v[36:37], v[6:7], s[0:1], v[44:45] op_sel_hi:[1,0,1]
	v_pk_fma_f32 v[42:43], v[8:9], s[0:1], v[46:47] op_sel_hi:[1,0,1]
	v_pk_fma_f32 v[40:41], v[10:11], s[0:1], v[48:49] op_sel_hi:[1,0,1]
	v_pk_fma_f32 v[48:49], v[12:13], s[0:1], v[50:51] op_sel_hi:[1,0,1]
	v_pk_fma_f32 v[46:47], v[14:15], s[0:1], v[52:53] op_sel_hi:[1,0,1]
	v_pk_fma_f32 v[50:51], v[18:19], s[0:1], v[56:57] op_sel_hi:[1,0,1]
	v_pk_fma_f32 v[54:55], v[16:17], s[0:1], v[54:55] op_sel_hi:[1,0,1]
	v_pk_fma_f32 v[60:61], v[20:21], s[0:1], v[58:59] op_sel_hi:[1,0,1]
	v_pk_fma_f32 v[56:57], v[22:23], s[0:1], v[62:63] op_sel_hi:[1,0,1]
	v_pk_fma_f32 v[44:45], v[24:25], s[0:1], v[64:65] op_sel_hi:[1,0,1]
	v_pk_fma_f32 v[64:65], v[26:27], s[0:1], v[66:67] op_sel_hi:[1,0,1]
	v_pk_fma_f32 v[18:19], v[28:29], s[0:1], v[68:69] op_sel_hi:[1,0,1]
	v_pk_fma_f32 v[24:25], v[30:31], s[0:1], v[70:71] op_sel_hi:[1,0,1]
	s_lshr_b32 s0, s58, 12
	s_ashr_i32 s59, s58, 31
	s_mul_i32 s4, s0, 0x3000
	s_lshl_b64 s[0:1], s[58:59], 12
	s_add_u32 s2, s71, s0
	v_lshlrev_b32_e32 v12, 2, v148
	s_addc_u32 s3, s74, s1
	v_ashrrev_i32_e32 v13, 31, v12
	v_lshlrev_b32_e32 v63, 3, v148
	v_lshl_add_u64 v[14:15], v[12:13], 1, s[2:3]
	v_add3_u32 v62, v201, s4, v63
	global_load_dwordx2 v[16:17], v[14:15], off
	ds_read2st64_b64 v[0:3], v62 offset1:1
	global_load_dwordx2 v[20:21], v[14:15], off offset:512
	global_load_dwordx2 v[22:23], v[14:15], off offset:1024
	ds_read2st64_b64 v[4:7], v62 offset0:2 offset1:3
	global_load_dwordx2 v[52:53], v[14:15], off offset:1536
	global_load_dwordx2 v[58:59], v[14:15], off offset:2048
	ds_read2st64_b64 v[8:11], v62 offset0:4 offset1:5
	global_load_dwordx2 v[66:67], v[14:15], off offset:2560
	global_load_dwordx2 v[68:69], v[14:15], off offset:3072
	global_load_dwordx2 v[26:27], v[14:15], off offset:3584
	ds_read2st64_b64 v[28:31], v62 offset0:6 offset1:7
	s_lshl_b64 s[2:3], s[58:59], 13
	s_add_u32 s4, s16, s2
	s_addc_u32 s5, s17, s3
	s_and_b64 vcc, exec, s[54:55]
	s_waitcnt lgkmcnt(0)
	v_lshlrev_b32_e32 v72, 16, v30
	v_and_b32_e32 v73, 0xffff0000, v30
	v_lshlrev_b32_e32 v30, 16, v31
	v_and_b32_e32 v31, 0xffff0000, v31
	v_pk_mul_f32 v[24:25], v[24:25], v[30:31]
	v_lshlrev_b32_e32 v30, 16, v28
	v_and_b32_e32 v31, 0xffff0000, v28
	v_pk_mul_f32 v[30:31], v[44:45], v[30:31]
	v_lshlrev_b32_e32 v28, 16, v29
	v_and_b32_e32 v29, 0xffff0000, v29
	v_pk_mul_f32 v[28:29], v[64:65], v[28:29]
	v_pk_mul_f32 v[18:19], v[18:19], v[72:73]
	s_waitcnt vmcnt(0)
	v_lshlrev_b32_e32 v70, 16, v26
	v_and_b32_e32 v71, 0xffff0000, v26
	v_lshlrev_b32_e32 v26, 16, v27
	v_and_b32_e32 v27, 0xffff0000, v27
	v_pk_fma_f32 v[24:25], v[26:27], s[38:39], v[24:25] op_sel_hi:[1,0,1]
	v_lshlrev_b32_e32 v26, 16, v68
	v_and_b32_e32 v27, 0xffff0000, v68
	v_pk_fma_f32 v[26:27], v[26:27], s[38:39], v[30:31] op_sel_hi:[1,0,1]
	v_lshlrev_b32_e32 v30, 16, v69
	v_and_b32_e32 v31, 0xffff0000, v69
	v_pk_fma_f32 v[44:45], v[30:31], s[38:39], v[28:29] op_sel_hi:[1,0,1]
	v_lshlrev_b32_e32 v30, 16, v10
	v_and_b32_e32 v31, 0xffff0000, v10
	v_lshlrev_b32_e32 v28, 16, v66
	v_and_b32_e32 v29, 0xffff0000, v66
	v_pk_mul_f32 v[30:31], v[60:61], v[30:31]
	v_lshlrev_b32_e32 v10, 16, v11
	v_and_b32_e32 v11, 0xffff0000, v11
	v_pk_fma_f32 v[28:29], v[28:29], s[38:39], v[30:31] op_sel_hi:[1,0,1]
	v_lshlrev_b32_e32 v30, 16, v67
	v_and_b32_e32 v31, 0xffff0000, v67
	v_pk_mul_f32 v[10:11], v[56:57], v[10:11]
	v_lshlrev_b32_e32 v56, 16, v8
	v_and_b32_e32 v57, 0xffff0000, v8
	v_pk_fma_f32 v[10:11], v[30:31], s[38:39], v[10:11] op_sel_hi:[1,0,1]
	v_lshlrev_b32_e32 v30, 16, v58
	v_and_b32_e32 v31, 0xffff0000, v58
	v_pk_mul_f32 v[54:55], v[54:55], v[56:57]
	v_lshlrev_b32_e32 v8, 16, v9
	v_and_b32_e32 v9, 0xffff0000, v9
	v_pk_fma_f32 v[30:31], v[30:31], s[38:39], v[54:55] op_sel_hi:[1,0,1]
	v_lshlrev_b32_e32 v54, 16, v59
	v_and_b32_e32 v55, 0xffff0000, v59
	v_pk_mul_f32 v[8:9], v[50:51], v[8:9]
	v_lshlrev_b32_e32 v50, 16, v52
	v_pk_fma_f32 v[8:9], v[54:55], s[38:39], v[8:9] op_sel_hi:[1,0,1]
	v_lshlrev_b32_e32 v54, 16, v6
	v_and_b32_e32 v55, 0xffff0000, v6
	v_and_b32_e32 v51, 0xffff0000, v52
	v_pk_mul_f32 v[48:49], v[48:49], v[54:55]
	v_lshlrev_b32_e32 v6, 16, v7
	v_and_b32_e32 v7, 0xffff0000, v7
	v_pk_fma_f32 v[48:49], v[50:51], s[38:39], v[48:49] op_sel_hi:[1,0,1]
	v_lshlrev_b32_e32 v50, 16, v53
	v_and_b32_e32 v51, 0xffff0000, v53
	v_pk_mul_f32 v[6:7], v[46:47], v[6:7]
	v_lshlrev_b32_e32 v46, 16, v22
	v_pk_fma_f32 v[6:7], v[50:51], s[38:39], v[6:7] op_sel_hi:[1,0,1]
	v_lshlrev_b32_e32 v50, 16, v4
	v_and_b32_e32 v51, 0xffff0000, v4
	v_lshlrev_b32_e32 v4, 16, v5
	v_and_b32_e32 v5, 0xffff0000, v5
	v_and_b32_e32 v47, 0xffff0000, v22
	v_lshlrev_b32_e32 v22, 16, v23
	v_and_b32_e32 v23, 0xffff0000, v23
	v_pk_mul_f32 v[4:5], v[40:41], v[4:5]
	v_lshlrev_b32_e32 v40, 16, v2
	v_and_b32_e32 v41, 0xffff0000, v2
	v_pk_fma_f32 v[4:5], v[22:23], s[38:39], v[4:5] op_sel_hi:[1,0,1]
	v_lshlrev_b32_e32 v22, 16, v20
	v_and_b32_e32 v23, 0xffff0000, v20
	v_pk_mul_f32 v[38:39], v[38:39], v[40:41]
	v_lshlrev_b32_e32 v40, 16, v0
	v_and_b32_e32 v41, 0xffff0000, v0
	v_pk_fma_f32 v[22:23], v[22:23], s[38:39], v[38:39] op_sel_hi:[1,0,1]
	v_lshlrev_b32_e32 v38, 16, v16
	v_and_b32_e32 v39, 0xffff0000, v16
	v_pk_mul_f32 v[34:35], v[34:35], v[40:41]
	v_lshlrev_b32_e32 v16, 16, v17
	v_pk_fma_f32 v[34:35], v[38:39], s[38:39], v[34:35] op_sel_hi:[1,0,1]
	v_and_b32_e32 v17, 0xffff0000, v17
	v_add_f32_e32 v0, 0, v34
	v_add_f32_e32 v38, v35, v0
	v_lshlrev_b32_e32 v0, 16, v1
	v_and_b32_e32 v1, 0xffff0000, v1
	v_pk_mul_f32 v[0:1], v[32:33], v[0:1]
	v_lshlrev_b32_e32 v2, 16, v3
	v_pk_fma_f32 v[0:1], v[16:17], s[38:39], v[0:1] op_sel_hi:[1,0,1]
	v_and_b32_e32 v3, 0xffff0000, v3
	v_add_f32_e32 v16, v0, v38
	v_add_f32_e32 v16, v1, v16
	v_lshlrev_b32_e32 v20, 16, v21
	v_and_b32_e32 v21, 0xffff0000, v21
	v_pk_mul_f32 v[2:3], v[36:37], v[2:3]
	v_add_f32_e32 v16, v22, v16
	v_pk_fma_f32 v[2:3], v[20:21], s[38:39], v[2:3] op_sel_hi:[1,0,1]
	v_add_f32_e32 v16, v23, v16
	v_pk_mul_f32 v[42:43], v[42:43], v[50:51]
	v_add_f32_e32 v16, v2, v16
	v_pk_fma_f32 v[52:53], v[46:47], s[38:39], v[42:43] op_sel_hi:[1,0,1]
	v_add_f32_e32 v16, v3, v16
	v_add_f32_e32 v16, v52, v16
	v_add_f32_e32 v16, v53, v16
	v_add_f32_e32 v16, v4, v16
	v_add_f32_e32 v16, v5, v16
	v_add_f32_e32 v16, v48, v16
	v_add_f32_e32 v16, v49, v16
	v_add_f32_e32 v16, v6, v16
	v_add_f32_e32 v16, v7, v16
	v_add_f32_e32 v16, v30, v16
	v_add_f32_e32 v16, v31, v16
	v_add_f32_e32 v16, v8, v16
	v_add_f32_e32 v16, v9, v16
	v_add_f32_e32 v16, v28, v16
	v_add_f32_e32 v16, v29, v16
	v_add_f32_e32 v16, v10, v16
	v_add_f32_e32 v16, v11, v16
	v_add_f32_e32 v16, v26, v16
	v_add_f32_e32 v16, v27, v16
	v_add_f32_e32 v16, v44, v16
	v_pk_fma_f32 v[18:19], v[70:71], s[38:39], v[18:19] op_sel_hi:[1,0,1]
	v_add_f32_e32 v16, v45, v16
	v_add_f32_e32 v16, v18, v16
	v_add_f32_e32 v16, v19, v16
	v_add_f32_e32 v16, v24, v16
	v_add_f32_e32 v16, v25, v16
	v_mov_b32_e32 v17, v105
	v_add_u32_e32 v50, v202, v63
	v_add_f32_dpp v16, v16, v16 quad_perm:[1,0,3,2] row_mask:0xf bank_mask:0xf bound_ctrl:1
	v_add_u32_e32 v51, v203, v63
	ds_read_b64 v[20:21], v50
	ds_read_b64 v[36:37], v51
	v_add_f32_dpp v16, v16, v16 quad_perm:[2,3,0,1] row_mask:0xf bank_mask:0xf bound_ctrl:1
	s_waitcnt lgkmcnt(1)
	v_lshlrev_b32_e32 v54, 16, v20
	v_add_f32_dpp v16, v16, v16 row_half_mirror row_mask:0xf bank_mask:0xf bound_ctrl:1
	s_waitcnt lgkmcnt(0)
	v_lshlrev_b32_e32 v56, 16, v36
	v_and_b32_e32 v57, 0xffff0000, v36
	v_add_f32_dpp v16, v16, v16 row_mirror row_mask:0xf bank_mask:0xf bound_ctrl:1
	v_lshlrev_b32_e32 v60, 16, v37
	v_and_b32_e32 v61, 0xffff0000, v37
	v_mov_b32_dpp v17, v16 row_bcast:15 row_mask:0xa bank_mask:0xf
	v_add_f32_e32 v16, v16, v17
	v_mov_b32_e32 v17, v105
	v_and_b32_e32 v55, 0xffff0000, v20
	v_lshlrev_b32_e32 v58, 16, v21
	v_mov_b32_dpp v17, v16 row_bcast:31 row_mask:0xc bank_mask:0xf
	v_add_f32_e32 v16, v16, v17
	v_and_b32_e32 v59, 0xffff0000, v21
	v_readlane_b32 s2, v16, 63
	s_nop 1
	v_mul_f32_e32 v64, s2, v187
	v_pk_add_f32 v[66:67], v[34:35], v[64:65] op_sel_hi:[1,0] neg_lo:[0,1] neg_hi:[0,1]
	v_pk_add_f32 v[70:71], v[0:1], v[64:65] op_sel_hi:[1,0] neg_lo:[0,1] neg_hi:[0,1]
	v_pk_mul_f32 v[68:69], v[66:67], v[66:67]
	v_pk_mul_f32 v[0:1], v[70:71], v[70:71]
	v_add_f32_e32 v63, v68, v69
	v_pk_add_f32 v[46:47], v[22:23], v[64:65] op_sel_hi:[1,0] neg_lo:[0,1] neg_hi:[0,1]
	v_add_f32_e32 v0, v0, v63
	v_pk_mul_f32 v[72:73], v[46:47], v[46:47]
	v_add_f32_e32 v0, v1, v0
	v_pk_add_f32 v[42:43], v[2:3], v[64:65] op_sel_hi:[1,0] neg_lo:[0,1] neg_hi:[0,1]
	v_add_f32_e32 v0, v72, v0
	v_pk_mul_f32 v[2:3], v[42:43], v[42:43]
	v_add_f32_e32 v0, v73, v0
	v_pk_add_f32 v[40:41], v[52:53], v[64:65] op_sel_hi:[1,0] neg_lo:[0,1] neg_hi:[0,1]
	v_add_f32_e32 v0, v2, v0
	v_pk_mul_f32 v[52:53], v[40:41], v[40:41]
	v_add_f32_e32 v0, v3, v0
	v_pk_add_f32 v[22:23], v[4:5], v[64:65] op_sel_hi:[1,0] neg_lo:[0,1] neg_hi:[0,1]
	v_add_f32_e32 v0, v52, v0
	v_pk_mul_f32 v[4:5], v[22:23], v[22:23]
	v_add_f32_e32 v0, v53, v0
	v_pk_add_f32 v[38:39], v[48:49], v[64:65] op_sel_hi:[1,0] neg_lo:[0,1] neg_hi:[0,1]
	v_add_f32_e32 v0, v4, v0
	v_pk_mul_f32 v[48:49], v[38:39], v[38:39]
	v_add_f32_e32 v0, v5, v0
	v_pk_add_f32 v[36:37], v[6:7], v[64:65] op_sel_hi:[1,0] neg_lo:[0,1] neg_hi:[0,1]
	v_add_f32_e32 v0, v48, v0
	v_pk_mul_f32 v[74:75], v[36:37], v[36:37]
	v_add_f32_e32 v0, v49, v0
	v_pk_add_f32 v[34:35], v[30:31], v[64:65] op_sel_hi:[1,0] neg_lo:[0,1] neg_hi:[0,1]
	v_add_f32_e32 v0, v74, v0
	v_pk_mul_f32 v[76:77], v[34:35], v[34:35]
	v_add_f32_e32 v0, v75, v0
	v_pk_add_f32 v[32:33], v[8:9], v[64:65] op_sel_hi:[1,0] neg_lo:[0,1] neg_hi:[0,1]
	v_add_f32_e32 v0, v76, v0
	v_pk_mul_f32 v[78:79], v[32:33], v[32:33]
	v_add_f32_e32 v0, v77, v0
	v_pk_add_f32 v[30:31], v[28:29], v[64:65] op_sel_hi:[1,0] neg_lo:[0,1] neg_hi:[0,1]
	v_add_f32_e32 v0, v78, v0
	v_pk_mul_f32 v[80:81], v[30:31], v[30:31]
	v_add_f32_e32 v0, v79, v0
	v_pk_add_f32 v[28:29], v[10:11], v[64:65] op_sel_hi:[1,0] neg_lo:[0,1] neg_hi:[0,1]
	v_add_f32_e32 v0, v80, v0
	v_pk_mul_f32 v[10:11], v[28:29], v[28:29]
	v_add_f32_e32 v0, v81, v0
	v_pk_add_f32 v[20:21], v[26:27], v[64:65] op_sel_hi:[1,0] neg_lo:[0,1] neg_hi:[0,1]
	v_add_f32_e32 v0, v10, v0
	v_pk_mul_f32 v[26:27], v[20:21], v[20:21]
	v_add_f32_e32 v0, v11, v0
	v_pk_add_f32 v[16:17], v[44:45], v[64:65] op_sel_hi:[1,0] neg_lo:[0,1] neg_hi:[0,1]
	v_add_f32_e32 v0, v26, v0
	v_pk_mul_f32 v[44:45], v[16:17], v[16:17]
	v_add_f32_e32 v0, v27, v0
	v_pk_add_f32 v[8:9], v[18:19], v[64:65] op_sel_hi:[1,0] neg_lo:[0,1] neg_hi:[0,1]
	v_add_f32_e32 v0, v44, v0
	v_pk_mul_f32 v[18:19], v[8:9], v[8:9]
	v_add_f32_e32 v0, v45, v0
	v_pk_add_f32 v[6:7], v[24:25], v[64:65] op_sel_hi:[1,0] neg_lo:[0,1] neg_hi:[0,1]
	v_add_f32_e32 v0, v18, v0
	v_pk_mul_f32 v[24:25], v[6:7], v[6:7]
	v_add_f32_e32 v0, v19, v0
	v_add_f32_e32 v0, v24, v0
	v_add_f32_e32 v0, v25, v0
	v_mov_b32_e32 v1, v105
	s_nop 0
	v_add_f32_dpp v0, v0, v0 quad_perm:[1,0,3,2] row_mask:0xf bank_mask:0xf bound_ctrl:1
	s_nop 1
	v_add_f32_dpp v0, v0, v0 quad_perm:[2,3,0,1] row_mask:0xf bank_mask:0xf bound_ctrl:1
	s_nop 1
	v_add_f32_dpp v0, v0, v0 row_half_mirror row_mask:0xf bank_mask:0xf bound_ctrl:1
	s_nop 1
	v_add_f32_dpp v0, v0, v0 row_mirror row_mask:0xf bank_mask:0xf bound_ctrl:1
	s_nop 1
	v_mov_b32_dpp v1, v0 row_bcast:15 row_mask:0xa bank_mask:0xf
	v_add_f32_e32 v0, v0, v1
	v_mov_b32_e32 v1, v105
	s_nop 1
	v_mov_b32_dpp v1, v0 row_bcast:31 row_mask:0xc bank_mask:0xf
	v_add_f32_e32 v0, v0, v1
	s_nop 0
	v_readlane_b32 s2, v0, 63
	s_nop 1
	v_fma_f32 v0, s2, v187, v183
	v_rsq_f32_e32 v10, v0
	s_mov_b64 s[2:3], -1
	v_pk_mul_f32 v[0:1], v[66:67], v[10:11] op_sel_hi:[1,0]
	v_pk_mul_f32 v[2:3], v[70:71], v[10:11] op_sel_hi:[1,0]
	v_pk_fma_f32 v[0:1], v[0:1], v[54:55], v[56:57]
	v_pk_fma_f32 v[2:3], v[2:3], v[58:59], v[60:61]
	s_cbranch_vccz .LBB0_1142
	ds_read2st64_b64 v[24:27], v62 offset0:8 offset1:16
	v_cvt_pk_bf16_f32 v4, v0, v1
	v_cvt_pk_bf16_f32 v5, v2, v3
	global_store_dwordx2 v[14:15], v[4:5], off
	s_mov_b64 s[2:3], 0
	s_waitcnt lgkmcnt(0)
	v_lshlrev_b32_e32 v18, 16, v26
	v_and_b32_e32 v19, 0xffff0000, v26
	v_lshlrev_b32_e32 v4, 16, v24
	v_and_b32_e32 v5, 0xffff0000, v24
	v_pk_add_f32 v[18:19], v[18:19], 1.0 op_sel_hi:[1,0]
	v_lshlrev_b32_e32 v24, 16, v27
	v_pk_fma_f32 v[4:5], v[0:1], v[18:19], v[4:5]
	v_lshlrev_b32_e32 v18, 16, v25
	v_and_b32_e32 v19, 0xffff0000, v25
	v_and_b32_e32 v25, 0xffff0000, v27
	v_pk_add_f32 v[24:25], v[24:25], 1.0 op_sel_hi:[1,0]
	v_cvt_pk_bf16_f32 v4, v4, v5
	v_pk_fma_f32 v[18:19], v[2:3], v[24:25], v[18:19]
	s_nop 0
	v_cvt_pk_bf16_f32 v5, v18, v19
